# thin phases: loads hipcc serialised behind stores are batched (P0 weights product, P2 spatial unit, P5 LN1 rows + router loop); P2 conv/pool tasks rewritten by hand with row loads up front
# speedup vs baseline: 1.0286x; 1.0286x over previous
; #define LAS __attribute__((address_space(3)))
; __device__ __forceinline__ unsigned f2bf(float f) { unsigned u = __float_as_uint(f); return (u + 0x7fffu + ((u >> 16) & 1u)) >> 16; }
; __device__ __forceinline__ unsigned pk2(float lo, float hi) { return f2bf(lo) | (f2bf(hi) << 16); }
; __device__ __forceinline__ void wcprime_tile(const Params& p, int tile, LAS bf16* sA, LAS bf16* sB, int tid) {
;     const int l = tile >> 8, g = (tile >> 6) & 3, tm = (tile >> 5) & 1, tn = tile & 31;
;     const int lane = tid & 63, wid = tid >> 6, wm = wid >> 1, wn = wid & 1, fr = lane & 15, fq = lane >> 4;
;     const float* Ap = p.in[7] + ((size_t)l * 4 + g) * 256 * 256; const float* sc = p.in[8] + (size_t)l * 1024 + g * 256;
;     const float* Wp = p.in[13] + (size_t)l * 1024 * D + (size_t)(g * 256) * D;
;     unsigned char* dst = p.ws + WS_W + (size_t)l * WL_BYTES + WL_ABC;
;     f32x4 acc[2][2];
; #pragma unroll
;     for (int a = 0; a < 2; ++a)
; #pragma unroll
;         for (int b = 0; b < 2; ++b) acc[a][b] = (f32x4){0.f, 0.f, 0.f, 0.f};
;     const int ar = tid >> 2, akseg = (tid & 3) * 8, wk = tid >> 4, wns = (tid & 15) * 4;
;     for (int k0 = 0; k0 < 256; k0 += 32) {
;         const float* ap = Ap + (size_t)(tm * 128 + ar) * 256 + k0 + akseg;
;         const f32x4 x0 = *(const f32x4*)ap, x1 = *(const f32x4*)(ap + 4), s0 = *(const f32x4*)(sc + k0 + akseg), s1 = *(const f32x4*)(sc + k0 + akseg + 4);
;         u32x4 av; av.x = pk2(x0.x * s0.x, x0.y * s0.y); av.y = pk2(x0.z * s0.z, x0.w * s0.w); av.z = pk2(x1.x * s1.x, x1.y * s1.y); av.w = pk2(x1.z * s1.z, x1.w * s1.w);
;         const f32x4 wv = *(const f32x4*)(Wp + (size_t)(k0 + wk) * D + tn * 64 + wns);
;         *(LAS u32x4*)(sA + ar * 40 + akseg) = av;
;         sB[(wns + 0) * 40 + wk] = (bf16)f2bf(wv.x); sB[(wns + 1) * 40 + wk] = (bf16)f2bf(wv.y); sB[(wns + 2) * 40 + wk] = (bf16)f2bf(wv.z); sB[(wns + 3) * 40 + wk] = (bf16)f2bf(wv.w);
.LBB0_118:
	s_ashr_i32 s0, s19, 8
	s_ashr_i32 s1, s0, 31
	s_bfe_u32 s30, s19, 0x20006
	s_lshl_b64 s[2:3], s[0:1], 20
	s_add_u32 s35, s12, s2
	s_mul_hi_i32 s31, s0, 0x1ca00000
	s_mul_i32 s34, s0, 0x1ca00000
	s_addc_u32 s36, s13, s3
	s_lshl_b64 s[2:3], s[0:1], 12
	s_lshl_b64 s[0:1], s[0:1], 23
	s_lshl_b32 s37, s30, 21
	s_add_u32 s38, s28, s34
	s_addc_u32 s31, s29, s31
	s_lshl_b32 s34, s30, 18
	s_add_u32 s34, s35, s34
	s_addc_u32 s35, s36, 0
	s_add_u32 s2, s14, s2
	s_addc_u32 s3, s15, s3
	s_lshl_b32 s36, s30, 10
	s_add_u32 s2, s2, s36
	s_addc_u32 s3, s3, 0
	s_add_u32 s0, s16, s0
	s_addc_u32 s1, s17, s1
	s_add_u32 s0, s0, s37
	s_addc_u32 s1, s1, 0
	s_and_b32 s36, s4, 0x80
	s_and_b32 s37, s6, 0x7c0
	v_add_u32_e32 v26, s36, v38
	s_lshl_b32 s39, s37, 2
	v_ashrrev_i32_e32 v27, 31, v26
	s_add_u32 s0, s0, s39
	v_lshlrev_b64 v[26:27], 10, v[26:27]
	v_add_u32_e32 v2, s36, v41
	v_or_b32_e32 v28, s37, v1
	s_addc_u32 s1, s1, 0
	v_lshl_add_u64 v[26:27], s[34:35], 0, v[26:27]
	global_load_dwordx4 v[62:65], v22, s[2:3] offset:16
	global_load_dwordx4 v[66:69], v22, s[2:3]
	v_ashrrev_i32_e32 v61, 6, v2
	v_lshlrev_b32_e32 v2, 6, v28
	v_lshl_add_u64 v[30:31], s[0:1], 0, v[24:25]
	v_lshl_add_u64 v[28:29], v[26:27], 0, v[22:23]
	v_lshl_add_u64 v[26:27], v[30:31], 0, v[4:5]
	global_load_dwordx4 v[70:73], v[28:29], off
	global_load_dwordx4 v[74:77], v[28:29], off offset:16
	global_load_dwordx4 v[78:81], v[26:27], off
	s_add_u32 s0, s38, 0.5
	s_addc_u32 s1, s31, 0
	s_lshl_b32 s30, s30, 2
	v_add3_u32 v26, v61, s30, 32
	v_lshl_add_u64 v[98:99], v[30:31], 0, v[6:7]
	v_lshl_add_u64 v[106:107], v[30:31], 0, v[8:9]
	v_lshl_add_u64 v[108:109], v[30:31], 0, v[10:11]
	v_lshl_add_u64 v[36:37], v[30:31], 0, v[12:13]
	v_lshl_add_u64 v[34:35], v[30:31], 0, v[14:15]
	v_lshl_add_u64 v[32:33], v[30:31], 0, v[16:17]
	v_lshl_add_u64 v[30:31], v[30:31], 0, v[18:19]
	global_load_dwordx4 v[110:113], v22, s[2:3] offset:128
	global_load_dwordx4 v[114:117], v[28:29], off offset:128
	global_load_dwordx4 v[118:121], v[28:29], off offset:144
	global_load_dwordx4 v[122:125], v22, s[2:3] offset:144
	global_load_dwordx4 v[126:129], v[98:99], off
	global_load_dwordx4 v[132:135], v22, s[2:3] offset:256
	global_load_dwordx4 v[136:139], v[28:29], off offset:256
	global_load_dwordx4 v[140:143], v[28:29], off offset:272
	global_load_dwordx4 v[144:147], v22, s[2:3] offset:272
	global_load_dwordx4 v[148:151], v[106:107], off
	global_load_dwordx4 v[152:155], v22, s[2:3] offset:384
	global_load_dwordx4 v[156:159], v[28:29], off offset:384
	global_load_dwordx4 v[160:163], v[28:29], off offset:400
	global_load_dwordx4 v[164:167], v22, s[2:3] offset:400
	global_load_dwordx4 v[168:171], v[108:109], off
	global_load_dwordx4 v[172:175], v22, s[2:3] offset:512
	global_load_dwordx4 v[176:179], v[28:29], off offset:512
	global_load_dwordx4 v[180:183], v[28:29], off offset:528
	global_load_dwordx4 v[184:187], v22, s[2:3] offset:528
	global_load_dwordx4 v[188:191], v[36:37], off
	global_load_dwordx4 v[192:195], v22, s[2:3] offset:640
	global_load_dwordx4 v[196:199], v[28:29], off offset:640
	global_load_dwordx4 v[200:203], v[28:29], off offset:656
	global_load_dwordx4 v[204:207], v22, s[2:3] offset:656
	global_load_dwordx4 v[208:211], v[34:35], off
	global_load_dwordx4 v[212:215], v22, s[2:3] offset:768
	global_load_dwordx4 v[216:219], v[28:29], off offset:768
	global_load_dwordx4 v[220:223], v[28:29], off offset:784
	global_load_dwordx4 v[224:227], v22, s[2:3] offset:784
	global_load_dwordx4 v[228:231], v[32:33], off
	global_load_dwordx4 v[232:235], v22, s[2:3] offset:896
	global_load_dwordx4 v[236:239], v[28:29], off offset:896
	global_load_dwordx4 v[240:243], v[28:29], off offset:912
	global_load_dwordx4 v[244:247], v22, s[2:3] offset:912
	global_load_dwordx4 v[250:253], v[30:31], off
	v_ashrrev_i32_e32 v27, 31, v26
	v_lshlrev_b64 v[26:27], 17, v[26:27]
	v_mov_b32_e32 v48, v3
	v_mov_b32_e32 v47, v3
	v_mov_b32_e32 v46, v3
	v_mov_b32_e32 v52, v3
	v_mov_b32_e32 v56, v3
	v_mov_b32_e32 v60, v3
	v_mov_b32_e32 v45, v3
	v_mov_b32_e32 v51, v3
	v_mov_b32_e32 v50, v3
	v_mov_b32_e32 v55, v3
	v_mov_b32_e32 v54, v3
	v_mov_b32_e32 v59, v3
	v_mov_b32_e32 v58, v3
	v_mov_b32_e32 v49, v3
	v_mov_b32_e32 v53, v3
	v_mov_b32_e32 v57, v3
	s_add_i32 s19, s19, s78
	s_add_i32 s4, s4, s5
	s_add_i32 s6, s6, s7
	s_cmpk_lt_i32 s19, 0x200
	s_waitcnt vmcnt(37)
	v_pk_mul_f32 v[68:69], v[72:73], v[68:69]
	v_pk_mul_f32 v[66:67], v[70:71], v[66:67]
	s_waitcnt vmcnt(36)
	v_pk_mul_f32 v[64:65], v[76:77], v[64:65]
	v_pk_mul_f32 v[62:63], v[74:75], v[62:63]
	v_bfe_u32 v73, v65, 16, 1
	v_bfe_u32 v75, v63, 16, 1
	v_bfe_u32 v77, v68, 16, 1
	v_bfe_u32 v82, v64, 16, 1
	v_bfe_u32 v83, v66, 16, 1
	v_bfe_u32 v84, v62, 16, 1
	v_bfe_u32 v74, v69, 16, 1
	v_bfe_u32 v76, v67, 16, 1
	v_add3_u32 v65, v65, v73, s8
	v_add3_u32 v73, v63, v75, s8
	v_add3_u32 v63, v64, v82, s8
	v_add3_u32 v64, v68, v77, s8
	v_add3_u32 v62, v62, v84, s8
	v_add3_u32 v66, v66, v83, s8
	s_waitcnt vmcnt(35)
	v_bfe_u32 v70, v79, 16, 1
	v_bfe_u32 v71, v80, 16, 1
	v_bfe_u32 v72, v81, 16, 1
	v_add3_u32 v69, v69, v74, s8
	v_add3_u32 v67, v67, v76, s8
	v_lshrrev_b32_e32 v64, 16, v64
	v_lshrrev_b32_e32 v63, 16, v63
	v_lshrrev_b32_e32 v66, 16, v66
	v_lshrrev_b32_e32 v62, 16, v62
	v_bfe_u32 v61, v78, 16, 1
	v_add3_u32 v70, v79, v70, s8
	v_add3_u32 v71, v80, v71, s8
	v_add3_u32 v72, v81, v72, s8
	v_and_or_b32 v65, v65, s9, v63
	v_and_or_b32 v63, v69, s9, v64
	v_and_or_b32 v64, v73, s9, v62
	v_and_or_b32 v62, v67, s9, v66
	v_add3_u32 v61, v78, v61, s8
	ds_write_b128 v39, v[62:65]
	ds_write_b16_d16_hi v40, v61 offset:16384
	ds_write_b16_d16_hi v40, v70 offset:16464
	ds_write_b16_d16_hi v40, v71 offset:16544
	ds_write_b16_d16_hi v40, v72 offset:16624
	s_waitcnt lgkmcnt(0)
	s_barrier
; #define LAS __attribute__((address_space(3)))
; __device__ __forceinline__ unsigned f2bf(float f) { unsigned u = __float_as_uint(f); return (u + 0x7fffu + ((u >> 16) & 1u)) >> 16; }
; __device__ __forceinline__ unsigned pk2(float lo, float hi) { return f2bf(lo) | (f2bf(hi) << 16); }
; __device__ __forceinline__ void wcprime_tile(const Params& p, int tile, LAS bf16* sA, LAS bf16* sB, int tid) {
;     ...
;     for (int k0 = 0; k0 < 256; k0 += 32) {
;         const float* ap = Ap + (size_t)(tm * 128 + ar) * 256 + k0 + akseg;
;         const f32x4 x0 = *(const f32x4*)ap, x1 = *(const f32x4*)(ap + 4), s0 = *(const f32x4*)(sc + k0 + akseg), s1 = *(const f32x4*)(sc + k0 + akseg + 4);
;         u32x4 av; av.x = pk2(x0.x * s0.x, x0.y * s0.y); av.y = pk2(x0.z * s0.z, x0.w * s0.w); av.z = pk2(x1.x * s1.x, x1.y * s1.y); av.w = pk2(x1.z * s1.z, x1.w * s1.w);
;         const f32x4 wv = *(const f32x4*)(Wp + (size_t)(k0 + wk) * D + tn * 64 + wns);
;         *(LAS u32x4*)(sA + ar * 40 + akseg) = av;
;         sB[(wns + 0) * 40 + wk] = (bf16)f2bf(wv.x); sB[(wns + 1) * 40 + wk] = (bf16)f2bf(wv.y); sB[(wns + 2) * 40 + wk] = (bf16)f2bf(wv.z); sB[(wns + 3) * 40 + wk] = (bf16)f2bf(wv.w);
;         __syncthreads();
; #pragma unroll
;         for (int mi = 0; mi < 2; ++mi) {
;             const bf16x8 a = *(const LAS bf16x8*)(sA + (wm * 32 + mi * 16 + fr) * 40 + fq * 8);
; #pragma unroll
;             for (int ni = 0; ni < 2; ++ni) {
;                 const bf16x8 b = *(const LAS bf16x8*)(sB + (wn * 32 + ni * 16 + fr) * 40 + fq * 8);
;                 acc[mi][ni] = __builtin_amdgcn_mfma_f32_16x16x32_bf16(a, b, acc[mi][ni], 0, 0, 0);
;             }
;         }
;         __syncthreads();
	ds_read_b128 v[62:65], v42
	ds_read_b128 v[66:69], v43 offset:16384
	ds_read_b128 v[70:73], v43 offset:17664
	ds_read_b128 v[74:77], v42 offset:1280
	s_waitcnt lgkmcnt(0)
	s_barrier
	s_waitcnt vmcnt(0)
	v_mov_b64_e32 v[82:83], v[110:111]
	v_mov_b64_e32 v[84:85], v[112:113]
	v_mov_b64_e32 v[86:87], v[114:115]
	v_mov_b64_e32 v[88:89], v[116:117]
	v_mov_b64_e32 v[90:91], v[118:119]
	v_mov_b64_e32 v[92:93], v[120:121]
	v_mov_b64_e32 v[94:95], v[122:123]
	v_mov_b64_e32 v[96:97], v[124:125]
	v_mfma_f32_16x16x32_bf16 v[78:81], v[62:65], v[66:69], 0
	v_mov_b64_e32 v[98:99], v[126:127]
	v_mov_b64_e32 v[100:101], v[128:129]
	s_waitcnt vmcnt(0)
	v_bfe_u32 v61, v98, 16, 1
	v_mfma_f32_16x16x32_bf16 v[62:65], v[62:65], v[70:73], 0
	v_add3_u32 v61, v98, v61, s8
	v_mfma_f32_16x16x32_bf16 v[66:69], v[74:77], v[66:69], 0
	v_mfma_f32_16x16x32_bf16 v[70:73], v[74:77], v[70:73], 0
	v_mul_f32_e64 v74, v88, v84
	v_mul_f32_e64 v75, v89, v85
	v_pk_mul_f32 v[76:77], v[86:87], v[82:83]
	v_pk_mul_f32 v[82:83], v[92:93], v[96:97]
	v_pk_mul_f32 v[84:85], v[90:91], v[94:95]
	v_bfe_u32 v89, v83, 16, 1
	v_bfe_u32 v92, v77, 16, 1
	v_bfe_u32 v93, v74, 16, 1
	v_bfe_u32 v94, v82, 16, 1
	v_bfe_u32 v95, v76, 16, 1
	v_bfe_u32 v96, v84, 16, 1
	v_bfe_u32 v90, v75, 16, 1
	v_bfe_u32 v91, v85, 16, 1
	v_add3_u32 v83, v83, v89, s8
	v_add3_u32 v89, v77, v92, s8
	v_add3_u32 v77, v82, v94, s8
	v_add3_u32 v74, v74, v93, s8
	v_add3_u32 v82, v84, v96, s8
	v_add3_u32 v76, v76, v95, s8
	v_bfe_u32 v86, v99, 16, 1
	v_bfe_u32 v87, v100, 16, 1
	v_bfe_u32 v88, v101, 16, 1
	v_add3_u32 v75, v75, v90, s8
	v_add3_u32 v85, v85, v91, s8
	v_lshrrev_b32_e32 v74, 16, v74
	v_lshrrev_b32_e32 v77, 16, v77
	v_lshrrev_b32_e32 v84, 16, v76
	v_lshrrev_b32_e32 v76, 16, v82
	v_add3_u32 v86, v99, v86, s8
	v_add3_u32 v87, v100, v87, s8
	v_add3_u32 v88, v101, v88, s8
	v_and_or_b32 v77, v83, s9, v77
	v_and_or_b32 v75, v75, s9, v74
	v_and_or_b32 v76, v85, s9, v76
	v_and_or_b32 v74, v89, s9, v84
	ds_write_b128 v39, v[74:77]
	ds_write_b16_d16_hi v40, v61 offset:16384
	ds_write_b16_d16_hi v40, v86 offset:16464
	ds_write_b16_d16_hi v40, v87 offset:16544
	ds_write_b16_d16_hi v40, v88 offset:16624
	s_waitcnt lgkmcnt(0)
	s_barrier
	ds_read_b128 v[74:77], v42
	ds_read_b128 v[82:85], v43 offset:16384
	ds_read_b128 v[86:89], v43 offset:17664
	ds_read_b128 v[90:93], v42 offset:1280
	s_waitcnt lgkmcnt(0)
	v_mfma_f32_16x16x32_bf16 v[78:81], v[74:77], v[82:85], v[78:81]
	s_barrier
	v_mov_b64_e32 v[94:95], v[132:133]
	v_mov_b64_e32 v[96:97], v[134:135]
	v_mfma_f32_16x16x32_bf16 v[62:65], v[74:77], v[86:89], v[62:65]
	v_mov_b64_e32 v[74:75], v[136:137]
	v_mov_b64_e32 v[76:77], v[138:139]
	v_mov_b64_e32 v[98:99], v[140:141]
	v_mov_b64_e32 v[100:101], v[142:143]
	v_mov_b64_e32 v[102:103], v[144:145]
	v_mov_b64_e32 v[104:105], v[146:147]
	s_waitcnt vmcnt(2)
	v_pk_mul_f32 v[76:77], v[76:77], v[96:97]
	v_mfma_f32_16x16x32_bf16 v[66:69], v[90:93], v[82:85], v[66:69]
	v_mov_b64_e32 v[82:83], v[148:149]
	v_mov_b64_e32 v[84:85], v[150:151]
	v_pk_mul_f32 v[74:75], v[74:75], v[94:95]
	v_bfe_u32 v94, v77, 16, 1
	v_mfma_f32_16x16x32_bf16 v[70:73], v[90:93], v[86:89], v[70:73]
	s_waitcnt vmcnt(1)
	v_pk_mul_f32 v[86:87], v[100:101], v[104:105]
	v_pk_mul_f32 v[88:89], v[98:99], v[102:103]
	v_bfe_u32 v93, v87, 16, 1
	v_bfe_u32 v96, v75, 16, 1
	v_bfe_u32 v97, v76, 16, 1
	v_bfe_u32 v98, v86, 16, 1
	v_bfe_u32 v99, v74, 16, 1
	v_bfe_u32 v100, v88, 16, 1
	v_bfe_u32 v95, v89, 16, 1
	v_add3_u32 v76, v76, v97, s8
	v_add3_u32 v74, v74, v99, s8
	v_add3_u32 v89, v89, v95, s8
	v_lshrrev_b32_e32 v76, 16, v76
	v_lshrrev_b32_e32 v74, 16, v74
	s_waitcnt vmcnt(0)
	v_bfe_u32 v61, v82, 16, 1
	v_bfe_u32 v90, v83, 16, 1
	v_bfe_u32 v91, v84, 16, 1
	v_bfe_u32 v92, v85, 16, 1
	v_add3_u32 v61, v82, v61, s8
	v_add3_u32 v82, v83, v90, s8
	v_add3_u32 v83, v84, v91, s8
	v_add3_u32 v84, v85, v92, s8
	v_add3_u32 v85, v77, v94, s8
	v_add3_u32 v77, v87, v93, s8
	v_add3_u32 v87, v75, v96, s8
	v_add3_u32 v75, v86, v98, s8
	v_add3_u32 v86, v88, v100, s8
	v_lshrrev_b32_e32 v75, 16, v75
	v_lshrrev_b32_e32 v86, 16, v86
	v_and_or_b32 v77, v77, s9, v75
	v_and_or_b32 v75, v85, s9, v76
	v_and_or_b32 v76, v89, s9, v86
	v_and_or_b32 v74, v87, s9, v74
	ds_write_b128 v39, v[74:77]
	ds_write_b16_d16_hi v40, v61 offset:16384
	ds_write_b16_d16_hi v40, v82 offset:16464
	ds_write_b16_d16_hi v40, v83 offset:16544
	ds_write_b16_d16_hi v40, v84 offset:16624
	s_waitcnt lgkmcnt(0)
	s_barrier
	ds_read_b128 v[74:77], v42
	ds_read_b128 v[82:85], v43 offset:16384
	ds_read_b128 v[86:89], v43 offset:17664
	ds_read_b128 v[90:93], v42 offset:1280
	s_waitcnt lgkmcnt(0)
	v_mfma_f32_16x16x32_bf16 v[78:81], v[74:77], v[82:85], v[78:81]
	s_barrier
; #define LAS __attribute__((address_space(3)))
; __device__ __forceinline__ unsigned f2bf(float f) { unsigned u = __float_as_uint(f); return (u + 0x7fffu + ((u >> 16) & 1u)) >> 16; }
; __device__ __forceinline__ unsigned pk2(float lo, float hi) { return f2bf(lo) | (f2bf(hi) << 16); }
; __device__ __forceinline__ void wcprime_tile(const Params& p, int tile, LAS bf16* sA, LAS bf16* sB, int tid) {
;     ...
;     for (int k0 = 0; k0 < 256; k0 += 32) {
;         const float* ap = Ap + (size_t)(tm * 128 + ar) * 256 + k0 + akseg;
;         const f32x4 x0 = *(const f32x4*)ap, x1 = *(const f32x4*)(ap + 4), s0 = *(const f32x4*)(sc + k0 + akseg), s1 = *(const f32x4*)(sc + k0 + akseg + 4);
;         u32x4 av; av.x = pk2(x0.x * s0.x, x0.y * s0.y); av.y = pk2(x0.z * s0.z, x0.w * s0.w); av.z = pk2(x1.x * s1.x, x1.y * s1.y); av.w = pk2(x1.z * s1.z, x1.w * s1.w);
;         const f32x4 wv = *(const f32x4*)(Wp + (size_t)(k0 + wk) * D + tn * 64 + wns);
;         *(LAS u32x4*)(sA + ar * 40 + akseg) = av;
;         sB[(wns + 0) * 40 + wk] = (bf16)f2bf(wv.x); sB[(wns + 1) * 40 + wk] = (bf16)f2bf(wv.y); sB[(wns + 2) * 40 + wk] = (bf16)f2bf(wv.z); sB[(wns + 3) * 40 + wk] = (bf16)f2bf(wv.w);
;         __syncthreads();
; #pragma unroll
;         for (int mi = 0; mi < 2; ++mi) {
;             const bf16x8 a = *(const LAS bf16x8*)(sA + (wm * 32 + mi * 16 + fr) * 40 + fq * 8);
; #pragma unroll
;             for (int ni = 0; ni < 2; ++ni) {
;                 const bf16x8 b = *(const LAS bf16x8*)(sB + (wn * 32 + ni * 16 + fr) * 40 + fq * 8);
;                 acc[mi][ni] = __builtin_amdgcn_mfma_f32_16x16x32_bf16(a, b, acc[mi][ni], 0, 0, 0);
;             }
;         }
;         __syncthreads();
	v_mov_b64_e32 v[94:95], v[152:153]
	v_mov_b64_e32 v[96:97], v[154:155]
	v_mfma_f32_16x16x32_bf16 v[62:65], v[74:77], v[86:89], v[62:65]
	v_mov_b64_e32 v[74:75], v[156:157]
	v_mov_b64_e32 v[76:77], v[158:159]
	v_mov_b64_e32 v[98:99], v[160:161]
	v_mov_b64_e32 v[100:101], v[162:163]
	v_mov_b64_e32 v[102:103], v[164:165]
	v_mov_b64_e32 v[104:105], v[166:167]
	s_waitcnt vmcnt(2)
	v_pk_mul_f32 v[76:77], v[76:77], v[96:97]
	v_mfma_f32_16x16x32_bf16 v[66:69], v[90:93], v[82:85], v[66:69]
	v_mov_b64_e32 v[82:83], v[168:169]
	v_mov_b64_e32 v[84:85], v[170:171]
	v_pk_mul_f32 v[74:75], v[74:75], v[94:95]
	v_bfe_u32 v94, v77, 16, 1
	v_mfma_f32_16x16x32_bf16 v[70:73], v[90:93], v[86:89], v[70:73]
	s_waitcnt vmcnt(1)
	v_pk_mul_f32 v[86:87], v[100:101], v[104:105]
	v_pk_mul_f32 v[88:89], v[98:99], v[102:103]
	v_bfe_u32 v93, v87, 16, 1
	v_bfe_u32 v96, v75, 16, 1
	v_bfe_u32 v97, v76, 16, 1
	v_bfe_u32 v98, v86, 16, 1
	v_bfe_u32 v99, v74, 16, 1
	v_bfe_u32 v100, v88, 16, 1
	v_bfe_u32 v95, v89, 16, 1
	v_add3_u32 v76, v76, v97, s8
	v_add3_u32 v74, v74, v99, s8
	v_add3_u32 v89, v89, v95, s8
	v_lshrrev_b32_e32 v76, 16, v76
	v_lshrrev_b32_e32 v74, 16, v74
	s_waitcnt vmcnt(0)
	v_bfe_u32 v61, v82, 16, 1
	v_bfe_u32 v90, v83, 16, 1
	v_bfe_u32 v91, v84, 16, 1
	v_bfe_u32 v92, v85, 16, 1
	v_add3_u32 v61, v82, v61, s8
	v_add3_u32 v82, v83, v90, s8
	v_add3_u32 v83, v84, v91, s8
	v_add3_u32 v84, v85, v92, s8
	v_add3_u32 v85, v77, v94, s8
	v_add3_u32 v77, v87, v93, s8
	v_add3_u32 v87, v75, v96, s8
	v_add3_u32 v75, v86, v98, s8
	v_add3_u32 v86, v88, v100, s8
	v_lshrrev_b32_e32 v75, 16, v75
	v_lshrrev_b32_e32 v86, 16, v86
	v_and_or_b32 v77, v77, s9, v75
	v_and_or_b32 v75, v85, s9, v76
	v_and_or_b32 v76, v89, s9, v86
	v_and_or_b32 v74, v87, s9, v74
	ds_write_b128 v39, v[74:77]
	ds_write_b16_d16_hi v40, v61 offset:16384
	ds_write_b16_d16_hi v40, v82 offset:16464
	ds_write_b16_d16_hi v40, v83 offset:16544
	ds_write_b16_d16_hi v40, v84 offset:16624
	s_waitcnt lgkmcnt(0)
	s_barrier
	ds_read_b128 v[74:77], v42
	ds_read_b128 v[82:85], v43 offset:16384
	ds_read_b128 v[86:89], v43 offset:17664
	ds_read_b128 v[90:93], v42 offset:1280
	s_waitcnt lgkmcnt(0)
	v_mfma_f32_16x16x32_bf16 v[78:81], v[74:77], v[82:85], v[78:81]
	s_barrier
	v_mov_b64_e32 v[94:95], v[172:173]
	v_mov_b64_e32 v[96:97], v[174:175]
	v_mfma_f32_16x16x32_bf16 v[62:65], v[74:77], v[86:89], v[62:65]
	v_mov_b64_e32 v[74:75], v[176:177]
	v_mov_b64_e32 v[76:77], v[178:179]
	v_mov_b64_e32 v[98:99], v[180:181]
	v_mov_b64_e32 v[100:101], v[182:183]
	v_mov_b64_e32 v[102:103], v[184:185]
	v_mov_b64_e32 v[104:105], v[186:187]
	s_waitcnt vmcnt(2)
	v_pk_mul_f32 v[74:75], v[74:75], v[94:95]
	v_mfma_f32_16x16x32_bf16 v[66:69], v[90:93], v[82:85], v[66:69]
	v_mov_b64_e32 v[82:83], v[188:189]
	v_mov_b64_e32 v[84:85], v[190:191]
	v_pk_mul_f32 v[36:37], v[76:77], v[96:97]
	s_waitcnt vmcnt(1)
	v_pk_mul_f32 v[76:77], v[100:101], v[104:105]
	v_mfma_f32_16x16x32_bf16 v[70:73], v[90:93], v[86:89], v[70:73]
	v_mul_f32_e64 v86, v98, v102
	v_mul_f32_e64 v87, v99, v103
	v_bfe_u32 v94, v75, 16, 1
	v_bfe_u32 v95, v36, 16, 1
	v_bfe_u32 v96, v76, 16, 1
	v_bfe_u32 v97, v74, 16, 1
	v_bfe_u32 v98, v86, 16, 1
	v_bfe_u32 v91, v77, 16, 1
	v_bfe_u32 v92, v37, 16, 1
	v_bfe_u32 v93, v87, 16, 1
	v_add3_u32 v36, v36, v95, s8
	v_add3_u32 v74, v74, v97, s8
	v_add3_u32 v37, v37, v92, s8
	v_add3_u32 v77, v77, v91, s8
	v_add3_u32 v87, v87, v93, s8
	v_lshrrev_b32_e32 v36, 16, v36
	v_lshrrev_b32_e32 v74, 16, v74
	s_waitcnt vmcnt(0)
	v_bfe_u32 v61, v82, 16, 1
	v_bfe_u32 v88, v83, 16, 1
	v_bfe_u32 v89, v84, 16, 1
	v_bfe_u32 v90, v85, 16, 1
	v_add3_u32 v61, v82, v61, s8
	v_add3_u32 v82, v83, v88, s8
	v_add3_u32 v83, v84, v89, s8
	v_add3_u32 v84, v85, v90, s8
	v_add3_u32 v85, v75, v94, s8
	v_add3_u32 v75, v76, v96, s8
	v_add3_u32 v76, v86, v98, s8
	v_lshrrev_b32_e32 v75, 16, v75
	v_lshrrev_b32_e32 v76, 16, v76
	v_and_or_b32 v77, v77, s9, v75
	v_and_or_b32 v75, v37, s9, v36
	v_and_or_b32 v76, v87, s9, v76
	v_and_or_b32 v74, v85, s9, v74
	ds_write_b128 v39, v[74:77]
	ds_write_b16_d16_hi v40, v61 offset:16384
	ds_write_b16_d16_hi v40, v82 offset:16464
	ds_write_b16_d16_hi v40, v83 offset:16544
	ds_write_b16_d16_hi v40, v84 offset:16624
	s_waitcnt lgkmcnt(0)
	s_barrier
	ds_read_b128 v[74:77], v42
	ds_read_b128 v[82:85], v43 offset:16384
	ds_read_b128 v[86:89], v43 offset:17664
	ds_read_b128 v[90:93], v42 offset:1280
	s_waitcnt lgkmcnt(0)
	v_mfma_f32_16x16x32_bf16 v[78:81], v[74:77], v[82:85], v[78:81]
	s_barrier
	v_mov_b64_e32 v[94:95], v[192:193]
	v_mov_b64_e32 v[96:97], v[194:195]
	v_mfma_f32_16x16x32_bf16 v[62:65], v[74:77], v[86:89], v[62:65]
	v_mov_b64_e32 v[74:75], v[196:197]
	v_mov_b64_e32 v[76:77], v[198:199]
	v_mov_b64_e32 v[98:99], v[200:201]
	v_mov_b64_e32 v[100:101], v[202:203]
	v_mov_b64_e32 v[102:103], v[204:205]
	v_mov_b64_e32 v[104:105], v[206:207]
	s_waitcnt vmcnt(2)
	v_pk_mul_f32 v[76:77], v[76:77], v[96:97]
	v_mov_b64_e32 v[34:35], v[208:209]
	v_mov_b64_e32 v[36:37], v[210:211]
	v_mfma_f32_16x16x32_bf16 v[66:69], v[90:93], v[82:85], v[66:69]
	v_mul_f32_e64 v74, v74, v94
	v_mul_f32_e64 v75, v75, v95
	s_waitcnt vmcnt(1)
	v_pk_mul_f32 v[82:83], v[100:101], v[104:105]
	v_pk_mul_f32 v[84:85], v[98:99], v[102:103]
	v_mfma_f32_16x16x32_bf16 v[70:73], v[90:93], v[86:89], v[70:73]
	v_bfe_u32 v90, v77, 16, 1
	v_bfe_u32 v93, v76, 16, 1
	v_bfe_u32 v94, v82, 16, 1
	v_bfe_u32 v95, v74, 16, 1
	v_bfe_u32 v96, v84, 16, 1
	v_bfe_u32 v89, v83, 16, 1
	v_bfe_u32 v91, v85, 16, 1
	v_bfe_u32 v92, v75, 16, 1
	v_add3_u32 v76, v76, v93, s8
	v_add3_u32 v74, v74, v95, s8
	v_add3_u32 v75, v75, v92, s8
	v_lshrrev_b32_e32 v76, 16, v76
	v_lshrrev_b32_e32 v74, 16, v74
	s_waitcnt vmcnt(0)
	v_bfe_u32 v61, v34, 16, 1
	v_bfe_u32 v88, v37, 16, 1
	v_bfe_u32 v86, v35, 16, 1
	v_bfe_u32 v87, v36, 16, 1
	v_add3_u32 v61, v34, v61, s8
	v_add3_u32 v88, v37, v88, s8
	v_add3_u32 v34, v77, v90, s8
	v_add3_u32 v37, v82, v94, s8
	v_add3_u32 v77, v84, v96, s8
	v_add3_u32 v86, v35, v86, s8
	v_add3_u32 v87, v36, v87, s8
	v_add3_u32 v35, v83, v89, s8
	v_add3_u32 v36, v85, v91, s8
	v_lshrrev_b32_e32 v37, 16, v37
	v_lshrrev_b32_e32 v77, 16, v77
	v_and_or_b32 v37, v35, s9, v37
	v_and_or_b32 v35, v34, s9, v76
	v_and_or_b32 v36, v36, s9, v77
	v_and_or_b32 v34, v75, s9, v74
	ds_write_b128 v39, v[34:37]
	ds_write_b16_d16_hi v40, v61 offset:16384
	ds_write_b16_d16_hi v40, v86 offset:16464
	ds_write_b16_d16_hi v40, v87 offset:16544
	ds_write_b16_d16_hi v40, v88 offset:16624
	s_waitcnt lgkmcnt(0)
	s_barrier
; #define LAS __attribute__((address_space(3)))
; __device__ __forceinline__ unsigned f2bf(float f) { unsigned u = __float_as_uint(f); return (u + 0x7fffu + ((u >> 16) & 1u)) >> 16; }
; __device__ __forceinline__ unsigned pk2(float lo, float hi) { return f2bf(lo) | (f2bf(hi) << 16); }
; __device__ __forceinline__ void wcprime_tile(const Params& p, int tile, LAS bf16* sA, LAS bf16* sB, int tid) {
;     ...
;     for (int k0 = 0; k0 < 256; k0 += 32) {
;         const float* ap = Ap + (size_t)(tm * 128 + ar) * 256 + k0 + akseg;
;         const f32x4 x0 = *(const f32x4*)ap, x1 = *(const f32x4*)(ap + 4), s0 = *(const f32x4*)(sc + k0 + akseg), s1 = *(const f32x4*)(sc + k0 + akseg + 4);
;         u32x4 av; av.x = pk2(x0.x * s0.x, x0.y * s0.y); av.y = pk2(x0.z * s0.z, x0.w * s0.w); av.z = pk2(x1.x * s1.x, x1.y * s1.y); av.w = pk2(x1.z * s1.z, x1.w * s1.w);
;         const f32x4 wv = *(const f32x4*)(Wp + (size_t)(k0 + wk) * D + tn * 64 + wns);
;         *(LAS u32x4*)(sA + ar * 40 + akseg) = av;
;         sB[(wns + 0) * 40 + wk] = (bf16)f2bf(wv.x); sB[(wns + 1) * 40 + wk] = (bf16)f2bf(wv.y); sB[(wns + 2) * 40 + wk] = (bf16)f2bf(wv.z); sB[(wns + 3) * 40 + wk] = (bf16)f2bf(wv.w);
;         __syncthreads();
; #pragma unroll
;         for (int mi = 0; mi < 2; ++mi) {
;             const bf16x8 a = *(const LAS bf16x8*)(sA + (wm * 32 + mi * 16 + fr) * 40 + fq * 8);
; #pragma unroll
;             for (int ni = 0; ni < 2; ++ni) {
;                 const bf16x8 b = *(const LAS bf16x8*)(sB + (wn * 32 + ni * 16 + fr) * 40 + fq * 8);
;                 acc[mi][ni] = __builtin_amdgcn_mfma_f32_16x16x32_bf16(a, b, acc[mi][ni], 0, 0, 0);
;             }
;         }
;         __syncthreads();
	ds_read_b128 v[34:37], v42
	ds_read_b128 v[74:77], v43 offset:16384
	ds_read_b128 v[82:85], v43 offset:17664
	ds_read_b128 v[86:89], v42 offset:1280
	s_waitcnt lgkmcnt(0)
	v_mfma_f32_16x16x32_bf16 v[78:81], v[34:37], v[74:77], v[78:81]
	s_barrier
	v_mov_b64_e32 v[90:91], v[212:213]
	v_mov_b64_e32 v[92:93], v[214:215]
	v_mfma_f32_16x16x32_bf16 v[34:37], v[34:37], v[82:85], v[62:65]
	s_nop 2
	v_mov_b64_e32 v[62:63], v[216:217]
	v_mov_b64_e32 v[64:65], v[218:219]
	v_mov_b64_e32 v[94:95], v[220:221]
	v_mov_b64_e32 v[96:97], v[222:223]
	v_mov_b64_e32 v[98:99], v[224:225]
	v_mov_b64_e32 v[100:101], v[226:227]
	s_waitcnt vmcnt(2)
	v_pk_mul_f32 v[62:63], v[62:63], v[90:91]
	v_mfma_f32_16x16x32_bf16 v[66:69], v[86:89], v[74:77], v[66:69]
	v_mov_b64_e32 v[74:75], v[228:229]
	v_mov_b64_e32 v[76:77], v[230:231]
	v_pk_mul_f32 v[32:33], v[64:65], v[92:93]
	s_waitcnt vmcnt(1)
	v_pk_mul_f32 v[64:65], v[96:97], v[100:101]
	v_mfma_f32_16x16x32_bf16 v[70:73], v[86:89], v[82:85], v[70:73]
	v_mul_f32_e64 v82, v94, v98
	v_mul_f32_e64 v83, v95, v99
	v_bfe_u32 v90, v63, 16, 1
	v_bfe_u32 v91, v32, 16, 1
	v_bfe_u32 v92, v64, 16, 1
	v_bfe_u32 v93, v62, 16, 1
	v_bfe_u32 v94, v82, 16, 1
	v_bfe_u32 v87, v65, 16, 1
	v_bfe_u32 v88, v33, 16, 1
	v_bfe_u32 v89, v83, 16, 1
	v_add3_u32 v32, v32, v91, s8
	v_add3_u32 v62, v62, v93, s8
	v_add3_u32 v33, v33, v88, s8
	v_add3_u32 v65, v65, v87, s8
	v_add3_u32 v83, v83, v89, s8
	v_lshrrev_b32_e32 v32, 16, v32
	v_lshrrev_b32_e32 v62, 16, v62
	s_waitcnt vmcnt(0)
	v_bfe_u32 v61, v74, 16, 1
	v_bfe_u32 v84, v75, 16, 1
	v_bfe_u32 v85, v76, 16, 1
	v_bfe_u32 v86, v77, 16, 1
	v_add3_u32 v61, v74, v61, s8
	v_add3_u32 v74, v75, v84, s8
	v_add3_u32 v75, v76, v85, s8
	v_add3_u32 v76, v77, v86, s8
	v_add3_u32 v77, v63, v90, s8
	v_add3_u32 v63, v64, v92, s8
	v_add3_u32 v64, v82, v94, s8
	v_lshrrev_b32_e32 v63, 16, v63
	v_lshrrev_b32_e32 v64, 16, v64
	v_and_or_b32 v65, v65, s9, v63
	v_and_or_b32 v63, v33, s9, v32
	v_and_or_b32 v64, v83, s9, v64
	v_and_or_b32 v62, v77, s9, v62
	ds_write_b128 v39, v[62:65]
	ds_write_b16_d16_hi v40, v61 offset:16384
	ds_write_b16_d16_hi v40, v74 offset:16464
	ds_write_b16_d16_hi v40, v75 offset:16544
	ds_write_b16_d16_hi v40, v76 offset:16624
	s_waitcnt lgkmcnt(0)
	s_barrier
	ds_read_b128 v[62:65], v42
	ds_read_b128 v[74:77], v43 offset:16384
	ds_read_b128 v[82:85], v43 offset:17664
	ds_read_b128 v[86:89], v42 offset:1280
	s_waitcnt lgkmcnt(0)
	v_mfma_f32_16x16x32_bf16 v[78:81], v[62:65], v[74:77], v[78:81]
	s_barrier
	v_mov_b64_e32 v[90:91], v[232:233]
	v_mov_b64_e32 v[92:93], v[234:235]
	v_mfma_f32_16x16x32_bf16 v[32:35], v[62:65], v[82:85], v[34:37]
	v_mov_b64_e32 v[62:63], v[236:237]
	v_mov_b64_e32 v[64:65], v[238:239]
	v_mov_b64_e32 v[94:95], v[240:241]
	v_mov_b64_e32 v[96:97], v[242:243]
	v_mov_b64_e32 v[98:99], v[244:245]
	v_mov_b64_e32 v[100:101], v[246:247]
	s_waitcnt vmcnt(2)
	v_pk_mul_f32 v[36:37], v[64:65], v[92:93]
	v_mov_b64_e32 v[28:29], v[250:251]
	v_mov_b64_e32 v[30:31], v[252:253]
	v_mfma_f32_16x16x32_bf16 v[66:69], v[86:89], v[74:77], v[66:69]
	v_mul_f32_e64 v62, v62, v90
	v_mul_f32_e64 v63, v63, v91
	s_waitcnt vmcnt(1)
	v_pk_mul_f32 v[64:65], v[96:97], v[100:101]
	v_pk_mul_f32 v[74:75], v[94:95], v[98:99]
	v_mfma_f32_16x16x32_bf16 v[70:73], v[86:89], v[82:85], v[70:73]
	v_bfe_u32 v84, v37, 16, 1
	v_bfe_u32 v86, v63, 16, 1
	v_bfe_u32 v87, v36, 16, 1
	v_bfe_u32 v88, v64, 16, 1
	v_bfe_u32 v89, v62, 16, 1
	v_bfe_u32 v90, v74, 16, 1
	v_bfe_u32 v83, v65, 16, 1
	v_bfe_u32 v85, v75, 16, 1
	v_add3_u32 v36, v36, v87, s8
	v_add3_u32 v62, v62, v89, s8
	v_lshrrev_b32_e32 v36, 16, v36
	v_lshrrev_b32_e32 v62, 16, v62
	s_waitcnt vmcnt(0)
	v_bfe_u32 v61, v28, 16, 1
	v_bfe_u32 v82, v31, 16, 1
	v_bfe_u32 v76, v29, 16, 1
	v_bfe_u32 v77, v30, 16, 1
	v_add3_u32 v61, v28, v61, s8
	v_add3_u32 v82, v31, v82, s8
	v_add3_u32 v28, v37, v84, s8
	v_add3_u32 v37, v63, v86, s8
	v_add3_u32 v31, v64, v88, s8
	v_add3_u32 v63, v74, v90, s8
	v_add3_u32 v76, v29, v76, s8
	v_add3_u32 v77, v30, v77, s8
	v_add3_u32 v29, v65, v83, s8
	v_add3_u32 v30, v75, v85, s8
	v_lshrrev_b32_e32 v31, 16, v31
	v_lshrrev_b32_e32 v63, 16, v63
	v_and_or_b32 v31, v29, s9, v31
	v_and_or_b32 v29, v28, s9, v36
	v_and_or_b32 v30, v30, s9, v63
	v_and_or_b32 v28, v37, s9, v62
	ds_write_b128 v39, v[28:31]
	ds_write_b16_d16_hi v40, v61 offset:16384
	ds_write_b16_d16_hi v40, v76 offset:16464
	ds_write_b16_d16_hi v40, v77 offset:16544
	ds_write_b16_d16_hi v40, v82 offset:16624
	s_waitcnt lgkmcnt(0)
	s_barrier
; #define LAS __attribute__((address_space(3)))
; __device__ __forceinline__ unsigned pk4_fp8(float a, float b, float c, float d) { unsigned w = 0u; w = __builtin_amdgcn_cvt_pk_fp8_f32(clamp8(a), clamp8(b), w, false); w = __builtin_amdgcn_cvt_pk_fp8_f32(clamp8(c), clamp8(d), w, true); return w; }
; __device__ __forceinline__ void wcprime_tile(const Params& p, int tile, LAS bf16* sA, LAS bf16* sB, int tid) {
;     ...
; #pragma unroll
;         for (int mi = 0; mi < 2; ++mi) {
;             const bf16x8 a = *(const LAS bf16x8*)(sA + (wm * 32 + mi * 16 + fr) * 40 + fq * 8);
; #pragma unroll
;             for (int ni = 0; ni < 2; ++ni) {
;                 const bf16x8 b = *(const LAS bf16x8*)(sB + (wn * 32 + ni * 16 + fr) * 40 + fq * 8);
;                 acc[mi][ni] = __builtin_amdgcn_mfma_f32_16x16x32_bf16(a, b, acc[mi][ni], 0, 0, 0);
;             }
;         }
;         __syncthreads();
;     }
; #pragma unroll
;     for (int mi = 0; mi < 2; ++mi)
; #pragma unroll
;         for (int ni = 0; ni < 2; ++ni)
; #pragma unroll
;             for (int j = 0; j < 4; ++j) { const int c = tm * 128 + wm * 32 + mi * 16 + fq * 4 + j, n = tn * 64 + wn * 32 + ni * 16 + fr;
;                 dst[((size_t)(32 + g * 4 + (c >> 6)) * 2048 + n) * 64 + (c & 63)] = (unsigned char)(pk4_fp8(64.f * acc[mi][ni][j], 0.f, 0.f, 0.f) & 255u); }
	ds_read_b128 v[28:31], v42
	ds_read_b128 v[62:65], v43 offset:16384
	ds_read_b128 v[74:77], v43 offset:17664
	ds_read_b128 v[82:85], v42 offset:1280
	s_waitcnt lgkmcnt(2)
	v_mfma_f32_16x16x32_bf16 v[78:81], v[28:31], v[62:65], v[78:81]
	v_lshl_add_u64 v[36:37], s[0:1], 0, v[26:27]
	v_or3_b32 v26, v2, v26, s18
	v_lshl_add_u64 v[36:37], v[36:37], 0, v[2:3]
	s_waitcnt lgkmcnt(1)
	v_mfma_f32_16x16x32_bf16 v[28:31], v[28:31], v[74:77], v[32:35]
	s_nop 2
	v_mul_f32_e32 v61, 0x42800000, v79
	v_mul_f32_e32 v2, 0x42800000, v78
	v_med3_f32 v61, v61, s10, v44
	s_waitcnt lgkmcnt(0)
	v_mfma_f32_16x16x32_bf16 v[32:35], v[82:85], v[62:65], v[66:69]
	v_med3_f32 v2, v2, s10, v44
	v_mul_f32_e32 v31, 0x42800000, v31
	v_mul_f32_e32 v29, 0x42800000, v29
	v_mfma_f32_16x16x32_bf16 v[62:65], v[82:85], v[74:77], v[70:73]
	v_mul_f32_e32 v67, 0x42800000, v81
	v_mul_f32_e32 v66, 0x42800000, v80
	s_nop 1
	v_mul_f32_e32 v35, 0x42800000, v35
	v_med3_f32 v67, v67, s10, v44
	v_mul_f32_e32 v30, 0x42800000, v30
	s_nop 0
	v_mul_f32_e32 v65, 0x42800000, v65
	v_mul_f32_e32 v33, 0x42800000, v33
	v_mul_f32_e32 v34, 0x42800000, v34
	v_mul_f32_e32 v63, 0x42800000, v63
	v_mul_f32_e32 v64, 0x42800000, v64
	v_med3_f32 v66, v66, s10, v44
	v_med3_f32 v31, v31, s10, v44
	v_med3_f32 v35, v35, s10, v44
	v_med3_f32 v65, v65, s10, v44
	v_cvt_pk_fp8_f32 v48, v67, 0
	v_mul_f32_e32 v28, 0x42800000, v28
	v_mul_f32_e32 v32, 0x42800000, v32
	v_mul_f32_e32 v62, 0x42800000, v62
	v_med3_f32 v29, v29, s10, v44
	v_med3_f32 v30, v30, s10, v44
	v_med3_f32 v33, v33, s10, v44
	v_med3_f32 v34, v34, s10, v44
	v_med3_f32 v63, v63, s10, v44
	v_med3_f32 v64, v64, s10, v44
	v_cvt_pk_fp8_f32 v47, v61, 0
	v_cvt_pk_fp8_f32 v46, v66, 0
	v_cvt_pk_fp8_f32 v52, v31, 0
	v_cvt_pk_fp8_f32 v56, v35, 0
	v_cvt_pk_fp8_f32 v60, v65, 0
	v_med3_f32 v28, v28, s10, v44
	v_med3_f32 v32, v32, s10, v44
	v_med3_f32 v62, v62, s10, v44
	v_cvt_pk_fp8_f32 v45, v2, 0
	v_cvt_pk_fp8_f32 v51, v29, 0
	v_cvt_pk_fp8_f32 v50, v30, 0
	v_cvt_pk_fp8_f32 v55, v33, 0
	v_cvt_pk_fp8_f32 v54, v34, 0
	v_cvt_pk_fp8_f32 v59, v63, 0
	v_cvt_pk_fp8_f32 v58, v64, 0
	v_cvt_pk_fp8_f32 v49, v28, 0
	v_cvt_pk_fp8_f32 v53, v32, 0
	v_cvt_pk_fp8_f32 v57, v62, 0
	v_cvt_pk_fp8_f32 v48, 0, 0 op_sel:[0,0,1]
	v_cvt_pk_fp8_f32 v47, 0, 0 op_sel:[0,0,1]
	v_cvt_pk_fp8_f32 v46, 0, 0 op_sel:[0,0,1]
	v_cvt_pk_fp8_f32 v52, 0, 0 op_sel:[0,0,1]
	v_cvt_pk_fp8_f32 v56, 0, 0 op_sel:[0,0,1]
	v_cvt_pk_fp8_f32 v60, 0, 0 op_sel:[0,0,1]
	v_cvt_pk_fp8_f32 v45, 0, 0 op_sel:[0,0,1]
	v_cvt_pk_fp8_f32 v51, 0, 0 op_sel:[0,0,1]
	v_cvt_pk_fp8_f32 v50, 0, 0 op_sel:[0,0,1]
	v_cvt_pk_fp8_f32 v55, 0, 0 op_sel:[0,0,1]
	v_cvt_pk_fp8_f32 v54, 0, 0 op_sel:[0,0,1]
	v_cvt_pk_fp8_f32 v59, 0, 0 op_sel:[0,0,1]
	v_cvt_pk_fp8_f32 v58, 0, 0 op_sel:[0,0,1]
	v_cvt_pk_fp8_f32 v49, 0, 0 op_sel:[0,0,1]
	v_cvt_pk_fp8_f32 v53, 0, 0 op_sel:[0,0,1]
	v_cvt_pk_fp8_f32 v57, 0, 0 op_sel:[0,0,1]
	v_lshlrev_b16_e32 v28, 8, v48
	v_lshlrev_b16_e32 v2, 8, v47
	v_lshlrev_b16_e32 v30, 8, v52
	v_lshlrev_b16_e32 v32, 8, v56
	v_lshlrev_b16_e32 v34, 8, v60
	v_bitop3_b16 v28, v46, v28, s11 bitop3:0xec
	v_lshlrev_b16_e32 v29, 8, v51
	v_lshlrev_b16_e32 v31, 8, v55
	v_lshlrev_b16_e32 v33, 8, v59
	v_bitop3_b16 v2, v45, v2, s11 bitop3:0xec
	v_bitop3_b16 v30, v50, v30, s11 bitop3:0xec
	v_bitop3_b16 v32, v54, v32, s11 bitop3:0xec
	v_bitop3_b16 v34, v58, v34, s11 bitop3:0xec
	v_lshlrev_b32_e32 v28, 16, v28
	v_lshl_add_u64 v[26:27], s[0:1], 0, v[26:27]
	v_lshl_add_u64 v[36:37], v[36:37], 0, v[20:21]
	v_bitop3_b16 v29, v49, v29, s11 bitop3:0xec
	v_bitop3_b16 v31, v53, v31, s11 bitop3:0xec
	v_bitop3_b16 v33, v57, v33, s11 bitop3:0xec
	v_lshlrev_b32_e32 v30, 16, v30
	v_lshlrev_b32_e32 v32, 16, v32
	v_lshlrev_b32_e32 v34, 16, v34
	v_or_b32_sdwa v2, v2, v28 dst_sel:DWORD dst_unused:UNUSED_PAD src0_sel:WORD_0 src1_sel:DWORD
	v_lshl_add_u64 v[26:27], v[26:27], 0, v[20:21]
	s_barrier
	v_or_b32_sdwa v28, v29, v30 dst_sel:DWORD dst_unused:UNUSED_PAD src0_sel:WORD_0 src1_sel:DWORD
	v_or_b32_sdwa v29, v31, v32 dst_sel:DWORD dst_unused:UNUSED_PAD src0_sel:WORD_0 src1_sel:DWORD
	v_or_b32_sdwa v30, v33, v34 dst_sel:DWORD dst_unused:UNUSED_PAD src0_sel:WORD_0 src1_sel:DWORD
	global_store_dword v[36:37], v2, off
	global_store_dword v[26:27], v28, off
	global_store_dword v[36:37], v29, off offset:16
	global_store_dword v[26:27], v30, off offset:16
	s_cbranch_scc1 .LBB0_118

; #define LAS __attribute__((address_space(3)))
; __device__ __forceinline__ float bflo(unsigned w) { return __uint_as_float(w << 16); }
; __device__ __forceinline__ float bfhi(unsigned w) { return __uint_as_float(w & 0xffff0000u); }
; __device__ __forceinline__ unsigned pk2(float lo, float hi) { return f2bf(lo) | (f2bf(hi) << 16); }
; __device__ __forceinline__ void spatial_unit(const Params& p, int l, int unit, LAS unsigned char* lds, int tid) {
;     const int nb = unit >> 2, g = unit & 3, lane = tid & 63, wid = __builtin_amdgcn_readfirstlane(tid >> 6), fr = lane & 15, fq = lane >> 4;
;     LAS bf16* VT = (LAS bf16*)lds; LAS bf16* WM = (LAS bf16*)(lds + 69632);
;     const bf16* PROJ = (const bf16*)(p.ws + WS_PROJ); unsigned char* YABC = p.ws + WS_YABC;
;     const float* ws = p.in[4] + ((size_t)l * 4 + g) * 128 * 128; const float* bs = p.in[5] + ((size_t)l * 4 + g) * 128;
; #pragma unroll
;     for (int q = 0; q < 8; ++q) { const int pc = tid + 512 * q, i = pc >> 5, j4 = (pc & 31) * 4; const f32x4 w = *(const f32x4*)(ws + i * 128 + j4);
;         u32x2 o; o.x = pk2(w.x, w.y); o.y = pk2(w.z, w.w); *(LAS u32x2*)(WM + i * 136 + j4) = o; }
;     {
;         const int j = wid * 16 + fr; const bf16* vp = PROJ + ((size_t)nb * 128 + j) * INC + 1024 + g * 256 + fq * 8;
;         float v[64];
; #pragma unroll
;         for (int q = 0; q < 8; ++q) { const u32x4 w = *(const u32x4*)(vp + q * 32);
;             v[8 * q] = bflo(w.x); v[8 * q + 1] = bfhi(w.x); v[8 * q + 2] = bflo(w.y); v[8 * q + 3] = bfhi(w.y); v[8 * q + 4] = bflo(w.z); v[8 * q + 5] = bfhi(w.z); v[8 * q + 6] = bflo(w.w); v[8 * q + 7] = bfhi(w.w); }
.LBB0_480:
	s_and_b32 s0, s5, 3
	s_lshl_b32 s2, s0, 7
	s_or_b32 s88, s2, s4
	s_lshl_b64 s[2:3], s[88:89], 9
	v_lshl_add_u64 v[4:5], v[68:69], 0, s[2:3]
	v_lshl_add_u64 v[212:213], v[70:71], 2, v[4:5]
	global_load_dwordx4 v[148:151], v[212:213], off
	v_lshl_add_u64 v[212:213], v[72:73], 2, v[4:5]
	global_load_dwordx4 v[152:155], v[212:213], off
	v_lshl_add_u64 v[212:213], v[74:75], 2, v[4:5]
	global_load_dwordx4 v[156:159], v[212:213], off
	v_lshl_add_u64 v[212:213], v[76:77], 2, v[4:5]
	global_load_dwordx4 v[160:163], v[212:213], off
	v_lshl_add_u64 v[212:213], v[78:79], 2, v[4:5]
	global_load_dwordx4 v[164:167], v[212:213], off
	v_lshl_add_u64 v[212:213], v[80:81], 2, v[4:5]
	global_load_dwordx4 v[168:171], v[212:213], off
	v_lshl_add_u64 v[212:213], v[82:83], 2, v[4:5]
	global_load_dwordx4 v[172:175], v[212:213], off
	v_lshl_add_u64 v[212:213], v[84:85], 2, v[4:5]
	global_load_dwordx4 v[176:179], v[212:213], off
	v_lshl_add_u64 v[0:1], v[70:71], 2, v[4:5]
	v_readfirstlane_b32 s1, v67
	s_ashr_i32 s2, s5, 2
	s_ashr_i32 s7, s1, 6
	s_ashr_i32 s3, s2, 31
	s_lshl_b64 s[2:3], s[2:3], 7
	v_mov_b64_e32 v[104:105], s[16:17]
	s_lshl_b32 s6, s0, 8
	s_lshl_b32 s0, s0, 9
	s_mov_b32 s1, s89
	s_add_i32 s5, s5, s78
	v_lshl_or_b32 v214, s7, 4, v66
	v_ashrrev_i32_e32 v215, 31, v214
	v_lshl_add_u64 v[216:217], s[2:3], 0, v[214:215]
	v_mad_u64_u32 v[218:219], s[8:9], v216, s97, v[104:105]
	v_mad_i32_i24 v219, v217, s97, v219
	v_lshl_add_u64 v[216:217], v[218:219], 0, s[0:1]
	v_lshl_add_u64 v[216:217], v[216:217], 0, v[64:65]
	global_load_dwordx4 v[180:183], v[216:217], off offset:2048
	global_load_dwordx4 v[184:187], v[216:217], off offset:2112
	global_load_dwordx4 v[188:191], v[216:217], off offset:2176
	global_load_dwordx4 v[192:195], v[216:217], off offset:2240
	global_load_dwordx4 v[196:199], v[216:217], off offset:2304
	global_load_dwordx4 v[200:203], v[216:217], off offset:2368
	global_load_dwordx4 v[204:207], v[216:217], off offset:2432
	global_load_dwordx4 v[208:211], v[216:217], off offset:2496
	s_waitcnt vmcnt(15)
	v_mov_b64_e32 v[0:1], v[148:149]
	v_mov_b64_e32 v[2:3], v[150:151]
	v_bfe_u32 v6, v0, 16, 1
	v_add3_u32 v0, v0, v6, s30
	v_bfe_u32 v6, v1, 16, 1
	v_lshrrev_b32_e32 v0, 16, v0
	v_add3_u32 v1, v1, v6, s30
	v_and_or_b32 v0, v1, s20, v0
	v_bfe_u32 v1, v2, 16, 1
	v_add3_u32 v1, v2, v1, s30
	v_bfe_u32 v2, v3, 16, 1
	v_lshrrev_b32_e32 v1, 16, v1
	v_add3_u32 v2, v3, v2, s30
	v_and_or_b32 v1, v2, s20, v1
	ds_write_b64 v95, v[0:1]
	v_lshl_add_u64 v[0:1], v[72:73], 2, v[4:5]
	s_waitcnt vmcnt(14)
	v_mov_b64_e32 v[0:1], v[152:153]
	v_mov_b64_e32 v[2:3], v[154:155]
	v_bfe_u32 v6, v0, 16, 1
	v_add3_u32 v0, v0, v6, s30
	v_bfe_u32 v6, v1, 16, 1
	v_lshrrev_b32_e32 v0, 16, v0
	v_add3_u32 v1, v1, v6, s30
	v_and_or_b32 v0, v1, s20, v0
	v_bfe_u32 v1, v2, 16, 1
	v_add3_u32 v1, v2, v1, s30
	v_bfe_u32 v2, v3, 16, 1
	v_lshrrev_b32_e32 v1, 16, v1
	v_add3_u32 v2, v3, v2, s30
	v_and_or_b32 v1, v2, s20, v1
	ds_write_b64 v97, v[0:1]
	v_lshl_add_u64 v[0:1], v[74:75], 2, v[4:5]
	s_waitcnt vmcnt(13)
	v_mov_b64_e32 v[0:1], v[156:157]
	v_mov_b64_e32 v[2:3], v[158:159]
	v_bfe_u32 v6, v0, 16, 1
	v_add3_u32 v0, v0, v6, s30
	v_bfe_u32 v6, v1, 16, 1
	v_lshrrev_b32_e32 v0, 16, v0
	v_add3_u32 v1, v1, v6, s30
	v_and_or_b32 v0, v1, s20, v0
	v_bfe_u32 v1, v2, 16, 1
	v_add3_u32 v1, v2, v1, s30
	v_bfe_u32 v2, v3, 16, 1
	v_lshrrev_b32_e32 v1, 16, v1
	v_add3_u32 v2, v3, v2, s30
	v_and_or_b32 v1, v2, s20, v1
	ds_write_b64 v99, v[0:1]
	v_lshl_add_u64 v[0:1], v[76:77], 2, v[4:5]
	s_waitcnt vmcnt(12)
	v_mov_b64_e32 v[0:1], v[160:161]
	v_mov_b64_e32 v[2:3], v[162:163]
	v_bfe_u32 v6, v0, 16, 1
	v_add3_u32 v0, v0, v6, s30
	v_bfe_u32 v6, v1, 16, 1
	v_lshrrev_b32_e32 v0, 16, v0
	v_add3_u32 v1, v1, v6, s30
	v_and_or_b32 v0, v1, s20, v0
	v_bfe_u32 v1, v2, 16, 1
	v_add3_u32 v1, v2, v1, s30
	v_bfe_u32 v2, v3, 16, 1
	v_lshrrev_b32_e32 v1, 16, v1
	v_add3_u32 v2, v3, v2, s30
	v_and_or_b32 v1, v2, s20, v1
	ds_write_b64 v101, v[0:1]
	v_lshl_add_u64 v[0:1], v[78:79], 2, v[4:5]
	s_waitcnt vmcnt(11)
	v_mov_b64_e32 v[0:1], v[164:165]
	v_mov_b64_e32 v[2:3], v[166:167]
	v_bfe_u32 v6, v0, 16, 1
	v_add3_u32 v0, v0, v6, s30
	v_bfe_u32 v6, v1, 16, 1
	v_lshrrev_b32_e32 v0, 16, v0
	v_add3_u32 v1, v1, v6, s30
	v_and_or_b32 v0, v1, s20, v0
	v_bfe_u32 v1, v2, 16, 1
	v_add3_u32 v1, v2, v1, s30
	v_bfe_u32 v2, v3, 16, 1
	v_lshrrev_b32_e32 v1, 16, v1
	v_add3_u32 v2, v3, v2, s30
	v_and_or_b32 v1, v2, s20, v1
	ds_write_b64 v116, v[0:1]
	v_lshl_add_u64 v[0:1], v[80:81], 2, v[4:5]
	s_waitcnt vmcnt(10)
	v_mov_b64_e32 v[0:1], v[168:169]
	v_mov_b64_e32 v[2:3], v[170:171]
	v_bfe_u32 v6, v0, 16, 1
	v_add3_u32 v0, v0, v6, s30
	v_bfe_u32 v6, v1, 16, 1
	v_lshrrev_b32_e32 v0, 16, v0
	v_add3_u32 v1, v1, v6, s30
	v_and_or_b32 v0, v1, s20, v0
	v_bfe_u32 v1, v2, 16, 1
	v_add3_u32 v1, v2, v1, s30
	v_bfe_u32 v2, v3, 16, 1
	v_lshrrev_b32_e32 v1, 16, v1
	v_add3_u32 v2, v3, v2, s30
	v_and_or_b32 v1, v2, s20, v1
	ds_write_b64 v117, v[0:1]
	v_lshl_add_u64 v[0:1], v[82:83], 2, v[4:5]
	s_waitcnt vmcnt(9)
	v_mov_b64_e32 v[0:1], v[172:173]
	v_mov_b64_e32 v[2:3], v[174:175]
	v_bfe_u32 v6, v0, 16, 1
	v_add3_u32 v0, v0, v6, s30
	v_bfe_u32 v6, v1, 16, 1
	v_lshrrev_b32_e32 v0, 16, v0
	v_add3_u32 v1, v1, v6, s30
	v_and_or_b32 v0, v1, s20, v0
	v_bfe_u32 v1, v2, 16, 1
	v_add3_u32 v1, v2, v1, s30
	v_bfe_u32 v2, v3, 16, 1
	v_lshrrev_b32_e32 v1, 16, v1
	v_add3_u32 v2, v3, v2, s30
	v_and_or_b32 v1, v2, s20, v1
	ds_write_b64 v118, v[0:1]
	v_lshl_add_u64 v[0:1], v[84:85], 2, v[4:5]
	s_waitcnt vmcnt(8)
; #define LAS __attribute__((address_space(3)))
; __device__ __forceinline__ float bflo(unsigned w) { return __uint_as_float(w << 16); }
; __device__ __forceinline__ float bfhi(unsigned w) { return __uint_as_float(w & 0xffff0000u); }
; __device__ __forceinline__ unsigned pk2(float lo, float hi) { return f2bf(lo) | (f2bf(hi) << 16); }
; __device__ __forceinline__ float shx(float v, int mask, int lane) { return __int_as_float(__builtin_amdgcn_ds_bpermute((lane ^ mask) << 2, __float_as_int(v))); }
; __device__ __forceinline__ void spatial_unit(const Params& p, int l, int unit, LAS unsigned char* lds, int tid) {
;     ...
;     for (int q = 0; q < 8; ++q) { const int pc = tid + 512 * q, i = pc >> 5, j4 = (pc & 31) * 4; const f32x4 w = *(const f32x4*)(ws + i * 128 + j4);
;         u32x2 o; o.x = pk2(w.x, w.y); o.y = pk2(w.z, w.w); *(LAS u32x2*)(WM + i * 136 + j4) = o; }
;     {
;         const int j = wid * 16 + fr; const bf16* vp = PROJ + ((size_t)nb * 128 + j) * INC + 1024 + g * 256 + fq * 8;
;         float v[64];
; #pragma unroll
;         for (int q = 0; q < 8; ++q) { const u32x4 w = *(const u32x4*)(vp + q * 32);
;             v[8 * q] = bflo(w.x); v[8 * q + 1] = bfhi(w.x); v[8 * q + 2] = bflo(w.y); v[8 * q + 3] = bfhi(w.y); v[8 * q + 4] = bflo(w.z); v[8 * q + 5] = bfhi(w.z); v[8 * q + 6] = bflo(w.w); v[8 * q + 7] = bfhi(w.w); }
;         float sm = 0.f;
; #pragma unroll
;         for (int i = 0; i < 64; ++i) sm += v[i];
;         sm += shx(sm, 16, lane); sm += shx(sm, 32, lane);
	v_mov_b64_e32 v[0:1], v[176:177]
	v_mov_b64_e32 v[2:3], v[178:179]
	v_bfe_u32 v4, v0, 16, 1
	v_add3_u32 v0, v0, v4, s30
	v_bfe_u32 v4, v1, 16, 1
	v_lshrrev_b32_e32 v0, 16, v0
	v_add3_u32 v1, v1, v4, s30
	v_and_or_b32 v0, v1, s20, v0
	v_bfe_u32 v1, v2, 16, 1
	v_add3_u32 v1, v2, v1, s30
	v_bfe_u32 v2, v3, 16, 1
	v_lshrrev_b32_e32 v1, 16, v1
	v_add3_u32 v2, v3, v2, s30
	v_and_or_b32 v1, v2, s20, v1
	ds_write_b64 v119, v[0:1]
	v_lshl_or_b32 v0, s7, 4, v66
	v_ashrrev_i32_e32 v1, 31, v0
	v_lshl_add_u64 v[2:3], s[2:3], 0, v[0:1]
	v_mad_u64_u32 v[4:5], s[8:9], v2, s97, v[104:105]
	v_mad_i32_i24 v5, v3, s97, v5
	v_lshl_add_u64 v[2:3], v[4:5], 0, s[0:1]
	v_lshl_add_u64 v[6:7], v[2:3], 0, v[64:65]
	s_waitcnt vmcnt(7)
	v_mov_b64_e32 v[2:3], v[180:181]
	v_mov_b64_e32 v[4:5], v[182:183]
	v_lshl_add_u32 v0, v0, 1, v91
	s_lshl_b32 s7, s7, 5
	v_lshlrev_b32_e32 v1, 16, v2
	v_and_b32_e32 v8, 0xffff0000, v2
	v_lshlrev_b32_e32 v9, 16, v3
	v_and_b32_e32 v10, 0xffff0000, v3
	v_lshlrev_b32_e32 v11, 16, v4
	v_and_b32_e32 v12, 0xffff0000, v4
	v_lshlrev_b32_e32 v13, 16, v5
	v_and_b32_e32 v14, 0xffff0000, v5
	s_waitcnt vmcnt(6)
	v_mov_b64_e32 v[2:3], v[184:185]
	v_mov_b64_e32 v[4:5], v[186:187]
	v_add_f32_e32 v107, 0, v1
	v_add_f32_e32 v107, v107, v8
	v_add_f32_e32 v107, v107, v9
	v_add_f32_e32 v107, v107, v10
	v_add_f32_e32 v107, v107, v11
	v_add_f32_e32 v107, v107, v12
	v_add_f32_e32 v107, v107, v13
	v_add_f32_e32 v107, v107, v14
	v_lshlrev_b32_e32 v15, 16, v2
	v_and_b32_e32 v16, 0xffff0000, v2
	v_lshlrev_b32_e32 v17, 16, v3
	v_and_b32_e32 v18, 0xffff0000, v3
	v_lshlrev_b32_e32 v19, 16, v4
	v_and_b32_e32 v20, 0xffff0000, v4
	v_lshlrev_b32_e32 v21, 16, v5
	v_and_b32_e32 v22, 0xffff0000, v5
	s_waitcnt vmcnt(5)
	v_mov_b64_e32 v[2:3], v[188:189]
	v_mov_b64_e32 v[4:5], v[190:191]
	v_add_f32_e32 v107, v107, v15
	v_add_f32_e32 v107, v107, v16
	v_add_f32_e32 v107, v107, v17
	v_add_f32_e32 v107, v107, v18
	v_add_f32_e32 v107, v107, v19
	v_add_f32_e32 v107, v107, v20
	v_add_f32_e32 v107, v107, v21
	v_add_f32_e32 v107, v107, v22
	v_lshlrev_b32_e32 v23, 16, v2
	v_and_b32_e32 v24, 0xffff0000, v2
	v_lshlrev_b32_e32 v25, 16, v3
	v_and_b32_e32 v26, 0xffff0000, v3
	v_lshlrev_b32_e32 v27, 16, v4
	v_and_b32_e32 v28, 0xffff0000, v4
	v_lshlrev_b32_e32 v29, 16, v5
	v_and_b32_e32 v30, 0xffff0000, v5
	s_waitcnt vmcnt(4)
	v_mov_b64_e32 v[2:3], v[192:193]
	v_mov_b64_e32 v[4:5], v[194:195]
	v_add_f32_e32 v107, v107, v23
	v_add_f32_e32 v107, v107, v24
	v_add_f32_e32 v107, v107, v25
	v_add_f32_e32 v107, v107, v26
	v_add_f32_e32 v107, v107, v27
	v_add_f32_e32 v107, v107, v28
	v_add_f32_e32 v107, v107, v29
	v_add_f32_e32 v107, v107, v30
	v_lshlrev_b32_e32 v31, 16, v2
	v_and_b32_e32 v32, 0xffff0000, v2
	v_lshlrev_b32_e32 v33, 16, v3
	v_and_b32_e32 v34, 0xffff0000, v3
	v_lshlrev_b32_e32 v35, 16, v4
	v_and_b32_e32 v36, 0xffff0000, v4
	v_lshlrev_b32_e32 v37, 16, v5
	v_and_b32_e32 v38, 0xffff0000, v5
	s_waitcnt vmcnt(3)
	v_mov_b64_e32 v[2:3], v[196:197]
	v_mov_b64_e32 v[4:5], v[198:199]
	v_add_f32_e32 v107, v107, v31
	v_add_f32_e32 v107, v107, v32
	v_add_f32_e32 v107, v107, v33
	v_add_f32_e32 v107, v107, v34
	v_add_f32_e32 v107, v107, v35
	v_add_f32_e32 v107, v107, v36
	v_add_f32_e32 v107, v107, v37
	v_add_f32_e32 v107, v107, v38
	v_lshlrev_b32_e32 v39, 16, v2
	v_and_b32_e32 v40, 0xffff0000, v2
	v_lshlrev_b32_e32 v41, 16, v3
	v_and_b32_e32 v42, 0xffff0000, v3
	v_lshlrev_b32_e32 v43, 16, v4
	v_and_b32_e32 v44, 0xffff0000, v4
	v_lshlrev_b32_e32 v45, 16, v5
	v_and_b32_e32 v46, 0xffff0000, v5
	s_waitcnt vmcnt(2)
	v_mov_b64_e32 v[2:3], v[200:201]
	v_mov_b64_e32 v[4:5], v[202:203]
	v_add_f32_e32 v107, v107, v39
	v_add_f32_e32 v107, v107, v40
	v_add_f32_e32 v107, v107, v41
	v_add_f32_e32 v107, v107, v42
	v_add_f32_e32 v107, v107, v43
	v_add_f32_e32 v107, v107, v44
	v_add_f32_e32 v107, v107, v45
	v_add_f32_e32 v107, v107, v46
	v_lshlrev_b32_e32 v47, 16, v2
	v_and_b32_e32 v48, 0xffff0000, v2
	v_lshlrev_b32_e32 v49, 16, v3
	v_and_b32_e32 v50, 0xffff0000, v3
	v_lshlrev_b32_e32 v51, 16, v4
	v_and_b32_e32 v52, 0xffff0000, v4
	v_lshlrev_b32_e32 v53, 16, v5
	v_and_b32_e32 v54, 0xffff0000, v5
	s_waitcnt vmcnt(1)
	v_mov_b64_e32 v[2:3], v[204:205]
	v_mov_b64_e32 v[4:5], v[206:207]
	v_add_f32_e32 v107, v107, v47
	v_add_f32_e32 v107, v107, v48
	v_add_f32_e32 v107, v107, v49
	v_add_f32_e32 v107, v107, v50
	v_add_f32_e32 v107, v107, v51
	v_add_f32_e32 v107, v107, v52
	v_add_f32_e32 v107, v107, v53
	v_add_f32_e32 v107, v107, v54
	v_lshlrev_b32_e32 v55, 16, v2
	v_and_b32_e32 v56, 0xffff0000, v2
	v_lshlrev_b32_e32 v57, 16, v3
	v_and_b32_e32 v58, 0xffff0000, v3
	v_lshlrev_b32_e32 v59, 16, v4
	v_and_b32_e32 v60, 0xffff0000, v4
	v_lshlrev_b32_e32 v61, 16, v5
	v_and_b32_e32 v62, 0xffff0000, v5
	s_waitcnt vmcnt(0)
	v_mov_b64_e32 v[2:3], v[208:209]
	v_mov_b64_e32 v[4:5], v[210:211]
	v_add_f32_e32 v107, v107, v55
	v_add_f32_e32 v107, v107, v56
	v_add_f32_e32 v107, v107, v57
	v_add_f32_e32 v107, v107, v58
	v_add_f32_e32 v107, v107, v59
	v_add_f32_e32 v107, v107, v60
	v_add_f32_e32 v107, v107, v61
	v_add_f32_e32 v107, v107, v62
	v_lshlrev_b32_e32 v6, 16, v2
	v_and_b32_e32 v2, 0xffff0000, v2
	v_add_f32_e32 v107, v107, v6
	v_lshlrev_b32_e32 v7, 16, v3
	v_add_f32_e32 v107, v107, v2
	v_and_b32_e32 v3, 0xffff0000, v3
	v_add_f32_e32 v107, v107, v7
	v_lshlrev_b32_e32 v63, 16, v4
	v_add_f32_e32 v107, v107, v3
	v_and_b32_e32 v4, 0xffff0000, v4
	v_add_f32_e32 v107, v107, v63
	v_lshlrev_b32_e32 v106, 16, v5
	v_add_f32_e32 v107, v107, v4
	v_and_b32_e32 v5, 0xffff0000, v5
	v_add_f32_e32 v107, v107, v106
	v_add_f32_e32 v107, v107, v5
	ds_bpermute_b32 v108, v87, v107
	s_waitcnt lgkmcnt(0)
	v_add_f32_e32 v107, v107, v108
	ds_bpermute_b32 v108, v89, v107
	s_waitcnt lgkmcnt(0)
; __device__ __forceinline__ float shx(float v, int mask, int lane) { return __int_as_float(__builtin_amdgcn_ds_bpermute((lane ^ mask) << 2, __float_as_int(v))); }
; __device__ __forceinline__ void spatial_unit(const Params& p, int l, int unit, LAS unsigned char* lds, int tid) {
;     ...
;         const float mean = sm * (1.0f / 256.0f); float sq = 0.f;
; #pragma unroll
;         for (int i = 0; i < 64; ++i) { v[i] -= mean; sq += v[i] * v[i]; }
;         sq += shx(sq, 16, lane); sq += shx(sq, 32, lane);
	v_add_f32_e32 v107, v107, v108
	v_fmac_f32_e32 v8, 0xbb800000, v107
	v_fmac_f32_e32 v1, 0xbb800000, v107
	v_mul_f32_e32 v108, v8, v8
	v_fmac_f32_e32 v108, v1, v1
	v_fmac_f32_e32 v9, 0xbb800000, v107
	v_fmac_f32_e32 v108, v9, v9
	v_fmac_f32_e32 v10, 0xbb800000, v107
	v_fmac_f32_e32 v108, v10, v10
	v_fmac_f32_e32 v11, 0xbb800000, v107
	v_fmac_f32_e32 v108, v11, v11
	v_fmac_f32_e32 v12, 0xbb800000, v107
	v_fmac_f32_e32 v108, v12, v12
	v_fmac_f32_e32 v13, 0xbb800000, v107
	v_fmac_f32_e32 v108, v13, v13
	v_fmac_f32_e32 v14, 0xbb800000, v107
	v_fmac_f32_e32 v108, v14, v14
	v_fmac_f32_e32 v15, 0xbb800000, v107
	v_fmac_f32_e32 v108, v15, v15
	v_fmac_f32_e32 v16, 0xbb800000, v107
	v_fmac_f32_e32 v108, v16, v16
	v_fmac_f32_e32 v17, 0xbb800000, v107
	v_fmac_f32_e32 v108, v17, v17
	v_fmac_f32_e32 v18, 0xbb800000, v107
	v_fmac_f32_e32 v108, v18, v18
	v_fmac_f32_e32 v19, 0xbb800000, v107
	v_fmac_f32_e32 v108, v19, v19
	v_fmac_f32_e32 v20, 0xbb800000, v107
	v_fmac_f32_e32 v108, v20, v20
	v_fmac_f32_e32 v21, 0xbb800000, v107
	v_fmac_f32_e32 v108, v21, v21
	v_fmac_f32_e32 v22, 0xbb800000, v107
	v_fmac_f32_e32 v108, v22, v22
	v_fmac_f32_e32 v23, 0xbb800000, v107
	v_fmac_f32_e32 v108, v23, v23
	v_fmac_f32_e32 v24, 0xbb800000, v107
	v_fmac_f32_e32 v108, v24, v24
	v_fmac_f32_e32 v25, 0xbb800000, v107
	v_fmac_f32_e32 v108, v25, v25
	v_fmac_f32_e32 v26, 0xbb800000, v107
	v_fmac_f32_e32 v108, v26, v26
	v_fmac_f32_e32 v27, 0xbb800000, v107
	v_fmac_f32_e32 v108, v27, v27
	v_fmac_f32_e32 v28, 0xbb800000, v107
	v_fmac_f32_e32 v108, v28, v28
	v_fmac_f32_e32 v29, 0xbb800000, v107
	v_fmac_f32_e32 v108, v29, v29
	v_fmac_f32_e32 v30, 0xbb800000, v107
	v_fmac_f32_e32 v108, v30, v30
	v_fmac_f32_e32 v31, 0xbb800000, v107
	v_fmac_f32_e32 v108, v31, v31
	v_fmac_f32_e32 v32, 0xbb800000, v107
	v_fmac_f32_e32 v108, v32, v32
	v_fmac_f32_e32 v33, 0xbb800000, v107
	v_fmac_f32_e32 v108, v33, v33
	v_fmac_f32_e32 v34, 0xbb800000, v107
	v_fmac_f32_e32 v108, v34, v34
	v_fmac_f32_e32 v35, 0xbb800000, v107
	v_fmac_f32_e32 v108, v35, v35
	v_fmac_f32_e32 v36, 0xbb800000, v107
	v_fmac_f32_e32 v108, v36, v36
	v_fmac_f32_e32 v37, 0xbb800000, v107
	v_fmac_f32_e32 v108, v37, v37
	v_fmac_f32_e32 v38, 0xbb800000, v107
	v_fmac_f32_e32 v108, v38, v38
	v_fmac_f32_e32 v39, 0xbb800000, v107
	v_fmac_f32_e32 v108, v39, v39
	v_fmac_f32_e32 v40, 0xbb800000, v107
	v_fmac_f32_e32 v108, v40, v40
	v_fmac_f32_e32 v41, 0xbb800000, v107
	v_fmac_f32_e32 v108, v41, v41
	v_fmac_f32_e32 v42, 0xbb800000, v107
	v_fmac_f32_e32 v108, v42, v42
	v_fmac_f32_e32 v43, 0xbb800000, v107
	v_fmac_f32_e32 v108, v43, v43
	v_fmac_f32_e32 v44, 0xbb800000, v107
	v_fmac_f32_e32 v108, v44, v44
	v_fmac_f32_e32 v45, 0xbb800000, v107
	v_fmac_f32_e32 v108, v45, v45
	v_fmac_f32_e32 v46, 0xbb800000, v107
	v_fmac_f32_e32 v108, v46, v46
	v_fmac_f32_e32 v47, 0xbb800000, v107
	v_fmac_f32_e32 v108, v47, v47
	v_fmac_f32_e32 v48, 0xbb800000, v107
	v_fmac_f32_e32 v108, v48, v48
	v_fmac_f32_e32 v49, 0xbb800000, v107
	v_fmac_f32_e32 v108, v49, v49
	v_fmac_f32_e32 v50, 0xbb800000, v107
	v_fmac_f32_e32 v108, v50, v50
	v_fmac_f32_e32 v51, 0xbb800000, v107
	v_fmac_f32_e32 v108, v51, v51
	v_fmac_f32_e32 v52, 0xbb800000, v107
	v_fmac_f32_e32 v108, v52, v52
	v_fmac_f32_e32 v53, 0xbb800000, v107
	v_fmac_f32_e32 v108, v53, v53
	v_fmac_f32_e32 v54, 0xbb800000, v107
	v_fmac_f32_e32 v108, v54, v54
	v_fmac_f32_e32 v55, 0xbb800000, v107
	v_fmac_f32_e32 v108, v55, v55
	v_fmac_f32_e32 v56, 0xbb800000, v107
	v_fmac_f32_e32 v108, v56, v56
	v_fmac_f32_e32 v57, 0xbb800000, v107
	v_fmac_f32_e32 v108, v57, v57
	v_fmac_f32_e32 v58, 0xbb800000, v107
	v_fmac_f32_e32 v108, v58, v58
	v_fmac_f32_e32 v59, 0xbb800000, v107
	v_fmac_f32_e32 v108, v59, v59
	v_fmac_f32_e32 v60, 0xbb800000, v107
	v_fmac_f32_e32 v108, v60, v60
	v_fmac_f32_e32 v61, 0xbb800000, v107
	v_fmac_f32_e32 v108, v61, v61
	v_fmac_f32_e32 v62, 0xbb800000, v107
	v_fmac_f32_e32 v108, v62, v62
	v_fmac_f32_e32 v6, 0xbb800000, v107
	v_fmac_f32_e32 v108, v6, v6
	v_fmac_f32_e32 v2, 0xbb800000, v107
	v_fmac_f32_e32 v108, v2, v2
	v_fmac_f32_e32 v7, 0xbb800000, v107
	v_fmac_f32_e32 v108, v7, v7
	v_fmac_f32_e32 v3, 0xbb800000, v107
	v_fmac_f32_e32 v108, v3, v3
	v_fmac_f32_e32 v63, 0xbb800000, v107
	v_fmac_f32_e32 v108, v63, v63
	v_fmac_f32_e32 v4, 0xbb800000, v107
	v_fmac_f32_e32 v108, v4, v4
	v_fmac_f32_e32 v106, 0xbb800000, v107
	v_fmac_f32_e32 v108, v106, v106
	v_fmac_f32_e32 v5, 0xbb800000, v107
	v_fmac_f32_e32 v108, v5, v5
	ds_bpermute_b32 v107, v87, v108
	s_waitcnt lgkmcnt(0)
	v_add_f32_e32 v107, v108, v107
	ds_bpermute_b32 v108, v89, v107
	s_waitcnt lgkmcnt(0)
; __device__ __forceinline__ unsigned f2bf(float f) { unsigned u = __float_as_uint(f); return (u + 0x7fffu + ((u >> 16) & 1u)) >> 16; }
; __device__ __forceinline__ void spatial_unit(const Params& p, int l, int unit, LAS unsigned char* lds, int tid) {
;     ...
;         const float rstd = 1.0f / sqrtf(sq * (1.0f / 256.0f) + LN_EPS);
; #pragma unroll
;         for (int q = 0; q < 8; ++q)
; #pragma unroll
;             for (int i = 0; i < 8; ++i) VT[(q * 32 + fq * 8 + i) * 136 + j] = (bf16)f2bf(v[8 * q + i] * rstd);
	v_add_f32_e32 v107, v107, v108
	v_fmamk_f32 v107, v107, 0x3b800000, v223
	v_cmp_gt_f32_e32 vcc, s21, v107
	v_mul_f32_e32 v108, 0x4f800000, v107
	s_nop 0
	v_cndmask_b32_e32 v107, v107, v108, vcc
	v_sqrt_f32_e32 v108, v107
	s_nop 0
	v_add_u32_e32 v109, -1, v108
	v_fma_f32 v110, -v109, v108, v107
	v_cmp_ge_f32_e64 s[0:1], 0, v110
	v_add_u32_e32 v110, 1, v108
	s_nop 0
	v_cndmask_b32_e64 v109, v108, v109, s[0:1]
	v_fma_f32 v108, -v110, v108, v107
	v_cmp_lt_f32_e64 s[0:1], 0, v108
	s_nop 1
	v_cndmask_b32_e64 v108, v109, v110, s[0:1]
	v_mul_f32_e32 v109, 0x37800000, v108
	v_cndmask_b32_e32 v108, v108, v109, vcc
	v_cmp_class_f32_e32 vcc, v107, v224
	s_nop 1
	v_cndmask_b32_e32 v107, v108, v107, vcc
	v_div_scale_f32 v108, s[0:1], v107, v107, 1.0
	v_rcp_f32_e32 v109, v108
	s_nop 0
	v_fma_f32 v110, -v108, v109, 1.0
	v_fmac_f32_e32 v109, v110, v109
	v_div_scale_f32 v110, vcc, 1.0, v107, 1.0
	v_mul_f32_e32 v111, v110, v109
	v_fma_f32 v112, -v108, v111, v110
	v_fmac_f32_e32 v111, v112, v109
	v_fma_f32 v108, -v108, v111, v110
	v_div_fmas_f32 v108, v108, v109, v111
	v_div_fixup_f32 v107, v108, v107, 1.0
	v_mul_f32_e32 v1, v1, v107
	v_bfe_u32 v108, v1, 16, 1
	v_add3_u32 v1, v1, v108, s30
	ds_write_b16_d16_hi v0, v1
	v_mul_f32_e32 v1, v8, v107
	v_bfe_u32 v8, v1, 16, 1
	v_add3_u32 v1, v1, v8, s30
	ds_write_b16_d16_hi v0, v1 offset:272
	v_mul_f32_e32 v1, v9, v107
	v_bfe_u32 v8, v1, 16, 1
	v_add3_u32 v1, v1, v8, s30
	ds_write_b16_d16_hi v0, v1 offset:544
	v_mul_f32_e32 v1, v10, v107
	v_bfe_u32 v8, v1, 16, 1
	v_add3_u32 v1, v1, v8, s30
	ds_write_b16_d16_hi v0, v1 offset:816
	v_mul_f32_e32 v1, v11, v107
	v_bfe_u32 v8, v1, 16, 1
	v_add3_u32 v1, v1, v8, s30
	ds_write_b16_d16_hi v0, v1 offset:1088
	v_mul_f32_e32 v1, v12, v107
	v_bfe_u32 v8, v1, 16, 1
	v_add3_u32 v1, v1, v8, s30
	ds_write_b16_d16_hi v0, v1 offset:1360
	v_mul_f32_e32 v1, v13, v107
	v_bfe_u32 v8, v1, 16, 1
	v_add3_u32 v1, v1, v8, s30
	ds_write_b16_d16_hi v0, v1 offset:1632
	v_mul_f32_e32 v1, v14, v107
	v_bfe_u32 v8, v1, 16, 1
	v_add3_u32 v1, v1, v8, s30
	ds_write_b16_d16_hi v0, v1 offset:1904
	v_mul_f32_e32 v1, v15, v107
	v_bfe_u32 v8, v1, 16, 1
	v_add3_u32 v1, v1, v8, s30
	ds_write_b16_d16_hi v0, v1 offset:8704
	v_mul_f32_e32 v1, v16, v107
	v_bfe_u32 v8, v1, 16, 1
	v_add3_u32 v1, v1, v8, s30
	ds_write_b16_d16_hi v0, v1 offset:8976
	v_mul_f32_e32 v1, v17, v107
	v_bfe_u32 v8, v1, 16, 1
	v_add3_u32 v1, v1, v8, s30
	ds_write_b16_d16_hi v0, v1 offset:9248
	v_mul_f32_e32 v1, v18, v107
	v_bfe_u32 v8, v1, 16, 1
	v_add3_u32 v1, v1, v8, s30
	ds_write_b16_d16_hi v0, v1 offset:9520
	v_mul_f32_e32 v1, v19, v107
	v_bfe_u32 v8, v1, 16, 1
	v_add3_u32 v1, v1, v8, s30
	ds_write_b16_d16_hi v0, v1 offset:9792
	v_mul_f32_e32 v1, v20, v107
	v_bfe_u32 v8, v1, 16, 1
	v_add3_u32 v1, v1, v8, s30
	ds_write_b16_d16_hi v0, v1 offset:10064
	v_mul_f32_e32 v1, v21, v107
	v_bfe_u32 v8, v1, 16, 1
	v_add3_u32 v1, v1, v8, s30
	ds_write_b16_d16_hi v0, v1 offset:10336
	v_mul_f32_e32 v1, v22, v107
	v_bfe_u32 v8, v1, 16, 1
	v_add3_u32 v1, v1, v8, s30
	ds_write_b16_d16_hi v0, v1 offset:10608
	v_mul_f32_e32 v1, v23, v107
	v_bfe_u32 v8, v1, 16, 1
	v_add3_u32 v1, v1, v8, s30
	ds_write_b16_d16_hi v0, v1 offset:17408
	v_mul_f32_e32 v1, v24, v107
	v_bfe_u32 v8, v1, 16, 1
	v_add3_u32 v1, v1, v8, s30
	ds_write_b16_d16_hi v0, v1 offset:17680
	v_mul_f32_e32 v1, v25, v107
	v_bfe_u32 v8, v1, 16, 1
	v_add3_u32 v1, v1, v8, s30
	ds_write_b16_d16_hi v0, v1 offset:17952
	v_mul_f32_e32 v1, v26, v107
	v_bfe_u32 v8, v1, 16, 1
	v_add3_u32 v1, v1, v8, s30
	ds_write_b16_d16_hi v0, v1 offset:18224
	v_mul_f32_e32 v1, v27, v107
	v_bfe_u32 v8, v1, 16, 1
	v_add3_u32 v1, v1, v8, s30
	ds_write_b16_d16_hi v0, v1 offset:18496
	v_mul_f32_e32 v1, v28, v107
	v_bfe_u32 v8, v1, 16, 1
	v_add3_u32 v1, v1, v8, s30
	ds_write_b16_d16_hi v0, v1 offset:18768
	v_mul_f32_e32 v1, v29, v107
	v_bfe_u32 v8, v1, 16, 1
	v_add3_u32 v1, v1, v8, s30
	ds_write_b16_d16_hi v0, v1 offset:19040
	v_mul_f32_e32 v1, v30, v107
	v_bfe_u32 v8, v1, 16, 1
	v_add3_u32 v1, v1, v8, s30
	ds_write_b16_d16_hi v0, v1 offset:19312
	v_mul_f32_e32 v1, v31, v107
	v_bfe_u32 v8, v1, 16, 1
	v_add3_u32 v1, v1, v8, s30
	ds_write_b16_d16_hi v0, v1 offset:26112
	v_mul_f32_e32 v1, v32, v107
	v_bfe_u32 v8, v1, 16, 1
	v_add3_u32 v1, v1, v8, s30
	ds_write_b16_d16_hi v0, v1 offset:26384
	v_mul_f32_e32 v1, v33, v107
	v_bfe_u32 v8, v1, 16, 1
	v_add3_u32 v1, v1, v8, s30
	ds_write_b16_d16_hi v0, v1 offset:26656
	v_mul_f32_e32 v1, v34, v107
	v_bfe_u32 v8, v1, 16, 1
	v_add3_u32 v1, v1, v8, s30
	ds_write_b16_d16_hi v0, v1 offset:26928
	v_mul_f32_e32 v1, v35, v107
	v_bfe_u32 v8, v1, 16, 1
	v_add3_u32 v1, v1, v8, s30
	ds_write_b16_d16_hi v0, v1 offset:27200
	v_mul_f32_e32 v1, v36, v107
	v_bfe_u32 v8, v1, 16, 1
	v_add3_u32 v1, v1, v8, s30
	ds_write_b16_d16_hi v0, v1 offset:27472
	v_mul_f32_e32 v1, v37, v107
	v_bfe_u32 v8, v1, 16, 1
	v_add3_u32 v1, v1, v8, s30
	ds_write_b16_d16_hi v0, v1 offset:27744
	v_mul_f32_e32 v1, v38, v107
	v_bfe_u32 v8, v1, 16, 1
	v_add3_u32 v1, v1, v8, s30
	ds_write_b16_d16_hi v0, v1 offset:28016
	v_mul_f32_e32 v1, v39, v107
	v_bfe_u32 v8, v1, 16, 1
	v_add3_u32 v1, v1, v8, s30
	ds_write_b16_d16_hi v0, v1 offset:34816
	v_mul_f32_e32 v1, v40, v107
	v_bfe_u32 v8, v1, 16, 1
	v_add3_u32 v1, v1, v8, s30
	ds_write_b16_d16_hi v0, v1 offset:35088
	v_mul_f32_e32 v1, v41, v107
	v_bfe_u32 v8, v1, 16, 1
	v_add3_u32 v1, v1, v8, s30
	ds_write_b16_d16_hi v0, v1 offset:35360
	v_mul_f32_e32 v1, v42, v107
	v_bfe_u32 v8, v1, 16, 1
	v_add3_u32 v1, v1, v8, s30
	ds_write_b16_d16_hi v0, v1 offset:35632
	v_mul_f32_e32 v1, v43, v107
	v_bfe_u32 v8, v1, 16, 1
	v_add3_u32 v1, v1, v8, s30
	ds_write_b16_d16_hi v0, v1 offset:35904
; #define LAS __attribute__((address_space(3)))
; __device__ __forceinline__ unsigned f2bf(float f) { unsigned u = __float_as_uint(f); return (u + 0x7fffu + ((u >> 16) & 1u)) >> 16; }
; __device__ __forceinline__ void spatial_unit(const Params& p, int l, int unit, LAS unsigned char* lds, int tid) {
;     ...
;             for (int i = 0; i < 8; ++i) VT[(q * 32 + fq * 8 + i) * 136 + j] = (bf16)f2bf(v[8 * q + i] * rstd);
;     }
;     __syncthreads();
;     f32x4 acc[2][8];
; #pragma unroll
;     for (int cf = 0; cf < 2; ++cf)
; #pragma unroll
;         for (int f = 0; f < 8; ++f) acc[cf][f] = (f32x4){0.f, 0.f, 0.f, 0.f};
; #pragma unroll
;     for (int ks = 0; ks < 4; ++ks) {
;         bf16x8 a[2];
; #pragma unroll
;         for (int cf = 0; cf < 2; ++cf) a[cf] = *(const LAS bf16x8*)(VT + (wid * 32 + cf * 16 + fr) * 136 + ks * 32 + fq * 8);
; #pragma unroll
;         for (int f = 0; f < 8; ++f) {
;             if (ks >= 2 && f < 4) continue;
;             const bf16x8 b = *(const LAS bf16x8*)(WM + (f * 16 + fr) * 136 + ks * 32 + fq * 8);
; #pragma unroll
;             for (int cf = 0; cf < 2; ++cf) acc[cf][f] = __builtin_amdgcn_mfma_f32_16x16x32_bf16(a[cf], b, acc[cf][f], 0, 0, 0);
;     ...
;         const int i = f * 16 + fr; const size_t t = (size_t)nb * 128 + i; const float bias = bs[i];
; #pragma unroll
;         for (int cf = 0; cf < 2; ++cf) { const int c = g * 256 + wid * 32 + cf * 16 + 4 * fq;
;             const u32x2 uw = __builtin_nontemporal_load((const u32x2*)(PROJ + t * INC + c));
	v_mul_f32_e32 v1, v44, v107
	v_bfe_u32 v8, v1, 16, 1
	v_add3_u32 v1, v1, v8, s30
	ds_write_b16_d16_hi v0, v1 offset:36176
	v_mul_f32_e32 v1, v45, v107
	v_bfe_u32 v8, v1, 16, 1
	v_add3_u32 v1, v1, v8, s30
	ds_write_b16_d16_hi v0, v1 offset:36448
	v_mul_f32_e32 v1, v46, v107
	v_bfe_u32 v8, v1, 16, 1
	v_add3_u32 v1, v1, v8, s30
	ds_write_b16_d16_hi v0, v1 offset:36720
	v_mul_f32_e32 v1, v47, v107
	v_bfe_u32 v8, v1, 16, 1
	v_add3_u32 v1, v1, v8, s30
	ds_write_b16_d16_hi v0, v1 offset:43520
	v_mul_f32_e32 v1, v48, v107
	v_bfe_u32 v8, v1, 16, 1
	v_add3_u32 v1, v1, v8, s30
	ds_write_b16_d16_hi v0, v1 offset:43792
	v_mul_f32_e32 v1, v49, v107
	v_bfe_u32 v8, v1, 16, 1
	v_add3_u32 v1, v1, v8, s30
	ds_write_b16_d16_hi v0, v1 offset:44064
	v_mul_f32_e32 v1, v50, v107
	v_bfe_u32 v8, v1, 16, 1
	v_add3_u32 v1, v1, v8, s30
	ds_write_b16_d16_hi v0, v1 offset:44336
	v_mul_f32_e32 v1, v51, v107
	v_bfe_u32 v8, v1, 16, 1
	v_add3_u32 v1, v1, v8, s30
	ds_write_b16_d16_hi v0, v1 offset:44608
	v_mul_f32_e32 v1, v52, v107
	v_bfe_u32 v8, v1, 16, 1
	v_add3_u32 v1, v1, v8, s30
	ds_write_b16_d16_hi v0, v1 offset:44880
	v_mul_f32_e32 v1, v53, v107
	v_bfe_u32 v8, v1, 16, 1
	v_add3_u32 v1, v1, v8, s30
	ds_write_b16_d16_hi v0, v1 offset:45152
	v_mul_f32_e32 v1, v54, v107
	v_bfe_u32 v8, v1, 16, 1
	v_add3_u32 v1, v1, v8, s30
	ds_write_b16_d16_hi v0, v1 offset:45424
	v_mul_f32_e32 v1, v55, v107
	v_bfe_u32 v8, v1, 16, 1
	v_add3_u32 v1, v1, v8, s30
	ds_write_b16_d16_hi v0, v1 offset:52224
	v_mul_f32_e32 v1, v56, v107
	v_bfe_u32 v8, v1, 16, 1
	v_add3_u32 v1, v1, v8, s30
	ds_write_b16_d16_hi v0, v1 offset:52496
	v_mul_f32_e32 v1, v57, v107
	v_bfe_u32 v8, v1, 16, 1
	v_add3_u32 v1, v1, v8, s30
	ds_write_b16_d16_hi v0, v1 offset:52768
	v_mul_f32_e32 v1, v58, v107
	v_bfe_u32 v8, v1, 16, 1
	v_add3_u32 v1, v1, v8, s30
	ds_write_b16_d16_hi v0, v1 offset:53040
	v_mul_f32_e32 v1, v59, v107
	v_bfe_u32 v8, v1, 16, 1
	v_add3_u32 v1, v1, v8, s30
	ds_write_b16_d16_hi v0, v1 offset:53312
	v_mul_f32_e32 v1, v60, v107
	v_bfe_u32 v8, v1, 16, 1
	v_add3_u32 v1, v1, v8, s30
	ds_write_b16_d16_hi v0, v1 offset:53584
	v_mul_f32_e32 v1, v61, v107
	v_bfe_u32 v8, v1, 16, 1
	v_add3_u32 v1, v1, v8, s30
	ds_write_b16_d16_hi v0, v1 offset:53856
	v_mul_f32_e32 v1, v62, v107
	v_bfe_u32 v8, v1, 16, 1
	v_add3_u32 v1, v1, v8, s30
	ds_write_b16_d16_hi v0, v1 offset:54128
	v_mul_f32_e32 v1, v6, v107
	v_bfe_u32 v6, v1, 16, 1
	v_add3_u32 v1, v1, v6, s30
	ds_write_b16_d16_hi v0, v1 offset:60928
	v_mul_f32_e32 v1, v2, v107
	v_bfe_u32 v2, v1, 16, 1
	v_add3_u32 v1, v1, v2, s30
	ds_write_b16_d16_hi v0, v1 offset:61200
	v_mul_f32_e32 v1, v7, v107
	v_bfe_u32 v2, v1, 16, 1
	v_add3_u32 v1, v1, v2, s30
	ds_write_b16_d16_hi v0, v1 offset:61472
	v_mul_f32_e32 v1, v3, v107
	v_bfe_u32 v2, v1, 16, 1
	v_add3_u32 v1, v1, v2, s30
	ds_write_b16_d16_hi v0, v1 offset:61744
	v_mul_f32_e32 v1, v63, v107
	v_bfe_u32 v2, v1, 16, 1
	v_add3_u32 v1, v1, v2, s30
	ds_write_b16_d16_hi v0, v1 offset:62016
	v_mul_f32_e32 v1, v4, v107
	v_bfe_u32 v2, v1, 16, 1
	v_add3_u32 v1, v1, v2, s30
	ds_write_b16_d16_hi v0, v1 offset:62288
	v_mul_f32_e32 v1, v106, v107
	v_bfe_u32 v2, v1, 16, 1
	v_add3_u32 v1, v1, v2, s30
	ds_write_b16_d16_hi v0, v1 offset:62560
	v_mul_f32_e32 v1, v5, v107
	v_bfe_u32 v2, v1, 16, 1
	v_add3_u32 v1, v1, v2, s30
	ds_write_b16_d16_hi v0, v1 offset:62832
	v_or_b32_e32 v0, s7, v66
	v_mad_u64_u32 v[114:115], s[0:1], v0, s19, v[86:87]
	s_waitcnt lgkmcnt(0)
	s_barrier
	ds_read_b128 v[0:3], v114
	ds_read_b128 v[4:7], v114 offset:4352
	ds_read_b128 v[8:11], v120
	ds_read_b128 v[32:35], v120 offset:13056
	ds_read_b128 v[40:43], v120 offset:17408
	s_waitcnt lgkmcnt(0)
	v_mfma_f32_16x16x32_bf16 v[106:109], v[0:3], v[40:43], 0
	ds_read_b128 v[16:19], v120 offset:4352
	ds_read_b128 v[24:27], v120 offset:8704
	s_add_i32 s7, s7, s6
	v_or_b32_e32 v212, s7, v93
	v_ashrrev_i32_e32 v213, 31, v212
	v_lshlrev_b64 v[212:213], 1, v[212:213]
	v_lshl_add_u64 v[214:215], s[88:89], 2, v[102:103]
	v_or_b32_e32 v216, s2, v66
	v_mad_u64_u32 v[218:219], s[0:1], v216, s97, v[104:105]
	v_mad_i32_i24 v219, s3, v146, v219
	v_lshl_add_u64 v[218:219], v[218:219], 0, v[212:213]
	global_load_dwordx2 v[148:149], v[218:219], off nt
	global_load_dwordx2 v[150:151], v[218:219], off offset:32 nt
	global_load_dword v180, v[214:215], off
	v_or_b32_e32 v216, s2, v90
	v_mad_u64_u32 v[218:219], s[0:1], v216, s97, v[104:105]
	v_mad_i32_i24 v219, s3, v146, v219
	v_lshl_add_u64 v[218:219], v[218:219], 0, v[212:213]
	global_load_dwordx2 v[152:153], v[218:219], off nt
	global_load_dwordx2 v[154:155], v[218:219], off offset:32 nt
	global_load_dword v181, v[214:215], off offset:64
	v_or_b32_e32 v216, s2, v92
	v_mad_u64_u32 v[218:219], s[0:1], v216, s97, v[104:105]
	v_mad_i32_i24 v219, s3, v146, v219
	v_lshl_add_u64 v[218:219], v[218:219], 0, v[212:213]
	global_load_dwordx2 v[156:157], v[218:219], off nt
	global_load_dwordx2 v[158:159], v[218:219], off offset:32 nt
	global_load_dword v182, v[214:215], off offset:128
	v_or_b32_e32 v216, s2, v94
	v_mad_u64_u32 v[218:219], s[0:1], v216, s97, v[104:105]
	v_mad_i32_i24 v219, s3, v146, v219
	v_lshl_add_u64 v[218:219], v[218:219], 0, v[212:213]
	global_load_dwordx2 v[160:161], v[218:219], off nt
	global_load_dwordx2 v[162:163], v[218:219], off offset:32 nt
	global_load_dword v183, v[214:215], off offset:192
	v_or_b32_e32 v216, s2, v96
	v_mad_u64_u32 v[218:219], s[0:1], v216, s97, v[104:105]
	v_mad_i32_i24 v219, s3, v146, v219
	v_lshl_add_u64 v[218:219], v[218:219], 0, v[212:213]
	global_load_dwordx2 v[164:165], v[218:219], off nt
	global_load_dwordx2 v[166:167], v[218:219], off offset:32 nt
	global_load_dword v184, v[214:215], off offset:256
	v_or_b32_e32 v216, s2, v98
	v_mad_u64_u32 v[218:219], s[0:1], v216, s97, v[104:105]
	v_mad_i32_i24 v219, s3, v146, v219
	v_lshl_add_u64 v[218:219], v[218:219], 0, v[212:213]
	global_load_dwordx2 v[168:169], v[218:219], off nt
	global_load_dwordx2 v[170:171], v[218:219], off offset:32 nt
	global_load_dword v185, v[214:215], off offset:320
	v_or_b32_e32 v216, s2, v100
	v_mad_u64_u32 v[218:219], s[0:1], v216, s97, v[104:105]
	v_mad_i32_i24 v219, s3, v146, v219
	v_lshl_add_u64 v[218:219], v[218:219], 0, v[212:213]
	global_load_dwordx2 v[172:173], v[218:219], off nt
	global_load_dwordx2 v[174:175], v[218:219], off offset:32 nt
	global_load_dword v186, v[214:215], off offset:384
	v_or_b32_e32 v216, s2, v88
	v_mad_u64_u32 v[218:219], s[0:1], v216, s97, v[104:105]
	v_mad_i32_i24 v219, s3, v146, v219
	v_lshl_add_u64 v[218:219], v[218:219], 0, v[212:213]
	global_load_dwordx2 v[176:177], v[218:219], off nt
	global_load_dwordx2 v[178:179], v[218:219], off offset:32 nt
	global_load_dword v187, v[214:215], off offset:448
	v_mfma_f32_16x16x32_bf16 v[110:113], v[4:7], v[40:43], 0
	ds_read_b128 v[40:43], v120 offset:21760
	s_cmpk_gt_i32 s5, 0xff
	s_waitcnt lgkmcnt(0)
; #define LAS __attribute__((address_space(3)))
; __device__ __forceinline__ void spatial_unit(const Params& p, int l, int unit, LAS unsigned char* lds, int tid) {
;     ...
; #pragma unroll
;     for (int ks = 0; ks < 4; ++ks) {
;         bf16x8 a[2];
; #pragma unroll
;         for (int cf = 0; cf < 2; ++cf) a[cf] = *(const LAS bf16x8*)(VT + (wid * 32 + cf * 16 + fr) * 136 + ks * 32 + fq * 8);
; #pragma unroll
;         for (int f = 0; f < 8; ++f) {
;             if (ks >= 2 && f < 4) continue;
;             const bf16x8 b = *(const LAS bf16x8*)(WM + (f * 16 + fr) * 136 + ks * 32 + fq * 8);
; #pragma unroll
;             for (int cf = 0; cf < 2; ++cf) acc[cf][f] = __builtin_amdgcn_mfma_f32_16x16x32_bf16(a[cf], b, acc[cf][f], 0, 0, 0);
;         }
;     }
; #pragma unroll
;     for (int f = 0; f < 8; ++f) {
;         const int i = f * 16 + fr; const size_t t = (size_t)nb * 128 + i; const float bias = bs[i];
; #pragma unroll
;         for (int cf = 0; cf < 2; ++cf) { const int c = g * 256 + wid * 32 + cf * 16 + 4 * fq;
;             const u32x2 uw = __builtin_nontemporal_load((const u32x2*)(PROJ + t * INC + c));
	v_mfma_f32_16x16x32_bf16 v[122:125], v[0:3], v[40:43], 0
	v_mfma_f32_16x16x32_bf16 v[126:129], v[4:7], v[40:43], 0
	ds_read_b128 v[40:43], v120 offset:26112
	s_waitcnt lgkmcnt(0)
	v_mfma_f32_16x16x32_bf16 v[130:133], v[0:3], v[40:43], 0
	v_mfma_f32_16x16x32_bf16 v[134:137], v[4:7], v[40:43], 0
	ds_read_b128 v[40:43], v120 offset:30464
	v_mfma_f32_16x16x32_bf16 v[12:15], v[0:3], v[8:11], 0
	v_mfma_f32_16x16x32_bf16 v[8:11], v[4:7], v[8:11], 0
	v_mfma_f32_16x16x32_bf16 v[20:23], v[0:3], v[16:19], 0
	v_mfma_f32_16x16x32_bf16 v[16:19], v[4:7], v[16:19], 0
	v_mfma_f32_16x16x32_bf16 v[28:31], v[0:3], v[24:27], 0
	v_mfma_f32_16x16x32_bf16 v[24:27], v[4:7], v[24:27], 0
	v_mfma_f32_16x16x32_bf16 v[36:39], v[0:3], v[32:35], 0
	v_mfma_f32_16x16x32_bf16 v[32:35], v[4:7], v[32:35], 0
	s_waitcnt lgkmcnt(0)
	v_mfma_f32_16x16x32_bf16 v[0:3], v[0:3], v[40:43], 0
	v_mfma_f32_16x16x32_bf16 v[4:7], v[4:7], v[40:43], 0
	ds_read_b128 v[138:141], v114 offset:64
	ds_read_b128 v[142:145], v114 offset:4416
	ds_read_b128 v[40:43], v120 offset:64
	s_waitcnt lgkmcnt(0)
	v_mfma_f32_16x16x32_bf16 v[56:59], v[142:145], v[40:43], v[8:11]
	s_nop 2
	ds_read_b128 v[8:11], v120 offset:4416
	s_waitcnt lgkmcnt(0)
	v_mfma_f32_16x16x32_bf16 v[52:55], v[138:141], v[8:11], v[20:23]
	v_mfma_f32_16x16x32_bf16 v[48:51], v[142:145], v[8:11], v[16:19]
	ds_read_b128 v[8:11], v120 offset:8768
	s_nop 1
	ds_read_b128 v[16:19], v120 offset:21824
	v_mfma_f32_16x16x32_bf16 v[60:63], v[138:141], v[40:43], v[12:15]
	s_waitcnt lgkmcnt(1)
	v_mfma_f32_16x16x32_bf16 v[44:47], v[138:141], v[8:11], v[28:31]
	v_mfma_f32_16x16x32_bf16 v[40:43], v[142:145], v[8:11], v[24:27]
	ds_read_b128 v[8:11], v120 offset:13120
	s_nop 1
	ds_read_b128 v[24:27], v120 offset:26176
	s_waitcnt lgkmcnt(1)
	v_mfma_f32_16x16x32_bf16 v[36:39], v[138:141], v[8:11], v[36:39]
	v_mfma_f32_16x16x32_bf16 v[32:35], v[142:145], v[8:11], v[32:35]
	ds_read_b128 v[8:11], v120 offset:17472
	s_waitcnt lgkmcnt(0)
	v_mfma_f32_16x16x32_bf16 v[12:15], v[138:141], v[8:11], v[106:109]
	s_nop 2
	ds_read_b128 v[106:109], v120 offset:30528
	v_mfma_f32_16x16x32_bf16 v[8:11], v[142:145], v[8:11], v[110:113]
	v_mfma_f32_16x16x32_bf16 v[20:23], v[138:141], v[16:19], v[122:125]
	s_waitcnt lgkmcnt(0)
	v_mfma_f32_16x16x32_bf16 v[0:3], v[138:141], v[106:109], v[0:3]
	v_mfma_f32_16x16x32_bf16 v[4:7], v[142:145], v[106:109], v[4:7]
	ds_read_b128 v[106:109], v114 offset:128
	ds_read_b128 v[110:113], v114 offset:4480
	ds_read_b128 v[122:125], v120 offset:17536
	s_waitcnt lgkmcnt(0)
	v_mfma_f32_16x16x32_bf16 v[12:15], v[106:109], v[122:125], v[12:15]
	v_mfma_f32_16x16x32_bf16 v[8:11], v[110:113], v[122:125], v[8:11]
	ds_read_b128 v[122:125], v120 offset:21888
	v_mfma_f32_16x16x32_bf16 v[16:19], v[142:145], v[16:19], v[126:129]
	s_waitcnt lgkmcnt(0)
	v_mfma_f32_16x16x32_bf16 v[20:23], v[106:109], v[122:125], v[20:23]
	v_mfma_f32_16x16x32_bf16 v[16:19], v[110:113], v[122:125], v[16:19]
	ds_read_b128 v[122:125], v120 offset:26240
	v_mfma_f32_16x16x32_bf16 v[28:31], v[138:141], v[24:27], v[130:133]
	v_mfma_f32_16x16x32_bf16 v[24:27], v[142:145], v[24:27], v[134:137]
	s_waitcnt lgkmcnt(0)
	v_mfma_f32_16x16x32_bf16 v[126:129], v[106:109], v[122:125], v[28:31]
	v_mfma_f32_16x16x32_bf16 v[122:125], v[110:113], v[122:125], v[24:27]
	s_nop 4
	ds_read_b128 v[24:27], v120 offset:30592
	s_waitcnt lgkmcnt(0)
	v_mfma_f32_16x16x32_bf16 v[0:3], v[106:109], v[24:27], v[0:3]
	v_mfma_f32_16x16x32_bf16 v[106:109], v[110:113], v[24:27], v[4:7]
	s_nop 2
	ds_read_b128 v[4:7], v114 offset:192
	ds_read_b128 v[110:113], v114 offset:4544
	ds_read_b128 v[24:27], v120 offset:17600
	s_waitcnt lgkmcnt(0)
	v_mfma_f32_16x16x32_bf16 v[28:31], v[4:7], v[24:27], v[12:15]
	v_mfma_f32_16x16x32_bf16 v[24:27], v[110:113], v[24:27], v[8:11]
	s_nop 2
	ds_read_b128 v[8:11], v120 offset:21952
	s_waitcnt lgkmcnt(0)
	v_mfma_f32_16x16x32_bf16 v[20:23], v[4:7], v[8:11], v[20:23]
	v_mfma_f32_16x16x32_bf16 v[16:19], v[110:113], v[8:11], v[16:19]
	ds_read_b128 v[8:11], v120 offset:26304
	s_waitcnt lgkmcnt(0)
	v_mfma_f32_16x16x32_bf16 v[12:15], v[4:7], v[8:11], v[126:129]
	v_mfma_f32_16x16x32_bf16 v[8:11], v[110:113], v[8:11], v[122:125]
	s_nop 2
	ds_read_b128 v[122:125], v120 offset:30656
	s_waitcnt lgkmcnt(0)
	v_mfma_f32_16x16x32_bf16 v[4:7], v[4:7], v[122:125], v[0:3]
	v_mfma_f32_16x16x32_bf16 v[0:3], v[110:113], v[122:125], v[106:109]
	v_or_b32_e32 v110, s2, v66
	v_mad_u64_u32 v[114:115], s[0:1], v110, s97, v[104:105]
	s_nop 0
	v_or_b32_e32 v106, s7, v93
	v_ashrrev_i32_e32 v107, 31, v106
	v_mov_b64_e32 v[112:113], s[34:35]
	v_mad_i32_i24 v115, s3, v146, v115
	v_mad_u64_u32 v[122:123], s[0:1], v110, s18, v[112:113]
	v_lshlrev_b64 v[110:111], 1, v[106:107]
	v_lshl_add_u64 v[114:115], v[114:115], 0, v[110:111]
	v_lshl_add_u64 v[108:109], s[88:89], 2, v[102:103]
	s_waitcnt vmcnt(0)
; __device__ __forceinline__ float bflo(unsigned w) { return __uint_as_float(w << 16); }
; __device__ __forceinline__ float bfhi(unsigned w) { return __uint_as_float(w & 0xffff0000u); }
; __device__ __forceinline__ unsigned pk4_fp8(float a, float b, float c, float d) { unsigned w = 0u; w = __builtin_amdgcn_cvt_pk_fp8_f32(clamp8(a), clamp8(b), w, false); w = __builtin_amdgcn_cvt_pk_fp8_f32(clamp8(c), clamp8(d), w, true); return w; }
; __device__ __forceinline__ void spatial_unit(const Params& p, int l, int unit, LAS unsigned char* lds, int tid) {
;     ...
; #pragma unroll
;     for (int f = 0; f < 8; ++f) {
;         const int i = f * 16 + fr; const size_t t = (size_t)nb * 128 + i; const float bias = bs[i];
; #pragma unroll
;         for (int cf = 0; cf < 2; ++cf) { const int c = g * 256 + wid * 32 + cf * 16 + 4 * fq;
;             const u32x2 uw = __builtin_nontemporal_load((const u32x2*)(PROJ + t * INC + c));
;             *(unsigned*)(YABC + t * 3072 + c) = pk4_fp8(4.f * bflo(uw.x) * (acc[cf][f][0] + bias), 4.f * bfhi(uw.x) * (acc[cf][f][1] + bias), 4.f * bflo(uw.y) * (acc[cf][f][2] + bias), 4.f * bfhi(uw.y) * (acc[cf][f][3] + bias)); }
;     }
	v_mov_b64_e32 v[124:125], v[148:149]
	v_mov_b32_e32 v121, v180
	v_mad_i32_i24 v123, s3, v147, v123
	v_lshlrev_b32_e32 v126, 16, v124
	v_and_b32_e32 v124, 0xffff0000, v124
	v_mul_f32_e32 v124, 4.0, v124
	v_add_f32_e32 v61, v61, v121
	v_mul_f32_e32 v61, v61, v124
	v_lshlrev_b32_e32 v124, 16, v125
	v_mul_f32_e32 v124, 4.0, v124
	v_add_f32_e32 v62, v62, v121
	v_mul_f32_e32 v126, 4.0, v126
	v_add_f32_e32 v60, v60, v121
	v_mul_f32_e32 v62, v62, v124
	v_and_b32_e32 v124, 0xffff0000, v125
	v_mul_f32_e32 v60, v60, v126
	v_mul_f32_e32 v124, 4.0, v124
	v_add_f32_e32 v63, v63, v121
	v_mul_f32_e32 v63, v63, v124
	v_med3_f32 v60, v60, s33, v229
	v_med3_f32 v61, v61, s33, v229
	v_mov_b32_e32 v124, v65
	v_cvt_pk_fp8_f32 v124, v60, v61
	v_med3_f32 v60, v62, s33, v229
	v_med3_f32 v61, v63, s33, v229
	v_add_f32_e32 v57, v57, v121
	v_cvt_pk_fp8_f32 v124, v60, v61 op_sel:[0,0,1]
	v_lshl_add_u64 v[60:61], v[122:123], 0, v[106:107]
	v_add_f32_e32 v58, v58, v121
	v_add_f32_e32 v56, v56, v121
	global_store_dword v[60:61], v124, off
	v_mov_b64_e32 v[62:63], v[150:151]
	v_add_f32_e32 v59, v59, v121
	v_lshlrev_b32_e32 v114, 16, v62
	v_and_b32_e32 v62, 0xffff0000, v62
	v_mul_f32_e32 v62, 4.0, v62
	v_mul_f32_e32 v57, v57, v62
	v_lshlrev_b32_e32 v62, 16, v63
	v_mul_f32_e32 v62, 4.0, v62
	v_mul_f32_e32 v114, 4.0, v114
	v_mul_f32_e32 v58, v58, v62
	v_and_b32_e32 v62, 0xffff0000, v63
	v_mul_f32_e32 v56, v56, v114
	v_mul_f32_e32 v62, 4.0, v62
	v_mul_f32_e32 v59, v59, v62
	v_med3_f32 v56, v56, s33, v229
	v_med3_f32 v57, v57, s33, v229
	v_mov_b32_e32 v62, v65
	v_cvt_pk_fp8_f32 v62, v56, v57
	v_med3_f32 v56, v58, s33, v229
	v_med3_f32 v57, v59, s33, v229
	v_or_b32_e32 v58, s2, v90
	v_cvt_pk_fp8_f32 v62, v56, v57 op_sel:[0,0,1]
	v_mad_u64_u32 v[56:57], s[0:1], v58, s97, v[104:105]
	v_mad_i32_i24 v57, s3, v146, v57
	global_store_dword v[60:61], v62, off offset:16
	v_lshl_add_u64 v[56:57], v[56:57], 0, v[110:111]
	v_mov_b64_e32 v[60:61], v[152:153]
	v_mov_b32_e32 v62, v181
	v_mad_u64_u32 v[58:59], s[0:1], v58, s18, v[112:113]
	v_mad_i32_i24 v59, s3, v147, v59
	v_lshlrev_b32_e32 v63, 16, v60
	v_and_b32_e32 v60, 0xffff0000, v60
	v_mul_f32_e32 v60, 4.0, v60
	v_add_f32_e32 v53, v53, v62
	v_mul_f32_e32 v53, v53, v60
	v_lshlrev_b32_e32 v60, 16, v61
	v_mul_f32_e32 v60, 4.0, v60
	v_add_f32_e32 v54, v54, v62
	v_mul_f32_e32 v63, 4.0, v63
	v_add_f32_e32 v52, v52, v62
	v_mul_f32_e32 v54, v54, v60
	v_and_b32_e32 v60, 0xffff0000, v61
	v_mul_f32_e32 v52, v52, v63
	v_mul_f32_e32 v60, 4.0, v60
	v_add_f32_e32 v55, v55, v62
	v_mul_f32_e32 v55, v55, v60
	v_med3_f32 v52, v52, s33, v229
	v_med3_f32 v53, v53, s33, v229
	v_mov_b32_e32 v60, v65
	v_cvt_pk_fp8_f32 v60, v52, v53
	v_med3_f32 v52, v54, s33, v229
	v_med3_f32 v53, v55, s33, v229
	v_add_f32_e32 v49, v49, v62
	v_cvt_pk_fp8_f32 v60, v52, v53 op_sel:[0,0,1]
	v_lshl_add_u64 v[52:53], v[58:59], 0, v[106:107]
	v_add_f32_e32 v50, v50, v62
	v_add_f32_e32 v48, v48, v62
	global_store_dword v[52:53], v60, off
	v_mov_b64_e32 v[54:55], v[154:155]
	v_add_f32_e32 v51, v51, v62
	v_lshlrev_b32_e32 v56, 16, v54
	v_and_b32_e32 v54, 0xffff0000, v54
	v_mul_f32_e32 v54, 4.0, v54
	v_mul_f32_e32 v49, v49, v54
	v_lshlrev_b32_e32 v54, 16, v55
	v_mul_f32_e32 v54, 4.0, v54
	v_mul_f32_e32 v56, 4.0, v56
	v_mul_f32_e32 v50, v50, v54
	v_and_b32_e32 v54, 0xffff0000, v55
	v_mul_f32_e32 v48, v48, v56
	v_mul_f32_e32 v54, 4.0, v54
	v_mul_f32_e32 v51, v51, v54
	v_med3_f32 v48, v48, s33, v229
	v_med3_f32 v49, v49, s33, v229
	v_mov_b32_e32 v54, v65
	v_cvt_pk_fp8_f32 v54, v48, v49
	v_med3_f32 v48, v50, s33, v229
	v_med3_f32 v49, v51, s33, v229
	v_or_b32_e32 v50, s2, v92
	v_cvt_pk_fp8_f32 v54, v48, v49 op_sel:[0,0,1]
	v_mad_u64_u32 v[48:49], s[0:1], v50, s97, v[104:105]
	v_mad_i32_i24 v49, s3, v146, v49
	global_store_dword v[52:53], v54, off offset:16
	v_lshl_add_u64 v[48:49], v[48:49], 0, v[110:111]
	v_mov_b64_e32 v[52:53], v[156:157]
	v_mov_b32_e32 v54, v182
	v_mad_u64_u32 v[50:51], s[0:1], v50, s18, v[112:113]
	v_mad_i32_i24 v51, s3, v147, v51
	v_lshlrev_b32_e32 v55, 16, v52
	v_and_b32_e32 v52, 0xffff0000, v52
	v_mul_f32_e32 v52, 4.0, v52
	v_add_f32_e32 v45, v45, v54
	v_mul_f32_e32 v45, v45, v52
	v_lshlrev_b32_e32 v52, 16, v53
	v_mul_f32_e32 v52, 4.0, v52
	v_add_f32_e32 v46, v46, v54
	v_mul_f32_e32 v55, 4.0, v55
	v_add_f32_e32 v44, v44, v54
	v_mul_f32_e32 v46, v46, v52
	v_and_b32_e32 v52, 0xffff0000, v53
	v_mul_f32_e32 v44, v44, v55
	v_mul_f32_e32 v52, 4.0, v52
	v_add_f32_e32 v47, v47, v54
	v_mul_f32_e32 v47, v47, v52
	v_med3_f32 v44, v44, s33, v229
	v_med3_f32 v45, v45, s33, v229
	v_mov_b32_e32 v52, v65
	v_cvt_pk_fp8_f32 v52, v44, v45
	v_med3_f32 v44, v46, s33, v229
	v_med3_f32 v45, v47, s33, v229
	v_add_f32_e32 v41, v41, v54
	v_cvt_pk_fp8_f32 v52, v44, v45 op_sel:[0,0,1]
	v_lshl_add_u64 v[44:45], v[50:51], 0, v[106:107]
	v_add_f32_e32 v42, v42, v54
	v_add_f32_e32 v40, v40, v54
	global_store_dword v[44:45], v52, off
	v_mov_b64_e32 v[46:47], v[158:159]
	v_add_f32_e32 v43, v43, v54
	v_lshlrev_b32_e32 v48, 16, v46
	v_and_b32_e32 v46, 0xffff0000, v46
	v_mul_f32_e32 v46, 4.0, v46
	v_mul_f32_e32 v41, v41, v46
	v_lshlrev_b32_e32 v46, 16, v47
	v_mul_f32_e32 v46, 4.0, v46
	v_mul_f32_e32 v48, 4.0, v48
	v_mul_f32_e32 v42, v42, v46
	v_and_b32_e32 v46, 0xffff0000, v47
	v_mul_f32_e32 v40, v40, v48
	v_mul_f32_e32 v46, 4.0, v46
	v_mul_f32_e32 v43, v43, v46
	v_med3_f32 v40, v40, s33, v229
	v_med3_f32 v41, v41, s33, v229
	v_mov_b32_e32 v46, v65
	v_cvt_pk_fp8_f32 v46, v40, v41
	v_med3_f32 v40, v42, s33, v229
	v_med3_f32 v41, v43, s33, v229
	v_or_b32_e32 v42, s2, v94
	v_cvt_pk_fp8_f32 v46, v40, v41 op_sel:[0,0,1]
	v_mad_u64_u32 v[40:41], s[0:1], v42, s97, v[104:105]
	v_mad_i32_i24 v41, s3, v146, v41
; __device__ __forceinline__ float bflo(unsigned w) { return __uint_as_float(w << 16); }
; __device__ __forceinline__ float bfhi(unsigned w) { return __uint_as_float(w & 0xffff0000u); }
; __device__ __forceinline__ unsigned pk4_fp8(float a, float b, float c, float d) { unsigned w = 0u; w = __builtin_amdgcn_cvt_pk_fp8_f32(clamp8(a), clamp8(b), w, false); w = __builtin_amdgcn_cvt_pk_fp8_f32(clamp8(c), clamp8(d), w, true); return w; }
; __device__ __forceinline__ void spatial_unit(const Params& p, int l, int unit, LAS unsigned char* lds, int tid) {
;     ...
; #pragma unroll
;     for (int f = 0; f < 8; ++f) {
;         const int i = f * 16 + fr; const size_t t = (size_t)nb * 128 + i; const float bias = bs[i];
; #pragma unroll
;         for (int cf = 0; cf < 2; ++cf) { const int c = g * 256 + wid * 32 + cf * 16 + 4 * fq;
;             const u32x2 uw = __builtin_nontemporal_load((const u32x2*)(PROJ + t * INC + c));
;             *(unsigned*)(YABC + t * 3072 + c) = pk4_fp8(4.f * bflo(uw.x) * (acc[cf][f][0] + bias), 4.f * bfhi(uw.x) * (acc[cf][f][1] + bias), 4.f * bflo(uw.y) * (acc[cf][f][2] + bias), 4.f * bfhi(uw.y) * (acc[cf][f][3] + bias)); }
;     }
	global_store_dword v[44:45], v46, off offset:16
	v_lshl_add_u64 v[40:41], v[40:41], 0, v[110:111]
	v_mov_b64_e32 v[44:45], v[160:161]
	v_mov_b32_e32 v46, v183
	v_mad_u64_u32 v[42:43], s[0:1], v42, s18, v[112:113]
	v_mad_i32_i24 v43, s3, v147, v43
	v_lshlrev_b32_e32 v47, 16, v44
	v_and_b32_e32 v44, 0xffff0000, v44
	v_mul_f32_e32 v44, 4.0, v44
	v_add_f32_e32 v37, v37, v46
	v_mul_f32_e32 v37, v37, v44
	v_lshlrev_b32_e32 v44, 16, v45
	v_mul_f32_e32 v44, 4.0, v44
	v_add_f32_e32 v38, v38, v46
	v_mul_f32_e32 v47, 4.0, v47
	v_add_f32_e32 v36, v36, v46
	v_mul_f32_e32 v38, v38, v44
	v_and_b32_e32 v44, 0xffff0000, v45
	v_mul_f32_e32 v36, v36, v47
	v_mul_f32_e32 v44, 4.0, v44
	v_add_f32_e32 v39, v39, v46
	v_mul_f32_e32 v39, v39, v44
	v_med3_f32 v36, v36, s33, v229
	v_med3_f32 v37, v37, s33, v229
	v_mov_b32_e32 v44, v65
	v_cvt_pk_fp8_f32 v44, v36, v37
	v_med3_f32 v36, v38, s33, v229
	v_med3_f32 v37, v39, s33, v229
	v_add_f32_e32 v33, v33, v46
	v_cvt_pk_fp8_f32 v44, v36, v37 op_sel:[0,0,1]
	v_lshl_add_u64 v[36:37], v[42:43], 0, v[106:107]
	v_add_f32_e32 v34, v34, v46
	v_add_f32_e32 v32, v32, v46
	global_store_dword v[36:37], v44, off
	v_mov_b64_e32 v[38:39], v[162:163]
	v_add_f32_e32 v35, v35, v46
	v_lshlrev_b32_e32 v40, 16, v38
	v_and_b32_e32 v38, 0xffff0000, v38
	v_mul_f32_e32 v38, 4.0, v38
	v_mul_f32_e32 v33, v33, v38
	v_lshlrev_b32_e32 v38, 16, v39
	v_mul_f32_e32 v38, 4.0, v38
	v_mul_f32_e32 v40, 4.0, v40
	v_mul_f32_e32 v34, v34, v38
	v_and_b32_e32 v38, 0xffff0000, v39
	v_mul_f32_e32 v32, v32, v40
	v_mul_f32_e32 v38, 4.0, v38
	v_mul_f32_e32 v35, v35, v38
	v_med3_f32 v32, v32, s33, v229
	v_med3_f32 v33, v33, s33, v229
	v_mov_b32_e32 v38, v65
	v_cvt_pk_fp8_f32 v38, v32, v33
	v_med3_f32 v32, v34, s33, v229
	v_med3_f32 v33, v35, s33, v229
	v_or_b32_e32 v34, s2, v96
	v_cvt_pk_fp8_f32 v38, v32, v33 op_sel:[0,0,1]
	v_mad_u64_u32 v[32:33], s[0:1], v34, s97, v[104:105]
	v_mad_i32_i24 v33, s3, v146, v33
	global_store_dword v[36:37], v38, off offset:16
	v_lshl_add_u64 v[32:33], v[32:33], 0, v[110:111]
	v_mov_b64_e32 v[38:39], v[164:165]
	v_mov_b32_e32 v36, v184
	v_mad_u64_u32 v[34:35], s[0:1], v34, s18, v[112:113]
	v_mad_i32_i24 v35, s3, v147, v35
	v_lshlrev_b32_e32 v37, 16, v38
	v_mul_f32_e32 v37, 4.0, v37
	v_add_f32_e32 v28, v28, v36
	v_mul_f32_e32 v37, v28, v37
	v_and_b32_e32 v28, 0xffff0000, v38
	v_mul_f32_e32 v28, 4.0, v28
	v_add_f32_e32 v29, v29, v36
	v_mul_f32_e32 v38, v29, v28
	v_lshlrev_b32_e32 v28, 16, v39
	v_mul_f32_e32 v28, 4.0, v28
	v_add_f32_e32 v29, v30, v36
	v_mul_f32_e32 v28, v29, v28
	v_and_b32_e32 v29, 0xffff0000, v39
	v_mul_f32_e32 v29, 4.0, v29
	v_add_f32_e32 v30, v31, v36
	v_mul_f32_e32 v29, v30, v29
	v_med3_f32 v30, v37, s33, v229
	v_med3_f32 v31, v38, s33, v229
	v_mov_b32_e32 v37, v65
	v_cvt_pk_fp8_f32 v37, v30, v31
	v_med3_f32 v28, v28, s33, v229
	v_med3_f32 v29, v29, s33, v229
	v_add_f32_e32 v25, v25, v36
	v_cvt_pk_fp8_f32 v37, v28, v29 op_sel:[0,0,1]
	v_lshl_add_u64 v[28:29], v[34:35], 0, v[106:107]
	v_add_f32_e32 v26, v26, v36
	v_add_f32_e32 v24, v24, v36
	global_store_dword v[28:29], v37, off
	v_mov_b64_e32 v[30:31], v[166:167]
	v_add_f32_e32 v27, v27, v36
	v_lshlrev_b32_e32 v32, 16, v30
	v_and_b32_e32 v30, 0xffff0000, v30
	v_mul_f32_e32 v30, 4.0, v30
	v_mul_f32_e32 v25, v25, v30
	v_lshlrev_b32_e32 v30, 16, v31
	v_mul_f32_e32 v30, 4.0, v30
	v_mul_f32_e32 v32, 4.0, v32
	v_mul_f32_e32 v26, v26, v30
	v_and_b32_e32 v30, 0xffff0000, v31
	v_mul_f32_e32 v24, v24, v32
	v_mul_f32_e32 v30, 4.0, v30
	v_mul_f32_e32 v27, v27, v30
	v_med3_f32 v24, v24, s33, v229
	v_med3_f32 v25, v25, s33, v229
	v_mov_b32_e32 v30, v65
	v_cvt_pk_fp8_f32 v30, v24, v25
	v_med3_f32 v24, v26, s33, v229
	v_med3_f32 v25, v27, s33, v229
	v_or_b32_e32 v26, s2, v98
	v_cvt_pk_fp8_f32 v30, v24, v25 op_sel:[0,0,1]
	v_mad_u64_u32 v[24:25], s[0:1], v26, s97, v[104:105]
	v_mad_i32_i24 v25, s3, v146, v25
	global_store_dword v[28:29], v30, off offset:16
	v_lshl_add_u64 v[24:25], v[24:25], 0, v[110:111]
	v_mov_b64_e32 v[28:29], v[168:169]
	v_mov_b32_e32 v30, v185
	v_mad_u64_u32 v[26:27], s[0:1], v26, s18, v[112:113]
	v_mad_i32_i24 v27, s3, v147, v27
	v_lshlrev_b32_e32 v31, 16, v28
	v_and_b32_e32 v28, 0xffff0000, v28
	v_mul_f32_e32 v28, 4.0, v28
	v_add_f32_e32 v21, v21, v30
	v_mul_f32_e32 v21, v21, v28
	v_lshlrev_b32_e32 v28, 16, v29
	v_mul_f32_e32 v28, 4.0, v28
	v_add_f32_e32 v22, v22, v30
	v_mul_f32_e32 v31, 4.0, v31
	v_add_f32_e32 v20, v20, v30
	v_mul_f32_e32 v22, v22, v28
	v_and_b32_e32 v28, 0xffff0000, v29
	v_mul_f32_e32 v20, v20, v31
	v_mul_f32_e32 v28, 4.0, v28
	v_add_f32_e32 v23, v23, v30
	v_mul_f32_e32 v23, v23, v28
	v_med3_f32 v20, v20, s33, v229
	v_med3_f32 v21, v21, s33, v229
	v_mov_b32_e32 v28, v65
	v_cvt_pk_fp8_f32 v28, v20, v21
	v_med3_f32 v20, v22, s33, v229
	v_med3_f32 v21, v23, s33, v229
	v_add_f32_e32 v17, v17, v30
	v_cvt_pk_fp8_f32 v28, v20, v21 op_sel:[0,0,1]
	v_lshl_add_u64 v[20:21], v[26:27], 0, v[106:107]
	v_add_f32_e32 v18, v18, v30
	v_add_f32_e32 v16, v16, v30
	global_store_dword v[20:21], v28, off
	v_mov_b64_e32 v[22:23], v[170:171]
	v_add_f32_e32 v19, v19, v30
	v_lshlrev_b32_e32 v24, 16, v22
	v_and_b32_e32 v22, 0xffff0000, v22
	v_mul_f32_e32 v22, 4.0, v22
	v_mul_f32_e32 v17, v17, v22
	v_lshlrev_b32_e32 v22, 16, v23
	v_mul_f32_e32 v22, 4.0, v22
	v_mul_f32_e32 v24, 4.0, v24
	v_mul_f32_e32 v18, v18, v22
	v_and_b32_e32 v22, 0xffff0000, v23
	v_mul_f32_e32 v16, v16, v24
	v_mul_f32_e32 v22, 4.0, v22
	v_mul_f32_e32 v19, v19, v22
	v_med3_f32 v16, v16, s33, v229
	v_med3_f32 v17, v17, s33, v229
	v_mov_b32_e32 v22, v65
	v_cvt_pk_fp8_f32 v22, v16, v17
	v_med3_f32 v16, v18, s33, v229
	v_med3_f32 v17, v19, s33, v229
	v_or_b32_e32 v18, s2, v100
; __device__ __forceinline__ float bflo(unsigned w) { return __uint_as_float(w << 16); }
; __device__ __forceinline__ float bfhi(unsigned w) { return __uint_as_float(w & 0xffff0000u); }
; __device__ __forceinline__ unsigned pk4_fp8(float a, float b, float c, float d) { unsigned w = 0u; w = __builtin_amdgcn_cvt_pk_fp8_f32(clamp8(a), clamp8(b), w, false); w = __builtin_amdgcn_cvt_pk_fp8_f32(clamp8(c), clamp8(d), w, true); return w; }
; __device__ __forceinline__ void spatial_unit(const Params& p, int l, int unit, LAS unsigned char* lds, int tid) {
;     ...
; #pragma unroll
;     for (int f = 0; f < 8; ++f) {
;         const int i = f * 16 + fr; const size_t t = (size_t)nb * 128 + i; const float bias = bs[i];
; #pragma unroll
;         for (int cf = 0; cf < 2; ++cf) { const int c = g * 256 + wid * 32 + cf * 16 + 4 * fq;
;             const u32x2 uw = __builtin_nontemporal_load((const u32x2*)(PROJ + t * INC + c));
;             *(unsigned*)(YABC + t * 3072 + c) = pk4_fp8(4.f * bflo(uw.x) * (acc[cf][f][0] + bias), 4.f * bfhi(uw.x) * (acc[cf][f][1] + bias), 4.f * bflo(uw.y) * (acc[cf][f][2] + bias), 4.f * bfhi(uw.y) * (acc[cf][f][3] + bias)); }
;     }
; __device__ __forceinline__ void conv_task(const Params& p, int l, int t0, int c) {
;     const bf16* PROJ = (const bf16*)(p.ws + WS_PROJ); unsigned char* YABC = p.ws + WS_YABC;
;     float w0[8], w1[8], w2[8], z2[8], z1[8];
;     { const float* wc = p.in[6] + (size_t)l * 3 * 1024 + c;
;       const f32x4 a0 = *(const f32x4*)wc, a1 = *(const f32x4*)(wc + 4), b0 = *(const f32x4*)(wc + 1024), b1 = *(const f32x4*)(wc + 1028), c0 = *(const f32x4*)(wc + 2048), c1 = *(const f32x4*)(wc + 2052);
;       w0[0] = a0.x; w0[1] = a0.y; w0[2] = a0.z; w0[3] = a0.w; w0[4] = a1.x; w0[5] = a1.y; w0[6] = a1.z; w0[7] = a1.w;
;       w1[0] = b0.x; w1[1] = b0.y; w1[2] = b0.z; w1[3] = b0.w; w1[4] = b1.x; w1[5] = b1.y; w1[6] = b1.z; w1[7] = b1.w;
;       w2[0] = c0.x; w2[1] = c0.y; w2[2] = c0.z; w2[3] = c0.w; w2[4] = c1.x; w2[5] = c1.y; w2[6] = c1.z; w2[7] = c1.w; }
; #pragma unroll
;     for (int i = 0; i < 8; ++i) { z2[i] = 0.f; z1[i] = 0.f; }
;     if (t0 >= 2) { float cg[8], hh[8]; ld8(PROJ + (size_t)(t0 - 2) * INC + 3072 + c, cg); ld8(PROJ + (size_t)(t0 - 2) * INC + 4096 + c, hh);
	v_cvt_pk_fp8_f32 v22, v16, v17 op_sel:[0,0,1]
	v_mad_u64_u32 v[16:17], s[0:1], v18, s97, v[104:105]
	v_mad_i32_i24 v17, s3, v146, v17
	global_store_dword v[20:21], v22, off offset:16
	v_lshl_add_u64 v[16:17], v[16:17], 0, v[110:111]
	v_mov_b64_e32 v[20:21], v[172:173]
	v_mov_b32_e32 v22, v186
	v_mad_u64_u32 v[18:19], s[0:1], v18, s18, v[112:113]
	v_mad_i32_i24 v19, s3, v147, v19
	v_lshlrev_b32_e32 v23, 16, v20
	v_and_b32_e32 v20, 0xffff0000, v20
	v_mul_f32_e32 v20, 4.0, v20
	v_add_f32_e32 v13, v13, v22
	v_mul_f32_e32 v13, v13, v20
	v_lshlrev_b32_e32 v20, 16, v21
	v_mul_f32_e32 v20, 4.0, v20
	v_add_f32_e32 v14, v14, v22
	v_mul_f32_e32 v23, 4.0, v23
	v_add_f32_e32 v12, v12, v22
	v_mul_f32_e32 v14, v14, v20
	v_and_b32_e32 v20, 0xffff0000, v21
	v_mul_f32_e32 v12, v12, v23
	v_mul_f32_e32 v20, 4.0, v20
	v_add_f32_e32 v15, v15, v22
	v_mul_f32_e32 v15, v15, v20
	v_med3_f32 v12, v12, s33, v229
	v_med3_f32 v13, v13, s33, v229
	v_mov_b32_e32 v20, v65
	v_cvt_pk_fp8_f32 v20, v12, v13
	v_med3_f32 v12, v14, s33, v229
	v_med3_f32 v13, v15, s33, v229
	v_add_f32_e32 v9, v9, v22
	v_cvt_pk_fp8_f32 v20, v12, v13 op_sel:[0,0,1]
	v_lshl_add_u64 v[12:13], v[18:19], 0, v[106:107]
	v_add_f32_e32 v10, v10, v22
	v_add_f32_e32 v8, v8, v22
	global_store_dword v[12:13], v20, off
	v_mov_b64_e32 v[14:15], v[174:175]
	v_add_f32_e32 v11, v11, v22
	v_lshlrev_b32_e32 v16, 16, v14
	v_and_b32_e32 v14, 0xffff0000, v14
	v_mul_f32_e32 v14, 4.0, v14
	v_mul_f32_e32 v9, v9, v14
	v_lshlrev_b32_e32 v14, 16, v15
	v_mul_f32_e32 v14, 4.0, v14
	v_mul_f32_e32 v16, 4.0, v16
	v_mul_f32_e32 v10, v10, v14
	v_and_b32_e32 v14, 0xffff0000, v15
	v_mul_f32_e32 v8, v8, v16
	v_mul_f32_e32 v14, 4.0, v14
	v_mul_f32_e32 v11, v11, v14
	v_med3_f32 v8, v8, s33, v229
	v_med3_f32 v9, v9, s33, v229
	v_mov_b32_e32 v14, v65
	v_cvt_pk_fp8_f32 v14, v8, v9
	v_med3_f32 v8, v10, s33, v229
	v_med3_f32 v9, v11, s33, v229
	v_mov_b32_e32 v10, v187
	v_cvt_pk_fp8_f32 v14, v8, v9 op_sel:[0,0,1]
	v_or_b32_e32 v8, s2, v88
	global_store_dword v[12:13], v14, off offset:16
	v_mad_u64_u32 v[12:13], s[0:1], v8, s97, v[104:105]
	v_mad_i32_i24 v13, s3, v146, v13
	v_mad_u64_u32 v[14:15], s[0:1], v8, s18, v[112:113]
	v_lshl_add_u64 v[8:9], v[12:13], 0, v[110:111]
	v_mov_b64_e32 v[12:13], v[176:177]
	v_mad_i32_i24 v15, s3, v147, v15
	v_add_f32_e32 v4, v4, v10
	v_add_f32_e32 v5, v5, v10
	v_add_f32_e32 v6, v6, v10
	v_add_f32_e32 v7, v7, v10
	v_add_f32_e32 v1, v1, v10
	v_add_f32_e32 v2, v2, v10
	v_add_f32_e32 v0, v0, v10
	v_add_f32_e32 v3, v3, v10
	v_lshlrev_b32_e32 v11, 16, v12
	v_mul_f32_e32 v11, 4.0, v11
	v_mul_f32_e32 v4, v4, v11
	v_and_b32_e32 v11, 0xffff0000, v12
	v_mul_f32_e32 v11, 4.0, v11
	v_mul_f32_e32 v5, v5, v11
	v_lshlrev_b32_e32 v11, 16, v13
	v_mul_f32_e32 v11, 4.0, v11
	v_mul_f32_e32 v6, v6, v11
	v_and_b32_e32 v11, 0xffff0000, v13
	v_mul_f32_e32 v11, 4.0, v11
	v_mul_f32_e32 v7, v7, v11
	v_med3_f32 v4, v4, s33, v229
	v_med3_f32 v5, v5, s33, v229
	v_mov_b32_e32 v11, v65
	v_cvt_pk_fp8_f32 v11, v4, v5
	v_med3_f32 v4, v6, s33, v229
	v_med3_f32 v5, v7, s33, v229
	v_cvt_pk_fp8_f32 v11, v4, v5 op_sel:[0,0,1]
	v_lshl_add_u64 v[4:5], v[14:15], 0, v[106:107]
	global_store_dword v[4:5], v11, off
	v_mov_b64_e32 v[6:7], v[178:179]
	v_lshlrev_b32_e32 v8, 16, v6
	v_and_b32_e32 v6, 0xffff0000, v6
	v_mul_f32_e32 v6, 4.0, v6
	v_mul_f32_e32 v1, v1, v6
	v_lshlrev_b32_e32 v6, 16, v7
	v_mul_f32_e32 v6, 4.0, v6
	v_mul_f32_e32 v8, 4.0, v8
	v_mul_f32_e32 v2, v2, v6
	v_and_b32_e32 v6, 0xffff0000, v7
	v_mul_f32_e32 v0, v0, v8
	v_mul_f32_e32 v6, 4.0, v6
	v_mul_f32_e32 v3, v3, v6
	v_med3_f32 v0, v0, s33, v229
	v_med3_f32 v1, v1, s33, v229
	v_mov_b32_e32 v6, v65
	v_cvt_pk_fp8_f32 v6, v0, v1
	v_med3_f32 v0, v2, s33, v229
	v_med3_f32 v1, v3, s33, v229
	v_cvt_pk_fp8_f32 v6, v0, v1 op_sel:[0,0,1]
	global_store_dword v[4:5], v6, off offset:16
	s_barrier
	s_cbranch_scc0 .LBB0_480
.LBB0_481:
	s_mov_b64 s[0:1], exec
	s_add_u32 s2, s52, 0x6801800
	s_addc_u32 s3, s53, 0
	s_add_u32 s4, s52, 0x12800000
	s_addc_u32 s5, s53, 0
	v_readlane_b32 s8, v249, 20
	v_readlane_b32 s9, v249, 21
	s_mul_i32 s10, s60, 0x3000
	s_mov_b32 s6, s75
	s_add_u32 s8, s8, s10
	s_addc_u32 s9, s9, 0
.Lmy_cp_loop:
	s_cmpk_lt_i32 s6, 0x100
	s_cbranch_scc0 .Lmy_cp_done
	s_lshr_b32 s7, s6, 1
	s_bitcmp1_b32 s6, 0
	s_cbranch_scc1 .Lmy_pool
; __device__ __forceinline__ void conv_task(const Params& p, int l, int t0, int c) {
;     const bf16* PROJ = (const bf16*)(p.ws + WS_PROJ); unsigned char* YABC = p.ws + WS_YABC;
;     float w0[8], w1[8], w2[8], z2[8], z1[8];
;     { const float* wc = p.in[6] + (size_t)l * 3 * 1024 + c;
;       const f32x4 a0 = *(const f32x4*)wc, a1 = *(const f32x4*)(wc + 4), b0 = *(const f32x4*)(wc + 1024), b1 = *(const f32x4*)(wc + 1028), c0 = *(const f32x4*)(wc + 2048), c1 = *(const f32x4*)(wc + 2052);
;       w0[0] = a0.x; w0[1] = a0.y; w0[2] = a0.z; w0[3] = a0.w; w0[4] = a1.x; w0[5] = a1.y; w0[6] = a1.z; w0[7] = a1.w;
;       w1[0] = b0.x; w1[1] = b0.y; w1[2] = b0.z; w1[3] = b0.w; w1[4] = b1.x; w1[5] = b1.y; w1[6] = b1.z; w1[7] = b1.w;
;       w2[0] = c0.x; w2[1] = c0.y; w2[2] = c0.z; w2[3] = c0.w; w2[4] = c1.x; w2[5] = c1.y; w2[6] = c1.z; w2[7] = c1.w; }
; #pragma unroll
;     for (int i = 0; i < 8; ++i) { z2[i] = 0.f; z1[i] = 0.f; }
;     if (t0 >= 2) { float cg[8], hh[8]; ld8(PROJ + (size_t)(t0 - 2) * INC + 3072 + c, cg); ld8(PROJ + (size_t)(t0 - 2) * INC + 4096 + c, hh);
; #pragma unroll
;         for (int i = 0; i < 8; ++i) z2[i] = cg[i] * hh[i];
;         ld8(PROJ + (size_t)(t0 - 1) * INC + 3072 + c, cg); ld8(PROJ + (size_t)(t0 - 1) * INC + 4096 + c, hh);
; #pragma unroll
;         for (int i = 0; i < 8; ++i) z1[i] = cg[i] * hh[i]; }
	v_and_b32_e32 v66, 0x7f, v67
	v_lshrrev_b32_e32 v180, 7, v67
	s_lshl_b32 s10, s7, 6
	v_lshl_add_u32 v180, v180, 4, s10
	v_lshlrev_b32_e32 v64, 5, v66
	v_mul_u32_u24_e32 v181, 0x3000, v180
	v_lshl_add_u32 v181, v66, 4, v181
	v_mul_u32_u24_e32 v182, 0xc00, v180
	v_lshl_add_u32 v182, v66, 3, v182
	v_add_u32_e32 v182, 0x400, v182
	global_load_dwordx4 v[0:3], v64, s[8:9]
	global_load_dwordx4 v[4:7], v64, s[8:9] offset:16
	v_add_u32_e32 v66, 0x1000, v64
	global_load_dwordx4 v[8:11], v66, s[8:9]
	global_load_dwordx4 v[12:15], v66, s[8:9] offset:16
	v_add_u32_e32 v66, 0x2000, v64
	global_load_dwordx4 v[16:19], v66, s[8:9]
	global_load_dwordx4 v[20:23], v66, s[8:9] offset:16
	v_mov_b32_e32 v68, 0
	v_mov_b32_e32 v69, 0
	v_mov_b32_e32 v70, 0
	v_mov_b32_e32 v71, 0
	v_mov_b32_e32 v72, 0
	v_mov_b32_e32 v73, 0
	v_mov_b32_e32 v74, 0
	v_mov_b32_e32 v75, 0
	v_mov_b32_e32 v76, 0
	v_mov_b32_e32 v77, 0
	v_mov_b32_e32 v78, 0
	v_mov_b32_e32 v79, 0
	v_mov_b32_e32 v80, 0
	v_mov_b32_e32 v81, 0
	v_mov_b32_e32 v82, 0
	v_mov_b32_e32 v83, 0
	v_cmp_ne_u32_e32 vcc, 0, v180
	s_and_saveexec_b64 s[10:11], vcc
	v_add_u32_e32 v66, 0xffffa000, v181
	global_load_dwordx4 v[68:71], v66, s[2:3] nt
	v_add_u32_e32 v66, 0xffffa000, v181
	global_load_dwordx4 v[72:75], v66, s[2:3] offset:2048 nt
	v_add_u32_e32 v66, 0xffffd000, v181
	global_load_dwordx4 v[76:79], v66, s[2:3] nt
	v_add_u32_e32 v66, 0xffffd000, v181
	global_load_dwordx4 v[80:83], v66, s[2:3] offset:2048 nt
	s_mov_b64 exec, s[0:1]
	global_load_dwordx4 v[84:87], v181, s[2:3] offset:-2048 nt
	global_load_dwordx4 v[88:91], v181, s[2:3] nt
	global_load_dwordx4 v[92:95], v181, s[2:3] offset:2048 nt
	v_add_u32_e32 v66, 0x3000, v181
	global_load_dwordx4 v[96:99], v66, s[2:3] offset:-2048 nt
	global_load_dwordx4 v[100:103], v66, s[2:3] nt
	global_load_dwordx4 v[104:107], v66, s[2:3] offset:2048 nt
	v_add_u32_e32 v66, 0x6000, v181
	global_load_dwordx4 v[108:111], v66, s[2:3] offset:-2048 nt
	global_load_dwordx4 v[112:115], v66, s[2:3] nt
	global_load_dwordx4 v[116:119], v66, s[2:3] offset:2048 nt
	v_add_u32_e32 v66, 0x9000, v181
	global_load_dwordx4 v[120:123], v66, s[2:3] offset:-2048 nt
	global_load_dwordx4 v[124:127], v66, s[2:3] nt
	global_load_dwordx4 v[128:131], v66, s[2:3] offset:2048 nt
	v_add_u32_e32 v66, 0xc000, v181
	global_load_dwordx4 v[132:135], v66, s[2:3] offset:-2048 nt
	global_load_dwordx4 v[136:139], v66, s[2:3] nt
	global_load_dwordx4 v[140:143], v66, s[2:3] offset:2048 nt
	v_add_u32_e32 v66, 0xf000, v181
	global_load_dwordx4 v[144:147], v66, s[2:3] offset:-2048 nt
	global_load_dwordx4 v[148:151], v66, s[2:3] nt
	global_load_dwordx4 v[152:155], v66, s[2:3] offset:2048 nt
	v_add_u32_e32 v66, 0x12000, v181
	global_load_dwordx4 v[156:159], v66, s[2:3] offset:-2048 nt
	global_load_dwordx4 v[160:163], v66, s[2:3] nt
	global_load_dwordx4 v[164:167], v66, s[2:3] offset:2048 nt
	v_add_u32_e32 v66, 0x15000, v181
	global_load_dwordx4 v[168:171], v66, s[2:3] offset:-2048 nt
	global_load_dwordx4 v[172:175], v66, s[2:3] nt
	global_load_dwordx4 v[176:179], v66, s[2:3] offset:2048 nt
	s_waitcnt vmcnt(24)
	v_lshlrev_b32_e32 v48, 16, v68
	v_and_b32_e32 v49, 0xffff0000, v68
	v_lshlrev_b32_e32 v50, 16, v69
	v_and_b32_e32 v51, 0xffff0000, v69
	v_lshlrev_b32_e32 v52, 16, v70
	v_and_b32_e32 v53, 0xffff0000, v70
	v_lshlrev_b32_e32 v54, 16, v71
	v_and_b32_e32 v55, 0xffff0000, v71
	v_lshlrev_b32_e32 v56, 16, v72
	v_and_b32_e32 v57, 0xffff0000, v72
	v_lshlrev_b32_e32 v58, 16, v73
	v_and_b32_e32 v59, 0xffff0000, v73
	v_lshlrev_b32_e32 v60, 16, v74
	v_and_b32_e32 v61, 0xffff0000, v74
	v_lshlrev_b32_e32 v62, 16, v75
	v_and_b32_e32 v63, 0xffff0000, v75
	v_pk_mul_f32 v[24:25], v[48:49], v[56:57]
	v_pk_mul_f32 v[26:27], v[50:51], v[58:59]
	v_pk_mul_f32 v[28:29], v[52:53], v[60:61]
	v_pk_mul_f32 v[30:31], v[54:55], v[62:63]
	v_lshlrev_b32_e32 v48, 16, v76
	v_and_b32_e32 v49, 0xffff0000, v76
	v_lshlrev_b32_e32 v50, 16, v77
	v_and_b32_e32 v51, 0xffff0000, v77
	v_lshlrev_b32_e32 v52, 16, v78
	v_and_b32_e32 v53, 0xffff0000, v78
	v_lshlrev_b32_e32 v54, 16, v79
	v_and_b32_e32 v55, 0xffff0000, v79
	v_lshlrev_b32_e32 v56, 16, v80
	v_and_b32_e32 v57, 0xffff0000, v80
	v_lshlrev_b32_e32 v58, 16, v81
	v_and_b32_e32 v59, 0xffff0000, v81
	v_lshlrev_b32_e32 v60, 16, v82
	v_and_b32_e32 v61, 0xffff0000, v82
	v_lshlrev_b32_e32 v62, 16, v83
	v_and_b32_e32 v63, 0xffff0000, v83
	v_pk_mul_f32 v[32:33], v[48:49], v[56:57]
	v_pk_mul_f32 v[34:35], v[50:51], v[58:59]
	v_pk_mul_f32 v[36:37], v[52:53], v[60:61]
	v_pk_mul_f32 v[38:39], v[54:55], v[62:63]
	s_waitcnt vmcnt(21)
; __device__ __forceinline__ unsigned pk4_fp8(float a, float b, float c, float d) { unsigned w = 0u; w = __builtin_amdgcn_cvt_pk_fp8_f32(clamp8(a), clamp8(b), w, false); w = __builtin_amdgcn_cvt_pk_fp8_f32(clamp8(c), clamp8(d), w, true); return w; }
; __device__ __forceinline__ void st8q(unsigned char* ptr, const float (&f)[8]) {
;     u32x2 w; w.x = pk4_fp8(4.f * f[0], 4.f * f[1], 4.f * f[2], 4.f * f[3]); w.y = pk4_fp8(4.f * f[4], 4.f * f[5], 4.f * f[6], 4.f * f[7]); *(u32x2*)ptr = w;
; }
; __device__ __forceinline__ void conv_task(const Params& p, int l, int t0, int c) {
;     ...
;     for (int k = 0; k < 16; ++k) { const size_t t = (size_t)(t0 + k);
;         float bgv[8], cg[8], hh[8], o[8]; ld8(PROJ + t * INC + 2048 + c, bgv); ld8(PROJ + t * INC + 3072 + c, cg); ld8(PROJ + t * INC + 4096 + c, hh);
; #pragma unroll
;         for (int i = 0; i < 8; ++i) { const float z0 = cg[i] * hh[i]; o[i] = bgv[i] * (w0[i] * z2[i] + w1[i] * z1[i] + w2[i] * z0); z2[i] = z1[i]; z1[i] = z0; }
;         st8q(YABC + t * 3072 + 1024 + c, o); }
	v_lshlrev_b32_e32 v48, 16, v88
	v_and_b32_e32 v49, 0xffff0000, v88
	v_lshlrev_b32_e32 v50, 16, v89
	v_and_b32_e32 v51, 0xffff0000, v89
	v_lshlrev_b32_e32 v52, 16, v90
	v_and_b32_e32 v53, 0xffff0000, v90
	v_lshlrev_b32_e32 v54, 16, v91
	v_and_b32_e32 v55, 0xffff0000, v91
	v_lshlrev_b32_e32 v56, 16, v92
	v_and_b32_e32 v57, 0xffff0000, v92
	v_lshlrev_b32_e32 v58, 16, v93
	v_and_b32_e32 v59, 0xffff0000, v93
	v_lshlrev_b32_e32 v60, 16, v94
	v_and_b32_e32 v61, 0xffff0000, v94
	v_lshlrev_b32_e32 v62, 16, v95
	v_and_b32_e32 v63, 0xffff0000, v95
	v_pk_mul_f32 v[40:41], v[48:49], v[56:57]
	v_pk_mul_f32 v[42:43], v[50:51], v[58:59]
	v_pk_mul_f32 v[44:45], v[52:53], v[60:61]
	v_pk_mul_f32 v[46:47], v[54:55], v[62:63]
	v_pk_mul_f32 v[48:49], v[0:1], v[24:25]
	v_pk_mul_f32 v[56:57], v[8:9], v[32:33]
	v_pk_mul_f32 v[50:51], v[2:3], v[26:27]
	v_pk_mul_f32 v[58:59], v[10:11], v[34:35]
	v_pk_mul_f32 v[52:53], v[4:5], v[28:29]
	v_pk_mul_f32 v[60:61], v[12:13], v[36:37]
	v_pk_mul_f32 v[54:55], v[6:7], v[30:31]
	v_pk_mul_f32 v[62:63], v[14:15], v[38:39]
	v_pk_add_f32 v[48:49], v[48:49], v[56:57]
	v_pk_add_f32 v[50:51], v[50:51], v[58:59]
	v_pk_add_f32 v[52:53], v[52:53], v[60:61]
	v_pk_add_f32 v[54:55], v[54:55], v[62:63]
	v_pk_fma_f32 v[48:49], v[16:17], v[40:41], v[48:49]
	v_pk_fma_f32 v[50:51], v[18:19], v[42:43], v[50:51]
	v_pk_fma_f32 v[52:53], v[20:21], v[44:45], v[52:53]
	v_pk_fma_f32 v[54:55], v[22:23], v[46:47], v[54:55]
	v_lshlrev_b32_e32 v56, 16, v84
	v_and_b32_e32 v57, 0xffff0000, v84
	v_lshlrev_b32_e32 v58, 16, v85
	v_and_b32_e32 v59, 0xffff0000, v85
	v_lshlrev_b32_e32 v60, 16, v86
	v_and_b32_e32 v61, 0xffff0000, v86
	v_lshlrev_b32_e32 v62, 16, v87
	v_and_b32_e32 v63, 0xffff0000, v87
	v_pk_mul_f32 v[48:49], v[48:49], v[56:57]
	v_pk_mul_f32 v[50:51], v[50:51], v[58:59]
	v_pk_mul_f32 v[52:53], v[52:53], v[60:61]
	v_pk_mul_f32 v[54:55], v[54:55], v[62:63]
	v_pk_mul_f32 v[48:49], v[48:49], 4.0 op_sel_hi:[1,0]
	v_pk_mul_f32 v[50:51], v[50:51], 4.0 op_sel_hi:[1,0]
	v_pk_mul_f32 v[52:53], v[52:53], 4.0 op_sel_hi:[1,0]
	v_pk_mul_f32 v[54:55], v[54:55], 4.0 op_sel_hi:[1,0]
	v_med3_f32 v48, v48, s33, v229
	v_med3_f32 v49, v49, s33, v229
	v_med3_f32 v50, v50, s33, v229
	v_med3_f32 v51, v51, s33, v229
	v_med3_f32 v52, v52, s33, v229
	v_med3_f32 v53, v53, s33, v229
	v_med3_f32 v54, v54, s33, v229
	v_med3_f32 v55, v55, s33, v229
	v_cvt_pk_fp8_f32 v62, v48, v49
	v_cvt_pk_fp8_f32 v63, v52, v53
	v_cvt_pk_fp8_f32 v62, v50, v51 op_sel:[0,0,1]
	v_cvt_pk_fp8_f32 v63, v54, v55 op_sel:[0,0,1]
	global_store_dwordx2 v182, v[62:63], s[4:5]
	v_add_u32_e32 v66, 0x18000, v181
	global_load_dwordx4 v[84:87], v66, s[2:3] offset:-2048 nt
	global_load_dwordx4 v[88:91], v66, s[2:3] nt
	global_load_dwordx4 v[92:95], v66, s[2:3] offset:2048 nt
	s_waitcnt vmcnt(22)
	v_lshlrev_b32_e32 v48, 16, v100
	v_and_b32_e32 v49, 0xffff0000, v100
	v_lshlrev_b32_e32 v50, 16, v101
	v_and_b32_e32 v51, 0xffff0000, v101
	v_lshlrev_b32_e32 v52, 16, v102
	v_and_b32_e32 v53, 0xffff0000, v102
	v_lshlrev_b32_e32 v54, 16, v103
	v_and_b32_e32 v55, 0xffff0000, v103
	v_lshlrev_b32_e32 v56, 16, v104
	v_and_b32_e32 v57, 0xffff0000, v104
	v_lshlrev_b32_e32 v58, 16, v105
	v_and_b32_e32 v59, 0xffff0000, v105
	v_lshlrev_b32_e32 v60, 16, v106
	v_and_b32_e32 v61, 0xffff0000, v106
	v_lshlrev_b32_e32 v62, 16, v107
	v_and_b32_e32 v63, 0xffff0000, v107
	v_pk_mul_f32 v[24:25], v[48:49], v[56:57]
	v_pk_mul_f32 v[26:27], v[50:51], v[58:59]
	v_pk_mul_f32 v[28:29], v[52:53], v[60:61]
	v_pk_mul_f32 v[30:31], v[54:55], v[62:63]
	v_pk_mul_f32 v[48:49], v[0:1], v[32:33]
	v_pk_mul_f32 v[56:57], v[8:9], v[40:41]
	v_pk_mul_f32 v[50:51], v[2:3], v[34:35]
	v_pk_mul_f32 v[58:59], v[10:11], v[42:43]
	v_pk_mul_f32 v[52:53], v[4:5], v[36:37]
	v_pk_mul_f32 v[60:61], v[12:13], v[44:45]
	v_pk_mul_f32 v[54:55], v[6:7], v[38:39]
	v_pk_mul_f32 v[62:63], v[14:15], v[46:47]
	v_pk_add_f32 v[48:49], v[48:49], v[56:57]
	v_pk_add_f32 v[50:51], v[50:51], v[58:59]
	v_pk_add_f32 v[52:53], v[52:53], v[60:61]
	v_pk_add_f32 v[54:55], v[54:55], v[62:63]
	v_pk_fma_f32 v[48:49], v[16:17], v[24:25], v[48:49]
	v_pk_fma_f32 v[50:51], v[18:19], v[26:27], v[50:51]
	v_pk_fma_f32 v[52:53], v[20:21], v[28:29], v[52:53]
	v_pk_fma_f32 v[54:55], v[22:23], v[30:31], v[54:55]
	v_lshlrev_b32_e32 v56, 16, v96
	v_and_b32_e32 v57, 0xffff0000, v96
	v_lshlrev_b32_e32 v58, 16, v97
	v_and_b32_e32 v59, 0xffff0000, v97
	v_lshlrev_b32_e32 v60, 16, v98
	v_and_b32_e32 v61, 0xffff0000, v98
	v_lshlrev_b32_e32 v62, 16, v99
	v_and_b32_e32 v63, 0xffff0000, v99
	v_pk_mul_f32 v[48:49], v[48:49], v[56:57]
	v_pk_mul_f32 v[50:51], v[50:51], v[58:59]
	v_pk_mul_f32 v[52:53], v[52:53], v[60:61]
	v_pk_mul_f32 v[54:55], v[54:55], v[62:63]
	v_pk_mul_f32 v[48:49], v[48:49], 4.0 op_sel_hi:[1,0]
	v_pk_mul_f32 v[50:51], v[50:51], 4.0 op_sel_hi:[1,0]
	v_pk_mul_f32 v[52:53], v[52:53], 4.0 op_sel_hi:[1,0]
	v_pk_mul_f32 v[54:55], v[54:55], 4.0 op_sel_hi:[1,0]
	v_med3_f32 v48, v48, s33, v229
	v_med3_f32 v49, v49, s33, v229
	v_med3_f32 v50, v50, s33, v229
	v_med3_f32 v51, v51, s33, v229
	v_med3_f32 v52, v52, s33, v229
	v_med3_f32 v53, v53, s33, v229
	v_med3_f32 v54, v54, s33, v229
	v_med3_f32 v55, v55, s33, v229
	v_add_u32_e32 v66, 0xc00, v182
	v_cvt_pk_fp8_f32 v62, v48, v49
	v_cvt_pk_fp8_f32 v63, v52, v53
	v_cvt_pk_fp8_f32 v62, v50, v51 op_sel:[0,0,1]
	v_cvt_pk_fp8_f32 v63, v54, v55 op_sel:[0,0,1]
	global_store_dwordx2 v66, v[62:63], s[4:5]
	v_add_u32_e32 v66, 0x1b000, v181
	global_load_dwordx4 v[96:99], v66, s[2:3] offset:-2048 nt
	global_load_dwordx4 v[100:103], v66, s[2:3] nt
	global_load_dwordx4 v[104:107], v66, s[2:3] offset:2048 nt
	s_waitcnt vmcnt(23)
; __device__ __forceinline__ void conv_task(const Params& p, int l, int t0, int c) {
;     ...
;     for (int k = 0; k < 16; ++k) { const size_t t = (size_t)(t0 + k);
;         float bgv[8], cg[8], hh[8], o[8]; ld8(PROJ + t * INC + 2048 + c, bgv); ld8(PROJ + t * INC + 3072 + c, cg); ld8(PROJ + t * INC + 4096 + c, hh);
; #pragma unroll
;         for (int i = 0; i < 8; ++i) { const float z0 = cg[i] * hh[i]; o[i] = bgv[i] * (w0[i] * z2[i] + w1[i] * z1[i] + w2[i] * z0); z2[i] = z1[i]; z1[i] = z0; }
;         st8q(YABC + t * 3072 + 1024 + c, o); }
	v_lshlrev_b32_e32 v48, 16, v112
	v_and_b32_e32 v49, 0xffff0000, v112
	v_lshlrev_b32_e32 v50, 16, v113
	v_and_b32_e32 v51, 0xffff0000, v113
	v_lshlrev_b32_e32 v52, 16, v114
	v_and_b32_e32 v53, 0xffff0000, v114
	v_lshlrev_b32_e32 v54, 16, v115
	v_and_b32_e32 v55, 0xffff0000, v115
	v_lshlrev_b32_e32 v56, 16, v116
	v_and_b32_e32 v57, 0xffff0000, v116
	v_lshlrev_b32_e32 v58, 16, v117
	v_and_b32_e32 v59, 0xffff0000, v117
	v_lshlrev_b32_e32 v60, 16, v118
	v_and_b32_e32 v61, 0xffff0000, v118
	v_lshlrev_b32_e32 v62, 16, v119
	v_and_b32_e32 v63, 0xffff0000, v119
	v_pk_mul_f32 v[32:33], v[48:49], v[56:57]
	v_pk_mul_f32 v[34:35], v[50:51], v[58:59]
	v_pk_mul_f32 v[36:37], v[52:53], v[60:61]
	v_pk_mul_f32 v[38:39], v[54:55], v[62:63]
	v_pk_mul_f32 v[48:49], v[0:1], v[40:41]
	v_pk_mul_f32 v[56:57], v[8:9], v[24:25]
	v_pk_mul_f32 v[50:51], v[2:3], v[42:43]
	v_pk_mul_f32 v[58:59], v[10:11], v[26:27]
	v_pk_mul_f32 v[52:53], v[4:5], v[44:45]
	v_pk_mul_f32 v[60:61], v[12:13], v[28:29]
	v_pk_mul_f32 v[54:55], v[6:7], v[46:47]
	v_pk_mul_f32 v[62:63], v[14:15], v[30:31]
	v_pk_add_f32 v[48:49], v[48:49], v[56:57]
	v_pk_add_f32 v[50:51], v[50:51], v[58:59]
	v_pk_add_f32 v[52:53], v[52:53], v[60:61]
	v_pk_add_f32 v[54:55], v[54:55], v[62:63]
	v_pk_fma_f32 v[48:49], v[16:17], v[32:33], v[48:49]
	v_pk_fma_f32 v[50:51], v[18:19], v[34:35], v[50:51]
	v_pk_fma_f32 v[52:53], v[20:21], v[36:37], v[52:53]
	v_pk_fma_f32 v[54:55], v[22:23], v[38:39], v[54:55]
	v_lshlrev_b32_e32 v56, 16, v108
	v_and_b32_e32 v57, 0xffff0000, v108
	v_lshlrev_b32_e32 v58, 16, v109
	v_and_b32_e32 v59, 0xffff0000, v109
	v_lshlrev_b32_e32 v60, 16, v110
	v_and_b32_e32 v61, 0xffff0000, v110
	v_lshlrev_b32_e32 v62, 16, v111
	v_and_b32_e32 v63, 0xffff0000, v111
	v_pk_mul_f32 v[48:49], v[48:49], v[56:57]
	v_pk_mul_f32 v[50:51], v[50:51], v[58:59]
	v_pk_mul_f32 v[52:53], v[52:53], v[60:61]
	v_pk_mul_f32 v[54:55], v[54:55], v[62:63]
	v_pk_mul_f32 v[48:49], v[48:49], 4.0 op_sel_hi:[1,0]
	v_pk_mul_f32 v[50:51], v[50:51], 4.0 op_sel_hi:[1,0]
	v_pk_mul_f32 v[52:53], v[52:53], 4.0 op_sel_hi:[1,0]
	v_pk_mul_f32 v[54:55], v[54:55], 4.0 op_sel_hi:[1,0]
	v_med3_f32 v48, v48, s33, v229
	v_med3_f32 v49, v49, s33, v229
	v_med3_f32 v50, v50, s33, v229
	v_med3_f32 v51, v51, s33, v229
	v_med3_f32 v52, v52, s33, v229
	v_med3_f32 v53, v53, s33, v229
	v_med3_f32 v54, v54, s33, v229
	v_med3_f32 v55, v55, s33, v229
	v_add_u32_e32 v66, 0x1800, v182
	v_cvt_pk_fp8_f32 v62, v48, v49
	v_cvt_pk_fp8_f32 v63, v52, v53
	v_cvt_pk_fp8_f32 v62, v50, v51 op_sel:[0,0,1]
	v_cvt_pk_fp8_f32 v63, v54, v55 op_sel:[0,0,1]
	global_store_dwordx2 v66, v[62:63], s[4:5]
	v_add_u32_e32 v66, 0x1e000, v181
	global_load_dwordx4 v[108:111], v66, s[2:3] offset:-2048 nt
	global_load_dwordx4 v[112:115], v66, s[2:3] nt
	global_load_dwordx4 v[116:119], v66, s[2:3] offset:2048 nt
	s_waitcnt vmcnt(24)
	v_lshlrev_b32_e32 v48, 16, v124
	v_and_b32_e32 v49, 0xffff0000, v124
	v_lshlrev_b32_e32 v50, 16, v125
	v_and_b32_e32 v51, 0xffff0000, v125
	v_lshlrev_b32_e32 v52, 16, v126
	v_and_b32_e32 v53, 0xffff0000, v126
	v_lshlrev_b32_e32 v54, 16, v127
	v_and_b32_e32 v55, 0xffff0000, v127
	v_lshlrev_b32_e32 v56, 16, v128
	v_and_b32_e32 v57, 0xffff0000, v128
	v_lshlrev_b32_e32 v58, 16, v129
	v_and_b32_e32 v59, 0xffff0000, v129
	v_lshlrev_b32_e32 v60, 16, v130
	v_and_b32_e32 v61, 0xffff0000, v130
	v_lshlrev_b32_e32 v62, 16, v131
	v_and_b32_e32 v63, 0xffff0000, v131
	v_pk_mul_f32 v[40:41], v[48:49], v[56:57]
	v_pk_mul_f32 v[42:43], v[50:51], v[58:59]
	v_pk_mul_f32 v[44:45], v[52:53], v[60:61]
	v_pk_mul_f32 v[46:47], v[54:55], v[62:63]
	v_pk_mul_f32 v[48:49], v[0:1], v[24:25]
	v_pk_mul_f32 v[56:57], v[8:9], v[32:33]
	v_pk_mul_f32 v[50:51], v[2:3], v[26:27]
	v_pk_mul_f32 v[58:59], v[10:11], v[34:35]
	v_pk_mul_f32 v[52:53], v[4:5], v[28:29]
	v_pk_mul_f32 v[60:61], v[12:13], v[36:37]
	v_pk_mul_f32 v[54:55], v[6:7], v[30:31]
	v_pk_mul_f32 v[62:63], v[14:15], v[38:39]
	v_pk_add_f32 v[48:49], v[48:49], v[56:57]
	v_pk_add_f32 v[50:51], v[50:51], v[58:59]
	v_pk_add_f32 v[52:53], v[52:53], v[60:61]
	v_pk_add_f32 v[54:55], v[54:55], v[62:63]
	v_pk_fma_f32 v[48:49], v[16:17], v[40:41], v[48:49]
	v_pk_fma_f32 v[50:51], v[18:19], v[42:43], v[50:51]
	v_pk_fma_f32 v[52:53], v[20:21], v[44:45], v[52:53]
	v_pk_fma_f32 v[54:55], v[22:23], v[46:47], v[54:55]
	v_lshlrev_b32_e32 v56, 16, v120
	v_and_b32_e32 v57, 0xffff0000, v120
	v_lshlrev_b32_e32 v58, 16, v121
	v_and_b32_e32 v59, 0xffff0000, v121
	v_lshlrev_b32_e32 v60, 16, v122
	v_and_b32_e32 v61, 0xffff0000, v122
	v_lshlrev_b32_e32 v62, 16, v123
	v_and_b32_e32 v63, 0xffff0000, v123
	v_pk_mul_f32 v[48:49], v[48:49], v[56:57]
	v_pk_mul_f32 v[50:51], v[50:51], v[58:59]
	v_pk_mul_f32 v[52:53], v[52:53], v[60:61]
	v_pk_mul_f32 v[54:55], v[54:55], v[62:63]
	v_pk_mul_f32 v[48:49], v[48:49], 4.0 op_sel_hi:[1,0]
	v_pk_mul_f32 v[50:51], v[50:51], 4.0 op_sel_hi:[1,0]
	v_pk_mul_f32 v[52:53], v[52:53], 4.0 op_sel_hi:[1,0]
	v_pk_mul_f32 v[54:55], v[54:55], 4.0 op_sel_hi:[1,0]
	v_med3_f32 v48, v48, s33, v229
	v_med3_f32 v49, v49, s33, v229
	v_med3_f32 v50, v50, s33, v229
	v_med3_f32 v51, v51, s33, v229
	v_med3_f32 v52, v52, s33, v229
	v_med3_f32 v53, v53, s33, v229
	v_med3_f32 v54, v54, s33, v229
	v_med3_f32 v55, v55, s33, v229
	v_add_u32_e32 v66, 0x2400, v182
	v_cvt_pk_fp8_f32 v62, v48, v49
	v_cvt_pk_fp8_f32 v63, v52, v53
	v_cvt_pk_fp8_f32 v62, v50, v51 op_sel:[0,0,1]
	v_cvt_pk_fp8_f32 v63, v54, v55 op_sel:[0,0,1]
	global_store_dwordx2 v66, v[62:63], s[4:5]
	v_add_u32_e32 v66, 0x21000, v181
	global_load_dwordx4 v[120:123], v66, s[2:3] offset:-2048 nt
	global_load_dwordx4 v[124:127], v66, s[2:3] nt
	global_load_dwordx4 v[128:131], v66, s[2:3] offset:2048 nt
	s_waitcnt vmcnt(25)
; __device__ __forceinline__ void conv_task(const Params& p, int l, int t0, int c) {
;     ...
;     for (int k = 0; k < 16; ++k) { const size_t t = (size_t)(t0 + k);
;         float bgv[8], cg[8], hh[8], o[8]; ld8(PROJ + t * INC + 2048 + c, bgv); ld8(PROJ + t * INC + 3072 + c, cg); ld8(PROJ + t * INC + 4096 + c, hh);
; #pragma unroll
;         for (int i = 0; i < 8; ++i) { const float z0 = cg[i] * hh[i]; o[i] = bgv[i] * (w0[i] * z2[i] + w1[i] * z1[i] + w2[i] * z0); z2[i] = z1[i]; z1[i] = z0; }
;         st8q(YABC + t * 3072 + 1024 + c, o); }
	v_lshlrev_b32_e32 v48, 16, v136
	v_and_b32_e32 v49, 0xffff0000, v136
	v_lshlrev_b32_e32 v50, 16, v137
	v_and_b32_e32 v51, 0xffff0000, v137
	v_lshlrev_b32_e32 v52, 16, v138
	v_and_b32_e32 v53, 0xffff0000, v138
	v_lshlrev_b32_e32 v54, 16, v139
	v_and_b32_e32 v55, 0xffff0000, v139
	v_lshlrev_b32_e32 v56, 16, v140
	v_and_b32_e32 v57, 0xffff0000, v140
	v_lshlrev_b32_e32 v58, 16, v141
	v_and_b32_e32 v59, 0xffff0000, v141
	v_lshlrev_b32_e32 v60, 16, v142
	v_and_b32_e32 v61, 0xffff0000, v142
	v_lshlrev_b32_e32 v62, 16, v143
	v_and_b32_e32 v63, 0xffff0000, v143
	v_pk_mul_f32 v[24:25], v[48:49], v[56:57]
	v_pk_mul_f32 v[26:27], v[50:51], v[58:59]
	v_pk_mul_f32 v[28:29], v[52:53], v[60:61]
	v_pk_mul_f32 v[30:31], v[54:55], v[62:63]
	v_pk_mul_f32 v[48:49], v[0:1], v[32:33]
	v_pk_mul_f32 v[56:57], v[8:9], v[40:41]
	v_pk_mul_f32 v[50:51], v[2:3], v[34:35]
	v_pk_mul_f32 v[58:59], v[10:11], v[42:43]
	v_pk_mul_f32 v[52:53], v[4:5], v[36:37]
	v_pk_mul_f32 v[60:61], v[12:13], v[44:45]
	v_pk_mul_f32 v[54:55], v[6:7], v[38:39]
	v_pk_mul_f32 v[62:63], v[14:15], v[46:47]
	v_pk_add_f32 v[48:49], v[48:49], v[56:57]
	v_pk_add_f32 v[50:51], v[50:51], v[58:59]
	v_pk_add_f32 v[52:53], v[52:53], v[60:61]
	v_pk_add_f32 v[54:55], v[54:55], v[62:63]
	v_pk_fma_f32 v[48:49], v[16:17], v[24:25], v[48:49]
	v_pk_fma_f32 v[50:51], v[18:19], v[26:27], v[50:51]
	v_pk_fma_f32 v[52:53], v[20:21], v[28:29], v[52:53]
	v_pk_fma_f32 v[54:55], v[22:23], v[30:31], v[54:55]
	v_lshlrev_b32_e32 v56, 16, v132
	v_and_b32_e32 v57, 0xffff0000, v132
	v_lshlrev_b32_e32 v58, 16, v133
	v_and_b32_e32 v59, 0xffff0000, v133
	v_lshlrev_b32_e32 v60, 16, v134
	v_and_b32_e32 v61, 0xffff0000, v134
	v_lshlrev_b32_e32 v62, 16, v135
	v_and_b32_e32 v63, 0xffff0000, v135
	v_pk_mul_f32 v[48:49], v[48:49], v[56:57]
	v_pk_mul_f32 v[50:51], v[50:51], v[58:59]
	v_pk_mul_f32 v[52:53], v[52:53], v[60:61]
	v_pk_mul_f32 v[54:55], v[54:55], v[62:63]
	v_pk_mul_f32 v[48:49], v[48:49], 4.0 op_sel_hi:[1,0]
	v_pk_mul_f32 v[50:51], v[50:51], 4.0 op_sel_hi:[1,0]
	v_pk_mul_f32 v[52:53], v[52:53], 4.0 op_sel_hi:[1,0]
	v_pk_mul_f32 v[54:55], v[54:55], 4.0 op_sel_hi:[1,0]
	v_med3_f32 v48, v48, s33, v229
	v_med3_f32 v49, v49, s33, v229
	v_med3_f32 v50, v50, s33, v229
	v_med3_f32 v51, v51, s33, v229
	v_med3_f32 v52, v52, s33, v229
	v_med3_f32 v53, v53, s33, v229
	v_med3_f32 v54, v54, s33, v229
	v_med3_f32 v55, v55, s33, v229
	v_add_u32_e32 v66, 0x3000, v182
	v_cvt_pk_fp8_f32 v62, v48, v49
	v_cvt_pk_fp8_f32 v63, v52, v53
	v_cvt_pk_fp8_f32 v62, v50, v51 op_sel:[0,0,1]
	v_cvt_pk_fp8_f32 v63, v54, v55 op_sel:[0,0,1]
	global_store_dwordx2 v66, v[62:63], s[4:5]
	v_add_u32_e32 v66, 0x24000, v181
	global_load_dwordx4 v[132:135], v66, s[2:3] offset:-2048 nt
	global_load_dwordx4 v[136:139], v66, s[2:3] nt
	global_load_dwordx4 v[140:143], v66, s[2:3] offset:2048 nt
	s_waitcnt vmcnt(26)
	v_lshlrev_b32_e32 v48, 16, v148
	v_and_b32_e32 v49, 0xffff0000, v148
	v_lshlrev_b32_e32 v50, 16, v149
	v_and_b32_e32 v51, 0xffff0000, v149
	v_lshlrev_b32_e32 v52, 16, v150
	v_and_b32_e32 v53, 0xffff0000, v150
	v_lshlrev_b32_e32 v54, 16, v151
	v_and_b32_e32 v55, 0xffff0000, v151
	v_lshlrev_b32_e32 v56, 16, v152
	v_and_b32_e32 v57, 0xffff0000, v152
	v_lshlrev_b32_e32 v58, 16, v153
	v_and_b32_e32 v59, 0xffff0000, v153
	v_lshlrev_b32_e32 v60, 16, v154
	v_and_b32_e32 v61, 0xffff0000, v154
	v_lshlrev_b32_e32 v62, 16, v155
	v_and_b32_e32 v63, 0xffff0000, v155
	v_pk_mul_f32 v[32:33], v[48:49], v[56:57]
	v_pk_mul_f32 v[34:35], v[50:51], v[58:59]
	v_pk_mul_f32 v[36:37], v[52:53], v[60:61]
	v_pk_mul_f32 v[38:39], v[54:55], v[62:63]
	v_pk_mul_f32 v[48:49], v[0:1], v[40:41]
	v_pk_mul_f32 v[56:57], v[8:9], v[24:25]
	v_pk_mul_f32 v[50:51], v[2:3], v[42:43]
	v_pk_mul_f32 v[58:59], v[10:11], v[26:27]
	v_pk_mul_f32 v[52:53], v[4:5], v[44:45]
	v_pk_mul_f32 v[60:61], v[12:13], v[28:29]
	v_pk_mul_f32 v[54:55], v[6:7], v[46:47]
	v_pk_mul_f32 v[62:63], v[14:15], v[30:31]
	v_pk_add_f32 v[48:49], v[48:49], v[56:57]
	v_pk_add_f32 v[50:51], v[50:51], v[58:59]
	v_pk_add_f32 v[52:53], v[52:53], v[60:61]
	v_pk_add_f32 v[54:55], v[54:55], v[62:63]
	v_pk_fma_f32 v[48:49], v[16:17], v[32:33], v[48:49]
	v_pk_fma_f32 v[50:51], v[18:19], v[34:35], v[50:51]
	v_pk_fma_f32 v[52:53], v[20:21], v[36:37], v[52:53]
	v_pk_fma_f32 v[54:55], v[22:23], v[38:39], v[54:55]
	v_lshlrev_b32_e32 v56, 16, v144
	v_and_b32_e32 v57, 0xffff0000, v144
	v_lshlrev_b32_e32 v58, 16, v145
	v_and_b32_e32 v59, 0xffff0000, v145
	v_lshlrev_b32_e32 v60, 16, v146
	v_and_b32_e32 v61, 0xffff0000, v146
	v_lshlrev_b32_e32 v62, 16, v147
	v_and_b32_e32 v63, 0xffff0000, v147
	v_pk_mul_f32 v[48:49], v[48:49], v[56:57]
	v_pk_mul_f32 v[50:51], v[50:51], v[58:59]
	v_pk_mul_f32 v[52:53], v[52:53], v[60:61]
	v_pk_mul_f32 v[54:55], v[54:55], v[62:63]
	v_pk_mul_f32 v[48:49], v[48:49], 4.0 op_sel_hi:[1,0]
	v_pk_mul_f32 v[50:51], v[50:51], 4.0 op_sel_hi:[1,0]
	v_pk_mul_f32 v[52:53], v[52:53], 4.0 op_sel_hi:[1,0]
	v_pk_mul_f32 v[54:55], v[54:55], 4.0 op_sel_hi:[1,0]
	v_med3_f32 v48, v48, s33, v229
	v_med3_f32 v49, v49, s33, v229
	v_med3_f32 v50, v50, s33, v229
	v_med3_f32 v51, v51, s33, v229
	v_med3_f32 v52, v52, s33, v229
	v_med3_f32 v53, v53, s33, v229
	v_med3_f32 v54, v54, s33, v229
	v_med3_f32 v55, v55, s33, v229
	v_add_u32_e32 v66, 0x3c00, v182
	v_cvt_pk_fp8_f32 v62, v48, v49
	v_cvt_pk_fp8_f32 v63, v52, v53
	v_cvt_pk_fp8_f32 v62, v50, v51 op_sel:[0,0,1]
	v_cvt_pk_fp8_f32 v63, v54, v55 op_sel:[0,0,1]
	global_store_dwordx2 v66, v[62:63], s[4:5]
	v_add_u32_e32 v66, 0x27000, v181
	global_load_dwordx4 v[144:147], v66, s[2:3] offset:-2048 nt
	global_load_dwordx4 v[148:151], v66, s[2:3] nt
	global_load_dwordx4 v[152:155], v66, s[2:3] offset:2048 nt
	s_waitcnt vmcnt(27)
; __device__ __forceinline__ void conv_task(const Params& p, int l, int t0, int c) {
;     ...
;     for (int k = 0; k < 16; ++k) { const size_t t = (size_t)(t0 + k);
;         float bgv[8], cg[8], hh[8], o[8]; ld8(PROJ + t * INC + 2048 + c, bgv); ld8(PROJ + t * INC + 3072 + c, cg); ld8(PROJ + t * INC + 4096 + c, hh);
; #pragma unroll
;         for (int i = 0; i < 8; ++i) { const float z0 = cg[i] * hh[i]; o[i] = bgv[i] * (w0[i] * z2[i] + w1[i] * z1[i] + w2[i] * z0); z2[i] = z1[i]; z1[i] = z0; }
;         st8q(YABC + t * 3072 + 1024 + c, o); }
	v_lshlrev_b32_e32 v48, 16, v160
	v_and_b32_e32 v49, 0xffff0000, v160
	v_lshlrev_b32_e32 v50, 16, v161
	v_and_b32_e32 v51, 0xffff0000, v161
	v_lshlrev_b32_e32 v52, 16, v162
	v_and_b32_e32 v53, 0xffff0000, v162
	v_lshlrev_b32_e32 v54, 16, v163
	v_and_b32_e32 v55, 0xffff0000, v163
	v_lshlrev_b32_e32 v56, 16, v164
	v_and_b32_e32 v57, 0xffff0000, v164
	v_lshlrev_b32_e32 v58, 16, v165
	v_and_b32_e32 v59, 0xffff0000, v165
	v_lshlrev_b32_e32 v60, 16, v166
	v_and_b32_e32 v61, 0xffff0000, v166
	v_lshlrev_b32_e32 v62, 16, v167
	v_and_b32_e32 v63, 0xffff0000, v167
	v_pk_mul_f32 v[40:41], v[48:49], v[56:57]
	v_pk_mul_f32 v[42:43], v[50:51], v[58:59]
	v_pk_mul_f32 v[44:45], v[52:53], v[60:61]
	v_pk_mul_f32 v[46:47], v[54:55], v[62:63]
	v_pk_mul_f32 v[48:49], v[0:1], v[24:25]
	v_pk_mul_f32 v[56:57], v[8:9], v[32:33]
	v_pk_mul_f32 v[50:51], v[2:3], v[26:27]
	v_pk_mul_f32 v[58:59], v[10:11], v[34:35]
	v_pk_mul_f32 v[52:53], v[4:5], v[28:29]
	v_pk_mul_f32 v[60:61], v[12:13], v[36:37]
	v_pk_mul_f32 v[54:55], v[6:7], v[30:31]
	v_pk_mul_f32 v[62:63], v[14:15], v[38:39]
	v_pk_add_f32 v[48:49], v[48:49], v[56:57]
	v_pk_add_f32 v[50:51], v[50:51], v[58:59]
	v_pk_add_f32 v[52:53], v[52:53], v[60:61]
	v_pk_add_f32 v[54:55], v[54:55], v[62:63]
	v_pk_fma_f32 v[48:49], v[16:17], v[40:41], v[48:49]
	v_pk_fma_f32 v[50:51], v[18:19], v[42:43], v[50:51]
	v_pk_fma_f32 v[52:53], v[20:21], v[44:45], v[52:53]
	v_pk_fma_f32 v[54:55], v[22:23], v[46:47], v[54:55]
	v_lshlrev_b32_e32 v56, 16, v156
	v_and_b32_e32 v57, 0xffff0000, v156
	v_lshlrev_b32_e32 v58, 16, v157
	v_and_b32_e32 v59, 0xffff0000, v157
	v_lshlrev_b32_e32 v60, 16, v158
	v_and_b32_e32 v61, 0xffff0000, v158
	v_lshlrev_b32_e32 v62, 16, v159
	v_and_b32_e32 v63, 0xffff0000, v159
	v_pk_mul_f32 v[48:49], v[48:49], v[56:57]
	v_pk_mul_f32 v[50:51], v[50:51], v[58:59]
	v_pk_mul_f32 v[52:53], v[52:53], v[60:61]
	v_pk_mul_f32 v[54:55], v[54:55], v[62:63]
	v_pk_mul_f32 v[48:49], v[48:49], 4.0 op_sel_hi:[1,0]
	v_pk_mul_f32 v[50:51], v[50:51], 4.0 op_sel_hi:[1,0]
	v_pk_mul_f32 v[52:53], v[52:53], 4.0 op_sel_hi:[1,0]
	v_pk_mul_f32 v[54:55], v[54:55], 4.0 op_sel_hi:[1,0]
	v_med3_f32 v48, v48, s33, v229
	v_med3_f32 v49, v49, s33, v229
	v_med3_f32 v50, v50, s33, v229
	v_med3_f32 v51, v51, s33, v229
	v_med3_f32 v52, v52, s33, v229
	v_med3_f32 v53, v53, s33, v229
	v_med3_f32 v54, v54, s33, v229
	v_med3_f32 v55, v55, s33, v229
	v_add_u32_e32 v66, 0x4800, v182
	v_cvt_pk_fp8_f32 v62, v48, v49
	v_cvt_pk_fp8_f32 v63, v52, v53
	v_cvt_pk_fp8_f32 v62, v50, v51 op_sel:[0,0,1]
	v_cvt_pk_fp8_f32 v63, v54, v55 op_sel:[0,0,1]
	global_store_dwordx2 v66, v[62:63], s[4:5]
	v_add_u32_e32 v66, 0x2a000, v181
	global_load_dwordx4 v[156:159], v66, s[2:3] offset:-2048 nt
	global_load_dwordx4 v[160:163], v66, s[2:3] nt
	global_load_dwordx4 v[164:167], v66, s[2:3] offset:2048 nt
	s_waitcnt vmcnt(28)
	v_lshlrev_b32_e32 v48, 16, v172
	v_and_b32_e32 v49, 0xffff0000, v172
	v_lshlrev_b32_e32 v50, 16, v173
	v_and_b32_e32 v51, 0xffff0000, v173
	v_lshlrev_b32_e32 v52, 16, v174
	v_and_b32_e32 v53, 0xffff0000, v174
	v_lshlrev_b32_e32 v54, 16, v175
	v_and_b32_e32 v55, 0xffff0000, v175
	v_lshlrev_b32_e32 v56, 16, v176
	v_and_b32_e32 v57, 0xffff0000, v176
	v_lshlrev_b32_e32 v58, 16, v177
	v_and_b32_e32 v59, 0xffff0000, v177
	v_lshlrev_b32_e32 v60, 16, v178
	v_and_b32_e32 v61, 0xffff0000, v178
	v_lshlrev_b32_e32 v62, 16, v179
	v_and_b32_e32 v63, 0xffff0000, v179
	v_pk_mul_f32 v[24:25], v[48:49], v[56:57]
	v_pk_mul_f32 v[26:27], v[50:51], v[58:59]
	v_pk_mul_f32 v[28:29], v[52:53], v[60:61]
	v_pk_mul_f32 v[30:31], v[54:55], v[62:63]
	v_pk_mul_f32 v[48:49], v[0:1], v[32:33]
	v_pk_mul_f32 v[56:57], v[8:9], v[40:41]
	v_pk_mul_f32 v[50:51], v[2:3], v[34:35]
	v_pk_mul_f32 v[58:59], v[10:11], v[42:43]
	v_pk_mul_f32 v[52:53], v[4:5], v[36:37]
	v_pk_mul_f32 v[60:61], v[12:13], v[44:45]
	v_pk_mul_f32 v[54:55], v[6:7], v[38:39]
	v_pk_mul_f32 v[62:63], v[14:15], v[46:47]
	v_pk_add_f32 v[48:49], v[48:49], v[56:57]
	v_pk_add_f32 v[50:51], v[50:51], v[58:59]
	v_pk_add_f32 v[52:53], v[52:53], v[60:61]
	v_pk_add_f32 v[54:55], v[54:55], v[62:63]
	v_pk_fma_f32 v[48:49], v[16:17], v[24:25], v[48:49]
	v_pk_fma_f32 v[50:51], v[18:19], v[26:27], v[50:51]
	v_pk_fma_f32 v[52:53], v[20:21], v[28:29], v[52:53]
	v_pk_fma_f32 v[54:55], v[22:23], v[30:31], v[54:55]
	v_lshlrev_b32_e32 v56, 16, v168
	v_and_b32_e32 v57, 0xffff0000, v168
	v_lshlrev_b32_e32 v58, 16, v169
	v_and_b32_e32 v59, 0xffff0000, v169
	v_lshlrev_b32_e32 v60, 16, v170
	v_and_b32_e32 v61, 0xffff0000, v170
	v_lshlrev_b32_e32 v62, 16, v171
	v_and_b32_e32 v63, 0xffff0000, v171
	v_pk_mul_f32 v[48:49], v[48:49], v[56:57]
	v_pk_mul_f32 v[50:51], v[50:51], v[58:59]
	v_pk_mul_f32 v[52:53], v[52:53], v[60:61]
	v_pk_mul_f32 v[54:55], v[54:55], v[62:63]
	v_pk_mul_f32 v[48:49], v[48:49], 4.0 op_sel_hi:[1,0]
	v_pk_mul_f32 v[50:51], v[50:51], 4.0 op_sel_hi:[1,0]
	v_pk_mul_f32 v[52:53], v[52:53], 4.0 op_sel_hi:[1,0]
	v_pk_mul_f32 v[54:55], v[54:55], 4.0 op_sel_hi:[1,0]
	v_med3_f32 v48, v48, s33, v229
	v_med3_f32 v49, v49, s33, v229
	v_med3_f32 v50, v50, s33, v229
	v_med3_f32 v51, v51, s33, v229
	v_med3_f32 v52, v52, s33, v229
	v_med3_f32 v53, v53, s33, v229
	v_med3_f32 v54, v54, s33, v229
	v_med3_f32 v55, v55, s33, v229
	v_add_u32_e32 v66, 0x5400, v182
	v_cvt_pk_fp8_f32 v62, v48, v49
	v_cvt_pk_fp8_f32 v63, v52, v53
	v_cvt_pk_fp8_f32 v62, v50, v51 op_sel:[0,0,1]
	v_cvt_pk_fp8_f32 v63, v54, v55 op_sel:[0,0,1]
	global_store_dwordx2 v66, v[62:63], s[4:5]
	v_add_u32_e32 v66, 0x2d000, v181
	global_load_dwordx4 v[168:171], v66, s[2:3] offset:-2048 nt
	global_load_dwordx4 v[172:175], v66, s[2:3] nt
	global_load_dwordx4 v[176:179], v66, s[2:3] offset:2048 nt
	s_waitcnt vmcnt(28)
; __device__ __forceinline__ void conv_task(const Params& p, int l, int t0, int c) {
;     ...
;     for (int k = 0; k < 16; ++k) { const size_t t = (size_t)(t0 + k);
;         float bgv[8], cg[8], hh[8], o[8]; ld8(PROJ + t * INC + 2048 + c, bgv); ld8(PROJ + t * INC + 3072 + c, cg); ld8(PROJ + t * INC + 4096 + c, hh);
; #pragma unroll
;         for (int i = 0; i < 8; ++i) { const float z0 = cg[i] * hh[i]; o[i] = bgv[i] * (w0[i] * z2[i] + w1[i] * z1[i] + w2[i] * z0); z2[i] = z1[i]; z1[i] = z0; }
;         st8q(YABC + t * 3072 + 1024 + c, o); }
	v_lshlrev_b32_e32 v48, 16, v88
	v_and_b32_e32 v49, 0xffff0000, v88
	v_lshlrev_b32_e32 v50, 16, v89
	v_and_b32_e32 v51, 0xffff0000, v89
	v_lshlrev_b32_e32 v52, 16, v90
	v_and_b32_e32 v53, 0xffff0000, v90
	v_lshlrev_b32_e32 v54, 16, v91
	v_and_b32_e32 v55, 0xffff0000, v91
	v_lshlrev_b32_e32 v56, 16, v92
	v_and_b32_e32 v57, 0xffff0000, v92
	v_lshlrev_b32_e32 v58, 16, v93
	v_and_b32_e32 v59, 0xffff0000, v93
	v_lshlrev_b32_e32 v60, 16, v94
	v_and_b32_e32 v61, 0xffff0000, v94
	v_lshlrev_b32_e32 v62, 16, v95
	v_and_b32_e32 v63, 0xffff0000, v95
	v_pk_mul_f32 v[32:33], v[48:49], v[56:57]
	v_pk_mul_f32 v[34:35], v[50:51], v[58:59]
	v_pk_mul_f32 v[36:37], v[52:53], v[60:61]
	v_pk_mul_f32 v[38:39], v[54:55], v[62:63]
	v_pk_mul_f32 v[48:49], v[0:1], v[40:41]
	v_pk_mul_f32 v[56:57], v[8:9], v[24:25]
	v_pk_mul_f32 v[50:51], v[2:3], v[42:43]
	v_pk_mul_f32 v[58:59], v[10:11], v[26:27]
	v_pk_mul_f32 v[52:53], v[4:5], v[44:45]
	v_pk_mul_f32 v[60:61], v[12:13], v[28:29]
	v_pk_mul_f32 v[54:55], v[6:7], v[46:47]
	v_pk_mul_f32 v[62:63], v[14:15], v[30:31]
	v_pk_add_f32 v[48:49], v[48:49], v[56:57]
	v_pk_add_f32 v[50:51], v[50:51], v[58:59]
	v_pk_add_f32 v[52:53], v[52:53], v[60:61]
	v_pk_add_f32 v[54:55], v[54:55], v[62:63]
	v_pk_fma_f32 v[48:49], v[16:17], v[32:33], v[48:49]
	v_pk_fma_f32 v[50:51], v[18:19], v[34:35], v[50:51]
	v_pk_fma_f32 v[52:53], v[20:21], v[36:37], v[52:53]
	v_pk_fma_f32 v[54:55], v[22:23], v[38:39], v[54:55]
	v_lshlrev_b32_e32 v56, 16, v84
	v_and_b32_e32 v57, 0xffff0000, v84
	v_lshlrev_b32_e32 v58, 16, v85
	v_and_b32_e32 v59, 0xffff0000, v85
	v_lshlrev_b32_e32 v60, 16, v86
	v_and_b32_e32 v61, 0xffff0000, v86
	v_lshlrev_b32_e32 v62, 16, v87
	v_and_b32_e32 v63, 0xffff0000, v87
	v_pk_mul_f32 v[48:49], v[48:49], v[56:57]
	v_pk_mul_f32 v[50:51], v[50:51], v[58:59]
	v_pk_mul_f32 v[52:53], v[52:53], v[60:61]
	v_pk_mul_f32 v[54:55], v[54:55], v[62:63]
	v_pk_mul_f32 v[48:49], v[48:49], 4.0 op_sel_hi:[1,0]
	v_pk_mul_f32 v[50:51], v[50:51], 4.0 op_sel_hi:[1,0]
	v_pk_mul_f32 v[52:53], v[52:53], 4.0 op_sel_hi:[1,0]
	v_pk_mul_f32 v[54:55], v[54:55], 4.0 op_sel_hi:[1,0]
	v_med3_f32 v48, v48, s33, v229
	v_med3_f32 v49, v49, s33, v229
	v_med3_f32 v50, v50, s33, v229
	v_med3_f32 v51, v51, s33, v229
	v_med3_f32 v52, v52, s33, v229
	v_med3_f32 v53, v53, s33, v229
	v_med3_f32 v54, v54, s33, v229
	v_med3_f32 v55, v55, s33, v229
	v_add_u32_e32 v66, 0x6000, v182
	v_cvt_pk_fp8_f32 v62, v48, v49
	v_cvt_pk_fp8_f32 v63, v52, v53
	v_cvt_pk_fp8_f32 v62, v50, v51 op_sel:[0,0,1]
	v_cvt_pk_fp8_f32 v63, v54, v55 op_sel:[0,0,1]
	global_store_dwordx2 v66, v[62:63], s[4:5]
	s_waitcnt vmcnt(25)
	v_lshlrev_b32_e32 v48, 16, v100
	v_and_b32_e32 v49, 0xffff0000, v100
	v_lshlrev_b32_e32 v50, 16, v101
	v_and_b32_e32 v51, 0xffff0000, v101
	v_lshlrev_b32_e32 v52, 16, v102
	v_and_b32_e32 v53, 0xffff0000, v102
	v_lshlrev_b32_e32 v54, 16, v103
	v_and_b32_e32 v55, 0xffff0000, v103
	v_lshlrev_b32_e32 v56, 16, v104
	v_and_b32_e32 v57, 0xffff0000, v104
	v_lshlrev_b32_e32 v58, 16, v105
	v_and_b32_e32 v59, 0xffff0000, v105
	v_lshlrev_b32_e32 v60, 16, v106
	v_and_b32_e32 v61, 0xffff0000, v106
	v_lshlrev_b32_e32 v62, 16, v107
	v_and_b32_e32 v63, 0xffff0000, v107
	v_pk_mul_f32 v[40:41], v[48:49], v[56:57]
	v_pk_mul_f32 v[42:43], v[50:51], v[58:59]
	v_pk_mul_f32 v[44:45], v[52:53], v[60:61]
	v_pk_mul_f32 v[46:47], v[54:55], v[62:63]
	v_pk_mul_f32 v[48:49], v[0:1], v[24:25]
	v_pk_mul_f32 v[56:57], v[8:9], v[32:33]
	v_pk_mul_f32 v[50:51], v[2:3], v[26:27]
	v_pk_mul_f32 v[58:59], v[10:11], v[34:35]
	v_pk_mul_f32 v[52:53], v[4:5], v[28:29]
	v_pk_mul_f32 v[60:61], v[12:13], v[36:37]
	v_pk_mul_f32 v[54:55], v[6:7], v[30:31]
	v_pk_mul_f32 v[62:63], v[14:15], v[38:39]
	v_pk_add_f32 v[48:49], v[48:49], v[56:57]
	v_pk_add_f32 v[50:51], v[50:51], v[58:59]
	v_pk_add_f32 v[52:53], v[52:53], v[60:61]
	v_pk_add_f32 v[54:55], v[54:55], v[62:63]
	v_pk_fma_f32 v[48:49], v[16:17], v[40:41], v[48:49]
	v_pk_fma_f32 v[50:51], v[18:19], v[42:43], v[50:51]
	v_pk_fma_f32 v[52:53], v[20:21], v[44:45], v[52:53]
	v_pk_fma_f32 v[54:55], v[22:23], v[46:47], v[54:55]
	v_lshlrev_b32_e32 v56, 16, v96
	v_and_b32_e32 v57, 0xffff0000, v96
	v_lshlrev_b32_e32 v58, 16, v97
	v_and_b32_e32 v59, 0xffff0000, v97
	v_lshlrev_b32_e32 v60, 16, v98
	v_and_b32_e32 v61, 0xffff0000, v98
	v_lshlrev_b32_e32 v62, 16, v99
	v_and_b32_e32 v63, 0xffff0000, v99
	v_pk_mul_f32 v[48:49], v[48:49], v[56:57]
	v_pk_mul_f32 v[50:51], v[50:51], v[58:59]
	v_pk_mul_f32 v[52:53], v[52:53], v[60:61]
	v_pk_mul_f32 v[54:55], v[54:55], v[62:63]
	v_pk_mul_f32 v[48:49], v[48:49], 4.0 op_sel_hi:[1,0]
	v_pk_mul_f32 v[50:51], v[50:51], 4.0 op_sel_hi:[1,0]
	v_pk_mul_f32 v[52:53], v[52:53], 4.0 op_sel_hi:[1,0]
	v_pk_mul_f32 v[54:55], v[54:55], 4.0 op_sel_hi:[1,0]
	v_med3_f32 v48, v48, s33, v229
	v_med3_f32 v49, v49, s33, v229
	v_med3_f32 v50, v50, s33, v229
	v_med3_f32 v51, v51, s33, v229
	v_med3_f32 v52, v52, s33, v229
	v_med3_f32 v53, v53, s33, v229
	v_med3_f32 v54, v54, s33, v229
	v_med3_f32 v55, v55, s33, v229
	v_add_u32_e32 v66, 0x6c00, v182
	v_cvt_pk_fp8_f32 v62, v48, v49
	v_cvt_pk_fp8_f32 v63, v52, v53
	v_cvt_pk_fp8_f32 v62, v50, v51 op_sel:[0,0,1]
	v_cvt_pk_fp8_f32 v63, v54, v55 op_sel:[0,0,1]
	global_store_dwordx2 v66, v[62:63], s[4:5]
	s_waitcnt vmcnt(22)
; __device__ __forceinline__ void conv_task(const Params& p, int l, int t0, int c) {
;     ...
;     for (int k = 0; k < 16; ++k) { const size_t t = (size_t)(t0 + k);
;         float bgv[8], cg[8], hh[8], o[8]; ld8(PROJ + t * INC + 2048 + c, bgv); ld8(PROJ + t * INC + 3072 + c, cg); ld8(PROJ + t * INC + 4096 + c, hh);
; #pragma unroll
;         for (int i = 0; i < 8; ++i) { const float z0 = cg[i] * hh[i]; o[i] = bgv[i] * (w0[i] * z2[i] + w1[i] * z1[i] + w2[i] * z0); z2[i] = z1[i]; z1[i] = z0; }
;         st8q(YABC + t * 3072 + 1024 + c, o); }
	v_lshlrev_b32_e32 v48, 16, v112
	v_and_b32_e32 v49, 0xffff0000, v112
	v_lshlrev_b32_e32 v50, 16, v113
	v_and_b32_e32 v51, 0xffff0000, v113
	v_lshlrev_b32_e32 v52, 16, v114
	v_and_b32_e32 v53, 0xffff0000, v114
	v_lshlrev_b32_e32 v54, 16, v115
	v_and_b32_e32 v55, 0xffff0000, v115
	v_lshlrev_b32_e32 v56, 16, v116
	v_and_b32_e32 v57, 0xffff0000, v116
	v_lshlrev_b32_e32 v58, 16, v117
	v_and_b32_e32 v59, 0xffff0000, v117
	v_lshlrev_b32_e32 v60, 16, v118
	v_and_b32_e32 v61, 0xffff0000, v118
	v_lshlrev_b32_e32 v62, 16, v119
	v_and_b32_e32 v63, 0xffff0000, v119
	v_pk_mul_f32 v[24:25], v[48:49], v[56:57]
	v_pk_mul_f32 v[26:27], v[50:51], v[58:59]
	v_pk_mul_f32 v[28:29], v[52:53], v[60:61]
	v_pk_mul_f32 v[30:31], v[54:55], v[62:63]
	v_pk_mul_f32 v[48:49], v[0:1], v[32:33]
	v_pk_mul_f32 v[56:57], v[8:9], v[40:41]
	v_pk_mul_f32 v[50:51], v[2:3], v[34:35]
	v_pk_mul_f32 v[58:59], v[10:11], v[42:43]
	v_pk_mul_f32 v[52:53], v[4:5], v[36:37]
	v_pk_mul_f32 v[60:61], v[12:13], v[44:45]
	v_pk_mul_f32 v[54:55], v[6:7], v[38:39]
	v_pk_mul_f32 v[62:63], v[14:15], v[46:47]
	v_pk_add_f32 v[48:49], v[48:49], v[56:57]
	v_pk_add_f32 v[50:51], v[50:51], v[58:59]
	v_pk_add_f32 v[52:53], v[52:53], v[60:61]
	v_pk_add_f32 v[54:55], v[54:55], v[62:63]
	v_pk_fma_f32 v[48:49], v[16:17], v[24:25], v[48:49]
	v_pk_fma_f32 v[50:51], v[18:19], v[26:27], v[50:51]
	v_pk_fma_f32 v[52:53], v[20:21], v[28:29], v[52:53]
	v_pk_fma_f32 v[54:55], v[22:23], v[30:31], v[54:55]
	v_lshlrev_b32_e32 v56, 16, v108
	v_and_b32_e32 v57, 0xffff0000, v108
	v_lshlrev_b32_e32 v58, 16, v109
	v_and_b32_e32 v59, 0xffff0000, v109
	v_lshlrev_b32_e32 v60, 16, v110
	v_and_b32_e32 v61, 0xffff0000, v110
	v_lshlrev_b32_e32 v62, 16, v111
	v_and_b32_e32 v63, 0xffff0000, v111
	v_pk_mul_f32 v[48:49], v[48:49], v[56:57]
	v_pk_mul_f32 v[50:51], v[50:51], v[58:59]
	v_pk_mul_f32 v[52:53], v[52:53], v[60:61]
	v_pk_mul_f32 v[54:55], v[54:55], v[62:63]
	v_pk_mul_f32 v[48:49], v[48:49], 4.0 op_sel_hi:[1,0]
	v_pk_mul_f32 v[50:51], v[50:51], 4.0 op_sel_hi:[1,0]
	v_pk_mul_f32 v[52:53], v[52:53], 4.0 op_sel_hi:[1,0]
	v_pk_mul_f32 v[54:55], v[54:55], 4.0 op_sel_hi:[1,0]
	v_med3_f32 v48, v48, s33, v229
	v_med3_f32 v49, v49, s33, v229
	v_med3_f32 v50, v50, s33, v229
	v_med3_f32 v51, v51, s33, v229
	v_med3_f32 v52, v52, s33, v229
	v_med3_f32 v53, v53, s33, v229
	v_med3_f32 v54, v54, s33, v229
	v_med3_f32 v55, v55, s33, v229
	v_add_u32_e32 v66, 0x7800, v182
	v_cvt_pk_fp8_f32 v62, v48, v49
	v_cvt_pk_fp8_f32 v63, v52, v53
	v_cvt_pk_fp8_f32 v62, v50, v51 op_sel:[0,0,1]
	v_cvt_pk_fp8_f32 v63, v54, v55 op_sel:[0,0,1]
	global_store_dwordx2 v66, v[62:63], s[4:5]
	s_waitcnt vmcnt(19)
	v_lshlrev_b32_e32 v48, 16, v124
	v_and_b32_e32 v49, 0xffff0000, v124
	v_lshlrev_b32_e32 v50, 16, v125
	v_and_b32_e32 v51, 0xffff0000, v125
	v_lshlrev_b32_e32 v52, 16, v126
	v_and_b32_e32 v53, 0xffff0000, v126
	v_lshlrev_b32_e32 v54, 16, v127
	v_and_b32_e32 v55, 0xffff0000, v127
	v_lshlrev_b32_e32 v56, 16, v128
	v_and_b32_e32 v57, 0xffff0000, v128
	v_lshlrev_b32_e32 v58, 16, v129
	v_and_b32_e32 v59, 0xffff0000, v129
	v_lshlrev_b32_e32 v60, 16, v130
	v_and_b32_e32 v61, 0xffff0000, v130
	v_lshlrev_b32_e32 v62, 16, v131
	v_and_b32_e32 v63, 0xffff0000, v131
	v_pk_mul_f32 v[32:33], v[48:49], v[56:57]
	v_pk_mul_f32 v[34:35], v[50:51], v[58:59]
	v_pk_mul_f32 v[36:37], v[52:53], v[60:61]
	v_pk_mul_f32 v[38:39], v[54:55], v[62:63]
	v_pk_mul_f32 v[48:49], v[0:1], v[40:41]
	v_pk_mul_f32 v[56:57], v[8:9], v[24:25]
	v_pk_mul_f32 v[50:51], v[2:3], v[42:43]
	v_pk_mul_f32 v[58:59], v[10:11], v[26:27]
	v_pk_mul_f32 v[52:53], v[4:5], v[44:45]
	v_pk_mul_f32 v[60:61], v[12:13], v[28:29]
	v_pk_mul_f32 v[54:55], v[6:7], v[46:47]
	v_pk_mul_f32 v[62:63], v[14:15], v[30:31]
	v_pk_add_f32 v[48:49], v[48:49], v[56:57]
	v_pk_add_f32 v[50:51], v[50:51], v[58:59]
	v_pk_add_f32 v[52:53], v[52:53], v[60:61]
	v_pk_add_f32 v[54:55], v[54:55], v[62:63]
	v_pk_fma_f32 v[48:49], v[16:17], v[32:33], v[48:49]
	v_pk_fma_f32 v[50:51], v[18:19], v[34:35], v[50:51]
	v_pk_fma_f32 v[52:53], v[20:21], v[36:37], v[52:53]
	v_pk_fma_f32 v[54:55], v[22:23], v[38:39], v[54:55]
	v_lshlrev_b32_e32 v56, 16, v120
	v_and_b32_e32 v57, 0xffff0000, v120
	v_lshlrev_b32_e32 v58, 16, v121
	v_and_b32_e32 v59, 0xffff0000, v121
	v_lshlrev_b32_e32 v60, 16, v122
	v_and_b32_e32 v61, 0xffff0000, v122
	v_lshlrev_b32_e32 v62, 16, v123
	v_and_b32_e32 v63, 0xffff0000, v123
	v_pk_mul_f32 v[48:49], v[48:49], v[56:57]
	v_pk_mul_f32 v[50:51], v[50:51], v[58:59]
	v_pk_mul_f32 v[52:53], v[52:53], v[60:61]
	v_pk_mul_f32 v[54:55], v[54:55], v[62:63]
	v_pk_mul_f32 v[48:49], v[48:49], 4.0 op_sel_hi:[1,0]
	v_pk_mul_f32 v[50:51], v[50:51], 4.0 op_sel_hi:[1,0]
	v_pk_mul_f32 v[52:53], v[52:53], 4.0 op_sel_hi:[1,0]
	v_pk_mul_f32 v[54:55], v[54:55], 4.0 op_sel_hi:[1,0]
	v_med3_f32 v48, v48, s33, v229
	v_med3_f32 v49, v49, s33, v229
	v_med3_f32 v50, v50, s33, v229
	v_med3_f32 v51, v51, s33, v229
	v_med3_f32 v52, v52, s33, v229
	v_med3_f32 v53, v53, s33, v229
	v_med3_f32 v54, v54, s33, v229
	v_med3_f32 v55, v55, s33, v229
	v_add_u32_e32 v66, 0x8400, v182
	v_cvt_pk_fp8_f32 v62, v48, v49
	v_cvt_pk_fp8_f32 v63, v52, v53
	v_cvt_pk_fp8_f32 v62, v50, v51 op_sel:[0,0,1]
	v_cvt_pk_fp8_f32 v63, v54, v55 op_sel:[0,0,1]
	global_store_dwordx2 v66, v[62:63], s[4:5]
	s_waitcnt vmcnt(16)
; __device__ __forceinline__ void conv_task(const Params& p, int l, int t0, int c) {
;     ...
;     for (int k = 0; k < 16; ++k) { const size_t t = (size_t)(t0 + k);
;         float bgv[8], cg[8], hh[8], o[8]; ld8(PROJ + t * INC + 2048 + c, bgv); ld8(PROJ + t * INC + 3072 + c, cg); ld8(PROJ + t * INC + 4096 + c, hh);
; #pragma unroll
;         for (int i = 0; i < 8; ++i) { const float z0 = cg[i] * hh[i]; o[i] = bgv[i] * (w0[i] * z2[i] + w1[i] * z1[i] + w2[i] * z0); z2[i] = z1[i]; z1[i] = z0; }
;         st8q(YABC + t * 3072 + 1024 + c, o); }
	v_lshlrev_b32_e32 v48, 16, v136
	v_and_b32_e32 v49, 0xffff0000, v136
	v_lshlrev_b32_e32 v50, 16, v137
	v_and_b32_e32 v51, 0xffff0000, v137
	v_lshlrev_b32_e32 v52, 16, v138
	v_and_b32_e32 v53, 0xffff0000, v138
	v_lshlrev_b32_e32 v54, 16, v139
	v_and_b32_e32 v55, 0xffff0000, v139
	v_lshlrev_b32_e32 v56, 16, v140
	v_and_b32_e32 v57, 0xffff0000, v140
	v_lshlrev_b32_e32 v58, 16, v141
	v_and_b32_e32 v59, 0xffff0000, v141
	v_lshlrev_b32_e32 v60, 16, v142
	v_and_b32_e32 v61, 0xffff0000, v142
	v_lshlrev_b32_e32 v62, 16, v143
	v_and_b32_e32 v63, 0xffff0000, v143
	v_pk_mul_f32 v[40:41], v[48:49], v[56:57]
	v_pk_mul_f32 v[42:43], v[50:51], v[58:59]
	v_pk_mul_f32 v[44:45], v[52:53], v[60:61]
	v_pk_mul_f32 v[46:47], v[54:55], v[62:63]
	v_pk_mul_f32 v[48:49], v[0:1], v[24:25]
	v_pk_mul_f32 v[56:57], v[8:9], v[32:33]
	v_pk_mul_f32 v[50:51], v[2:3], v[26:27]
	v_pk_mul_f32 v[58:59], v[10:11], v[34:35]
	v_pk_mul_f32 v[52:53], v[4:5], v[28:29]
	v_pk_mul_f32 v[60:61], v[12:13], v[36:37]
	v_pk_mul_f32 v[54:55], v[6:7], v[30:31]
	v_pk_mul_f32 v[62:63], v[14:15], v[38:39]
	v_pk_add_f32 v[48:49], v[48:49], v[56:57]
	v_pk_add_f32 v[50:51], v[50:51], v[58:59]
	v_pk_add_f32 v[52:53], v[52:53], v[60:61]
	v_pk_add_f32 v[54:55], v[54:55], v[62:63]
	v_pk_fma_f32 v[48:49], v[16:17], v[40:41], v[48:49]
	v_pk_fma_f32 v[50:51], v[18:19], v[42:43], v[50:51]
	v_pk_fma_f32 v[52:53], v[20:21], v[44:45], v[52:53]
	v_pk_fma_f32 v[54:55], v[22:23], v[46:47], v[54:55]
	v_lshlrev_b32_e32 v56, 16, v132
	v_and_b32_e32 v57, 0xffff0000, v132
	v_lshlrev_b32_e32 v58, 16, v133
	v_and_b32_e32 v59, 0xffff0000, v133
	v_lshlrev_b32_e32 v60, 16, v134
	v_and_b32_e32 v61, 0xffff0000, v134
	v_lshlrev_b32_e32 v62, 16, v135
	v_and_b32_e32 v63, 0xffff0000, v135
	v_pk_mul_f32 v[48:49], v[48:49], v[56:57]
	v_pk_mul_f32 v[50:51], v[50:51], v[58:59]
	v_pk_mul_f32 v[52:53], v[52:53], v[60:61]
	v_pk_mul_f32 v[54:55], v[54:55], v[62:63]
	v_pk_mul_f32 v[48:49], v[48:49], 4.0 op_sel_hi:[1,0]
	v_pk_mul_f32 v[50:51], v[50:51], 4.0 op_sel_hi:[1,0]
	v_pk_mul_f32 v[52:53], v[52:53], 4.0 op_sel_hi:[1,0]
	v_pk_mul_f32 v[54:55], v[54:55], 4.0 op_sel_hi:[1,0]
	v_med3_f32 v48, v48, s33, v229
	v_med3_f32 v49, v49, s33, v229
	v_med3_f32 v50, v50, s33, v229
	v_med3_f32 v51, v51, s33, v229
	v_med3_f32 v52, v52, s33, v229
	v_med3_f32 v53, v53, s33, v229
	v_med3_f32 v54, v54, s33, v229
	v_med3_f32 v55, v55, s33, v229
	v_add_u32_e32 v66, 0x9000, v182
	v_cvt_pk_fp8_f32 v62, v48, v49
	v_cvt_pk_fp8_f32 v63, v52, v53
	v_cvt_pk_fp8_f32 v62, v50, v51 op_sel:[0,0,1]
	v_cvt_pk_fp8_f32 v63, v54, v55 op_sel:[0,0,1]
	global_store_dwordx2 v66, v[62:63], s[4:5]
	s_waitcnt vmcnt(13)
	v_lshlrev_b32_e32 v48, 16, v148
	v_and_b32_e32 v49, 0xffff0000, v148
	v_lshlrev_b32_e32 v50, 16, v149
	v_and_b32_e32 v51, 0xffff0000, v149
	v_lshlrev_b32_e32 v52, 16, v150
	v_and_b32_e32 v53, 0xffff0000, v150
	v_lshlrev_b32_e32 v54, 16, v151
	v_and_b32_e32 v55, 0xffff0000, v151
	v_lshlrev_b32_e32 v56, 16, v152
	v_and_b32_e32 v57, 0xffff0000, v152
	v_lshlrev_b32_e32 v58, 16, v153
	v_and_b32_e32 v59, 0xffff0000, v153
	v_lshlrev_b32_e32 v60, 16, v154
	v_and_b32_e32 v61, 0xffff0000, v154
	v_lshlrev_b32_e32 v62, 16, v155
	v_and_b32_e32 v63, 0xffff0000, v155
	v_pk_mul_f32 v[24:25], v[48:49], v[56:57]
	v_pk_mul_f32 v[26:27], v[50:51], v[58:59]
	v_pk_mul_f32 v[28:29], v[52:53], v[60:61]
	v_pk_mul_f32 v[30:31], v[54:55], v[62:63]
	v_pk_mul_f32 v[48:49], v[0:1], v[32:33]
	v_pk_mul_f32 v[56:57], v[8:9], v[40:41]
	v_pk_mul_f32 v[50:51], v[2:3], v[34:35]
	v_pk_mul_f32 v[58:59], v[10:11], v[42:43]
	v_pk_mul_f32 v[52:53], v[4:5], v[36:37]
	v_pk_mul_f32 v[60:61], v[12:13], v[44:45]
	v_pk_mul_f32 v[54:55], v[6:7], v[38:39]
	v_pk_mul_f32 v[62:63], v[14:15], v[46:47]
	v_pk_add_f32 v[48:49], v[48:49], v[56:57]
	v_pk_add_f32 v[50:51], v[50:51], v[58:59]
	v_pk_add_f32 v[52:53], v[52:53], v[60:61]
	v_pk_add_f32 v[54:55], v[54:55], v[62:63]
	v_pk_fma_f32 v[48:49], v[16:17], v[24:25], v[48:49]
	v_pk_fma_f32 v[50:51], v[18:19], v[26:27], v[50:51]
	v_pk_fma_f32 v[52:53], v[20:21], v[28:29], v[52:53]
	v_pk_fma_f32 v[54:55], v[22:23], v[30:31], v[54:55]
	v_lshlrev_b32_e32 v56, 16, v144
	v_and_b32_e32 v57, 0xffff0000, v144
	v_lshlrev_b32_e32 v58, 16, v145
	v_and_b32_e32 v59, 0xffff0000, v145
	v_lshlrev_b32_e32 v60, 16, v146
	v_and_b32_e32 v61, 0xffff0000, v146
	v_lshlrev_b32_e32 v62, 16, v147
	v_and_b32_e32 v63, 0xffff0000, v147
	v_pk_mul_f32 v[48:49], v[48:49], v[56:57]
	v_pk_mul_f32 v[50:51], v[50:51], v[58:59]
	v_pk_mul_f32 v[52:53], v[52:53], v[60:61]
	v_pk_mul_f32 v[54:55], v[54:55], v[62:63]
	v_pk_mul_f32 v[48:49], v[48:49], 4.0 op_sel_hi:[1,0]
	v_pk_mul_f32 v[50:51], v[50:51], 4.0 op_sel_hi:[1,0]
	v_pk_mul_f32 v[52:53], v[52:53], 4.0 op_sel_hi:[1,0]
	v_pk_mul_f32 v[54:55], v[54:55], 4.0 op_sel_hi:[1,0]
	v_med3_f32 v48, v48, s33, v229
	v_med3_f32 v49, v49, s33, v229
	v_med3_f32 v50, v50, s33, v229
	v_med3_f32 v51, v51, s33, v229
	v_med3_f32 v52, v52, s33, v229
	v_med3_f32 v53, v53, s33, v229
	v_med3_f32 v54, v54, s33, v229
	v_med3_f32 v55, v55, s33, v229
	v_add_u32_e32 v66, 0x9c00, v182
	v_cvt_pk_fp8_f32 v62, v48, v49
	v_cvt_pk_fp8_f32 v63, v52, v53
	v_cvt_pk_fp8_f32 v62, v50, v51 op_sel:[0,0,1]
	v_cvt_pk_fp8_f32 v63, v54, v55 op_sel:[0,0,1]
	global_store_dwordx2 v66, v[62:63], s[4:5]
	s_waitcnt vmcnt(10)
; __device__ __forceinline__ unsigned pk4_fp8(float a, float b, float c, float d) { unsigned w = 0u; w = __builtin_amdgcn_cvt_pk_fp8_f32(clamp8(a), clamp8(b), w, false); w = __builtin_amdgcn_cvt_pk_fp8_f32(clamp8(c), clamp8(d), w, true); return w; }
; __device__ __forceinline__ void st8q(unsigned char* ptr, const float (&f)[8]) {
;     u32x2 w; w.x = pk4_fp8(4.f * f[0], 4.f * f[1], 4.f * f[2], 4.f * f[3]); w.y = pk4_fp8(4.f * f[4], 4.f * f[5], 4.f * f[6], 4.f * f[7]); *(u32x2*)ptr = w;
; }
; __device__ __forceinline__ void conv_task(const Params& p, int l, int t0, int c) {
;     ...
;     for (int k = 0; k < 16; ++k) { const size_t t = (size_t)(t0 + k);
;         float bgv[8], cg[8], hh[8], o[8]; ld8(PROJ + t * INC + 2048 + c, bgv); ld8(PROJ + t * INC + 3072 + c, cg); ld8(PROJ + t * INC + 4096 + c, hh);
; #pragma unroll
;         for (int i = 0; i < 8; ++i) { const float z0 = cg[i] * hh[i]; o[i] = bgv[i] * (w0[i] * z2[i] + w1[i] * z1[i] + w2[i] * z0); z2[i] = z1[i]; z1[i] = z0; }
;         st8q(YABC + t * 3072 + 1024 + c, o); }
	v_lshlrev_b32_e32 v48, 16, v160
	v_and_b32_e32 v49, 0xffff0000, v160
	v_lshlrev_b32_e32 v50, 16, v161
	v_and_b32_e32 v51, 0xffff0000, v161
	v_lshlrev_b32_e32 v52, 16, v162
	v_and_b32_e32 v53, 0xffff0000, v162
	v_lshlrev_b32_e32 v54, 16, v163
	v_and_b32_e32 v55, 0xffff0000, v163
	v_lshlrev_b32_e32 v56, 16, v164
	v_and_b32_e32 v57, 0xffff0000, v164
	v_lshlrev_b32_e32 v58, 16, v165
	v_and_b32_e32 v59, 0xffff0000, v165
	v_lshlrev_b32_e32 v60, 16, v166
	v_and_b32_e32 v61, 0xffff0000, v166
	v_lshlrev_b32_e32 v62, 16, v167
	v_and_b32_e32 v63, 0xffff0000, v167
	v_pk_mul_f32 v[32:33], v[48:49], v[56:57]
	v_pk_mul_f32 v[34:35], v[50:51], v[58:59]
	v_pk_mul_f32 v[36:37], v[52:53], v[60:61]
	v_pk_mul_f32 v[38:39], v[54:55], v[62:63]
	v_pk_mul_f32 v[48:49], v[0:1], v[40:41]
	v_pk_mul_f32 v[56:57], v[8:9], v[24:25]
	v_pk_mul_f32 v[50:51], v[2:3], v[42:43]
	v_pk_mul_f32 v[58:59], v[10:11], v[26:27]
	v_pk_mul_f32 v[52:53], v[4:5], v[44:45]
	v_pk_mul_f32 v[60:61], v[12:13], v[28:29]
	v_pk_mul_f32 v[54:55], v[6:7], v[46:47]
	v_pk_mul_f32 v[62:63], v[14:15], v[30:31]
	v_pk_add_f32 v[48:49], v[48:49], v[56:57]
	v_pk_add_f32 v[50:51], v[50:51], v[58:59]
	v_pk_add_f32 v[52:53], v[52:53], v[60:61]
	v_pk_add_f32 v[54:55], v[54:55], v[62:63]
	v_pk_fma_f32 v[48:49], v[16:17], v[32:33], v[48:49]
	v_pk_fma_f32 v[50:51], v[18:19], v[34:35], v[50:51]
	v_pk_fma_f32 v[52:53], v[20:21], v[36:37], v[52:53]
	v_pk_fma_f32 v[54:55], v[22:23], v[38:39], v[54:55]
	v_lshlrev_b32_e32 v56, 16, v156
	v_and_b32_e32 v57, 0xffff0000, v156
	v_lshlrev_b32_e32 v58, 16, v157
	v_and_b32_e32 v59, 0xffff0000, v157
	v_lshlrev_b32_e32 v60, 16, v158
	v_and_b32_e32 v61, 0xffff0000, v158
	v_lshlrev_b32_e32 v62, 16, v159
	v_and_b32_e32 v63, 0xffff0000, v159
	v_pk_mul_f32 v[48:49], v[48:49], v[56:57]
	v_pk_mul_f32 v[50:51], v[50:51], v[58:59]
	v_pk_mul_f32 v[52:53], v[52:53], v[60:61]
	v_pk_mul_f32 v[54:55], v[54:55], v[62:63]
	v_pk_mul_f32 v[48:49], v[48:49], 4.0 op_sel_hi:[1,0]
	v_pk_mul_f32 v[50:51], v[50:51], 4.0 op_sel_hi:[1,0]
	v_pk_mul_f32 v[52:53], v[52:53], 4.0 op_sel_hi:[1,0]
	v_pk_mul_f32 v[54:55], v[54:55], 4.0 op_sel_hi:[1,0]
	v_med3_f32 v48, v48, s33, v229
	v_med3_f32 v49, v49, s33, v229
	v_med3_f32 v50, v50, s33, v229
	v_med3_f32 v51, v51, s33, v229
	v_med3_f32 v52, v52, s33, v229
	v_med3_f32 v53, v53, s33, v229
	v_med3_f32 v54, v54, s33, v229
	v_med3_f32 v55, v55, s33, v229
	v_add_u32_e32 v66, 0xa800, v182
	v_cvt_pk_fp8_f32 v62, v48, v49
	v_cvt_pk_fp8_f32 v63, v52, v53
	v_cvt_pk_fp8_f32 v62, v50, v51 op_sel:[0,0,1]
	v_cvt_pk_fp8_f32 v63, v54, v55 op_sel:[0,0,1]
	global_store_dwordx2 v66, v[62:63], s[4:5]
	s_waitcnt vmcnt(7)
	v_lshlrev_b32_e32 v48, 16, v172
	v_and_b32_e32 v49, 0xffff0000, v172
	v_lshlrev_b32_e32 v50, 16, v173
	v_and_b32_e32 v51, 0xffff0000, v173
	v_lshlrev_b32_e32 v52, 16, v174
	v_and_b32_e32 v53, 0xffff0000, v174
	v_lshlrev_b32_e32 v54, 16, v175
	v_and_b32_e32 v55, 0xffff0000, v175
	v_lshlrev_b32_e32 v56, 16, v176
	v_and_b32_e32 v57, 0xffff0000, v176
	v_lshlrev_b32_e32 v58, 16, v177
	v_and_b32_e32 v59, 0xffff0000, v177
	v_lshlrev_b32_e32 v60, 16, v178
	v_and_b32_e32 v61, 0xffff0000, v178
	v_lshlrev_b32_e32 v62, 16, v179
	v_and_b32_e32 v63, 0xffff0000, v179
	v_pk_mul_f32 v[40:41], v[48:49], v[56:57]
	v_pk_mul_f32 v[42:43], v[50:51], v[58:59]
	v_pk_mul_f32 v[44:45], v[52:53], v[60:61]
	v_pk_mul_f32 v[46:47], v[54:55], v[62:63]
	v_pk_mul_f32 v[48:49], v[0:1], v[24:25]
	v_pk_mul_f32 v[56:57], v[8:9], v[32:33]
	v_pk_mul_f32 v[50:51], v[2:3], v[26:27]
	v_pk_mul_f32 v[58:59], v[10:11], v[34:35]
	v_pk_mul_f32 v[52:53], v[4:5], v[28:29]
	v_pk_mul_f32 v[60:61], v[12:13], v[36:37]
	v_pk_mul_f32 v[54:55], v[6:7], v[30:31]
	v_pk_mul_f32 v[62:63], v[14:15], v[38:39]
	v_pk_add_f32 v[48:49], v[48:49], v[56:57]
	v_pk_add_f32 v[50:51], v[50:51], v[58:59]
	v_pk_add_f32 v[52:53], v[52:53], v[60:61]
	v_pk_add_f32 v[54:55], v[54:55], v[62:63]
	v_pk_fma_f32 v[48:49], v[16:17], v[40:41], v[48:49]
	v_pk_fma_f32 v[50:51], v[18:19], v[42:43], v[50:51]
	v_pk_fma_f32 v[52:53], v[20:21], v[44:45], v[52:53]
	v_pk_fma_f32 v[54:55], v[22:23], v[46:47], v[54:55]
	v_lshlrev_b32_e32 v56, 16, v168
	v_and_b32_e32 v57, 0xffff0000, v168
	v_lshlrev_b32_e32 v58, 16, v169
	v_and_b32_e32 v59, 0xffff0000, v169
	v_lshlrev_b32_e32 v60, 16, v170
	v_and_b32_e32 v61, 0xffff0000, v170
	v_lshlrev_b32_e32 v62, 16, v171
	v_and_b32_e32 v63, 0xffff0000, v171
	v_pk_mul_f32 v[48:49], v[48:49], v[56:57]
	v_pk_mul_f32 v[50:51], v[50:51], v[58:59]
	v_pk_mul_f32 v[52:53], v[52:53], v[60:61]
	v_pk_mul_f32 v[54:55], v[54:55], v[62:63]
	v_pk_mul_f32 v[48:49], v[48:49], 4.0 op_sel_hi:[1,0]
	v_pk_mul_f32 v[50:51], v[50:51], 4.0 op_sel_hi:[1,0]
	v_pk_mul_f32 v[52:53], v[52:53], 4.0 op_sel_hi:[1,0]
	v_pk_mul_f32 v[54:55], v[54:55], 4.0 op_sel_hi:[1,0]
	v_med3_f32 v48, v48, s33, v229
	v_med3_f32 v49, v49, s33, v229
	v_med3_f32 v50, v50, s33, v229
	v_med3_f32 v51, v51, s33, v229
	v_med3_f32 v52, v52, s33, v229
	v_med3_f32 v53, v53, s33, v229
	v_med3_f32 v54, v54, s33, v229
	v_med3_f32 v55, v55, s33, v229
	v_add_u32_e32 v66, 0xb400, v182
	v_cvt_pk_fp8_f32 v62, v48, v49
	v_cvt_pk_fp8_f32 v63, v52, v53
	v_cvt_pk_fp8_f32 v62, v50, v51 op_sel:[0,0,1]
	v_cvt_pk_fp8_f32 v63, v54, v55 op_sel:[0,0,1]
	global_store_dwordx2 v66, v[62:63], s[4:5]
	s_branch .Lmy_cp_next
; template <int WIN> __device__ __forceinline__ void pool_task(const Params& p, int t0, int c) {
;     const bf16* PROJ = (const bf16*)(p.ws + WS_PROJ); unsigned char* YABC = p.ws + WS_YABC;
;     float ring[WIN][8], tot[8];
; #pragma unroll
;     for (int i = 0; i < 8; ++i) tot[i] = 0.f;
; #pragma unroll
;     for (int d = 1 - WIN; d < 0; ++d) {
;         if (t0 > 0) { ld8(PROJ + (size_t)(t0 + d) * INC + 5120 + c, ring[(d + WIN) % WIN]);
; #pragma unroll
;             for (int i = 0; i < 8; ++i) tot[i] += ring[(d + WIN) % WIN][i]; }
;         else {
; #pragma unroll
;             for (int i = 0; i < 8; ++i) ring[(d + WIN) % WIN][i] = 0.f; }
;     }
; #pragma unroll
;     for (int k = 0; k < 16; ++k) { const int t = t0 + k;
;         float cur[8], o[8]; ld8(PROJ + (size_t)t * INC + 5120 + c, cur);
;         const float inv = (k + 1 < WIN && t0 == 0) ? 1.0f / (float)(k + 1) : 1.0f / (float)WIN;
; #pragma unroll
;         for (int i = 0; i < 8; ++i) { tot[i] += cur[i]; o[i] = tot[i] * inv - cur[i]; ring[k % WIN][i] = cur[i]; }
;         st8q(YABC + (size_t)t * 3072 + 2048 + c, o);
; #pragma unroll
;         for (int i = 0; i < 8; ++i) tot[i] -= ring[(k + 1) % WIN][i];
;     }
; }
; __device__ __forceinline__ void convpool_task(const Params& p, int l, int task) {
;     if (task < 65536) { conv_task(p, l, (task >> 7) * 16, (task & 127) * 8); return; }
;     const int k = task - 65536, g = __builtin_amdgcn_readfirstlane((k >> 6) & 3), run = ((k >> 8) << 1) + ((k >> 5) & 1), c = (g * 32 + (k & 31)) * 8, t0 = run * 16;
;     if (g == 0) pool_task<2>(p, t0, c); else if (g == 1) pool_task<4>(p, t0, c); else if (g == 2) pool_task<8>(p, t0, c); else pool_task<16>(p, t0, c);
.Lmy_pool:
	v_readfirstlane_b32 s10, v67
	s_bfe_u32 s10, s10, 0x20006
	s_cmp_eq_u32 s10, 0
	s_cbranch_scc1 .Lmy_pool_w2
	s_cmp_eq_u32 s10, 1
	s_cbranch_scc1 .Lmy_pool_w4
	s_cmp_eq_u32 s10, 2
	s_cbranch_scc1 .Lmy_pool_w8
	v_and_b32_e32 v35, 31, v67
	v_lshrrev_b32_e32 v32, 8, v67
	s_lshl_b32 s10, s7, 1
	v_add_lshl_u32 v32, v32, s10, 1
	v_bfe_u32 v38, v67, 5, 1
	v_add_lshl_u32 v32, v32, v38, 4
	v_or_b32_e32 v35, 96, v35
	v_mul_u32_u24_e32 v33, 0x3000, v32
	v_lshl_add_u32 v33, v35, 4, v33
	v_add_u32_e32 v33, 0x1000, v33
	v_mul_u32_u24_e32 v34, 0xc00, v32
	v_lshl_add_u32 v34, v35, 3, v34
	v_add_u32_e32 v34, 0x800, v34
	v_mov_b32_e32 v56, 0
	v_mov_b32_e32 v57, 0
	v_mov_b32_e32 v58, 0
	v_mov_b32_e32 v59, 0
	v_mov_b32_e32 v60, 0
	v_mov_b32_e32 v61, 0
	v_mov_b32_e32 v62, 0
	v_mov_b32_e32 v63, 0
	v_mov_b32_e32 v68, 0
	v_mov_b32_e32 v69, 0
	v_mov_b32_e32 v70, 0
	v_mov_b32_e32 v71, 0
	v_mov_b32_e32 v72, 0
	v_mov_b32_e32 v73, 0
	v_mov_b32_e32 v74, 0
	v_mov_b32_e32 v75, 0
	v_mov_b32_e32 v76, 0
	v_mov_b32_e32 v77, 0
	v_mov_b32_e32 v78, 0
	v_mov_b32_e32 v79, 0
	v_mov_b32_e32 v80, 0
	v_mov_b32_e32 v81, 0
	v_mov_b32_e32 v82, 0
	v_mov_b32_e32 v83, 0
	v_mov_b32_e32 v84, 0
	v_mov_b32_e32 v85, 0
	v_mov_b32_e32 v86, 0
	v_mov_b32_e32 v87, 0
	v_mov_b32_e32 v88, 0
	v_mov_b32_e32 v89, 0
	v_mov_b32_e32 v90, 0
	v_mov_b32_e32 v91, 0
	v_mov_b32_e32 v92, 0
	v_mov_b32_e32 v93, 0
	v_mov_b32_e32 v94, 0
	v_mov_b32_e32 v95, 0
	v_mov_b32_e32 v96, 0
	v_mov_b32_e32 v97, 0
	v_mov_b32_e32 v98, 0
	v_mov_b32_e32 v99, 0
	v_mov_b32_e32 v100, 0
	v_mov_b32_e32 v101, 0
	v_mov_b32_e32 v102, 0
	v_mov_b32_e32 v103, 0
	v_mov_b32_e32 v104, 0
	v_mov_b32_e32 v105, 0
	v_mov_b32_e32 v106, 0
	v_mov_b32_e32 v107, 0
	v_mov_b32_e32 v108, 0
	v_mov_b32_e32 v109, 0
	v_mov_b32_e32 v110, 0
	v_mov_b32_e32 v111, 0
	v_mov_b32_e32 v112, 0
	v_mov_b32_e32 v113, 0
	v_mov_b32_e32 v114, 0
	v_mov_b32_e32 v115, 0
	v_mov_b32_e32 v116, 0
	v_mov_b32_e32 v117, 0
	v_mov_b32_e32 v118, 0
	v_mov_b32_e32 v119, 0
	v_cmp_ne_u32_e32 vcc, 0, v32
	s_and_saveexec_b64 s[10:11], vcc
	v_add_u32_e32 v35, 0xfffd3000, v33
	global_load_dwordx4 v[56:59], v35, s[2:3] nt
	v_add_u32_e32 v35, 0xfffd6000, v33
	global_load_dwordx4 v[60:63], v35, s[2:3] nt
	v_add_u32_e32 v35, 0xfffd9000, v33
	global_load_dwordx4 v[68:71], v35, s[2:3] nt
	v_add_u32_e32 v35, 0xfffdc000, v33
	global_load_dwordx4 v[72:75], v35, s[2:3] nt
	v_add_u32_e32 v35, 0xfffdf000, v33
	global_load_dwordx4 v[76:79], v35, s[2:3] nt
	v_add_u32_e32 v35, 0xfffe2000, v33
	global_load_dwordx4 v[80:83], v35, s[2:3] nt
	v_add_u32_e32 v35, 0xfffe5000, v33
	global_load_dwordx4 v[84:87], v35, s[2:3] nt
	v_add_u32_e32 v35, 0xfffe8000, v33
	global_load_dwordx4 v[88:91], v35, s[2:3] nt
	v_add_u32_e32 v35, 0xfffeb000, v33
	global_load_dwordx4 v[92:95], v35, s[2:3] nt
	v_add_u32_e32 v35, 0xfffee000, v33
	global_load_dwordx4 v[96:99], v35, s[2:3] nt
	v_add_u32_e32 v35, 0xffff1000, v33
	global_load_dwordx4 v[100:103], v35, s[2:3] nt
	v_add_u32_e32 v35, 0xffff4000, v33
	global_load_dwordx4 v[104:107], v35, s[2:3] nt
	v_add_u32_e32 v35, 0xffff7000, v33
	global_load_dwordx4 v[108:111], v35, s[2:3] nt
	v_add_u32_e32 v35, 0xffffa000, v33
	global_load_dwordx4 v[112:115], v35, s[2:3] nt
	v_add_u32_e32 v35, 0xffffd000, v33
	global_load_dwordx4 v[116:119], v35, s[2:3] nt
	s_mov_b64 exec, s[0:1]
	global_load_dwordx4 v[120:123], v33, s[2:3] nt
	v_add_u32_e32 v35, 0x3000, v33
	global_load_dwordx4 v[124:127], v35, s[2:3] nt
	v_add_u32_e32 v35, 0x6000, v33
	global_load_dwordx4 v[128:131], v35, s[2:3] nt
	v_add_u32_e32 v35, 0x9000, v33
	global_load_dwordx4 v[132:135], v35, s[2:3] nt
	v_add_u32_e32 v35, 0xc000, v33
	global_load_dwordx4 v[136:139], v35, s[2:3] nt
	v_add_u32_e32 v35, 0xf000, v33
	global_load_dwordx4 v[140:143], v35, s[2:3] nt
	v_add_u32_e32 v35, 0x12000, v33
	global_load_dwordx4 v[144:147], v35, s[2:3] nt
	v_add_u32_e32 v35, 0x15000, v33
	global_load_dwordx4 v[148:151], v35, s[2:3] nt
	v_add_u32_e32 v35, 0x18000, v33
	global_load_dwordx4 v[152:155], v35, s[2:3] nt
	v_add_u32_e32 v35, 0x1b000, v33
	global_load_dwordx4 v[156:159], v35, s[2:3] nt
	v_add_u32_e32 v35, 0x1e000, v33
	global_load_dwordx4 v[160:163], v35, s[2:3] nt
	v_add_u32_e32 v35, 0x21000, v33
	global_load_dwordx4 v[164:167], v35, s[2:3] nt
	v_add_u32_e32 v35, 0x24000, v33
	global_load_dwordx4 v[168:171], v35, s[2:3] nt
	v_add_u32_e32 v35, 0x27000, v33
	global_load_dwordx4 v[172:175], v35, s[2:3] nt
	v_add_u32_e32 v35, 0x2a000, v33
	global_load_dwordx4 v[176:179], v35, s[2:3] nt
	v_add_u32_e32 v35, 0x2d000, v33
	global_load_dwordx4 v[180:183], v35, s[2:3] nt
	v_cmp_eq_u32_e32 vcc, 0, v32
	v_mov_b32_e32 v36, 0x3d800000
	v_mov_b64_e32 v[0:1], 0
	v_mov_b64_e32 v[2:3], 0
	v_mov_b64_e32 v[4:5], 0
	v_mov_b64_e32 v[6:7], 0
	s_waitcnt vmcnt(30)
	v_lshlrev_b32_e32 v8, 16, v56
	v_and_b32_e32 v9, 0xffff0000, v56
	v_lshlrev_b32_e32 v10, 16, v57
	v_and_b32_e32 v11, 0xffff0000, v57
	v_lshlrev_b32_e32 v12, 16, v58
	v_and_b32_e32 v13, 0xffff0000, v58
	v_lshlrev_b32_e32 v14, 16, v59
	v_and_b32_e32 v15, 0xffff0000, v59
	v_pk_add_f32 v[0:1], v[0:1], v[8:9]
	v_pk_add_f32 v[2:3], v[2:3], v[10:11]
	v_pk_add_f32 v[4:5], v[4:5], v[12:13]
	v_pk_add_f32 v[6:7], v[6:7], v[14:15]
	s_waitcnt vmcnt(29)
	v_lshlrev_b32_e32 v8, 16, v60
	v_and_b32_e32 v9, 0xffff0000, v60
	v_lshlrev_b32_e32 v10, 16, v61
	v_and_b32_e32 v11, 0xffff0000, v61
	v_lshlrev_b32_e32 v12, 16, v62
	v_and_b32_e32 v13, 0xffff0000, v62
	v_lshlrev_b32_e32 v14, 16, v63
	v_and_b32_e32 v15, 0xffff0000, v63
	v_pk_add_f32 v[0:1], v[0:1], v[8:9]
	v_pk_add_f32 v[2:3], v[2:3], v[10:11]
	v_pk_add_f32 v[4:5], v[4:5], v[12:13]
	v_pk_add_f32 v[6:7], v[6:7], v[14:15]
	s_waitcnt vmcnt(28)
; template <int WIN> __device__ __forceinline__ void pool_task(const Params& p, int t0, int c) {
;     ...
; #pragma unroll
;     for (int d = 1 - WIN; d < 0; ++d) {
;         if (t0 > 0) { ld8(PROJ + (size_t)(t0 + d) * INC + 5120 + c, ring[(d + WIN) % WIN]);
; #pragma unroll
;             for (int i = 0; i < 8; ++i) tot[i] += ring[(d + WIN) % WIN][i]; }
;         else {
; #pragma unroll
;             for (int i = 0; i < 8; ++i) ring[(d + WIN) % WIN][i] = 0.f; }
;     }
	v_lshlrev_b32_e32 v8, 16, v68
	v_and_b32_e32 v9, 0xffff0000, v68
	v_lshlrev_b32_e32 v10, 16, v69
	v_and_b32_e32 v11, 0xffff0000, v69
	v_lshlrev_b32_e32 v12, 16, v70
	v_and_b32_e32 v13, 0xffff0000, v70
	v_lshlrev_b32_e32 v14, 16, v71
	v_and_b32_e32 v15, 0xffff0000, v71
	v_pk_add_f32 v[0:1], v[0:1], v[8:9]
	v_pk_add_f32 v[2:3], v[2:3], v[10:11]
	v_pk_add_f32 v[4:5], v[4:5], v[12:13]
	v_pk_add_f32 v[6:7], v[6:7], v[14:15]
	s_waitcnt vmcnt(27)
	v_lshlrev_b32_e32 v8, 16, v72
	v_and_b32_e32 v9, 0xffff0000, v72
	v_lshlrev_b32_e32 v10, 16, v73
	v_and_b32_e32 v11, 0xffff0000, v73
	v_lshlrev_b32_e32 v12, 16, v74
	v_and_b32_e32 v13, 0xffff0000, v74
	v_lshlrev_b32_e32 v14, 16, v75
	v_and_b32_e32 v15, 0xffff0000, v75
	v_pk_add_f32 v[0:1], v[0:1], v[8:9]
	v_pk_add_f32 v[2:3], v[2:3], v[10:11]
	v_pk_add_f32 v[4:5], v[4:5], v[12:13]
	v_pk_add_f32 v[6:7], v[6:7], v[14:15]
	s_waitcnt vmcnt(26)
	v_lshlrev_b32_e32 v8, 16, v76
	v_and_b32_e32 v9, 0xffff0000, v76
	v_lshlrev_b32_e32 v10, 16, v77
	v_and_b32_e32 v11, 0xffff0000, v77
	v_lshlrev_b32_e32 v12, 16, v78
	v_and_b32_e32 v13, 0xffff0000, v78
	v_lshlrev_b32_e32 v14, 16, v79
	v_and_b32_e32 v15, 0xffff0000, v79
	v_pk_add_f32 v[0:1], v[0:1], v[8:9]
	v_pk_add_f32 v[2:3], v[2:3], v[10:11]
	v_pk_add_f32 v[4:5], v[4:5], v[12:13]
	v_pk_add_f32 v[6:7], v[6:7], v[14:15]
	s_waitcnt vmcnt(25)
	v_lshlrev_b32_e32 v8, 16, v80
	v_and_b32_e32 v9, 0xffff0000, v80
	v_lshlrev_b32_e32 v10, 16, v81
	v_and_b32_e32 v11, 0xffff0000, v81
	v_lshlrev_b32_e32 v12, 16, v82
	v_and_b32_e32 v13, 0xffff0000, v82
	v_lshlrev_b32_e32 v14, 16, v83
	v_and_b32_e32 v15, 0xffff0000, v83
	v_pk_add_f32 v[0:1], v[0:1], v[8:9]
	v_pk_add_f32 v[2:3], v[2:3], v[10:11]
	v_pk_add_f32 v[4:5], v[4:5], v[12:13]
	v_pk_add_f32 v[6:7], v[6:7], v[14:15]
	s_waitcnt vmcnt(24)
	v_lshlrev_b32_e32 v8, 16, v84
	v_and_b32_e32 v9, 0xffff0000, v84
	v_lshlrev_b32_e32 v10, 16, v85
	v_and_b32_e32 v11, 0xffff0000, v85
	v_lshlrev_b32_e32 v12, 16, v86
	v_and_b32_e32 v13, 0xffff0000, v86
	v_lshlrev_b32_e32 v14, 16, v87
	v_and_b32_e32 v15, 0xffff0000, v87
	v_pk_add_f32 v[0:1], v[0:1], v[8:9]
	v_pk_add_f32 v[2:3], v[2:3], v[10:11]
	v_pk_add_f32 v[4:5], v[4:5], v[12:13]
	v_pk_add_f32 v[6:7], v[6:7], v[14:15]
	s_waitcnt vmcnt(23)
	v_lshlrev_b32_e32 v8, 16, v88
	v_and_b32_e32 v9, 0xffff0000, v88
	v_lshlrev_b32_e32 v10, 16, v89
	v_and_b32_e32 v11, 0xffff0000, v89
	v_lshlrev_b32_e32 v12, 16, v90
	v_and_b32_e32 v13, 0xffff0000, v90
	v_lshlrev_b32_e32 v14, 16, v91
	v_and_b32_e32 v15, 0xffff0000, v91
	v_pk_add_f32 v[0:1], v[0:1], v[8:9]
	v_pk_add_f32 v[2:3], v[2:3], v[10:11]
	v_pk_add_f32 v[4:5], v[4:5], v[12:13]
	v_pk_add_f32 v[6:7], v[6:7], v[14:15]
	s_waitcnt vmcnt(22)
	v_lshlrev_b32_e32 v8, 16, v92
	v_and_b32_e32 v9, 0xffff0000, v92
	v_lshlrev_b32_e32 v10, 16, v93
	v_and_b32_e32 v11, 0xffff0000, v93
	v_lshlrev_b32_e32 v12, 16, v94
	v_and_b32_e32 v13, 0xffff0000, v94
	v_lshlrev_b32_e32 v14, 16, v95
	v_and_b32_e32 v15, 0xffff0000, v95
	v_pk_add_f32 v[0:1], v[0:1], v[8:9]
	v_pk_add_f32 v[2:3], v[2:3], v[10:11]
	v_pk_add_f32 v[4:5], v[4:5], v[12:13]
	v_pk_add_f32 v[6:7], v[6:7], v[14:15]
	s_waitcnt vmcnt(21)
	v_lshlrev_b32_e32 v8, 16, v96
	v_and_b32_e32 v9, 0xffff0000, v96
	v_lshlrev_b32_e32 v10, 16, v97
	v_and_b32_e32 v11, 0xffff0000, v97
	v_lshlrev_b32_e32 v12, 16, v98
	v_and_b32_e32 v13, 0xffff0000, v98
	v_lshlrev_b32_e32 v14, 16, v99
	v_and_b32_e32 v15, 0xffff0000, v99
	v_pk_add_f32 v[0:1], v[0:1], v[8:9]
	v_pk_add_f32 v[2:3], v[2:3], v[10:11]
	v_pk_add_f32 v[4:5], v[4:5], v[12:13]
	v_pk_add_f32 v[6:7], v[6:7], v[14:15]
	s_waitcnt vmcnt(20)
	v_lshlrev_b32_e32 v8, 16, v100
	v_and_b32_e32 v9, 0xffff0000, v100
	v_lshlrev_b32_e32 v10, 16, v101
	v_and_b32_e32 v11, 0xffff0000, v101
	v_lshlrev_b32_e32 v12, 16, v102
	v_and_b32_e32 v13, 0xffff0000, v102
	v_lshlrev_b32_e32 v14, 16, v103
	v_and_b32_e32 v15, 0xffff0000, v103
	v_pk_add_f32 v[0:1], v[0:1], v[8:9]
	v_pk_add_f32 v[2:3], v[2:3], v[10:11]
	v_pk_add_f32 v[4:5], v[4:5], v[12:13]
	v_pk_add_f32 v[6:7], v[6:7], v[14:15]
	s_waitcnt vmcnt(19)
	v_lshlrev_b32_e32 v8, 16, v104
	v_and_b32_e32 v9, 0xffff0000, v104
	v_lshlrev_b32_e32 v10, 16, v105
	v_and_b32_e32 v11, 0xffff0000, v105
	v_lshlrev_b32_e32 v12, 16, v106
	v_and_b32_e32 v13, 0xffff0000, v106
	v_lshlrev_b32_e32 v14, 16, v107
	v_and_b32_e32 v15, 0xffff0000, v107
	v_pk_add_f32 v[0:1], v[0:1], v[8:9]
	v_pk_add_f32 v[2:3], v[2:3], v[10:11]
	v_pk_add_f32 v[4:5], v[4:5], v[12:13]
	v_pk_add_f32 v[6:7], v[6:7], v[14:15]
	s_waitcnt vmcnt(18)
	v_lshlrev_b32_e32 v8, 16, v108
	v_and_b32_e32 v9, 0xffff0000, v108
	v_lshlrev_b32_e32 v10, 16, v109
	v_and_b32_e32 v11, 0xffff0000, v109
	v_lshlrev_b32_e32 v12, 16, v110
	v_and_b32_e32 v13, 0xffff0000, v110
	v_lshlrev_b32_e32 v14, 16, v111
	v_and_b32_e32 v15, 0xffff0000, v111
	v_pk_add_f32 v[0:1], v[0:1], v[8:9]
	v_pk_add_f32 v[2:3], v[2:3], v[10:11]
	v_pk_add_f32 v[4:5], v[4:5], v[12:13]
	v_pk_add_f32 v[6:7], v[6:7], v[14:15]
	s_waitcnt vmcnt(17)
	v_lshlrev_b32_e32 v8, 16, v112
	v_and_b32_e32 v9, 0xffff0000, v112
	v_lshlrev_b32_e32 v10, 16, v113
	v_and_b32_e32 v11, 0xffff0000, v113
	v_lshlrev_b32_e32 v12, 16, v114
	v_and_b32_e32 v13, 0xffff0000, v114
	v_lshlrev_b32_e32 v14, 16, v115
	v_and_b32_e32 v15, 0xffff0000, v115
	v_pk_add_f32 v[0:1], v[0:1], v[8:9]
	v_pk_add_f32 v[2:3], v[2:3], v[10:11]
	v_pk_add_f32 v[4:5], v[4:5], v[12:13]
	v_pk_add_f32 v[6:7], v[6:7], v[14:15]
	s_waitcnt vmcnt(16)
	v_lshlrev_b32_e32 v8, 16, v116
	v_and_b32_e32 v9, 0xffff0000, v116
	v_lshlrev_b32_e32 v10, 16, v117
	v_and_b32_e32 v11, 0xffff0000, v117
	v_lshlrev_b32_e32 v12, 16, v118
	v_and_b32_e32 v13, 0xffff0000, v118
	v_lshlrev_b32_e32 v14, 16, v119
	v_and_b32_e32 v15, 0xffff0000, v119
	v_pk_add_f32 v[0:1], v[0:1], v[8:9]
	v_pk_add_f32 v[2:3], v[2:3], v[10:11]
	v_pk_add_f32 v[4:5], v[4:5], v[12:13]
	v_pk_add_f32 v[6:7], v[6:7], v[14:15]
	s_waitcnt vmcnt(15)
; __device__ __forceinline__ unsigned pk4_fp8(float a, float b, float c, float d) { unsigned w = 0u; w = __builtin_amdgcn_cvt_pk_fp8_f32(clamp8(a), clamp8(b), w, false); w = __builtin_amdgcn_cvt_pk_fp8_f32(clamp8(c), clamp8(d), w, true); return w; }
; __device__ __forceinline__ void st8q(unsigned char* ptr, const float (&f)[8]) {
;     u32x2 w; w.x = pk4_fp8(4.f * f[0], 4.f * f[1], 4.f * f[2], 4.f * f[3]); w.y = pk4_fp8(4.f * f[4], 4.f * f[5], 4.f * f[6], 4.f * f[7]); *(u32x2*)ptr = w;
; }
; template <int WIN> __device__ __forceinline__ void pool_task(const Params& p, int t0, int c) {
;     ...
; #pragma unroll
;     for (int k = 0; k < 16; ++k) { const int t = t0 + k;
;         float cur[8], o[8]; ld8(PROJ + (size_t)t * INC + 5120 + c, cur);
;         const float inv = (k + 1 < WIN && t0 == 0) ? 1.0f / (float)(k + 1) : 1.0f / (float)WIN;
; #pragma unroll
;         for (int i = 0; i < 8; ++i) { tot[i] += cur[i]; o[i] = tot[i] * inv - cur[i]; ring[k % WIN][i] = cur[i]; }
;         st8q(YABC + (size_t)t * 3072 + 2048 + c, o);
; #pragma unroll
;         for (int i = 0; i < 8; ++i) tot[i] -= ring[(k + 1) % WIN][i];
;     }
; }
	v_lshlrev_b32_e32 v8, 16, v120
	v_and_b32_e32 v9, 0xffff0000, v120
	v_lshlrev_b32_e32 v10, 16, v121
	v_and_b32_e32 v11, 0xffff0000, v121
	v_lshlrev_b32_e32 v12, 16, v122
	v_and_b32_e32 v13, 0xffff0000, v122
	v_lshlrev_b32_e32 v14, 16, v123
	v_and_b32_e32 v15, 0xffff0000, v123
	v_pk_add_f32 v[0:1], v[0:1], v[8:9]
	v_pk_add_f32 v[2:3], v[2:3], v[10:11]
	v_pk_add_f32 v[4:5], v[4:5], v[12:13]
	v_pk_add_f32 v[6:7], v[6:7], v[14:15]
	v_mov_b32_e32 v38, 0x3f800000
	v_cndmask_b32_e32 v37, v36, v38, vcc
	v_fma_f32 v24, v37, v0, -v8
	v_fma_f32 v25, v37, v1, -v9
	v_fma_f32 v26, v37, v2, -v10
	v_fma_f32 v27, v37, v3, -v11
	v_fma_f32 v28, v37, v4, -v12
	v_fma_f32 v29, v37, v5, -v13
	v_fma_f32 v30, v37, v6, -v14
	v_fma_f32 v31, v37, v7, -v15
	v_pk_mul_f32 v[24:25], v[24:25], 4.0 op_sel_hi:[1,0]
	v_pk_mul_f32 v[26:27], v[26:27], 4.0 op_sel_hi:[1,0]
	v_pk_mul_f32 v[28:29], v[28:29], 4.0 op_sel_hi:[1,0]
	v_pk_mul_f32 v[30:31], v[30:31], 4.0 op_sel_hi:[1,0]
	v_med3_f32 v24, v24, s33, v229
	v_med3_f32 v25, v25, s33, v229
	v_med3_f32 v26, v26, s33, v229
	v_med3_f32 v27, v27, s33, v229
	v_med3_f32 v28, v28, s33, v229
	v_med3_f32 v29, v29, s33, v229
	v_med3_f32 v30, v30, s33, v229
	v_med3_f32 v31, v31, s33, v229
	v_cvt_pk_fp8_f32 v40, v24, v25
	v_cvt_pk_fp8_f32 v41, v28, v29
	v_cvt_pk_fp8_f32 v40, v26, v27 op_sel:[0,0,1]
	v_cvt_pk_fp8_f32 v41, v30, v31 op_sel:[0,0,1]
	global_store_dwordx2 v34, v[40:41], s[4:5]
	v_lshlrev_b32_e32 v16, 16, v56
	v_and_b32_e32 v17, 0xffff0000, v56
	v_lshlrev_b32_e32 v18, 16, v57
	v_and_b32_e32 v19, 0xffff0000, v57
	v_lshlrev_b32_e32 v20, 16, v58
	v_and_b32_e32 v21, 0xffff0000, v58
	v_lshlrev_b32_e32 v22, 16, v59
	v_and_b32_e32 v23, 0xffff0000, v59
	v_pk_add_f32 v[0:1], v[0:1], v[16:17] neg_lo:[0,1] neg_hi:[0,1]
	v_pk_add_f32 v[2:3], v[2:3], v[18:19] neg_lo:[0,1] neg_hi:[0,1]
	v_pk_add_f32 v[4:5], v[4:5], v[20:21] neg_lo:[0,1] neg_hi:[0,1]
	v_pk_add_f32 v[6:7], v[6:7], v[22:23] neg_lo:[0,1] neg_hi:[0,1]
	s_waitcnt vmcnt(15)
	v_lshlrev_b32_e32 v8, 16, v124
	v_and_b32_e32 v9, 0xffff0000, v124
	v_lshlrev_b32_e32 v10, 16, v125
	v_and_b32_e32 v11, 0xffff0000, v125
	v_lshlrev_b32_e32 v12, 16, v126
	v_and_b32_e32 v13, 0xffff0000, v126
	v_lshlrev_b32_e32 v14, 16, v127
	v_and_b32_e32 v15, 0xffff0000, v127
	v_pk_add_f32 v[0:1], v[0:1], v[8:9]
	v_pk_add_f32 v[2:3], v[2:3], v[10:11]
	v_pk_add_f32 v[4:5], v[4:5], v[12:13]
	v_pk_add_f32 v[6:7], v[6:7], v[14:15]
	v_mov_b32_e32 v38, 0x3f000000
	v_cndmask_b32_e32 v37, v36, v38, vcc
	v_fma_f32 v24, v37, v0, -v8
	v_fma_f32 v25, v37, v1, -v9
	v_fma_f32 v26, v37, v2, -v10
	v_fma_f32 v27, v37, v3, -v11
	v_fma_f32 v28, v37, v4, -v12
	v_fma_f32 v29, v37, v5, -v13
	v_fma_f32 v30, v37, v6, -v14
	v_fma_f32 v31, v37, v7, -v15
	v_pk_mul_f32 v[24:25], v[24:25], 4.0 op_sel_hi:[1,0]
	v_pk_mul_f32 v[26:27], v[26:27], 4.0 op_sel_hi:[1,0]
	v_pk_mul_f32 v[28:29], v[28:29], 4.0 op_sel_hi:[1,0]
	v_pk_mul_f32 v[30:31], v[30:31], 4.0 op_sel_hi:[1,0]
	v_med3_f32 v24, v24, s33, v229
	v_med3_f32 v25, v25, s33, v229
	v_med3_f32 v26, v26, s33, v229
	v_med3_f32 v27, v27, s33, v229
	v_med3_f32 v28, v28, s33, v229
	v_med3_f32 v29, v29, s33, v229
	v_med3_f32 v30, v30, s33, v229
	v_med3_f32 v31, v31, s33, v229
	v_add_u32_e32 v35, 0xc00, v34
	v_cvt_pk_fp8_f32 v40, v24, v25
	v_cvt_pk_fp8_f32 v41, v28, v29
	v_cvt_pk_fp8_f32 v40, v26, v27 op_sel:[0,0,1]
	v_cvt_pk_fp8_f32 v41, v30, v31 op_sel:[0,0,1]
	global_store_dwordx2 v35, v[40:41], s[4:5]
	v_lshlrev_b32_e32 v16, 16, v60
	v_and_b32_e32 v17, 0xffff0000, v60
	v_lshlrev_b32_e32 v18, 16, v61
	v_and_b32_e32 v19, 0xffff0000, v61
	v_lshlrev_b32_e32 v20, 16, v62
	v_and_b32_e32 v21, 0xffff0000, v62
	v_lshlrev_b32_e32 v22, 16, v63
	v_and_b32_e32 v23, 0xffff0000, v63
	v_pk_add_f32 v[0:1], v[0:1], v[16:17] neg_lo:[0,1] neg_hi:[0,1]
	v_pk_add_f32 v[2:3], v[2:3], v[18:19] neg_lo:[0,1] neg_hi:[0,1]
	v_pk_add_f32 v[4:5], v[4:5], v[20:21] neg_lo:[0,1] neg_hi:[0,1]
	v_pk_add_f32 v[6:7], v[6:7], v[22:23] neg_lo:[0,1] neg_hi:[0,1]
	s_waitcnt vmcnt(15)
	v_lshlrev_b32_e32 v8, 16, v128
	v_and_b32_e32 v9, 0xffff0000, v128
	v_lshlrev_b32_e32 v10, 16, v129
	v_and_b32_e32 v11, 0xffff0000, v129
	v_lshlrev_b32_e32 v12, 16, v130
	v_and_b32_e32 v13, 0xffff0000, v130
	v_lshlrev_b32_e32 v14, 16, v131
	v_and_b32_e32 v15, 0xffff0000, v131
	v_pk_add_f32 v[0:1], v[0:1], v[8:9]
	v_pk_add_f32 v[2:3], v[2:3], v[10:11]
	v_pk_add_f32 v[4:5], v[4:5], v[12:13]
	v_pk_add_f32 v[6:7], v[6:7], v[14:15]
	v_mov_b32_e32 v38, 0x3eaaaaab
	v_cndmask_b32_e32 v37, v36, v38, vcc
	v_fma_f32 v24, v37, v0, -v8
	v_fma_f32 v25, v37, v1, -v9
	v_fma_f32 v26, v37, v2, -v10
	v_fma_f32 v27, v37, v3, -v11
	v_fma_f32 v28, v37, v4, -v12
	v_fma_f32 v29, v37, v5, -v13
	v_fma_f32 v30, v37, v6, -v14
	v_fma_f32 v31, v37, v7, -v15
	v_pk_mul_f32 v[24:25], v[24:25], 4.0 op_sel_hi:[1,0]
	v_pk_mul_f32 v[26:27], v[26:27], 4.0 op_sel_hi:[1,0]
	v_pk_mul_f32 v[28:29], v[28:29], 4.0 op_sel_hi:[1,0]
	v_pk_mul_f32 v[30:31], v[30:31], 4.0 op_sel_hi:[1,0]
	v_med3_f32 v24, v24, s33, v229
	v_med3_f32 v25, v25, s33, v229
	v_med3_f32 v26, v26, s33, v229
	v_med3_f32 v27, v27, s33, v229
	v_med3_f32 v28, v28, s33, v229
	v_med3_f32 v29, v29, s33, v229
	v_med3_f32 v30, v30, s33, v229
	v_med3_f32 v31, v31, s33, v229
	v_add_u32_e32 v35, 0x1800, v34
	v_cvt_pk_fp8_f32 v40, v24, v25
	v_cvt_pk_fp8_f32 v41, v28, v29
	v_cvt_pk_fp8_f32 v40, v26, v27 op_sel:[0,0,1]
	v_cvt_pk_fp8_f32 v41, v30, v31 op_sel:[0,0,1]
	global_store_dwordx2 v35, v[40:41], s[4:5]
	v_lshlrev_b32_e32 v16, 16, v68
	v_and_b32_e32 v17, 0xffff0000, v68
	v_lshlrev_b32_e32 v18, 16, v69
	v_and_b32_e32 v19, 0xffff0000, v69
	v_lshlrev_b32_e32 v20, 16, v70
	v_and_b32_e32 v21, 0xffff0000, v70
	v_lshlrev_b32_e32 v22, 16, v71
	v_and_b32_e32 v23, 0xffff0000, v71
	v_pk_add_f32 v[0:1], v[0:1], v[16:17] neg_lo:[0,1] neg_hi:[0,1]
	v_pk_add_f32 v[2:3], v[2:3], v[18:19] neg_lo:[0,1] neg_hi:[0,1]
	v_pk_add_f32 v[4:5], v[4:5], v[20:21] neg_lo:[0,1] neg_hi:[0,1]
	v_pk_add_f32 v[6:7], v[6:7], v[22:23] neg_lo:[0,1] neg_hi:[0,1]
	s_waitcnt vmcnt(15)
; __device__ __forceinline__ unsigned pk4_fp8(float a, float b, float c, float d) { unsigned w = 0u; w = __builtin_amdgcn_cvt_pk_fp8_f32(clamp8(a), clamp8(b), w, false); w = __builtin_amdgcn_cvt_pk_fp8_f32(clamp8(c), clamp8(d), w, true); return w; }
; __device__ __forceinline__ void st8q(unsigned char* ptr, const float (&f)[8]) {
;     u32x2 w; w.x = pk4_fp8(4.f * f[0], 4.f * f[1], 4.f * f[2], 4.f * f[3]); w.y = pk4_fp8(4.f * f[4], 4.f * f[5], 4.f * f[6], 4.f * f[7]); *(u32x2*)ptr = w;
; }
; template <int WIN> __device__ __forceinline__ void pool_task(const Params& p, int t0, int c) {
;     ...
; #pragma unroll
;     for (int k = 0; k < 16; ++k) { const int t = t0 + k;
;         float cur[8], o[8]; ld8(PROJ + (size_t)t * INC + 5120 + c, cur);
;         const float inv = (k + 1 < WIN && t0 == 0) ? 1.0f / (float)(k + 1) : 1.0f / (float)WIN;
; #pragma unroll
;         for (int i = 0; i < 8; ++i) { tot[i] += cur[i]; o[i] = tot[i] * inv - cur[i]; ring[k % WIN][i] = cur[i]; }
;         st8q(YABC + (size_t)t * 3072 + 2048 + c, o);
; #pragma unroll
;         for (int i = 0; i < 8; ++i) tot[i] -= ring[(k + 1) % WIN][i];
;     }
; }
	v_lshlrev_b32_e32 v8, 16, v132
	v_and_b32_e32 v9, 0xffff0000, v132
	v_lshlrev_b32_e32 v10, 16, v133
	v_and_b32_e32 v11, 0xffff0000, v133
	v_lshlrev_b32_e32 v12, 16, v134
	v_and_b32_e32 v13, 0xffff0000, v134
	v_lshlrev_b32_e32 v14, 16, v135
	v_and_b32_e32 v15, 0xffff0000, v135
	v_pk_add_f32 v[0:1], v[0:1], v[8:9]
	v_pk_add_f32 v[2:3], v[2:3], v[10:11]
	v_pk_add_f32 v[4:5], v[4:5], v[12:13]
	v_pk_add_f32 v[6:7], v[6:7], v[14:15]
	v_mov_b32_e32 v38, 0x3e800000
	v_cndmask_b32_e32 v37, v36, v38, vcc
	v_fma_f32 v24, v37, v0, -v8
	v_fma_f32 v25, v37, v1, -v9
	v_fma_f32 v26, v37, v2, -v10
	v_fma_f32 v27, v37, v3, -v11
	v_fma_f32 v28, v37, v4, -v12
	v_fma_f32 v29, v37, v5, -v13
	v_fma_f32 v30, v37, v6, -v14
	v_fma_f32 v31, v37, v7, -v15
	v_pk_mul_f32 v[24:25], v[24:25], 4.0 op_sel_hi:[1,0]
	v_pk_mul_f32 v[26:27], v[26:27], 4.0 op_sel_hi:[1,0]
	v_pk_mul_f32 v[28:29], v[28:29], 4.0 op_sel_hi:[1,0]
	v_pk_mul_f32 v[30:31], v[30:31], 4.0 op_sel_hi:[1,0]
	v_med3_f32 v24, v24, s33, v229
	v_med3_f32 v25, v25, s33, v229
	v_med3_f32 v26, v26, s33, v229
	v_med3_f32 v27, v27, s33, v229
	v_med3_f32 v28, v28, s33, v229
	v_med3_f32 v29, v29, s33, v229
	v_med3_f32 v30, v30, s33, v229
	v_med3_f32 v31, v31, s33, v229
	v_add_u32_e32 v35, 0x2400, v34
	v_cvt_pk_fp8_f32 v40, v24, v25
	v_cvt_pk_fp8_f32 v41, v28, v29
	v_cvt_pk_fp8_f32 v40, v26, v27 op_sel:[0,0,1]
	v_cvt_pk_fp8_f32 v41, v30, v31 op_sel:[0,0,1]
	global_store_dwordx2 v35, v[40:41], s[4:5]
	v_lshlrev_b32_e32 v16, 16, v72
	v_and_b32_e32 v17, 0xffff0000, v72
	v_lshlrev_b32_e32 v18, 16, v73
	v_and_b32_e32 v19, 0xffff0000, v73
	v_lshlrev_b32_e32 v20, 16, v74
	v_and_b32_e32 v21, 0xffff0000, v74
	v_lshlrev_b32_e32 v22, 16, v75
	v_and_b32_e32 v23, 0xffff0000, v75
	v_pk_add_f32 v[0:1], v[0:1], v[16:17] neg_lo:[0,1] neg_hi:[0,1]
	v_pk_add_f32 v[2:3], v[2:3], v[18:19] neg_lo:[0,1] neg_hi:[0,1]
	v_pk_add_f32 v[4:5], v[4:5], v[20:21] neg_lo:[0,1] neg_hi:[0,1]
	v_pk_add_f32 v[6:7], v[6:7], v[22:23] neg_lo:[0,1] neg_hi:[0,1]
	s_waitcnt vmcnt(15)
	v_lshlrev_b32_e32 v8, 16, v136
	v_and_b32_e32 v9, 0xffff0000, v136
	v_lshlrev_b32_e32 v10, 16, v137
	v_and_b32_e32 v11, 0xffff0000, v137
	v_lshlrev_b32_e32 v12, 16, v138
	v_and_b32_e32 v13, 0xffff0000, v138
	v_lshlrev_b32_e32 v14, 16, v139
	v_and_b32_e32 v15, 0xffff0000, v139
	v_pk_add_f32 v[0:1], v[0:1], v[8:9]
	v_pk_add_f32 v[2:3], v[2:3], v[10:11]
	v_pk_add_f32 v[4:5], v[4:5], v[12:13]
	v_pk_add_f32 v[6:7], v[6:7], v[14:15]
	v_mov_b32_e32 v38, 0x3e4ccccd
	v_cndmask_b32_e32 v37, v36, v38, vcc
	v_fma_f32 v24, v37, v0, -v8
	v_fma_f32 v25, v37, v1, -v9
	v_fma_f32 v26, v37, v2, -v10
	v_fma_f32 v27, v37, v3, -v11
	v_fma_f32 v28, v37, v4, -v12
	v_fma_f32 v29, v37, v5, -v13
	v_fma_f32 v30, v37, v6, -v14
	v_fma_f32 v31, v37, v7, -v15
	v_pk_mul_f32 v[24:25], v[24:25], 4.0 op_sel_hi:[1,0]
	v_pk_mul_f32 v[26:27], v[26:27], 4.0 op_sel_hi:[1,0]
	v_pk_mul_f32 v[28:29], v[28:29], 4.0 op_sel_hi:[1,0]
	v_pk_mul_f32 v[30:31], v[30:31], 4.0 op_sel_hi:[1,0]
	v_med3_f32 v24, v24, s33, v229
	v_med3_f32 v25, v25, s33, v229
	v_med3_f32 v26, v26, s33, v229
	v_med3_f32 v27, v27, s33, v229
	v_med3_f32 v28, v28, s33, v229
	v_med3_f32 v29, v29, s33, v229
	v_med3_f32 v30, v30, s33, v229
	v_med3_f32 v31, v31, s33, v229
	v_add_u32_e32 v35, 0x3000, v34
	v_cvt_pk_fp8_f32 v40, v24, v25
	v_cvt_pk_fp8_f32 v41, v28, v29
	v_cvt_pk_fp8_f32 v40, v26, v27 op_sel:[0,0,1]
	v_cvt_pk_fp8_f32 v41, v30, v31 op_sel:[0,0,1]
	global_store_dwordx2 v35, v[40:41], s[4:5]
	v_lshlrev_b32_e32 v16, 16, v76
	v_and_b32_e32 v17, 0xffff0000, v76
	v_lshlrev_b32_e32 v18, 16, v77
	v_and_b32_e32 v19, 0xffff0000, v77
	v_lshlrev_b32_e32 v20, 16, v78
	v_and_b32_e32 v21, 0xffff0000, v78
	v_lshlrev_b32_e32 v22, 16, v79
	v_and_b32_e32 v23, 0xffff0000, v79
	v_pk_add_f32 v[0:1], v[0:1], v[16:17] neg_lo:[0,1] neg_hi:[0,1]
	v_pk_add_f32 v[2:3], v[2:3], v[18:19] neg_lo:[0,1] neg_hi:[0,1]
	v_pk_add_f32 v[4:5], v[4:5], v[20:21] neg_lo:[0,1] neg_hi:[0,1]
	v_pk_add_f32 v[6:7], v[6:7], v[22:23] neg_lo:[0,1] neg_hi:[0,1]
	s_waitcnt vmcnt(15)
	v_lshlrev_b32_e32 v8, 16, v140
	v_and_b32_e32 v9, 0xffff0000, v140
	v_lshlrev_b32_e32 v10, 16, v141
	v_and_b32_e32 v11, 0xffff0000, v141
	v_lshlrev_b32_e32 v12, 16, v142
	v_and_b32_e32 v13, 0xffff0000, v142
	v_lshlrev_b32_e32 v14, 16, v143
	v_and_b32_e32 v15, 0xffff0000, v143
	v_pk_add_f32 v[0:1], v[0:1], v[8:9]
	v_pk_add_f32 v[2:3], v[2:3], v[10:11]
	v_pk_add_f32 v[4:5], v[4:5], v[12:13]
	v_pk_add_f32 v[6:7], v[6:7], v[14:15]
	v_mov_b32_e32 v38, 0x3e2aaaab
	v_cndmask_b32_e32 v37, v36, v38, vcc
	v_fma_f32 v24, v37, v0, -v8
	v_fma_f32 v25, v37, v1, -v9
	v_fma_f32 v26, v37, v2, -v10
	v_fma_f32 v27, v37, v3, -v11
	v_fma_f32 v28, v37, v4, -v12
	v_fma_f32 v29, v37, v5, -v13
	v_fma_f32 v30, v37, v6, -v14
	v_fma_f32 v31, v37, v7, -v15
	v_pk_mul_f32 v[24:25], v[24:25], 4.0 op_sel_hi:[1,0]
	v_pk_mul_f32 v[26:27], v[26:27], 4.0 op_sel_hi:[1,0]
	v_pk_mul_f32 v[28:29], v[28:29], 4.0 op_sel_hi:[1,0]
	v_pk_mul_f32 v[30:31], v[30:31], 4.0 op_sel_hi:[1,0]
	v_med3_f32 v24, v24, s33, v229
	v_med3_f32 v25, v25, s33, v229
	v_med3_f32 v26, v26, s33, v229
	v_med3_f32 v27, v27, s33, v229
	v_med3_f32 v28, v28, s33, v229
	v_med3_f32 v29, v29, s33, v229
	v_med3_f32 v30, v30, s33, v229
	v_med3_f32 v31, v31, s33, v229
	v_add_u32_e32 v35, 0x3c00, v34
	v_cvt_pk_fp8_f32 v40, v24, v25
	v_cvt_pk_fp8_f32 v41, v28, v29
	v_cvt_pk_fp8_f32 v40, v26, v27 op_sel:[0,0,1]
	v_cvt_pk_fp8_f32 v41, v30, v31 op_sel:[0,0,1]
	global_store_dwordx2 v35, v[40:41], s[4:5]
	v_lshlrev_b32_e32 v16, 16, v80
	v_and_b32_e32 v17, 0xffff0000, v80
	v_lshlrev_b32_e32 v18, 16, v81
	v_and_b32_e32 v19, 0xffff0000, v81
	v_lshlrev_b32_e32 v20, 16, v82
	v_and_b32_e32 v21, 0xffff0000, v82
	v_lshlrev_b32_e32 v22, 16, v83
	v_and_b32_e32 v23, 0xffff0000, v83
	v_pk_add_f32 v[0:1], v[0:1], v[16:17] neg_lo:[0,1] neg_hi:[0,1]
	v_pk_add_f32 v[2:3], v[2:3], v[18:19] neg_lo:[0,1] neg_hi:[0,1]
	v_pk_add_f32 v[4:5], v[4:5], v[20:21] neg_lo:[0,1] neg_hi:[0,1]
	v_pk_add_f32 v[6:7], v[6:7], v[22:23] neg_lo:[0,1] neg_hi:[0,1]
	s_waitcnt vmcnt(15)
; __device__ __forceinline__ unsigned pk4_fp8(float a, float b, float c, float d) { unsigned w = 0u; w = __builtin_amdgcn_cvt_pk_fp8_f32(clamp8(a), clamp8(b), w, false); w = __builtin_amdgcn_cvt_pk_fp8_f32(clamp8(c), clamp8(d), w, true); return w; }
; __device__ __forceinline__ void st8q(unsigned char* ptr, const float (&f)[8]) {
;     u32x2 w; w.x = pk4_fp8(4.f * f[0], 4.f * f[1], 4.f * f[2], 4.f * f[3]); w.y = pk4_fp8(4.f * f[4], 4.f * f[5], 4.f * f[6], 4.f * f[7]); *(u32x2*)ptr = w;
; }
; template <int WIN> __device__ __forceinline__ void pool_task(const Params& p, int t0, int c) {
;     ...
; #pragma unroll
;     for (int k = 0; k < 16; ++k) { const int t = t0 + k;
;         float cur[8], o[8]; ld8(PROJ + (size_t)t * INC + 5120 + c, cur);
;         const float inv = (k + 1 < WIN && t0 == 0) ? 1.0f / (float)(k + 1) : 1.0f / (float)WIN;
; #pragma unroll
;         for (int i = 0; i < 8; ++i) { tot[i] += cur[i]; o[i] = tot[i] * inv - cur[i]; ring[k % WIN][i] = cur[i]; }
;         st8q(YABC + (size_t)t * 3072 + 2048 + c, o);
; #pragma unroll
;         for (int i = 0; i < 8; ++i) tot[i] -= ring[(k + 1) % WIN][i];
;     }
; }
	v_lshlrev_b32_e32 v8, 16, v144
	v_and_b32_e32 v9, 0xffff0000, v144
	v_lshlrev_b32_e32 v10, 16, v145
	v_and_b32_e32 v11, 0xffff0000, v145
	v_lshlrev_b32_e32 v12, 16, v146
	v_and_b32_e32 v13, 0xffff0000, v146
	v_lshlrev_b32_e32 v14, 16, v147
	v_and_b32_e32 v15, 0xffff0000, v147
	v_pk_add_f32 v[0:1], v[0:1], v[8:9]
	v_pk_add_f32 v[2:3], v[2:3], v[10:11]
	v_pk_add_f32 v[4:5], v[4:5], v[12:13]
	v_pk_add_f32 v[6:7], v[6:7], v[14:15]
	v_mov_b32_e32 v38, 0x3e124925
	v_cndmask_b32_e32 v37, v36, v38, vcc
	v_fma_f32 v24, v37, v0, -v8
	v_fma_f32 v25, v37, v1, -v9
	v_fma_f32 v26, v37, v2, -v10
	v_fma_f32 v27, v37, v3, -v11
	v_fma_f32 v28, v37, v4, -v12
	v_fma_f32 v29, v37, v5, -v13
	v_fma_f32 v30, v37, v6, -v14
	v_fma_f32 v31, v37, v7, -v15
	v_pk_mul_f32 v[24:25], v[24:25], 4.0 op_sel_hi:[1,0]
	v_pk_mul_f32 v[26:27], v[26:27], 4.0 op_sel_hi:[1,0]
	v_pk_mul_f32 v[28:29], v[28:29], 4.0 op_sel_hi:[1,0]
	v_pk_mul_f32 v[30:31], v[30:31], 4.0 op_sel_hi:[1,0]
	v_med3_f32 v24, v24, s33, v229
	v_med3_f32 v25, v25, s33, v229
	v_med3_f32 v26, v26, s33, v229
	v_med3_f32 v27, v27, s33, v229
	v_med3_f32 v28, v28, s33, v229
	v_med3_f32 v29, v29, s33, v229
	v_med3_f32 v30, v30, s33, v229
	v_med3_f32 v31, v31, s33, v229
	v_add_u32_e32 v35, 0x4800, v34
	v_cvt_pk_fp8_f32 v40, v24, v25
	v_cvt_pk_fp8_f32 v41, v28, v29
	v_cvt_pk_fp8_f32 v40, v26, v27 op_sel:[0,0,1]
	v_cvt_pk_fp8_f32 v41, v30, v31 op_sel:[0,0,1]
	global_store_dwordx2 v35, v[40:41], s[4:5]
	v_lshlrev_b32_e32 v16, 16, v84
	v_and_b32_e32 v17, 0xffff0000, v84
	v_lshlrev_b32_e32 v18, 16, v85
	v_and_b32_e32 v19, 0xffff0000, v85
	v_lshlrev_b32_e32 v20, 16, v86
	v_and_b32_e32 v21, 0xffff0000, v86
	v_lshlrev_b32_e32 v22, 16, v87
	v_and_b32_e32 v23, 0xffff0000, v87
	v_pk_add_f32 v[0:1], v[0:1], v[16:17] neg_lo:[0,1] neg_hi:[0,1]
	v_pk_add_f32 v[2:3], v[2:3], v[18:19] neg_lo:[0,1] neg_hi:[0,1]
	v_pk_add_f32 v[4:5], v[4:5], v[20:21] neg_lo:[0,1] neg_hi:[0,1]
	v_pk_add_f32 v[6:7], v[6:7], v[22:23] neg_lo:[0,1] neg_hi:[0,1]
	s_waitcnt vmcnt(15)
	v_lshlrev_b32_e32 v8, 16, v148
	v_and_b32_e32 v9, 0xffff0000, v148
	v_lshlrev_b32_e32 v10, 16, v149
	v_and_b32_e32 v11, 0xffff0000, v149
	v_lshlrev_b32_e32 v12, 16, v150
	v_and_b32_e32 v13, 0xffff0000, v150
	v_lshlrev_b32_e32 v14, 16, v151
	v_and_b32_e32 v15, 0xffff0000, v151
	v_pk_add_f32 v[0:1], v[0:1], v[8:9]
	v_pk_add_f32 v[2:3], v[2:3], v[10:11]
	v_pk_add_f32 v[4:5], v[4:5], v[12:13]
	v_pk_add_f32 v[6:7], v[6:7], v[14:15]
	v_mov_b32_e32 v38, 0x3e000000
	v_cndmask_b32_e32 v37, v36, v38, vcc
	v_fma_f32 v24, v37, v0, -v8
	v_fma_f32 v25, v37, v1, -v9
	v_fma_f32 v26, v37, v2, -v10
	v_fma_f32 v27, v37, v3, -v11
	v_fma_f32 v28, v37, v4, -v12
	v_fma_f32 v29, v37, v5, -v13
	v_fma_f32 v30, v37, v6, -v14
	v_fma_f32 v31, v37, v7, -v15
	v_pk_mul_f32 v[24:25], v[24:25], 4.0 op_sel_hi:[1,0]
	v_pk_mul_f32 v[26:27], v[26:27], 4.0 op_sel_hi:[1,0]
	v_pk_mul_f32 v[28:29], v[28:29], 4.0 op_sel_hi:[1,0]
	v_pk_mul_f32 v[30:31], v[30:31], 4.0 op_sel_hi:[1,0]
	v_med3_f32 v24, v24, s33, v229
	v_med3_f32 v25, v25, s33, v229
	v_med3_f32 v26, v26, s33, v229
	v_med3_f32 v27, v27, s33, v229
	v_med3_f32 v28, v28, s33, v229
	v_med3_f32 v29, v29, s33, v229
	v_med3_f32 v30, v30, s33, v229
	v_med3_f32 v31, v31, s33, v229
	v_add_u32_e32 v35, 0x5400, v34
	v_cvt_pk_fp8_f32 v40, v24, v25
	v_cvt_pk_fp8_f32 v41, v28, v29
	v_cvt_pk_fp8_f32 v40, v26, v27 op_sel:[0,0,1]
	v_cvt_pk_fp8_f32 v41, v30, v31 op_sel:[0,0,1]
	global_store_dwordx2 v35, v[40:41], s[4:5]
	v_lshlrev_b32_e32 v16, 16, v88
	v_and_b32_e32 v17, 0xffff0000, v88
	v_lshlrev_b32_e32 v18, 16, v89
	v_and_b32_e32 v19, 0xffff0000, v89
	v_lshlrev_b32_e32 v20, 16, v90
	v_and_b32_e32 v21, 0xffff0000, v90
	v_lshlrev_b32_e32 v22, 16, v91
	v_and_b32_e32 v23, 0xffff0000, v91
	v_pk_add_f32 v[0:1], v[0:1], v[16:17] neg_lo:[0,1] neg_hi:[0,1]
	v_pk_add_f32 v[2:3], v[2:3], v[18:19] neg_lo:[0,1] neg_hi:[0,1]
	v_pk_add_f32 v[4:5], v[4:5], v[20:21] neg_lo:[0,1] neg_hi:[0,1]
	v_pk_add_f32 v[6:7], v[6:7], v[22:23] neg_lo:[0,1] neg_hi:[0,1]
	s_waitcnt vmcnt(15)
	v_lshlrev_b32_e32 v8, 16, v152
	v_and_b32_e32 v9, 0xffff0000, v152
	v_lshlrev_b32_e32 v10, 16, v153
	v_and_b32_e32 v11, 0xffff0000, v153
	v_lshlrev_b32_e32 v12, 16, v154
	v_and_b32_e32 v13, 0xffff0000, v154
	v_lshlrev_b32_e32 v14, 16, v155
	v_and_b32_e32 v15, 0xffff0000, v155
	v_pk_add_f32 v[0:1], v[0:1], v[8:9]
	v_pk_add_f32 v[2:3], v[2:3], v[10:11]
	v_pk_add_f32 v[4:5], v[4:5], v[12:13]
	v_pk_add_f32 v[6:7], v[6:7], v[14:15]
	v_mov_b32_e32 v38, 0x3de38e39
	v_cndmask_b32_e32 v37, v36, v38, vcc
	v_fma_f32 v24, v37, v0, -v8
	v_fma_f32 v25, v37, v1, -v9
	v_fma_f32 v26, v37, v2, -v10
	v_fma_f32 v27, v37, v3, -v11
	v_fma_f32 v28, v37, v4, -v12
	v_fma_f32 v29, v37, v5, -v13
	v_fma_f32 v30, v37, v6, -v14
	v_fma_f32 v31, v37, v7, -v15
	v_pk_mul_f32 v[24:25], v[24:25], 4.0 op_sel_hi:[1,0]
	v_pk_mul_f32 v[26:27], v[26:27], 4.0 op_sel_hi:[1,0]
	v_pk_mul_f32 v[28:29], v[28:29], 4.0 op_sel_hi:[1,0]
	v_pk_mul_f32 v[30:31], v[30:31], 4.0 op_sel_hi:[1,0]
	v_med3_f32 v24, v24, s33, v229
	v_med3_f32 v25, v25, s33, v229
	v_med3_f32 v26, v26, s33, v229
	v_med3_f32 v27, v27, s33, v229
	v_med3_f32 v28, v28, s33, v229
	v_med3_f32 v29, v29, s33, v229
	v_med3_f32 v30, v30, s33, v229
	v_med3_f32 v31, v31, s33, v229
	v_add_u32_e32 v35, 0x6000, v34
	v_cvt_pk_fp8_f32 v40, v24, v25
	v_cvt_pk_fp8_f32 v41, v28, v29
	v_cvt_pk_fp8_f32 v40, v26, v27 op_sel:[0,0,1]
	v_cvt_pk_fp8_f32 v41, v30, v31 op_sel:[0,0,1]
	global_store_dwordx2 v35, v[40:41], s[4:5]
	v_lshlrev_b32_e32 v16, 16, v92
	v_and_b32_e32 v17, 0xffff0000, v92
	v_lshlrev_b32_e32 v18, 16, v93
	v_and_b32_e32 v19, 0xffff0000, v93
	v_lshlrev_b32_e32 v20, 16, v94
	v_and_b32_e32 v21, 0xffff0000, v94
	v_lshlrev_b32_e32 v22, 16, v95
	v_and_b32_e32 v23, 0xffff0000, v95
	v_pk_add_f32 v[0:1], v[0:1], v[16:17] neg_lo:[0,1] neg_hi:[0,1]
	v_pk_add_f32 v[2:3], v[2:3], v[18:19] neg_lo:[0,1] neg_hi:[0,1]
	v_pk_add_f32 v[4:5], v[4:5], v[20:21] neg_lo:[0,1] neg_hi:[0,1]
	v_pk_add_f32 v[6:7], v[6:7], v[22:23] neg_lo:[0,1] neg_hi:[0,1]
	s_waitcnt vmcnt(15)
; __device__ __forceinline__ unsigned pk4_fp8(float a, float b, float c, float d) { unsigned w = 0u; w = __builtin_amdgcn_cvt_pk_fp8_f32(clamp8(a), clamp8(b), w, false); w = __builtin_amdgcn_cvt_pk_fp8_f32(clamp8(c), clamp8(d), w, true); return w; }
; __device__ __forceinline__ void st8q(unsigned char* ptr, const float (&f)[8]) {
;     u32x2 w; w.x = pk4_fp8(4.f * f[0], 4.f * f[1], 4.f * f[2], 4.f * f[3]); w.y = pk4_fp8(4.f * f[4], 4.f * f[5], 4.f * f[6], 4.f * f[7]); *(u32x2*)ptr = w;
; }
; template <int WIN> __device__ __forceinline__ void pool_task(const Params& p, int t0, int c) {
;     ...
; #pragma unroll
;     for (int k = 0; k < 16; ++k) { const int t = t0 + k;
;         float cur[8], o[8]; ld8(PROJ + (size_t)t * INC + 5120 + c, cur);
;         const float inv = (k + 1 < WIN && t0 == 0) ? 1.0f / (float)(k + 1) : 1.0f / (float)WIN;
; #pragma unroll
;         for (int i = 0; i < 8; ++i) { tot[i] += cur[i]; o[i] = tot[i] * inv - cur[i]; ring[k % WIN][i] = cur[i]; }
;         st8q(YABC + (size_t)t * 3072 + 2048 + c, o);
; #pragma unroll
;         for (int i = 0; i < 8; ++i) tot[i] -= ring[(k + 1) % WIN][i];
;     }
; }
	v_lshlrev_b32_e32 v8, 16, v156
	v_and_b32_e32 v9, 0xffff0000, v156
	v_lshlrev_b32_e32 v10, 16, v157
	v_and_b32_e32 v11, 0xffff0000, v157
	v_lshlrev_b32_e32 v12, 16, v158
	v_and_b32_e32 v13, 0xffff0000, v158
	v_lshlrev_b32_e32 v14, 16, v159
	v_and_b32_e32 v15, 0xffff0000, v159
	v_pk_add_f32 v[0:1], v[0:1], v[8:9]
	v_pk_add_f32 v[2:3], v[2:3], v[10:11]
	v_pk_add_f32 v[4:5], v[4:5], v[12:13]
	v_pk_add_f32 v[6:7], v[6:7], v[14:15]
	v_mov_b32_e32 v38, 0x3dcccccd
	v_cndmask_b32_e32 v37, v36, v38, vcc
	v_fma_f32 v24, v37, v0, -v8
	v_fma_f32 v25, v37, v1, -v9
	v_fma_f32 v26, v37, v2, -v10
	v_fma_f32 v27, v37, v3, -v11
	v_fma_f32 v28, v37, v4, -v12
	v_fma_f32 v29, v37, v5, -v13
	v_fma_f32 v30, v37, v6, -v14
	v_fma_f32 v31, v37, v7, -v15
	v_pk_mul_f32 v[24:25], v[24:25], 4.0 op_sel_hi:[1,0]
	v_pk_mul_f32 v[26:27], v[26:27], 4.0 op_sel_hi:[1,0]
	v_pk_mul_f32 v[28:29], v[28:29], 4.0 op_sel_hi:[1,0]
	v_pk_mul_f32 v[30:31], v[30:31], 4.0 op_sel_hi:[1,0]
	v_med3_f32 v24, v24, s33, v229
	v_med3_f32 v25, v25, s33, v229
	v_med3_f32 v26, v26, s33, v229
	v_med3_f32 v27, v27, s33, v229
	v_med3_f32 v28, v28, s33, v229
	v_med3_f32 v29, v29, s33, v229
	v_med3_f32 v30, v30, s33, v229
	v_med3_f32 v31, v31, s33, v229
	v_add_u32_e32 v35, 0x6c00, v34
	v_cvt_pk_fp8_f32 v40, v24, v25
	v_cvt_pk_fp8_f32 v41, v28, v29
	v_cvt_pk_fp8_f32 v40, v26, v27 op_sel:[0,0,1]
	v_cvt_pk_fp8_f32 v41, v30, v31 op_sel:[0,0,1]
	global_store_dwordx2 v35, v[40:41], s[4:5]
	v_lshlrev_b32_e32 v16, 16, v96
	v_and_b32_e32 v17, 0xffff0000, v96
	v_lshlrev_b32_e32 v18, 16, v97
	v_and_b32_e32 v19, 0xffff0000, v97
	v_lshlrev_b32_e32 v20, 16, v98
	v_and_b32_e32 v21, 0xffff0000, v98
	v_lshlrev_b32_e32 v22, 16, v99
	v_and_b32_e32 v23, 0xffff0000, v99
	v_pk_add_f32 v[0:1], v[0:1], v[16:17] neg_lo:[0,1] neg_hi:[0,1]
	v_pk_add_f32 v[2:3], v[2:3], v[18:19] neg_lo:[0,1] neg_hi:[0,1]
	v_pk_add_f32 v[4:5], v[4:5], v[20:21] neg_lo:[0,1] neg_hi:[0,1]
	v_pk_add_f32 v[6:7], v[6:7], v[22:23] neg_lo:[0,1] neg_hi:[0,1]
	s_waitcnt vmcnt(15)
	v_lshlrev_b32_e32 v8, 16, v160
	v_and_b32_e32 v9, 0xffff0000, v160
	v_lshlrev_b32_e32 v10, 16, v161
	v_and_b32_e32 v11, 0xffff0000, v161
	v_lshlrev_b32_e32 v12, 16, v162
	v_and_b32_e32 v13, 0xffff0000, v162
	v_lshlrev_b32_e32 v14, 16, v163
	v_and_b32_e32 v15, 0xffff0000, v163
	v_pk_add_f32 v[0:1], v[0:1], v[8:9]
	v_pk_add_f32 v[2:3], v[2:3], v[10:11]
	v_pk_add_f32 v[4:5], v[4:5], v[12:13]
	v_pk_add_f32 v[6:7], v[6:7], v[14:15]
	v_mov_b32_e32 v38, 0x3dba2e8c
	v_cndmask_b32_e32 v37, v36, v38, vcc
	v_fma_f32 v24, v37, v0, -v8
	v_fma_f32 v25, v37, v1, -v9
	v_fma_f32 v26, v37, v2, -v10
	v_fma_f32 v27, v37, v3, -v11
	v_fma_f32 v28, v37, v4, -v12
	v_fma_f32 v29, v37, v5, -v13
	v_fma_f32 v30, v37, v6, -v14
	v_fma_f32 v31, v37, v7, -v15
	v_pk_mul_f32 v[24:25], v[24:25], 4.0 op_sel_hi:[1,0]
	v_pk_mul_f32 v[26:27], v[26:27], 4.0 op_sel_hi:[1,0]
	v_pk_mul_f32 v[28:29], v[28:29], 4.0 op_sel_hi:[1,0]
	v_pk_mul_f32 v[30:31], v[30:31], 4.0 op_sel_hi:[1,0]
	v_med3_f32 v24, v24, s33, v229
	v_med3_f32 v25, v25, s33, v229
	v_med3_f32 v26, v26, s33, v229
	v_med3_f32 v27, v27, s33, v229
	v_med3_f32 v28, v28, s33, v229
	v_med3_f32 v29, v29, s33, v229
	v_med3_f32 v30, v30, s33, v229
	v_med3_f32 v31, v31, s33, v229
	v_add_u32_e32 v35, 0x7800, v34
	v_cvt_pk_fp8_f32 v40, v24, v25
	v_cvt_pk_fp8_f32 v41, v28, v29
	v_cvt_pk_fp8_f32 v40, v26, v27 op_sel:[0,0,1]
	v_cvt_pk_fp8_f32 v41, v30, v31 op_sel:[0,0,1]
	global_store_dwordx2 v35, v[40:41], s[4:5]
	v_lshlrev_b32_e32 v16, 16, v100
	v_and_b32_e32 v17, 0xffff0000, v100
	v_lshlrev_b32_e32 v18, 16, v101
	v_and_b32_e32 v19, 0xffff0000, v101
	v_lshlrev_b32_e32 v20, 16, v102
	v_and_b32_e32 v21, 0xffff0000, v102
	v_lshlrev_b32_e32 v22, 16, v103
	v_and_b32_e32 v23, 0xffff0000, v103
	v_pk_add_f32 v[0:1], v[0:1], v[16:17] neg_lo:[0,1] neg_hi:[0,1]
	v_pk_add_f32 v[2:3], v[2:3], v[18:19] neg_lo:[0,1] neg_hi:[0,1]
	v_pk_add_f32 v[4:5], v[4:5], v[20:21] neg_lo:[0,1] neg_hi:[0,1]
	v_pk_add_f32 v[6:7], v[6:7], v[22:23] neg_lo:[0,1] neg_hi:[0,1]
	s_waitcnt vmcnt(15)
	v_lshlrev_b32_e32 v8, 16, v164
	v_and_b32_e32 v9, 0xffff0000, v164
	v_lshlrev_b32_e32 v10, 16, v165
	v_and_b32_e32 v11, 0xffff0000, v165
	v_lshlrev_b32_e32 v12, 16, v166
	v_and_b32_e32 v13, 0xffff0000, v166
	v_lshlrev_b32_e32 v14, 16, v167
	v_and_b32_e32 v15, 0xffff0000, v167
	v_pk_add_f32 v[0:1], v[0:1], v[8:9]
	v_pk_add_f32 v[2:3], v[2:3], v[10:11]
	v_pk_add_f32 v[4:5], v[4:5], v[12:13]
	v_pk_add_f32 v[6:7], v[6:7], v[14:15]
	v_mov_b32_e32 v38, 0x3daaaaab
	v_cndmask_b32_e32 v37, v36, v38, vcc
	v_fma_f32 v24, v37, v0, -v8
	v_fma_f32 v25, v37, v1, -v9
	v_fma_f32 v26, v37, v2, -v10
	v_fma_f32 v27, v37, v3, -v11
	v_fma_f32 v28, v37, v4, -v12
	v_fma_f32 v29, v37, v5, -v13
	v_fma_f32 v30, v37, v6, -v14
	v_fma_f32 v31, v37, v7, -v15
	v_pk_mul_f32 v[24:25], v[24:25], 4.0 op_sel_hi:[1,0]
	v_pk_mul_f32 v[26:27], v[26:27], 4.0 op_sel_hi:[1,0]
	v_pk_mul_f32 v[28:29], v[28:29], 4.0 op_sel_hi:[1,0]
	v_pk_mul_f32 v[30:31], v[30:31], 4.0 op_sel_hi:[1,0]
	v_med3_f32 v24, v24, s33, v229
	v_med3_f32 v25, v25, s33, v229
	v_med3_f32 v26, v26, s33, v229
	v_med3_f32 v27, v27, s33, v229
	v_med3_f32 v28, v28, s33, v229
	v_med3_f32 v29, v29, s33, v229
	v_med3_f32 v30, v30, s33, v229
	v_med3_f32 v31, v31, s33, v229
	v_add_u32_e32 v35, 0x8400, v34
	v_cvt_pk_fp8_f32 v40, v24, v25
	v_cvt_pk_fp8_f32 v41, v28, v29
	v_cvt_pk_fp8_f32 v40, v26, v27 op_sel:[0,0,1]
	v_cvt_pk_fp8_f32 v41, v30, v31 op_sel:[0,0,1]
	global_store_dwordx2 v35, v[40:41], s[4:5]
	v_lshlrev_b32_e32 v16, 16, v104
	v_and_b32_e32 v17, 0xffff0000, v104
	v_lshlrev_b32_e32 v18, 16, v105
	v_and_b32_e32 v19, 0xffff0000, v105
	v_lshlrev_b32_e32 v20, 16, v106
	v_and_b32_e32 v21, 0xffff0000, v106
	v_lshlrev_b32_e32 v22, 16, v107
	v_and_b32_e32 v23, 0xffff0000, v107
	v_pk_add_f32 v[0:1], v[0:1], v[16:17] neg_lo:[0,1] neg_hi:[0,1]
	v_pk_add_f32 v[2:3], v[2:3], v[18:19] neg_lo:[0,1] neg_hi:[0,1]
	v_pk_add_f32 v[4:5], v[4:5], v[20:21] neg_lo:[0,1] neg_hi:[0,1]
	v_pk_add_f32 v[6:7], v[6:7], v[22:23] neg_lo:[0,1] neg_hi:[0,1]
	s_waitcnt vmcnt(15)
; __device__ __forceinline__ unsigned pk4_fp8(float a, float b, float c, float d) { unsigned w = 0u; w = __builtin_amdgcn_cvt_pk_fp8_f32(clamp8(a), clamp8(b), w, false); w = __builtin_amdgcn_cvt_pk_fp8_f32(clamp8(c), clamp8(d), w, true); return w; }
; __device__ __forceinline__ void st8q(unsigned char* ptr, const float (&f)[8]) {
;     u32x2 w; w.x = pk4_fp8(4.f * f[0], 4.f * f[1], 4.f * f[2], 4.f * f[3]); w.y = pk4_fp8(4.f * f[4], 4.f * f[5], 4.f * f[6], 4.f * f[7]); *(u32x2*)ptr = w;
; }
; template <int WIN> __device__ __forceinline__ void pool_task(const Params& p, int t0, int c) {
;     ...
; #pragma unroll
;     for (int k = 0; k < 16; ++k) { const int t = t0 + k;
;         float cur[8], o[8]; ld8(PROJ + (size_t)t * INC + 5120 + c, cur);
;         const float inv = (k + 1 < WIN && t0 == 0) ? 1.0f / (float)(k + 1) : 1.0f / (float)WIN;
; #pragma unroll
;         for (int i = 0; i < 8; ++i) { tot[i] += cur[i]; o[i] = tot[i] * inv - cur[i]; ring[k % WIN][i] = cur[i]; }
;         st8q(YABC + (size_t)t * 3072 + 2048 + c, o);
; #pragma unroll
;         for (int i = 0; i < 8; ++i) tot[i] -= ring[(k + 1) % WIN][i];
;     }
; }
	v_lshlrev_b32_e32 v8, 16, v168
	v_and_b32_e32 v9, 0xffff0000, v168
	v_lshlrev_b32_e32 v10, 16, v169
	v_and_b32_e32 v11, 0xffff0000, v169
	v_lshlrev_b32_e32 v12, 16, v170
	v_and_b32_e32 v13, 0xffff0000, v170
	v_lshlrev_b32_e32 v14, 16, v171
	v_and_b32_e32 v15, 0xffff0000, v171
	v_pk_add_f32 v[0:1], v[0:1], v[8:9]
	v_pk_add_f32 v[2:3], v[2:3], v[10:11]
	v_pk_add_f32 v[4:5], v[4:5], v[12:13]
	v_pk_add_f32 v[6:7], v[6:7], v[14:15]
	v_mov_b32_e32 v38, 0x3d9d89d9
	v_cndmask_b32_e32 v37, v36, v38, vcc
	v_fma_f32 v24, v37, v0, -v8
	v_fma_f32 v25, v37, v1, -v9
	v_fma_f32 v26, v37, v2, -v10
	v_fma_f32 v27, v37, v3, -v11
	v_fma_f32 v28, v37, v4, -v12
	v_fma_f32 v29, v37, v5, -v13
	v_fma_f32 v30, v37, v6, -v14
	v_fma_f32 v31, v37, v7, -v15
	v_pk_mul_f32 v[24:25], v[24:25], 4.0 op_sel_hi:[1,0]
	v_pk_mul_f32 v[26:27], v[26:27], 4.0 op_sel_hi:[1,0]
	v_pk_mul_f32 v[28:29], v[28:29], 4.0 op_sel_hi:[1,0]
	v_pk_mul_f32 v[30:31], v[30:31], 4.0 op_sel_hi:[1,0]
	v_med3_f32 v24, v24, s33, v229
	v_med3_f32 v25, v25, s33, v229
	v_med3_f32 v26, v26, s33, v229
	v_med3_f32 v27, v27, s33, v229
	v_med3_f32 v28, v28, s33, v229
	v_med3_f32 v29, v29, s33, v229
	v_med3_f32 v30, v30, s33, v229
	v_med3_f32 v31, v31, s33, v229
	v_add_u32_e32 v35, 0x9000, v34
	v_cvt_pk_fp8_f32 v40, v24, v25
	v_cvt_pk_fp8_f32 v41, v28, v29
	v_cvt_pk_fp8_f32 v40, v26, v27 op_sel:[0,0,1]
	v_cvt_pk_fp8_f32 v41, v30, v31 op_sel:[0,0,1]
	global_store_dwordx2 v35, v[40:41], s[4:5]
	v_lshlrev_b32_e32 v16, 16, v108
	v_and_b32_e32 v17, 0xffff0000, v108
	v_lshlrev_b32_e32 v18, 16, v109
	v_and_b32_e32 v19, 0xffff0000, v109
	v_lshlrev_b32_e32 v20, 16, v110
	v_and_b32_e32 v21, 0xffff0000, v110
	v_lshlrev_b32_e32 v22, 16, v111
	v_and_b32_e32 v23, 0xffff0000, v111
	v_pk_add_f32 v[0:1], v[0:1], v[16:17] neg_lo:[0,1] neg_hi:[0,1]
	v_pk_add_f32 v[2:3], v[2:3], v[18:19] neg_lo:[0,1] neg_hi:[0,1]
	v_pk_add_f32 v[4:5], v[4:5], v[20:21] neg_lo:[0,1] neg_hi:[0,1]
	v_pk_add_f32 v[6:7], v[6:7], v[22:23] neg_lo:[0,1] neg_hi:[0,1]
	s_waitcnt vmcnt(15)
	v_lshlrev_b32_e32 v8, 16, v172
	v_and_b32_e32 v9, 0xffff0000, v172
	v_lshlrev_b32_e32 v10, 16, v173
	v_and_b32_e32 v11, 0xffff0000, v173
	v_lshlrev_b32_e32 v12, 16, v174
	v_and_b32_e32 v13, 0xffff0000, v174
	v_lshlrev_b32_e32 v14, 16, v175
	v_and_b32_e32 v15, 0xffff0000, v175
	v_pk_add_f32 v[0:1], v[0:1], v[8:9]
	v_pk_add_f32 v[2:3], v[2:3], v[10:11]
	v_pk_add_f32 v[4:5], v[4:5], v[12:13]
	v_pk_add_f32 v[6:7], v[6:7], v[14:15]
	v_mov_b32_e32 v38, 0x3d924925
	v_cndmask_b32_e32 v37, v36, v38, vcc
	v_fma_f32 v24, v37, v0, -v8
	v_fma_f32 v25, v37, v1, -v9
	v_fma_f32 v26, v37, v2, -v10
	v_fma_f32 v27, v37, v3, -v11
	v_fma_f32 v28, v37, v4, -v12
	v_fma_f32 v29, v37, v5, -v13
	v_fma_f32 v30, v37, v6, -v14
	v_fma_f32 v31, v37, v7, -v15
	v_pk_mul_f32 v[24:25], v[24:25], 4.0 op_sel_hi:[1,0]
	v_pk_mul_f32 v[26:27], v[26:27], 4.0 op_sel_hi:[1,0]
	v_pk_mul_f32 v[28:29], v[28:29], 4.0 op_sel_hi:[1,0]
	v_pk_mul_f32 v[30:31], v[30:31], 4.0 op_sel_hi:[1,0]
	v_med3_f32 v24, v24, s33, v229
	v_med3_f32 v25, v25, s33, v229
	v_med3_f32 v26, v26, s33, v229
	v_med3_f32 v27, v27, s33, v229
	v_med3_f32 v28, v28, s33, v229
	v_med3_f32 v29, v29, s33, v229
	v_med3_f32 v30, v30, s33, v229
	v_med3_f32 v31, v31, s33, v229
	v_add_u32_e32 v35, 0x9c00, v34
	v_cvt_pk_fp8_f32 v40, v24, v25
	v_cvt_pk_fp8_f32 v41, v28, v29
	v_cvt_pk_fp8_f32 v40, v26, v27 op_sel:[0,0,1]
	v_cvt_pk_fp8_f32 v41, v30, v31 op_sel:[0,0,1]
	global_store_dwordx2 v35, v[40:41], s[4:5]
	v_lshlrev_b32_e32 v16, 16, v112
	v_and_b32_e32 v17, 0xffff0000, v112
	v_lshlrev_b32_e32 v18, 16, v113
	v_and_b32_e32 v19, 0xffff0000, v113
	v_lshlrev_b32_e32 v20, 16, v114
	v_and_b32_e32 v21, 0xffff0000, v114
	v_lshlrev_b32_e32 v22, 16, v115
	v_and_b32_e32 v23, 0xffff0000, v115
	v_pk_add_f32 v[0:1], v[0:1], v[16:17] neg_lo:[0,1] neg_hi:[0,1]
	v_pk_add_f32 v[2:3], v[2:3], v[18:19] neg_lo:[0,1] neg_hi:[0,1]
	v_pk_add_f32 v[4:5], v[4:5], v[20:21] neg_lo:[0,1] neg_hi:[0,1]
	v_pk_add_f32 v[6:7], v[6:7], v[22:23] neg_lo:[0,1] neg_hi:[0,1]
	s_waitcnt vmcnt(15)
	v_lshlrev_b32_e32 v8, 16, v176
	v_and_b32_e32 v9, 0xffff0000, v176
	v_lshlrev_b32_e32 v10, 16, v177
	v_and_b32_e32 v11, 0xffff0000, v177
	v_lshlrev_b32_e32 v12, 16, v178
	v_and_b32_e32 v13, 0xffff0000, v178
	v_lshlrev_b32_e32 v14, 16, v179
	v_and_b32_e32 v15, 0xffff0000, v179
	v_pk_add_f32 v[0:1], v[0:1], v[8:9]
	v_pk_add_f32 v[2:3], v[2:3], v[10:11]
	v_pk_add_f32 v[4:5], v[4:5], v[12:13]
	v_pk_add_f32 v[6:7], v[6:7], v[14:15]
	v_mov_b32_e32 v38, 0x3d888889
	v_cndmask_b32_e32 v37, v36, v38, vcc
	v_fma_f32 v24, v37, v0, -v8
	v_fma_f32 v25, v37, v1, -v9
	v_fma_f32 v26, v37, v2, -v10
	v_fma_f32 v27, v37, v3, -v11
	v_fma_f32 v28, v37, v4, -v12
	v_fma_f32 v29, v37, v5, -v13
	v_fma_f32 v30, v37, v6, -v14
	v_fma_f32 v31, v37, v7, -v15
	v_pk_mul_f32 v[24:25], v[24:25], 4.0 op_sel_hi:[1,0]
	v_pk_mul_f32 v[26:27], v[26:27], 4.0 op_sel_hi:[1,0]
	v_pk_mul_f32 v[28:29], v[28:29], 4.0 op_sel_hi:[1,0]
	v_pk_mul_f32 v[30:31], v[30:31], 4.0 op_sel_hi:[1,0]
	v_med3_f32 v24, v24, s33, v229
	v_med3_f32 v25, v25, s33, v229
	v_med3_f32 v26, v26, s33, v229
	v_med3_f32 v27, v27, s33, v229
	v_med3_f32 v28, v28, s33, v229
	v_med3_f32 v29, v29, s33, v229
	v_med3_f32 v30, v30, s33, v229
	v_med3_f32 v31, v31, s33, v229
	v_add_u32_e32 v35, 0xa800, v34
	v_cvt_pk_fp8_f32 v40, v24, v25
	v_cvt_pk_fp8_f32 v41, v28, v29
	v_cvt_pk_fp8_f32 v40, v26, v27 op_sel:[0,0,1]
	v_cvt_pk_fp8_f32 v41, v30, v31 op_sel:[0,0,1]
	global_store_dwordx2 v35, v[40:41], s[4:5]
	v_lshlrev_b32_e32 v16, 16, v116
	v_and_b32_e32 v17, 0xffff0000, v116
	v_lshlrev_b32_e32 v18, 16, v117
	v_and_b32_e32 v19, 0xffff0000, v117
	v_lshlrev_b32_e32 v20, 16, v118
	v_and_b32_e32 v21, 0xffff0000, v118
	v_lshlrev_b32_e32 v22, 16, v119
	v_and_b32_e32 v23, 0xffff0000, v119
	v_pk_add_f32 v[0:1], v[0:1], v[16:17] neg_lo:[0,1] neg_hi:[0,1]
	v_pk_add_f32 v[2:3], v[2:3], v[18:19] neg_lo:[0,1] neg_hi:[0,1]
	v_pk_add_f32 v[4:5], v[4:5], v[20:21] neg_lo:[0,1] neg_hi:[0,1]
	v_pk_add_f32 v[6:7], v[6:7], v[22:23] neg_lo:[0,1] neg_hi:[0,1]
	s_waitcnt vmcnt(15)
; template <int WIN> __device__ __forceinline__ void pool_task(const Params& p, int t0, int c) {
;     const bf16* PROJ = (const bf16*)(p.ws + WS_PROJ); unsigned char* YABC = p.ws + WS_YABC;
;     float ring[WIN][8], tot[8];
; #pragma unroll
;     for (int i = 0; i < 8; ++i) tot[i] = 0.f;
; #pragma unroll
;     for (int d = 1 - WIN; d < 0; ++d) {
;         if (t0 > 0) { ld8(PROJ + (size_t)(t0 + d) * INC + 5120 + c, ring[(d + WIN) % WIN]);
; #pragma unroll
;             for (int i = 0; i < 8; ++i) tot[i] += ring[(d + WIN) % WIN][i]; }
;         else {
; #pragma unroll
;             for (int i = 0; i < 8; ++i) ring[(d + WIN) % WIN][i] = 0.f; }
;     }
; #pragma unroll
;     for (int k = 0; k < 16; ++k) { const int t = t0 + k;
;         float cur[8], o[8]; ld8(PROJ + (size_t)t * INC + 5120 + c, cur);
;         const float inv = (k + 1 < WIN && t0 == 0) ? 1.0f / (float)(k + 1) : 1.0f / (float)WIN;
; #pragma unroll
;         for (int i = 0; i < 8; ++i) { tot[i] += cur[i]; o[i] = tot[i] * inv - cur[i]; ring[k % WIN][i] = cur[i]; }
;         st8q(YABC + (size_t)t * 3072 + 2048 + c, o);
; #pragma unroll
;         for (int i = 0; i < 8; ++i) tot[i] -= ring[(k + 1) % WIN][i];
;     }
; }
	v_lshlrev_b32_e32 v8, 16, v180
	v_and_b32_e32 v9, 0xffff0000, v180
	v_lshlrev_b32_e32 v10, 16, v181
	v_and_b32_e32 v11, 0xffff0000, v181
	v_lshlrev_b32_e32 v12, 16, v182
	v_and_b32_e32 v13, 0xffff0000, v182
	v_lshlrev_b32_e32 v14, 16, v183
	v_and_b32_e32 v15, 0xffff0000, v183
	v_pk_add_f32 v[0:1], v[0:1], v[8:9]
	v_pk_add_f32 v[2:3], v[2:3], v[10:11]
	v_pk_add_f32 v[4:5], v[4:5], v[12:13]
	v_pk_add_f32 v[6:7], v[6:7], v[14:15]
	v_fma_f32 v24, v36, v0, -v8
	v_fma_f32 v25, v36, v1, -v9
	v_fma_f32 v26, v36, v2, -v10
	v_fma_f32 v27, v36, v3, -v11
	v_fma_f32 v28, v36, v4, -v12
	v_fma_f32 v29, v36, v5, -v13
	v_fma_f32 v30, v36, v6, -v14
	v_fma_f32 v31, v36, v7, -v15
	v_pk_mul_f32 v[24:25], v[24:25], 4.0 op_sel_hi:[1,0]
	v_pk_mul_f32 v[26:27], v[26:27], 4.0 op_sel_hi:[1,0]
	v_pk_mul_f32 v[28:29], v[28:29], 4.0 op_sel_hi:[1,0]
	v_pk_mul_f32 v[30:31], v[30:31], 4.0 op_sel_hi:[1,0]
	v_med3_f32 v24, v24, s33, v229
	v_med3_f32 v25, v25, s33, v229
	v_med3_f32 v26, v26, s33, v229
	v_med3_f32 v27, v27, s33, v229
	v_med3_f32 v28, v28, s33, v229
	v_med3_f32 v29, v29, s33, v229
	v_med3_f32 v30, v30, s33, v229
	v_med3_f32 v31, v31, s33, v229
	v_add_u32_e32 v35, 0xb400, v34
	v_cvt_pk_fp8_f32 v40, v24, v25
	v_cvt_pk_fp8_f32 v41, v28, v29
	v_cvt_pk_fp8_f32 v40, v26, v27 op_sel:[0,0,1]
	v_cvt_pk_fp8_f32 v41, v30, v31 op_sel:[0,0,1]
	global_store_dwordx2 v35, v[40:41], s[4:5]
	s_branch .Lmy_cp_next
.Lmy_pool_w2:
	v_and_b32_e32 v35, 31, v67
	v_lshrrev_b32_e32 v32, 8, v67
	s_lshl_b32 s10, s7, 1
	v_add_lshl_u32 v32, v32, s10, 1
	v_bfe_u32 v38, v67, 5, 1
	v_add_lshl_u32 v32, v32, v38, 4
	v_or_b32_e32 v35, 0, v35
	v_mul_u32_u24_e32 v33, 0x3000, v32
	v_lshl_add_u32 v33, v35, 4, v33
	v_add_u32_e32 v33, 0x1000, v33
	v_mul_u32_u24_e32 v34, 0xc00, v32
	v_lshl_add_u32 v34, v35, 3, v34
	v_add_u32_e32 v34, 0x800, v34
	v_mov_b32_e32 v56, 0
	v_mov_b32_e32 v57, 0
	v_mov_b32_e32 v58, 0
	v_mov_b32_e32 v59, 0
	v_cmp_ne_u32_e32 vcc, 0, v32
	s_and_saveexec_b64 s[10:11], vcc
	v_add_u32_e32 v35, 0xffffd000, v33
	global_load_dwordx4 v[56:59], v35, s[2:3] nt
	s_mov_b64 exec, s[0:1]
	global_load_dwordx4 v[60:63], v33, s[2:3] nt
	v_add_u32_e32 v35, 0x3000, v33
	global_load_dwordx4 v[68:71], v35, s[2:3] nt
	v_add_u32_e32 v35, 0x6000, v33
	global_load_dwordx4 v[72:75], v35, s[2:3] nt
	v_add_u32_e32 v35, 0x9000, v33
	global_load_dwordx4 v[76:79], v35, s[2:3] nt
	v_add_u32_e32 v35, 0xc000, v33
	global_load_dwordx4 v[80:83], v35, s[2:3] nt
	v_add_u32_e32 v35, 0xf000, v33
	global_load_dwordx4 v[84:87], v35, s[2:3] nt
	v_add_u32_e32 v35, 0x12000, v33
	global_load_dwordx4 v[88:91], v35, s[2:3] nt
	v_add_u32_e32 v35, 0x15000, v33
	global_load_dwordx4 v[92:95], v35, s[2:3] nt
	v_add_u32_e32 v35, 0x18000, v33
	global_load_dwordx4 v[96:99], v35, s[2:3] nt
	v_add_u32_e32 v35, 0x1b000, v33
	global_load_dwordx4 v[100:103], v35, s[2:3] nt
	v_add_u32_e32 v35, 0x1e000, v33
	global_load_dwordx4 v[104:107], v35, s[2:3] nt
	v_add_u32_e32 v35, 0x21000, v33
	global_load_dwordx4 v[108:111], v35, s[2:3] nt
	v_add_u32_e32 v35, 0x24000, v33
	global_load_dwordx4 v[112:115], v35, s[2:3] nt
	v_add_u32_e32 v35, 0x27000, v33
	global_load_dwordx4 v[116:119], v35, s[2:3] nt
	v_add_u32_e32 v35, 0x2a000, v33
	global_load_dwordx4 v[120:123], v35, s[2:3] nt
	v_add_u32_e32 v35, 0x2d000, v33
	global_load_dwordx4 v[124:127], v35, s[2:3] nt
	v_cmp_eq_u32_e32 vcc, 0, v32
	v_mov_b32_e32 v36, 0x3f000000
	v_mov_b64_e32 v[0:1], 0
	v_mov_b64_e32 v[2:3], 0
	v_mov_b64_e32 v[4:5], 0
	v_mov_b64_e32 v[6:7], 0
	s_waitcnt vmcnt(16)
	v_lshlrev_b32_e32 v8, 16, v56
	v_and_b32_e32 v9, 0xffff0000, v56
	v_lshlrev_b32_e32 v10, 16, v57
	v_and_b32_e32 v11, 0xffff0000, v57
	v_lshlrev_b32_e32 v12, 16, v58
	v_and_b32_e32 v13, 0xffff0000, v58
	v_lshlrev_b32_e32 v14, 16, v59
	v_and_b32_e32 v15, 0xffff0000, v59
	v_pk_add_f32 v[0:1], v[0:1], v[8:9]
	v_pk_add_f32 v[2:3], v[2:3], v[10:11]
	v_pk_add_f32 v[4:5], v[4:5], v[12:13]
	v_pk_add_f32 v[6:7], v[6:7], v[14:15]
	s_waitcnt vmcnt(15)
	v_lshlrev_b32_e32 v8, 16, v60
	v_and_b32_e32 v9, 0xffff0000, v60
	v_lshlrev_b32_e32 v10, 16, v61
	v_and_b32_e32 v11, 0xffff0000, v61
	v_lshlrev_b32_e32 v12, 16, v62
	v_and_b32_e32 v13, 0xffff0000, v62
	v_lshlrev_b32_e32 v14, 16, v63
	v_and_b32_e32 v15, 0xffff0000, v63
	v_pk_add_f32 v[0:1], v[0:1], v[8:9]
	v_pk_add_f32 v[2:3], v[2:3], v[10:11]
	v_pk_add_f32 v[4:5], v[4:5], v[12:13]
	v_pk_add_f32 v[6:7], v[6:7], v[14:15]
	v_mov_b32_e32 v38, 0x3f800000
	v_cndmask_b32_e32 v37, v36, v38, vcc
	v_fma_f32 v24, v37, v0, -v8
	v_fma_f32 v25, v37, v1, -v9
	v_fma_f32 v26, v37, v2, -v10
	v_fma_f32 v27, v37, v3, -v11
	v_fma_f32 v28, v37, v4, -v12
	v_fma_f32 v29, v37, v5, -v13
	v_fma_f32 v30, v37, v6, -v14
	v_fma_f32 v31, v37, v7, -v15
	v_pk_mul_f32 v[24:25], v[24:25], 4.0 op_sel_hi:[1,0]
	v_pk_mul_f32 v[26:27], v[26:27], 4.0 op_sel_hi:[1,0]
	v_pk_mul_f32 v[28:29], v[28:29], 4.0 op_sel_hi:[1,0]
	v_pk_mul_f32 v[30:31], v[30:31], 4.0 op_sel_hi:[1,0]
	v_med3_f32 v24, v24, s33, v229
	v_med3_f32 v25, v25, s33, v229
	v_med3_f32 v26, v26, s33, v229
	v_med3_f32 v27, v27, s33, v229
	v_med3_f32 v28, v28, s33, v229
	v_med3_f32 v29, v29, s33, v229
	v_med3_f32 v30, v30, s33, v229
	v_med3_f32 v31, v31, s33, v229
	v_cvt_pk_fp8_f32 v40, v24, v25
	v_cvt_pk_fp8_f32 v41, v28, v29
	v_cvt_pk_fp8_f32 v40, v26, v27 op_sel:[0,0,1]
	v_cvt_pk_fp8_f32 v41, v30, v31 op_sel:[0,0,1]
	global_store_dwordx2 v34, v[40:41], s[4:5]
	v_lshlrev_b32_e32 v16, 16, v56
	v_and_b32_e32 v17, 0xffff0000, v56
	v_lshlrev_b32_e32 v18, 16, v57
	v_and_b32_e32 v19, 0xffff0000, v57
	v_lshlrev_b32_e32 v20, 16, v58
	v_and_b32_e32 v21, 0xffff0000, v58
	v_lshlrev_b32_e32 v22, 16, v59
	v_and_b32_e32 v23, 0xffff0000, v59
	v_pk_add_f32 v[0:1], v[0:1], v[16:17] neg_lo:[0,1] neg_hi:[0,1]
	v_pk_add_f32 v[2:3], v[2:3], v[18:19] neg_lo:[0,1] neg_hi:[0,1]
	v_pk_add_f32 v[4:5], v[4:5], v[20:21] neg_lo:[0,1] neg_hi:[0,1]
	v_pk_add_f32 v[6:7], v[6:7], v[22:23] neg_lo:[0,1] neg_hi:[0,1]
	s_waitcnt vmcnt(15)
; __device__ __forceinline__ unsigned pk4_fp8(float a, float b, float c, float d) { unsigned w = 0u; w = __builtin_amdgcn_cvt_pk_fp8_f32(clamp8(a), clamp8(b), w, false); w = __builtin_amdgcn_cvt_pk_fp8_f32(clamp8(c), clamp8(d), w, true); return w; }
; __device__ __forceinline__ void st8q(unsigned char* ptr, const float (&f)[8]) {
;     u32x2 w; w.x = pk4_fp8(4.f * f[0], 4.f * f[1], 4.f * f[2], 4.f * f[3]); w.y = pk4_fp8(4.f * f[4], 4.f * f[5], 4.f * f[6], 4.f * f[7]); *(u32x2*)ptr = w;
; }
; template <int WIN> __device__ __forceinline__ void pool_task(const Params& p, int t0, int c) {
;     ...
; #pragma unroll
;     for (int k = 0; k < 16; ++k) { const int t = t0 + k;
;         float cur[8], o[8]; ld8(PROJ + (size_t)t * INC + 5120 + c, cur);
;         const float inv = (k + 1 < WIN && t0 == 0) ? 1.0f / (float)(k + 1) : 1.0f / (float)WIN;
; #pragma unroll
;         for (int i = 0; i < 8; ++i) { tot[i] += cur[i]; o[i] = tot[i] * inv - cur[i]; ring[k % WIN][i] = cur[i]; }
;         st8q(YABC + (size_t)t * 3072 + 2048 + c, o);
; #pragma unroll
;         for (int i = 0; i < 8; ++i) tot[i] -= ring[(k + 1) % WIN][i];
;     }
; }
	v_lshlrev_b32_e32 v8, 16, v68
	v_and_b32_e32 v9, 0xffff0000, v68
	v_lshlrev_b32_e32 v10, 16, v69
	v_and_b32_e32 v11, 0xffff0000, v69
	v_lshlrev_b32_e32 v12, 16, v70
	v_and_b32_e32 v13, 0xffff0000, v70
	v_lshlrev_b32_e32 v14, 16, v71
	v_and_b32_e32 v15, 0xffff0000, v71
	v_pk_add_f32 v[0:1], v[0:1], v[8:9]
	v_pk_add_f32 v[2:3], v[2:3], v[10:11]
	v_pk_add_f32 v[4:5], v[4:5], v[12:13]
	v_pk_add_f32 v[6:7], v[6:7], v[14:15]
	v_fma_f32 v24, v36, v0, -v8
	v_fma_f32 v25, v36, v1, -v9
	v_fma_f32 v26, v36, v2, -v10
	v_fma_f32 v27, v36, v3, -v11
	v_fma_f32 v28, v36, v4, -v12
	v_fma_f32 v29, v36, v5, -v13
	v_fma_f32 v30, v36, v6, -v14
	v_fma_f32 v31, v36, v7, -v15
	v_pk_mul_f32 v[24:25], v[24:25], 4.0 op_sel_hi:[1,0]
	v_pk_mul_f32 v[26:27], v[26:27], 4.0 op_sel_hi:[1,0]
	v_pk_mul_f32 v[28:29], v[28:29], 4.0 op_sel_hi:[1,0]
	v_pk_mul_f32 v[30:31], v[30:31], 4.0 op_sel_hi:[1,0]
	v_med3_f32 v24, v24, s33, v229
	v_med3_f32 v25, v25, s33, v229
	v_med3_f32 v26, v26, s33, v229
	v_med3_f32 v27, v27, s33, v229
	v_med3_f32 v28, v28, s33, v229
	v_med3_f32 v29, v29, s33, v229
	v_med3_f32 v30, v30, s33, v229
	v_med3_f32 v31, v31, s33, v229
	v_add_u32_e32 v35, 0xc00, v34
	v_cvt_pk_fp8_f32 v40, v24, v25
	v_cvt_pk_fp8_f32 v41, v28, v29
	v_cvt_pk_fp8_f32 v40, v26, v27 op_sel:[0,0,1]
	v_cvt_pk_fp8_f32 v41, v30, v31 op_sel:[0,0,1]
	global_store_dwordx2 v35, v[40:41], s[4:5]
	v_lshlrev_b32_e32 v16, 16, v60
	v_and_b32_e32 v17, 0xffff0000, v60
	v_lshlrev_b32_e32 v18, 16, v61
	v_and_b32_e32 v19, 0xffff0000, v61
	v_lshlrev_b32_e32 v20, 16, v62
	v_and_b32_e32 v21, 0xffff0000, v62
	v_lshlrev_b32_e32 v22, 16, v63
	v_and_b32_e32 v23, 0xffff0000, v63
	v_pk_add_f32 v[0:1], v[0:1], v[16:17] neg_lo:[0,1] neg_hi:[0,1]
	v_pk_add_f32 v[2:3], v[2:3], v[18:19] neg_lo:[0,1] neg_hi:[0,1]
	v_pk_add_f32 v[4:5], v[4:5], v[20:21] neg_lo:[0,1] neg_hi:[0,1]
	v_pk_add_f32 v[6:7], v[6:7], v[22:23] neg_lo:[0,1] neg_hi:[0,1]
	s_waitcnt vmcnt(15)
	v_lshlrev_b32_e32 v8, 16, v72
	v_and_b32_e32 v9, 0xffff0000, v72
	v_lshlrev_b32_e32 v10, 16, v73
	v_and_b32_e32 v11, 0xffff0000, v73
	v_lshlrev_b32_e32 v12, 16, v74
	v_and_b32_e32 v13, 0xffff0000, v74
	v_lshlrev_b32_e32 v14, 16, v75
	v_and_b32_e32 v15, 0xffff0000, v75
	v_pk_add_f32 v[0:1], v[0:1], v[8:9]
	v_pk_add_f32 v[2:3], v[2:3], v[10:11]
	v_pk_add_f32 v[4:5], v[4:5], v[12:13]
	v_pk_add_f32 v[6:7], v[6:7], v[14:15]
	v_fma_f32 v24, v36, v0, -v8
	v_fma_f32 v25, v36, v1, -v9
	v_fma_f32 v26, v36, v2, -v10
	v_fma_f32 v27, v36, v3, -v11
	v_fma_f32 v28, v36, v4, -v12
	v_fma_f32 v29, v36, v5, -v13
	v_fma_f32 v30, v36, v6, -v14
	v_fma_f32 v31, v36, v7, -v15
	v_pk_mul_f32 v[24:25], v[24:25], 4.0 op_sel_hi:[1,0]
	v_pk_mul_f32 v[26:27], v[26:27], 4.0 op_sel_hi:[1,0]
	v_pk_mul_f32 v[28:29], v[28:29], 4.0 op_sel_hi:[1,0]
	v_pk_mul_f32 v[30:31], v[30:31], 4.0 op_sel_hi:[1,0]
	v_med3_f32 v24, v24, s33, v229
	v_med3_f32 v25, v25, s33, v229
	v_med3_f32 v26, v26, s33, v229
	v_med3_f32 v27, v27, s33, v229
	v_med3_f32 v28, v28, s33, v229
	v_med3_f32 v29, v29, s33, v229
	v_med3_f32 v30, v30, s33, v229
	v_med3_f32 v31, v31, s33, v229
	v_add_u32_e32 v35, 0x1800, v34
	v_cvt_pk_fp8_f32 v40, v24, v25
	v_cvt_pk_fp8_f32 v41, v28, v29
	v_cvt_pk_fp8_f32 v40, v26, v27 op_sel:[0,0,1]
	v_cvt_pk_fp8_f32 v41, v30, v31 op_sel:[0,0,1]
	global_store_dwordx2 v35, v[40:41], s[4:5]
	v_lshlrev_b32_e32 v16, 16, v68
	v_and_b32_e32 v17, 0xffff0000, v68
	v_lshlrev_b32_e32 v18, 16, v69
	v_and_b32_e32 v19, 0xffff0000, v69
	v_lshlrev_b32_e32 v20, 16, v70
	v_and_b32_e32 v21, 0xffff0000, v70
	v_lshlrev_b32_e32 v22, 16, v71
	v_and_b32_e32 v23, 0xffff0000, v71
	v_pk_add_f32 v[0:1], v[0:1], v[16:17] neg_lo:[0,1] neg_hi:[0,1]
	v_pk_add_f32 v[2:3], v[2:3], v[18:19] neg_lo:[0,1] neg_hi:[0,1]
	v_pk_add_f32 v[4:5], v[4:5], v[20:21] neg_lo:[0,1] neg_hi:[0,1]
	v_pk_add_f32 v[6:7], v[6:7], v[22:23] neg_lo:[0,1] neg_hi:[0,1]
	s_waitcnt vmcnt(15)
	v_lshlrev_b32_e32 v8, 16, v76
	v_and_b32_e32 v9, 0xffff0000, v76
	v_lshlrev_b32_e32 v10, 16, v77
	v_and_b32_e32 v11, 0xffff0000, v77
	v_lshlrev_b32_e32 v12, 16, v78
	v_and_b32_e32 v13, 0xffff0000, v78
	v_lshlrev_b32_e32 v14, 16, v79
	v_and_b32_e32 v15, 0xffff0000, v79
	v_pk_add_f32 v[0:1], v[0:1], v[8:9]
	v_pk_add_f32 v[2:3], v[2:3], v[10:11]
	v_pk_add_f32 v[4:5], v[4:5], v[12:13]
	v_pk_add_f32 v[6:7], v[6:7], v[14:15]
	v_fma_f32 v24, v36, v0, -v8
	v_fma_f32 v25, v36, v1, -v9
	v_fma_f32 v26, v36, v2, -v10
	v_fma_f32 v27, v36, v3, -v11
	v_fma_f32 v28, v36, v4, -v12
	v_fma_f32 v29, v36, v5, -v13
	v_fma_f32 v30, v36, v6, -v14
	v_fma_f32 v31, v36, v7, -v15
	v_pk_mul_f32 v[24:25], v[24:25], 4.0 op_sel_hi:[1,0]
	v_pk_mul_f32 v[26:27], v[26:27], 4.0 op_sel_hi:[1,0]
	v_pk_mul_f32 v[28:29], v[28:29], 4.0 op_sel_hi:[1,0]
	v_pk_mul_f32 v[30:31], v[30:31], 4.0 op_sel_hi:[1,0]
	v_med3_f32 v24, v24, s33, v229
	v_med3_f32 v25, v25, s33, v229
	v_med3_f32 v26, v26, s33, v229
	v_med3_f32 v27, v27, s33, v229
	v_med3_f32 v28, v28, s33, v229
	v_med3_f32 v29, v29, s33, v229
	v_med3_f32 v30, v30, s33, v229
	v_med3_f32 v31, v31, s33, v229
	v_add_u32_e32 v35, 0x2400, v34
	v_cvt_pk_fp8_f32 v40, v24, v25
	v_cvt_pk_fp8_f32 v41, v28, v29
	v_cvt_pk_fp8_f32 v40, v26, v27 op_sel:[0,0,1]
	v_cvt_pk_fp8_f32 v41, v30, v31 op_sel:[0,0,1]
	global_store_dwordx2 v35, v[40:41], s[4:5]
	v_lshlrev_b32_e32 v16, 16, v72
	v_and_b32_e32 v17, 0xffff0000, v72
	v_lshlrev_b32_e32 v18, 16, v73
	v_and_b32_e32 v19, 0xffff0000, v73
	v_lshlrev_b32_e32 v20, 16, v74
	v_and_b32_e32 v21, 0xffff0000, v74
	v_lshlrev_b32_e32 v22, 16, v75
	v_and_b32_e32 v23, 0xffff0000, v75
	v_pk_add_f32 v[0:1], v[0:1], v[16:17] neg_lo:[0,1] neg_hi:[0,1]
	v_pk_add_f32 v[2:3], v[2:3], v[18:19] neg_lo:[0,1] neg_hi:[0,1]
	v_pk_add_f32 v[4:5], v[4:5], v[20:21] neg_lo:[0,1] neg_hi:[0,1]
	v_pk_add_f32 v[6:7], v[6:7], v[22:23] neg_lo:[0,1] neg_hi:[0,1]
	s_waitcnt vmcnt(15)
; __device__ __forceinline__ unsigned pk4_fp8(float a, float b, float c, float d) { unsigned w = 0u; w = __builtin_amdgcn_cvt_pk_fp8_f32(clamp8(a), clamp8(b), w, false); w = __builtin_amdgcn_cvt_pk_fp8_f32(clamp8(c), clamp8(d), w, true); return w; }
; __device__ __forceinline__ void st8q(unsigned char* ptr, const float (&f)[8]) {
;     u32x2 w; w.x = pk4_fp8(4.f * f[0], 4.f * f[1], 4.f * f[2], 4.f * f[3]); w.y = pk4_fp8(4.f * f[4], 4.f * f[5], 4.f * f[6], 4.f * f[7]); *(u32x2*)ptr = w;
; }
; template <int WIN> __device__ __forceinline__ void pool_task(const Params& p, int t0, int c) {
;     ...
; #pragma unroll
;     for (int k = 0; k < 16; ++k) { const int t = t0 + k;
;         float cur[8], o[8]; ld8(PROJ + (size_t)t * INC + 5120 + c, cur);
;         const float inv = (k + 1 < WIN && t0 == 0) ? 1.0f / (float)(k + 1) : 1.0f / (float)WIN;
; #pragma unroll
;         for (int i = 0; i < 8; ++i) { tot[i] += cur[i]; o[i] = tot[i] * inv - cur[i]; ring[k % WIN][i] = cur[i]; }
;         st8q(YABC + (size_t)t * 3072 + 2048 + c, o);
; #pragma unroll
;         for (int i = 0; i < 8; ++i) tot[i] -= ring[(k + 1) % WIN][i];
;     }
; }
	v_lshlrev_b32_e32 v8, 16, v80
	v_and_b32_e32 v9, 0xffff0000, v80
	v_lshlrev_b32_e32 v10, 16, v81
	v_and_b32_e32 v11, 0xffff0000, v81
	v_lshlrev_b32_e32 v12, 16, v82
	v_and_b32_e32 v13, 0xffff0000, v82
	v_lshlrev_b32_e32 v14, 16, v83
	v_and_b32_e32 v15, 0xffff0000, v83
	v_pk_add_f32 v[0:1], v[0:1], v[8:9]
	v_pk_add_f32 v[2:3], v[2:3], v[10:11]
	v_pk_add_f32 v[4:5], v[4:5], v[12:13]
	v_pk_add_f32 v[6:7], v[6:7], v[14:15]
	v_fma_f32 v24, v36, v0, -v8
	v_fma_f32 v25, v36, v1, -v9
	v_fma_f32 v26, v36, v2, -v10
	v_fma_f32 v27, v36, v3, -v11
	v_fma_f32 v28, v36, v4, -v12
	v_fma_f32 v29, v36, v5, -v13
	v_fma_f32 v30, v36, v6, -v14
	v_fma_f32 v31, v36, v7, -v15
	v_pk_mul_f32 v[24:25], v[24:25], 4.0 op_sel_hi:[1,0]
	v_pk_mul_f32 v[26:27], v[26:27], 4.0 op_sel_hi:[1,0]
	v_pk_mul_f32 v[28:29], v[28:29], 4.0 op_sel_hi:[1,0]
	v_pk_mul_f32 v[30:31], v[30:31], 4.0 op_sel_hi:[1,0]
	v_med3_f32 v24, v24, s33, v229
	v_med3_f32 v25, v25, s33, v229
	v_med3_f32 v26, v26, s33, v229
	v_med3_f32 v27, v27, s33, v229
	v_med3_f32 v28, v28, s33, v229
	v_med3_f32 v29, v29, s33, v229
	v_med3_f32 v30, v30, s33, v229
	v_med3_f32 v31, v31, s33, v229
	v_add_u32_e32 v35, 0x3000, v34
	v_cvt_pk_fp8_f32 v40, v24, v25
	v_cvt_pk_fp8_f32 v41, v28, v29
	v_cvt_pk_fp8_f32 v40, v26, v27 op_sel:[0,0,1]
	v_cvt_pk_fp8_f32 v41, v30, v31 op_sel:[0,0,1]
	global_store_dwordx2 v35, v[40:41], s[4:5]
	v_lshlrev_b32_e32 v16, 16, v76
	v_and_b32_e32 v17, 0xffff0000, v76
	v_lshlrev_b32_e32 v18, 16, v77
	v_and_b32_e32 v19, 0xffff0000, v77
	v_lshlrev_b32_e32 v20, 16, v78
	v_and_b32_e32 v21, 0xffff0000, v78
	v_lshlrev_b32_e32 v22, 16, v79
	v_and_b32_e32 v23, 0xffff0000, v79
	v_pk_add_f32 v[0:1], v[0:1], v[16:17] neg_lo:[0,1] neg_hi:[0,1]
	v_pk_add_f32 v[2:3], v[2:3], v[18:19] neg_lo:[0,1] neg_hi:[0,1]
	v_pk_add_f32 v[4:5], v[4:5], v[20:21] neg_lo:[0,1] neg_hi:[0,1]
	v_pk_add_f32 v[6:7], v[6:7], v[22:23] neg_lo:[0,1] neg_hi:[0,1]
	s_waitcnt vmcnt(15)
	v_lshlrev_b32_e32 v8, 16, v84
	v_and_b32_e32 v9, 0xffff0000, v84
	v_lshlrev_b32_e32 v10, 16, v85
	v_and_b32_e32 v11, 0xffff0000, v85
	v_lshlrev_b32_e32 v12, 16, v86
	v_and_b32_e32 v13, 0xffff0000, v86
	v_lshlrev_b32_e32 v14, 16, v87
	v_and_b32_e32 v15, 0xffff0000, v87
	v_pk_add_f32 v[0:1], v[0:1], v[8:9]
	v_pk_add_f32 v[2:3], v[2:3], v[10:11]
	v_pk_add_f32 v[4:5], v[4:5], v[12:13]
	v_pk_add_f32 v[6:7], v[6:7], v[14:15]
	v_fma_f32 v24, v36, v0, -v8
	v_fma_f32 v25, v36, v1, -v9
	v_fma_f32 v26, v36, v2, -v10
	v_fma_f32 v27, v36, v3, -v11
	v_fma_f32 v28, v36, v4, -v12
	v_fma_f32 v29, v36, v5, -v13
	v_fma_f32 v30, v36, v6, -v14
	v_fma_f32 v31, v36, v7, -v15
	v_pk_mul_f32 v[24:25], v[24:25], 4.0 op_sel_hi:[1,0]
	v_pk_mul_f32 v[26:27], v[26:27], 4.0 op_sel_hi:[1,0]
	v_pk_mul_f32 v[28:29], v[28:29], 4.0 op_sel_hi:[1,0]
	v_pk_mul_f32 v[30:31], v[30:31], 4.0 op_sel_hi:[1,0]
	v_med3_f32 v24, v24, s33, v229
	v_med3_f32 v25, v25, s33, v229
	v_med3_f32 v26, v26, s33, v229
	v_med3_f32 v27, v27, s33, v229
	v_med3_f32 v28, v28, s33, v229
	v_med3_f32 v29, v29, s33, v229
	v_med3_f32 v30, v30, s33, v229
	v_med3_f32 v31, v31, s33, v229
	v_add_u32_e32 v35, 0x3c00, v34
	v_cvt_pk_fp8_f32 v40, v24, v25
	v_cvt_pk_fp8_f32 v41, v28, v29
	v_cvt_pk_fp8_f32 v40, v26, v27 op_sel:[0,0,1]
	v_cvt_pk_fp8_f32 v41, v30, v31 op_sel:[0,0,1]
	global_store_dwordx2 v35, v[40:41], s[4:5]
	v_lshlrev_b32_e32 v16, 16, v80
	v_and_b32_e32 v17, 0xffff0000, v80
	v_lshlrev_b32_e32 v18, 16, v81
	v_and_b32_e32 v19, 0xffff0000, v81
	v_lshlrev_b32_e32 v20, 16, v82
	v_and_b32_e32 v21, 0xffff0000, v82
	v_lshlrev_b32_e32 v22, 16, v83
	v_and_b32_e32 v23, 0xffff0000, v83
	v_pk_add_f32 v[0:1], v[0:1], v[16:17] neg_lo:[0,1] neg_hi:[0,1]
	v_pk_add_f32 v[2:3], v[2:3], v[18:19] neg_lo:[0,1] neg_hi:[0,1]
	v_pk_add_f32 v[4:5], v[4:5], v[20:21] neg_lo:[0,1] neg_hi:[0,1]
	v_pk_add_f32 v[6:7], v[6:7], v[22:23] neg_lo:[0,1] neg_hi:[0,1]
	s_waitcnt vmcnt(15)
	v_lshlrev_b32_e32 v8, 16, v88
	v_and_b32_e32 v9, 0xffff0000, v88
	v_lshlrev_b32_e32 v10, 16, v89
	v_and_b32_e32 v11, 0xffff0000, v89
	v_lshlrev_b32_e32 v12, 16, v90
	v_and_b32_e32 v13, 0xffff0000, v90
	v_lshlrev_b32_e32 v14, 16, v91
	v_and_b32_e32 v15, 0xffff0000, v91
	v_pk_add_f32 v[0:1], v[0:1], v[8:9]
	v_pk_add_f32 v[2:3], v[2:3], v[10:11]
	v_pk_add_f32 v[4:5], v[4:5], v[12:13]
	v_pk_add_f32 v[6:7], v[6:7], v[14:15]
	v_fma_f32 v24, v36, v0, -v8
	v_fma_f32 v25, v36, v1, -v9
	v_fma_f32 v26, v36, v2, -v10
	v_fma_f32 v27, v36, v3, -v11
	v_fma_f32 v28, v36, v4, -v12
	v_fma_f32 v29, v36, v5, -v13
	v_fma_f32 v30, v36, v6, -v14
	v_fma_f32 v31, v36, v7, -v15
	v_pk_mul_f32 v[24:25], v[24:25], 4.0 op_sel_hi:[1,0]
	v_pk_mul_f32 v[26:27], v[26:27], 4.0 op_sel_hi:[1,0]
	v_pk_mul_f32 v[28:29], v[28:29], 4.0 op_sel_hi:[1,0]
	v_pk_mul_f32 v[30:31], v[30:31], 4.0 op_sel_hi:[1,0]
	v_med3_f32 v24, v24, s33, v229
	v_med3_f32 v25, v25, s33, v229
	v_med3_f32 v26, v26, s33, v229
	v_med3_f32 v27, v27, s33, v229
	v_med3_f32 v28, v28, s33, v229
	v_med3_f32 v29, v29, s33, v229
	v_med3_f32 v30, v30, s33, v229
	v_med3_f32 v31, v31, s33, v229
	v_add_u32_e32 v35, 0x4800, v34
	v_cvt_pk_fp8_f32 v40, v24, v25
	v_cvt_pk_fp8_f32 v41, v28, v29
	v_cvt_pk_fp8_f32 v40, v26, v27 op_sel:[0,0,1]
	v_cvt_pk_fp8_f32 v41, v30, v31 op_sel:[0,0,1]
	global_store_dwordx2 v35, v[40:41], s[4:5]
	v_lshlrev_b32_e32 v16, 16, v84
	v_and_b32_e32 v17, 0xffff0000, v84
	v_lshlrev_b32_e32 v18, 16, v85
	v_and_b32_e32 v19, 0xffff0000, v85
	v_lshlrev_b32_e32 v20, 16, v86
	v_and_b32_e32 v21, 0xffff0000, v86
	v_lshlrev_b32_e32 v22, 16, v87
	v_and_b32_e32 v23, 0xffff0000, v87
	v_pk_add_f32 v[0:1], v[0:1], v[16:17] neg_lo:[0,1] neg_hi:[0,1]
	v_pk_add_f32 v[2:3], v[2:3], v[18:19] neg_lo:[0,1] neg_hi:[0,1]
	v_pk_add_f32 v[4:5], v[4:5], v[20:21] neg_lo:[0,1] neg_hi:[0,1]
	v_pk_add_f32 v[6:7], v[6:7], v[22:23] neg_lo:[0,1] neg_hi:[0,1]
	s_waitcnt vmcnt(15)
; __device__ __forceinline__ unsigned pk4_fp8(float a, float b, float c, float d) { unsigned w = 0u; w = __builtin_amdgcn_cvt_pk_fp8_f32(clamp8(a), clamp8(b), w, false); w = __builtin_amdgcn_cvt_pk_fp8_f32(clamp8(c), clamp8(d), w, true); return w; }
; __device__ __forceinline__ void st8q(unsigned char* ptr, const float (&f)[8]) {
;     u32x2 w; w.x = pk4_fp8(4.f * f[0], 4.f * f[1], 4.f * f[2], 4.f * f[3]); w.y = pk4_fp8(4.f * f[4], 4.f * f[5], 4.f * f[6], 4.f * f[7]); *(u32x2*)ptr = w;
; }
; template <int WIN> __device__ __forceinline__ void pool_task(const Params& p, int t0, int c) {
;     ...
; #pragma unroll
;     for (int k = 0; k < 16; ++k) { const int t = t0 + k;
;         float cur[8], o[8]; ld8(PROJ + (size_t)t * INC + 5120 + c, cur);
;         const float inv = (k + 1 < WIN && t0 == 0) ? 1.0f / (float)(k + 1) : 1.0f / (float)WIN;
; #pragma unroll
;         for (int i = 0; i < 8; ++i) { tot[i] += cur[i]; o[i] = tot[i] * inv - cur[i]; ring[k % WIN][i] = cur[i]; }
;         st8q(YABC + (size_t)t * 3072 + 2048 + c, o);
; #pragma unroll
;         for (int i = 0; i < 8; ++i) tot[i] -= ring[(k + 1) % WIN][i];
;     }
; }
	v_lshlrev_b32_e32 v8, 16, v92
	v_and_b32_e32 v9, 0xffff0000, v92
	v_lshlrev_b32_e32 v10, 16, v93
	v_and_b32_e32 v11, 0xffff0000, v93
	v_lshlrev_b32_e32 v12, 16, v94
	v_and_b32_e32 v13, 0xffff0000, v94
	v_lshlrev_b32_e32 v14, 16, v95
	v_and_b32_e32 v15, 0xffff0000, v95
	v_pk_add_f32 v[0:1], v[0:1], v[8:9]
	v_pk_add_f32 v[2:3], v[2:3], v[10:11]
	v_pk_add_f32 v[4:5], v[4:5], v[12:13]
	v_pk_add_f32 v[6:7], v[6:7], v[14:15]
	v_fma_f32 v24, v36, v0, -v8
	v_fma_f32 v25, v36, v1, -v9
	v_fma_f32 v26, v36, v2, -v10
	v_fma_f32 v27, v36, v3, -v11
	v_fma_f32 v28, v36, v4, -v12
	v_fma_f32 v29, v36, v5, -v13
	v_fma_f32 v30, v36, v6, -v14
	v_fma_f32 v31, v36, v7, -v15
	v_pk_mul_f32 v[24:25], v[24:25], 4.0 op_sel_hi:[1,0]
	v_pk_mul_f32 v[26:27], v[26:27], 4.0 op_sel_hi:[1,0]
	v_pk_mul_f32 v[28:29], v[28:29], 4.0 op_sel_hi:[1,0]
	v_pk_mul_f32 v[30:31], v[30:31], 4.0 op_sel_hi:[1,0]
	v_med3_f32 v24, v24, s33, v229
	v_med3_f32 v25, v25, s33, v229
	v_med3_f32 v26, v26, s33, v229
	v_med3_f32 v27, v27, s33, v229
	v_med3_f32 v28, v28, s33, v229
	v_med3_f32 v29, v29, s33, v229
	v_med3_f32 v30, v30, s33, v229
	v_med3_f32 v31, v31, s33, v229
	v_add_u32_e32 v35, 0x5400, v34
	v_cvt_pk_fp8_f32 v40, v24, v25
	v_cvt_pk_fp8_f32 v41, v28, v29
	v_cvt_pk_fp8_f32 v40, v26, v27 op_sel:[0,0,1]
	v_cvt_pk_fp8_f32 v41, v30, v31 op_sel:[0,0,1]
	global_store_dwordx2 v35, v[40:41], s[4:5]
	v_lshlrev_b32_e32 v16, 16, v88
	v_and_b32_e32 v17, 0xffff0000, v88
	v_lshlrev_b32_e32 v18, 16, v89
	v_and_b32_e32 v19, 0xffff0000, v89
	v_lshlrev_b32_e32 v20, 16, v90
	v_and_b32_e32 v21, 0xffff0000, v90
	v_lshlrev_b32_e32 v22, 16, v91
	v_and_b32_e32 v23, 0xffff0000, v91
	v_pk_add_f32 v[0:1], v[0:1], v[16:17] neg_lo:[0,1] neg_hi:[0,1]
	v_pk_add_f32 v[2:3], v[2:3], v[18:19] neg_lo:[0,1] neg_hi:[0,1]
	v_pk_add_f32 v[4:5], v[4:5], v[20:21] neg_lo:[0,1] neg_hi:[0,1]
	v_pk_add_f32 v[6:7], v[6:7], v[22:23] neg_lo:[0,1] neg_hi:[0,1]
	s_waitcnt vmcnt(15)
	v_lshlrev_b32_e32 v8, 16, v96
	v_and_b32_e32 v9, 0xffff0000, v96
	v_lshlrev_b32_e32 v10, 16, v97
	v_and_b32_e32 v11, 0xffff0000, v97
	v_lshlrev_b32_e32 v12, 16, v98
	v_and_b32_e32 v13, 0xffff0000, v98
	v_lshlrev_b32_e32 v14, 16, v99
	v_and_b32_e32 v15, 0xffff0000, v99
	v_pk_add_f32 v[0:1], v[0:1], v[8:9]
	v_pk_add_f32 v[2:3], v[2:3], v[10:11]
	v_pk_add_f32 v[4:5], v[4:5], v[12:13]
	v_pk_add_f32 v[6:7], v[6:7], v[14:15]
	v_fma_f32 v24, v36, v0, -v8
	v_fma_f32 v25, v36, v1, -v9
	v_fma_f32 v26, v36, v2, -v10
	v_fma_f32 v27, v36, v3, -v11
	v_fma_f32 v28, v36, v4, -v12
	v_fma_f32 v29, v36, v5, -v13
	v_fma_f32 v30, v36, v6, -v14
	v_fma_f32 v31, v36, v7, -v15
	v_pk_mul_f32 v[24:25], v[24:25], 4.0 op_sel_hi:[1,0]
	v_pk_mul_f32 v[26:27], v[26:27], 4.0 op_sel_hi:[1,0]
	v_pk_mul_f32 v[28:29], v[28:29], 4.0 op_sel_hi:[1,0]
	v_pk_mul_f32 v[30:31], v[30:31], 4.0 op_sel_hi:[1,0]
	v_med3_f32 v24, v24, s33, v229
	v_med3_f32 v25, v25, s33, v229
	v_med3_f32 v26, v26, s33, v229
	v_med3_f32 v27, v27, s33, v229
	v_med3_f32 v28, v28, s33, v229
	v_med3_f32 v29, v29, s33, v229
	v_med3_f32 v30, v30, s33, v229
	v_med3_f32 v31, v31, s33, v229
	v_add_u32_e32 v35, 0x6000, v34
	v_cvt_pk_fp8_f32 v40, v24, v25
	v_cvt_pk_fp8_f32 v41, v28, v29
	v_cvt_pk_fp8_f32 v40, v26, v27 op_sel:[0,0,1]
	v_cvt_pk_fp8_f32 v41, v30, v31 op_sel:[0,0,1]
	global_store_dwordx2 v35, v[40:41], s[4:5]
	v_lshlrev_b32_e32 v16, 16, v92
	v_and_b32_e32 v17, 0xffff0000, v92
	v_lshlrev_b32_e32 v18, 16, v93
	v_and_b32_e32 v19, 0xffff0000, v93
	v_lshlrev_b32_e32 v20, 16, v94
	v_and_b32_e32 v21, 0xffff0000, v94
	v_lshlrev_b32_e32 v22, 16, v95
	v_and_b32_e32 v23, 0xffff0000, v95
	v_pk_add_f32 v[0:1], v[0:1], v[16:17] neg_lo:[0,1] neg_hi:[0,1]
	v_pk_add_f32 v[2:3], v[2:3], v[18:19] neg_lo:[0,1] neg_hi:[0,1]
	v_pk_add_f32 v[4:5], v[4:5], v[20:21] neg_lo:[0,1] neg_hi:[0,1]
	v_pk_add_f32 v[6:7], v[6:7], v[22:23] neg_lo:[0,1] neg_hi:[0,1]
	s_waitcnt vmcnt(15)
	v_lshlrev_b32_e32 v8, 16, v100
	v_and_b32_e32 v9, 0xffff0000, v100
	v_lshlrev_b32_e32 v10, 16, v101
	v_and_b32_e32 v11, 0xffff0000, v101
	v_lshlrev_b32_e32 v12, 16, v102
	v_and_b32_e32 v13, 0xffff0000, v102
	v_lshlrev_b32_e32 v14, 16, v103
	v_and_b32_e32 v15, 0xffff0000, v103
	v_pk_add_f32 v[0:1], v[0:1], v[8:9]
	v_pk_add_f32 v[2:3], v[2:3], v[10:11]
	v_pk_add_f32 v[4:5], v[4:5], v[12:13]
	v_pk_add_f32 v[6:7], v[6:7], v[14:15]
	v_fma_f32 v24, v36, v0, -v8
	v_fma_f32 v25, v36, v1, -v9
	v_fma_f32 v26, v36, v2, -v10
	v_fma_f32 v27, v36, v3, -v11
	v_fma_f32 v28, v36, v4, -v12
	v_fma_f32 v29, v36, v5, -v13
	v_fma_f32 v30, v36, v6, -v14
	v_fma_f32 v31, v36, v7, -v15
	v_pk_mul_f32 v[24:25], v[24:25], 4.0 op_sel_hi:[1,0]
	v_pk_mul_f32 v[26:27], v[26:27], 4.0 op_sel_hi:[1,0]
	v_pk_mul_f32 v[28:29], v[28:29], 4.0 op_sel_hi:[1,0]
	v_pk_mul_f32 v[30:31], v[30:31], 4.0 op_sel_hi:[1,0]
	v_med3_f32 v24, v24, s33, v229
	v_med3_f32 v25, v25, s33, v229
	v_med3_f32 v26, v26, s33, v229
	v_med3_f32 v27, v27, s33, v229
	v_med3_f32 v28, v28, s33, v229
	v_med3_f32 v29, v29, s33, v229
	v_med3_f32 v30, v30, s33, v229
	v_med3_f32 v31, v31, s33, v229
	v_add_u32_e32 v35, 0x6c00, v34
	v_cvt_pk_fp8_f32 v40, v24, v25
	v_cvt_pk_fp8_f32 v41, v28, v29
	v_cvt_pk_fp8_f32 v40, v26, v27 op_sel:[0,0,1]
	v_cvt_pk_fp8_f32 v41, v30, v31 op_sel:[0,0,1]
	global_store_dwordx2 v35, v[40:41], s[4:5]
	v_lshlrev_b32_e32 v16, 16, v96
	v_and_b32_e32 v17, 0xffff0000, v96
	v_lshlrev_b32_e32 v18, 16, v97
	v_and_b32_e32 v19, 0xffff0000, v97
	v_lshlrev_b32_e32 v20, 16, v98
	v_and_b32_e32 v21, 0xffff0000, v98
	v_lshlrev_b32_e32 v22, 16, v99
	v_and_b32_e32 v23, 0xffff0000, v99
	v_pk_add_f32 v[0:1], v[0:1], v[16:17] neg_lo:[0,1] neg_hi:[0,1]
	v_pk_add_f32 v[2:3], v[2:3], v[18:19] neg_lo:[0,1] neg_hi:[0,1]
	v_pk_add_f32 v[4:5], v[4:5], v[20:21] neg_lo:[0,1] neg_hi:[0,1]
	v_pk_add_f32 v[6:7], v[6:7], v[22:23] neg_lo:[0,1] neg_hi:[0,1]
	s_waitcnt vmcnt(15)
; __device__ __forceinline__ unsigned pk4_fp8(float a, float b, float c, float d) { unsigned w = 0u; w = __builtin_amdgcn_cvt_pk_fp8_f32(clamp8(a), clamp8(b), w, false); w = __builtin_amdgcn_cvt_pk_fp8_f32(clamp8(c), clamp8(d), w, true); return w; }
; __device__ __forceinline__ void st8q(unsigned char* ptr, const float (&f)[8]) {
;     u32x2 w; w.x = pk4_fp8(4.f * f[0], 4.f * f[1], 4.f * f[2], 4.f * f[3]); w.y = pk4_fp8(4.f * f[4], 4.f * f[5], 4.f * f[6], 4.f * f[7]); *(u32x2*)ptr = w;
; }
; template <int WIN> __device__ __forceinline__ void pool_task(const Params& p, int t0, int c) {
;     ...
; #pragma unroll
;     for (int k = 0; k < 16; ++k) { const int t = t0 + k;
;         float cur[8], o[8]; ld8(PROJ + (size_t)t * INC + 5120 + c, cur);
;         const float inv = (k + 1 < WIN && t0 == 0) ? 1.0f / (float)(k + 1) : 1.0f / (float)WIN;
; #pragma unroll
;         for (int i = 0; i < 8; ++i) { tot[i] += cur[i]; o[i] = tot[i] * inv - cur[i]; ring[k % WIN][i] = cur[i]; }
;         st8q(YABC + (size_t)t * 3072 + 2048 + c, o);
; #pragma unroll
;         for (int i = 0; i < 8; ++i) tot[i] -= ring[(k + 1) % WIN][i];
;     }
; }
	v_lshlrev_b32_e32 v8, 16, v104
	v_and_b32_e32 v9, 0xffff0000, v104
	v_lshlrev_b32_e32 v10, 16, v105
	v_and_b32_e32 v11, 0xffff0000, v105
	v_lshlrev_b32_e32 v12, 16, v106
	v_and_b32_e32 v13, 0xffff0000, v106
	v_lshlrev_b32_e32 v14, 16, v107
	v_and_b32_e32 v15, 0xffff0000, v107
	v_pk_add_f32 v[0:1], v[0:1], v[8:9]
	v_pk_add_f32 v[2:3], v[2:3], v[10:11]
	v_pk_add_f32 v[4:5], v[4:5], v[12:13]
	v_pk_add_f32 v[6:7], v[6:7], v[14:15]
	v_fma_f32 v24, v36, v0, -v8
	v_fma_f32 v25, v36, v1, -v9
	v_fma_f32 v26, v36, v2, -v10
	v_fma_f32 v27, v36, v3, -v11
	v_fma_f32 v28, v36, v4, -v12
	v_fma_f32 v29, v36, v5, -v13
	v_fma_f32 v30, v36, v6, -v14
	v_fma_f32 v31, v36, v7, -v15
	v_pk_mul_f32 v[24:25], v[24:25], 4.0 op_sel_hi:[1,0]
	v_pk_mul_f32 v[26:27], v[26:27], 4.0 op_sel_hi:[1,0]
	v_pk_mul_f32 v[28:29], v[28:29], 4.0 op_sel_hi:[1,0]
	v_pk_mul_f32 v[30:31], v[30:31], 4.0 op_sel_hi:[1,0]
	v_med3_f32 v24, v24, s33, v229
	v_med3_f32 v25, v25, s33, v229
	v_med3_f32 v26, v26, s33, v229
	v_med3_f32 v27, v27, s33, v229
	v_med3_f32 v28, v28, s33, v229
	v_med3_f32 v29, v29, s33, v229
	v_med3_f32 v30, v30, s33, v229
	v_med3_f32 v31, v31, s33, v229
	v_add_u32_e32 v35, 0x7800, v34
	v_cvt_pk_fp8_f32 v40, v24, v25
	v_cvt_pk_fp8_f32 v41, v28, v29
	v_cvt_pk_fp8_f32 v40, v26, v27 op_sel:[0,0,1]
	v_cvt_pk_fp8_f32 v41, v30, v31 op_sel:[0,0,1]
	global_store_dwordx2 v35, v[40:41], s[4:5]
	v_lshlrev_b32_e32 v16, 16, v100
	v_and_b32_e32 v17, 0xffff0000, v100
	v_lshlrev_b32_e32 v18, 16, v101
	v_and_b32_e32 v19, 0xffff0000, v101
	v_lshlrev_b32_e32 v20, 16, v102
	v_and_b32_e32 v21, 0xffff0000, v102
	v_lshlrev_b32_e32 v22, 16, v103
	v_and_b32_e32 v23, 0xffff0000, v103
	v_pk_add_f32 v[0:1], v[0:1], v[16:17] neg_lo:[0,1] neg_hi:[0,1]
	v_pk_add_f32 v[2:3], v[2:3], v[18:19] neg_lo:[0,1] neg_hi:[0,1]
	v_pk_add_f32 v[4:5], v[4:5], v[20:21] neg_lo:[0,1] neg_hi:[0,1]
	v_pk_add_f32 v[6:7], v[6:7], v[22:23] neg_lo:[0,1] neg_hi:[0,1]
	s_waitcnt vmcnt(15)
	v_lshlrev_b32_e32 v8, 16, v108
	v_and_b32_e32 v9, 0xffff0000, v108
	v_lshlrev_b32_e32 v10, 16, v109
	v_and_b32_e32 v11, 0xffff0000, v109
	v_lshlrev_b32_e32 v12, 16, v110
	v_and_b32_e32 v13, 0xffff0000, v110
	v_lshlrev_b32_e32 v14, 16, v111
	v_and_b32_e32 v15, 0xffff0000, v111
	v_pk_add_f32 v[0:1], v[0:1], v[8:9]
	v_pk_add_f32 v[2:3], v[2:3], v[10:11]
	v_pk_add_f32 v[4:5], v[4:5], v[12:13]
	v_pk_add_f32 v[6:7], v[6:7], v[14:15]
	v_fma_f32 v24, v36, v0, -v8
	v_fma_f32 v25, v36, v1, -v9
	v_fma_f32 v26, v36, v2, -v10
	v_fma_f32 v27, v36, v3, -v11
	v_fma_f32 v28, v36, v4, -v12
	v_fma_f32 v29, v36, v5, -v13
	v_fma_f32 v30, v36, v6, -v14
	v_fma_f32 v31, v36, v7, -v15
	v_pk_mul_f32 v[24:25], v[24:25], 4.0 op_sel_hi:[1,0]
	v_pk_mul_f32 v[26:27], v[26:27], 4.0 op_sel_hi:[1,0]
	v_pk_mul_f32 v[28:29], v[28:29], 4.0 op_sel_hi:[1,0]
	v_pk_mul_f32 v[30:31], v[30:31], 4.0 op_sel_hi:[1,0]
	v_med3_f32 v24, v24, s33, v229
	v_med3_f32 v25, v25, s33, v229
	v_med3_f32 v26, v26, s33, v229
	v_med3_f32 v27, v27, s33, v229
	v_med3_f32 v28, v28, s33, v229
	v_med3_f32 v29, v29, s33, v229
	v_med3_f32 v30, v30, s33, v229
	v_med3_f32 v31, v31, s33, v229
	v_add_u32_e32 v35, 0x8400, v34
	v_cvt_pk_fp8_f32 v40, v24, v25
	v_cvt_pk_fp8_f32 v41, v28, v29
	v_cvt_pk_fp8_f32 v40, v26, v27 op_sel:[0,0,1]
	v_cvt_pk_fp8_f32 v41, v30, v31 op_sel:[0,0,1]
	global_store_dwordx2 v35, v[40:41], s[4:5]
	v_lshlrev_b32_e32 v16, 16, v104
	v_and_b32_e32 v17, 0xffff0000, v104
	v_lshlrev_b32_e32 v18, 16, v105
	v_and_b32_e32 v19, 0xffff0000, v105
	v_lshlrev_b32_e32 v20, 16, v106
	v_and_b32_e32 v21, 0xffff0000, v106
	v_lshlrev_b32_e32 v22, 16, v107
	v_and_b32_e32 v23, 0xffff0000, v107
	v_pk_add_f32 v[0:1], v[0:1], v[16:17] neg_lo:[0,1] neg_hi:[0,1]
	v_pk_add_f32 v[2:3], v[2:3], v[18:19] neg_lo:[0,1] neg_hi:[0,1]
	v_pk_add_f32 v[4:5], v[4:5], v[20:21] neg_lo:[0,1] neg_hi:[0,1]
	v_pk_add_f32 v[6:7], v[6:7], v[22:23] neg_lo:[0,1] neg_hi:[0,1]
	s_waitcnt vmcnt(15)
	v_lshlrev_b32_e32 v8, 16, v112
	v_and_b32_e32 v9, 0xffff0000, v112
	v_lshlrev_b32_e32 v10, 16, v113
	v_and_b32_e32 v11, 0xffff0000, v113
	v_lshlrev_b32_e32 v12, 16, v114
	v_and_b32_e32 v13, 0xffff0000, v114
	v_lshlrev_b32_e32 v14, 16, v115
	v_and_b32_e32 v15, 0xffff0000, v115
	v_pk_add_f32 v[0:1], v[0:1], v[8:9]
	v_pk_add_f32 v[2:3], v[2:3], v[10:11]
	v_pk_add_f32 v[4:5], v[4:5], v[12:13]
	v_pk_add_f32 v[6:7], v[6:7], v[14:15]
	v_fma_f32 v24, v36, v0, -v8
	v_fma_f32 v25, v36, v1, -v9
	v_fma_f32 v26, v36, v2, -v10
	v_fma_f32 v27, v36, v3, -v11
	v_fma_f32 v28, v36, v4, -v12
	v_fma_f32 v29, v36, v5, -v13
	v_fma_f32 v30, v36, v6, -v14
	v_fma_f32 v31, v36, v7, -v15
	v_pk_mul_f32 v[24:25], v[24:25], 4.0 op_sel_hi:[1,0]
	v_pk_mul_f32 v[26:27], v[26:27], 4.0 op_sel_hi:[1,0]
	v_pk_mul_f32 v[28:29], v[28:29], 4.0 op_sel_hi:[1,0]
	v_pk_mul_f32 v[30:31], v[30:31], 4.0 op_sel_hi:[1,0]
	v_med3_f32 v24, v24, s33, v229
	v_med3_f32 v25, v25, s33, v229
	v_med3_f32 v26, v26, s33, v229
	v_med3_f32 v27, v27, s33, v229
	v_med3_f32 v28, v28, s33, v229
	v_med3_f32 v29, v29, s33, v229
	v_med3_f32 v30, v30, s33, v229
	v_med3_f32 v31, v31, s33, v229
	v_add_u32_e32 v35, 0x9000, v34
	v_cvt_pk_fp8_f32 v40, v24, v25
	v_cvt_pk_fp8_f32 v41, v28, v29
	v_cvt_pk_fp8_f32 v40, v26, v27 op_sel:[0,0,1]
	v_cvt_pk_fp8_f32 v41, v30, v31 op_sel:[0,0,1]
	global_store_dwordx2 v35, v[40:41], s[4:5]
	v_lshlrev_b32_e32 v16, 16, v108
	v_and_b32_e32 v17, 0xffff0000, v108
	v_lshlrev_b32_e32 v18, 16, v109
	v_and_b32_e32 v19, 0xffff0000, v109
	v_lshlrev_b32_e32 v20, 16, v110
	v_and_b32_e32 v21, 0xffff0000, v110
	v_lshlrev_b32_e32 v22, 16, v111
	v_and_b32_e32 v23, 0xffff0000, v111
	v_pk_add_f32 v[0:1], v[0:1], v[16:17] neg_lo:[0,1] neg_hi:[0,1]
	v_pk_add_f32 v[2:3], v[2:3], v[18:19] neg_lo:[0,1] neg_hi:[0,1]
	v_pk_add_f32 v[4:5], v[4:5], v[20:21] neg_lo:[0,1] neg_hi:[0,1]
	v_pk_add_f32 v[6:7], v[6:7], v[22:23] neg_lo:[0,1] neg_hi:[0,1]
	s_waitcnt vmcnt(15)
; __device__ __forceinline__ unsigned pk4_fp8(float a, float b, float c, float d) { unsigned w = 0u; w = __builtin_amdgcn_cvt_pk_fp8_f32(clamp8(a), clamp8(b), w, false); w = __builtin_amdgcn_cvt_pk_fp8_f32(clamp8(c), clamp8(d), w, true); return w; }
; __device__ __forceinline__ void st8q(unsigned char* ptr, const float (&f)[8]) {
;     u32x2 w; w.x = pk4_fp8(4.f * f[0], 4.f * f[1], 4.f * f[2], 4.f * f[3]); w.y = pk4_fp8(4.f * f[4], 4.f * f[5], 4.f * f[6], 4.f * f[7]); *(u32x2*)ptr = w;
; }
; template <int WIN> __device__ __forceinline__ void pool_task(const Params& p, int t0, int c) {
;     ...
; #pragma unroll
;     for (int k = 0; k < 16; ++k) { const int t = t0 + k;
;         float cur[8], o[8]; ld8(PROJ + (size_t)t * INC + 5120 + c, cur);
;         const float inv = (k + 1 < WIN && t0 == 0) ? 1.0f / (float)(k + 1) : 1.0f / (float)WIN;
; #pragma unroll
;         for (int i = 0; i < 8; ++i) { tot[i] += cur[i]; o[i] = tot[i] * inv - cur[i]; ring[k % WIN][i] = cur[i]; }
;         st8q(YABC + (size_t)t * 3072 + 2048 + c, o);
; #pragma unroll
;         for (int i = 0; i < 8; ++i) tot[i] -= ring[(k + 1) % WIN][i];
;     }
; }
	v_lshlrev_b32_e32 v8, 16, v116
	v_and_b32_e32 v9, 0xffff0000, v116
	v_lshlrev_b32_e32 v10, 16, v117
	v_and_b32_e32 v11, 0xffff0000, v117
	v_lshlrev_b32_e32 v12, 16, v118
	v_and_b32_e32 v13, 0xffff0000, v118
	v_lshlrev_b32_e32 v14, 16, v119
	v_and_b32_e32 v15, 0xffff0000, v119
	v_pk_add_f32 v[0:1], v[0:1], v[8:9]
	v_pk_add_f32 v[2:3], v[2:3], v[10:11]
	v_pk_add_f32 v[4:5], v[4:5], v[12:13]
	v_pk_add_f32 v[6:7], v[6:7], v[14:15]
	v_fma_f32 v24, v36, v0, -v8
	v_fma_f32 v25, v36, v1, -v9
	v_fma_f32 v26, v36, v2, -v10
	v_fma_f32 v27, v36, v3, -v11
	v_fma_f32 v28, v36, v4, -v12
	v_fma_f32 v29, v36, v5, -v13
	v_fma_f32 v30, v36, v6, -v14
	v_fma_f32 v31, v36, v7, -v15
	v_pk_mul_f32 v[24:25], v[24:25], 4.0 op_sel_hi:[1,0]
	v_pk_mul_f32 v[26:27], v[26:27], 4.0 op_sel_hi:[1,0]
	v_pk_mul_f32 v[28:29], v[28:29], 4.0 op_sel_hi:[1,0]
	v_pk_mul_f32 v[30:31], v[30:31], 4.0 op_sel_hi:[1,0]
	v_med3_f32 v24, v24, s33, v229
	v_med3_f32 v25, v25, s33, v229
	v_med3_f32 v26, v26, s33, v229
	v_med3_f32 v27, v27, s33, v229
	v_med3_f32 v28, v28, s33, v229
	v_med3_f32 v29, v29, s33, v229
	v_med3_f32 v30, v30, s33, v229
	v_med3_f32 v31, v31, s33, v229
	v_add_u32_e32 v35, 0x9c00, v34
	v_cvt_pk_fp8_f32 v40, v24, v25
	v_cvt_pk_fp8_f32 v41, v28, v29
	v_cvt_pk_fp8_f32 v40, v26, v27 op_sel:[0,0,1]
	v_cvt_pk_fp8_f32 v41, v30, v31 op_sel:[0,0,1]
	global_store_dwordx2 v35, v[40:41], s[4:5]
	v_lshlrev_b32_e32 v16, 16, v112
	v_and_b32_e32 v17, 0xffff0000, v112
	v_lshlrev_b32_e32 v18, 16, v113
	v_and_b32_e32 v19, 0xffff0000, v113
	v_lshlrev_b32_e32 v20, 16, v114
	v_and_b32_e32 v21, 0xffff0000, v114
	v_lshlrev_b32_e32 v22, 16, v115
	v_and_b32_e32 v23, 0xffff0000, v115
	v_pk_add_f32 v[0:1], v[0:1], v[16:17] neg_lo:[0,1] neg_hi:[0,1]
	v_pk_add_f32 v[2:3], v[2:3], v[18:19] neg_lo:[0,1] neg_hi:[0,1]
	v_pk_add_f32 v[4:5], v[4:5], v[20:21] neg_lo:[0,1] neg_hi:[0,1]
	v_pk_add_f32 v[6:7], v[6:7], v[22:23] neg_lo:[0,1] neg_hi:[0,1]
	s_waitcnt vmcnt(15)
	v_lshlrev_b32_e32 v8, 16, v120
	v_and_b32_e32 v9, 0xffff0000, v120
	v_lshlrev_b32_e32 v10, 16, v121
	v_and_b32_e32 v11, 0xffff0000, v121
	v_lshlrev_b32_e32 v12, 16, v122
	v_and_b32_e32 v13, 0xffff0000, v122
	v_lshlrev_b32_e32 v14, 16, v123
	v_and_b32_e32 v15, 0xffff0000, v123
	v_pk_add_f32 v[0:1], v[0:1], v[8:9]
	v_pk_add_f32 v[2:3], v[2:3], v[10:11]
	v_pk_add_f32 v[4:5], v[4:5], v[12:13]
	v_pk_add_f32 v[6:7], v[6:7], v[14:15]
	v_fma_f32 v24, v36, v0, -v8
	v_fma_f32 v25, v36, v1, -v9
	v_fma_f32 v26, v36, v2, -v10
	v_fma_f32 v27, v36, v3, -v11
	v_fma_f32 v28, v36, v4, -v12
	v_fma_f32 v29, v36, v5, -v13
	v_fma_f32 v30, v36, v6, -v14
	v_fma_f32 v31, v36, v7, -v15
	v_pk_mul_f32 v[24:25], v[24:25], 4.0 op_sel_hi:[1,0]
	v_pk_mul_f32 v[26:27], v[26:27], 4.0 op_sel_hi:[1,0]
	v_pk_mul_f32 v[28:29], v[28:29], 4.0 op_sel_hi:[1,0]
	v_pk_mul_f32 v[30:31], v[30:31], 4.0 op_sel_hi:[1,0]
	v_med3_f32 v24, v24, s33, v229
	v_med3_f32 v25, v25, s33, v229
	v_med3_f32 v26, v26, s33, v229
	v_med3_f32 v27, v27, s33, v229
	v_med3_f32 v28, v28, s33, v229
	v_med3_f32 v29, v29, s33, v229
	v_med3_f32 v30, v30, s33, v229
	v_med3_f32 v31, v31, s33, v229
	v_add_u32_e32 v35, 0xa800, v34
	v_cvt_pk_fp8_f32 v40, v24, v25
	v_cvt_pk_fp8_f32 v41, v28, v29
	v_cvt_pk_fp8_f32 v40, v26, v27 op_sel:[0,0,1]
	v_cvt_pk_fp8_f32 v41, v30, v31 op_sel:[0,0,1]
	global_store_dwordx2 v35, v[40:41], s[4:5]
	v_lshlrev_b32_e32 v16, 16, v116
	v_and_b32_e32 v17, 0xffff0000, v116
	v_lshlrev_b32_e32 v18, 16, v117
	v_and_b32_e32 v19, 0xffff0000, v117
	v_lshlrev_b32_e32 v20, 16, v118
	v_and_b32_e32 v21, 0xffff0000, v118
	v_lshlrev_b32_e32 v22, 16, v119
	v_and_b32_e32 v23, 0xffff0000, v119
	v_pk_add_f32 v[0:1], v[0:1], v[16:17] neg_lo:[0,1] neg_hi:[0,1]
	v_pk_add_f32 v[2:3], v[2:3], v[18:19] neg_lo:[0,1] neg_hi:[0,1]
	v_pk_add_f32 v[4:5], v[4:5], v[20:21] neg_lo:[0,1] neg_hi:[0,1]
	v_pk_add_f32 v[6:7], v[6:7], v[22:23] neg_lo:[0,1] neg_hi:[0,1]
	s_waitcnt vmcnt(15)
	v_lshlrev_b32_e32 v8, 16, v124
	v_and_b32_e32 v9, 0xffff0000, v124
	v_lshlrev_b32_e32 v10, 16, v125
	v_and_b32_e32 v11, 0xffff0000, v125
	v_lshlrev_b32_e32 v12, 16, v126
	v_and_b32_e32 v13, 0xffff0000, v126
	v_lshlrev_b32_e32 v14, 16, v127
	v_and_b32_e32 v15, 0xffff0000, v127
	v_pk_add_f32 v[0:1], v[0:1], v[8:9]
	v_pk_add_f32 v[2:3], v[2:3], v[10:11]
	v_pk_add_f32 v[4:5], v[4:5], v[12:13]
	v_pk_add_f32 v[6:7], v[6:7], v[14:15]
	v_fma_f32 v24, v36, v0, -v8
	v_fma_f32 v25, v36, v1, -v9
	v_fma_f32 v26, v36, v2, -v10
	v_fma_f32 v27, v36, v3, -v11
	v_fma_f32 v28, v36, v4, -v12
	v_fma_f32 v29, v36, v5, -v13
	v_fma_f32 v30, v36, v6, -v14
	v_fma_f32 v31, v36, v7, -v15
	v_pk_mul_f32 v[24:25], v[24:25], 4.0 op_sel_hi:[1,0]
	v_pk_mul_f32 v[26:27], v[26:27], 4.0 op_sel_hi:[1,0]
	v_pk_mul_f32 v[28:29], v[28:29], 4.0 op_sel_hi:[1,0]
	v_pk_mul_f32 v[30:31], v[30:31], 4.0 op_sel_hi:[1,0]
	v_med3_f32 v24, v24, s33, v229
	v_med3_f32 v25, v25, s33, v229
	v_med3_f32 v26, v26, s33, v229
	v_med3_f32 v27, v27, s33, v229
	v_med3_f32 v28, v28, s33, v229
	v_med3_f32 v29, v29, s33, v229
	v_med3_f32 v30, v30, s33, v229
	v_med3_f32 v31, v31, s33, v229
	v_add_u32_e32 v35, 0xb400, v34
	v_cvt_pk_fp8_f32 v40, v24, v25
	v_cvt_pk_fp8_f32 v41, v28, v29
	v_cvt_pk_fp8_f32 v40, v26, v27 op_sel:[0,0,1]
	v_cvt_pk_fp8_f32 v41, v30, v31 op_sel:[0,0,1]
	global_store_dwordx2 v35, v[40:41], s[4:5]
	s_branch .Lmy_cp_next
; template <int WIN> __device__ __forceinline__ void pool_task(const Params& p, int t0, int c) {
;     const bf16* PROJ = (const bf16*)(p.ws + WS_PROJ); unsigned char* YABC = p.ws + WS_YABC;
;     float ring[WIN][8], tot[8];
; #pragma unroll
;     for (int i = 0; i < 8; ++i) tot[i] = 0.f;
; #pragma unroll
;     for (int d = 1 - WIN; d < 0; ++d) {
;         if (t0 > 0) { ld8(PROJ + (size_t)(t0 + d) * INC + 5120 + c, ring[(d + WIN) % WIN]);
; #pragma unroll
;             for (int i = 0; i < 8; ++i) tot[i] += ring[(d + WIN) % WIN][i]; }
;         else {
; #pragma unroll
;             for (int i = 0; i < 8; ++i) ring[(d + WIN) % WIN][i] = 0.f; }
;     }
; #pragma unroll
;     for (int k = 0; k < 16; ++k) { const int t = t0 + k;
;         float cur[8], o[8]; ld8(PROJ + (size_t)t * INC + 5120 + c, cur);
;         const float inv = (k + 1 < WIN && t0 == 0) ? 1.0f / (float)(k + 1) : 1.0f / (float)WIN;
; #pragma unroll
;         for (int i = 0; i < 8; ++i) { tot[i] += cur[i]; o[i] = tot[i] * inv - cur[i]; ring[k % WIN][i] = cur[i]; }
;         st8q(YABC + (size_t)t * 3072 + 2048 + c, o);
; #pragma unroll
;         for (int i = 0; i < 8; ++i) tot[i] -= ring[(k + 1) % WIN][i];
;     }
; }
.Lmy_pool_w4:
	v_and_b32_e32 v35, 31, v67
	v_lshrrev_b32_e32 v32, 8, v67
	s_lshl_b32 s10, s7, 1
	v_add_lshl_u32 v32, v32, s10, 1
	v_bfe_u32 v38, v67, 5, 1
	v_add_lshl_u32 v32, v32, v38, 4
	v_or_b32_e32 v35, 32, v35
	v_mul_u32_u24_e32 v33, 0x3000, v32
	v_lshl_add_u32 v33, v35, 4, v33
	v_add_u32_e32 v33, 0x1000, v33
	v_mul_u32_u24_e32 v34, 0xc00, v32
	v_lshl_add_u32 v34, v35, 3, v34
	v_add_u32_e32 v34, 0x800, v34
	v_mov_b32_e32 v56, 0
	v_mov_b32_e32 v57, 0
	v_mov_b32_e32 v58, 0
	v_mov_b32_e32 v59, 0
	v_mov_b32_e32 v60, 0
	v_mov_b32_e32 v61, 0
	v_mov_b32_e32 v62, 0
	v_mov_b32_e32 v63, 0
	v_mov_b32_e32 v68, 0
	v_mov_b32_e32 v69, 0
	v_mov_b32_e32 v70, 0
	v_mov_b32_e32 v71, 0
	v_cmp_ne_u32_e32 vcc, 0, v32
	s_and_saveexec_b64 s[10:11], vcc
	v_add_u32_e32 v35, 0xffff7000, v33
	global_load_dwordx4 v[56:59], v35, s[2:3] nt
	v_add_u32_e32 v35, 0xffffa000, v33
	global_load_dwordx4 v[60:63], v35, s[2:3] nt
	v_add_u32_e32 v35, 0xffffd000, v33
	global_load_dwordx4 v[68:71], v35, s[2:3] nt
	s_mov_b64 exec, s[0:1]
	global_load_dwordx4 v[72:75], v33, s[2:3] nt
	v_add_u32_e32 v35, 0x3000, v33
	global_load_dwordx4 v[76:79], v35, s[2:3] nt
	v_add_u32_e32 v35, 0x6000, v33
	global_load_dwordx4 v[80:83], v35, s[2:3] nt
	v_add_u32_e32 v35, 0x9000, v33
	global_load_dwordx4 v[84:87], v35, s[2:3] nt
	v_add_u32_e32 v35, 0xc000, v33
	global_load_dwordx4 v[88:91], v35, s[2:3] nt
	v_add_u32_e32 v35, 0xf000, v33
	global_load_dwordx4 v[92:95], v35, s[2:3] nt
	v_add_u32_e32 v35, 0x12000, v33
	global_load_dwordx4 v[96:99], v35, s[2:3] nt
	v_add_u32_e32 v35, 0x15000, v33
	global_load_dwordx4 v[100:103], v35, s[2:3] nt
	v_add_u32_e32 v35, 0x18000, v33
	global_load_dwordx4 v[104:107], v35, s[2:3] nt
	v_add_u32_e32 v35, 0x1b000, v33
	global_load_dwordx4 v[108:111], v35, s[2:3] nt
	v_add_u32_e32 v35, 0x1e000, v33
	global_load_dwordx4 v[112:115], v35, s[2:3] nt
	v_add_u32_e32 v35, 0x21000, v33
	global_load_dwordx4 v[116:119], v35, s[2:3] nt
	v_add_u32_e32 v35, 0x24000, v33
	global_load_dwordx4 v[120:123], v35, s[2:3] nt
	v_add_u32_e32 v35, 0x27000, v33
	global_load_dwordx4 v[124:127], v35, s[2:3] nt
	v_add_u32_e32 v35, 0x2a000, v33
	global_load_dwordx4 v[128:131], v35, s[2:3] nt
	v_add_u32_e32 v35, 0x2d000, v33
	global_load_dwordx4 v[132:135], v35, s[2:3] nt
	v_cmp_eq_u32_e32 vcc, 0, v32
	v_mov_b32_e32 v36, 0x3e800000
	v_mov_b64_e32 v[0:1], 0
	v_mov_b64_e32 v[2:3], 0
	v_mov_b64_e32 v[4:5], 0
	v_mov_b64_e32 v[6:7], 0
	s_waitcnt vmcnt(18)
	v_lshlrev_b32_e32 v8, 16, v56
	v_and_b32_e32 v9, 0xffff0000, v56
	v_lshlrev_b32_e32 v10, 16, v57
	v_and_b32_e32 v11, 0xffff0000, v57
	v_lshlrev_b32_e32 v12, 16, v58
	v_and_b32_e32 v13, 0xffff0000, v58
	v_lshlrev_b32_e32 v14, 16, v59
	v_and_b32_e32 v15, 0xffff0000, v59
	v_pk_add_f32 v[0:1], v[0:1], v[8:9]
	v_pk_add_f32 v[2:3], v[2:3], v[10:11]
	v_pk_add_f32 v[4:5], v[4:5], v[12:13]
	v_pk_add_f32 v[6:7], v[6:7], v[14:15]
	s_waitcnt vmcnt(17)
	v_lshlrev_b32_e32 v8, 16, v60
	v_and_b32_e32 v9, 0xffff0000, v60
	v_lshlrev_b32_e32 v10, 16, v61
	v_and_b32_e32 v11, 0xffff0000, v61
	v_lshlrev_b32_e32 v12, 16, v62
	v_and_b32_e32 v13, 0xffff0000, v62
	v_lshlrev_b32_e32 v14, 16, v63
	v_and_b32_e32 v15, 0xffff0000, v63
	v_pk_add_f32 v[0:1], v[0:1], v[8:9]
	v_pk_add_f32 v[2:3], v[2:3], v[10:11]
	v_pk_add_f32 v[4:5], v[4:5], v[12:13]
	v_pk_add_f32 v[6:7], v[6:7], v[14:15]
	s_waitcnt vmcnt(16)
	v_lshlrev_b32_e32 v8, 16, v68
	v_and_b32_e32 v9, 0xffff0000, v68
	v_lshlrev_b32_e32 v10, 16, v69
	v_and_b32_e32 v11, 0xffff0000, v69
	v_lshlrev_b32_e32 v12, 16, v70
	v_and_b32_e32 v13, 0xffff0000, v70
	v_lshlrev_b32_e32 v14, 16, v71
	v_and_b32_e32 v15, 0xffff0000, v71
	v_pk_add_f32 v[0:1], v[0:1], v[8:9]
	v_pk_add_f32 v[2:3], v[2:3], v[10:11]
	v_pk_add_f32 v[4:5], v[4:5], v[12:13]
	v_pk_add_f32 v[6:7], v[6:7], v[14:15]
	s_waitcnt vmcnt(15)
	v_lshlrev_b32_e32 v8, 16, v72
	v_and_b32_e32 v9, 0xffff0000, v72
	v_lshlrev_b32_e32 v10, 16, v73
	v_and_b32_e32 v11, 0xffff0000, v73
	v_lshlrev_b32_e32 v12, 16, v74
	v_and_b32_e32 v13, 0xffff0000, v74
	v_lshlrev_b32_e32 v14, 16, v75
	v_and_b32_e32 v15, 0xffff0000, v75
	v_pk_add_f32 v[0:1], v[0:1], v[8:9]
	v_pk_add_f32 v[2:3], v[2:3], v[10:11]
	v_pk_add_f32 v[4:5], v[4:5], v[12:13]
	v_pk_add_f32 v[6:7], v[6:7], v[14:15]
	v_mov_b32_e32 v38, 0x3f800000
	v_cndmask_b32_e32 v37, v36, v38, vcc
	v_fma_f32 v24, v37, v0, -v8
	v_fma_f32 v25, v37, v1, -v9
	v_fma_f32 v26, v37, v2, -v10
	v_fma_f32 v27, v37, v3, -v11
	v_fma_f32 v28, v37, v4, -v12
	v_fma_f32 v29, v37, v5, -v13
	v_fma_f32 v30, v37, v6, -v14
	v_fma_f32 v31, v37, v7, -v15
	v_pk_mul_f32 v[24:25], v[24:25], 4.0 op_sel_hi:[1,0]
	v_pk_mul_f32 v[26:27], v[26:27], 4.0 op_sel_hi:[1,0]
	v_pk_mul_f32 v[28:29], v[28:29], 4.0 op_sel_hi:[1,0]
	v_pk_mul_f32 v[30:31], v[30:31], 4.0 op_sel_hi:[1,0]
	v_med3_f32 v24, v24, s33, v229
	v_med3_f32 v25, v25, s33, v229
	v_med3_f32 v26, v26, s33, v229
	v_med3_f32 v27, v27, s33, v229
	v_med3_f32 v28, v28, s33, v229
	v_med3_f32 v29, v29, s33, v229
	v_med3_f32 v30, v30, s33, v229
	v_med3_f32 v31, v31, s33, v229
	v_cvt_pk_fp8_f32 v40, v24, v25
	v_cvt_pk_fp8_f32 v41, v28, v29
	v_cvt_pk_fp8_f32 v40, v26, v27 op_sel:[0,0,1]
	v_cvt_pk_fp8_f32 v41, v30, v31 op_sel:[0,0,1]
	global_store_dwordx2 v34, v[40:41], s[4:5]
	v_lshlrev_b32_e32 v16, 16, v56
	v_and_b32_e32 v17, 0xffff0000, v56
	v_lshlrev_b32_e32 v18, 16, v57
	v_and_b32_e32 v19, 0xffff0000, v57
	v_lshlrev_b32_e32 v20, 16, v58
	v_and_b32_e32 v21, 0xffff0000, v58
	v_lshlrev_b32_e32 v22, 16, v59
	v_and_b32_e32 v23, 0xffff0000, v59
	v_pk_add_f32 v[0:1], v[0:1], v[16:17] neg_lo:[0,1] neg_hi:[0,1]
	v_pk_add_f32 v[2:3], v[2:3], v[18:19] neg_lo:[0,1] neg_hi:[0,1]
	v_pk_add_f32 v[4:5], v[4:5], v[20:21] neg_lo:[0,1] neg_hi:[0,1]
	v_pk_add_f32 v[6:7], v[6:7], v[22:23] neg_lo:[0,1] neg_hi:[0,1]
	s_waitcnt vmcnt(15)
; __device__ __forceinline__ unsigned pk4_fp8(float a, float b, float c, float d) { unsigned w = 0u; w = __builtin_amdgcn_cvt_pk_fp8_f32(clamp8(a), clamp8(b), w, false); w = __builtin_amdgcn_cvt_pk_fp8_f32(clamp8(c), clamp8(d), w, true); return w; }
; __device__ __forceinline__ void st8q(unsigned char* ptr, const float (&f)[8]) {
;     u32x2 w; w.x = pk4_fp8(4.f * f[0], 4.f * f[1], 4.f * f[2], 4.f * f[3]); w.y = pk4_fp8(4.f * f[4], 4.f * f[5], 4.f * f[6], 4.f * f[7]); *(u32x2*)ptr = w;
; }
; template <int WIN> __device__ __forceinline__ void pool_task(const Params& p, int t0, int c) {
;     ...
; #pragma unroll
;     for (int k = 0; k < 16; ++k) { const int t = t0 + k;
;         float cur[8], o[8]; ld8(PROJ + (size_t)t * INC + 5120 + c, cur);
;         const float inv = (k + 1 < WIN && t0 == 0) ? 1.0f / (float)(k + 1) : 1.0f / (float)WIN;
; #pragma unroll
;         for (int i = 0; i < 8; ++i) { tot[i] += cur[i]; o[i] = tot[i] * inv - cur[i]; ring[k % WIN][i] = cur[i]; }
;         st8q(YABC + (size_t)t * 3072 + 2048 + c, o);
; #pragma unroll
;         for (int i = 0; i < 8; ++i) tot[i] -= ring[(k + 1) % WIN][i];
;     }
; }
	v_lshlrev_b32_e32 v8, 16, v76
	v_and_b32_e32 v9, 0xffff0000, v76
	v_lshlrev_b32_e32 v10, 16, v77
	v_and_b32_e32 v11, 0xffff0000, v77
	v_lshlrev_b32_e32 v12, 16, v78
	v_and_b32_e32 v13, 0xffff0000, v78
	v_lshlrev_b32_e32 v14, 16, v79
	v_and_b32_e32 v15, 0xffff0000, v79
	v_pk_add_f32 v[0:1], v[0:1], v[8:9]
	v_pk_add_f32 v[2:3], v[2:3], v[10:11]
	v_pk_add_f32 v[4:5], v[4:5], v[12:13]
	v_pk_add_f32 v[6:7], v[6:7], v[14:15]
	v_mov_b32_e32 v38, 0x3f000000
	v_cndmask_b32_e32 v37, v36, v38, vcc
	v_fma_f32 v24, v37, v0, -v8
	v_fma_f32 v25, v37, v1, -v9
	v_fma_f32 v26, v37, v2, -v10
	v_fma_f32 v27, v37, v3, -v11
	v_fma_f32 v28, v37, v4, -v12
	v_fma_f32 v29, v37, v5, -v13
	v_fma_f32 v30, v37, v6, -v14
	v_fma_f32 v31, v37, v7, -v15
	v_pk_mul_f32 v[24:25], v[24:25], 4.0 op_sel_hi:[1,0]
	v_pk_mul_f32 v[26:27], v[26:27], 4.0 op_sel_hi:[1,0]
	v_pk_mul_f32 v[28:29], v[28:29], 4.0 op_sel_hi:[1,0]
	v_pk_mul_f32 v[30:31], v[30:31], 4.0 op_sel_hi:[1,0]
	v_med3_f32 v24, v24, s33, v229
	v_med3_f32 v25, v25, s33, v229
	v_med3_f32 v26, v26, s33, v229
	v_med3_f32 v27, v27, s33, v229
	v_med3_f32 v28, v28, s33, v229
	v_med3_f32 v29, v29, s33, v229
	v_med3_f32 v30, v30, s33, v229
	v_med3_f32 v31, v31, s33, v229
	v_add_u32_e32 v35, 0xc00, v34
	v_cvt_pk_fp8_f32 v40, v24, v25
	v_cvt_pk_fp8_f32 v41, v28, v29
	v_cvt_pk_fp8_f32 v40, v26, v27 op_sel:[0,0,1]
	v_cvt_pk_fp8_f32 v41, v30, v31 op_sel:[0,0,1]
	global_store_dwordx2 v35, v[40:41], s[4:5]
	v_lshlrev_b32_e32 v16, 16, v60
	v_and_b32_e32 v17, 0xffff0000, v60
	v_lshlrev_b32_e32 v18, 16, v61
	v_and_b32_e32 v19, 0xffff0000, v61
	v_lshlrev_b32_e32 v20, 16, v62
	v_and_b32_e32 v21, 0xffff0000, v62
	v_lshlrev_b32_e32 v22, 16, v63
	v_and_b32_e32 v23, 0xffff0000, v63
	v_pk_add_f32 v[0:1], v[0:1], v[16:17] neg_lo:[0,1] neg_hi:[0,1]
	v_pk_add_f32 v[2:3], v[2:3], v[18:19] neg_lo:[0,1] neg_hi:[0,1]
	v_pk_add_f32 v[4:5], v[4:5], v[20:21] neg_lo:[0,1] neg_hi:[0,1]
	v_pk_add_f32 v[6:7], v[6:7], v[22:23] neg_lo:[0,1] neg_hi:[0,1]
	s_waitcnt vmcnt(15)
	v_lshlrev_b32_e32 v8, 16, v80
	v_and_b32_e32 v9, 0xffff0000, v80
	v_lshlrev_b32_e32 v10, 16, v81
	v_and_b32_e32 v11, 0xffff0000, v81
	v_lshlrev_b32_e32 v12, 16, v82
	v_and_b32_e32 v13, 0xffff0000, v82
	v_lshlrev_b32_e32 v14, 16, v83
	v_and_b32_e32 v15, 0xffff0000, v83
	v_pk_add_f32 v[0:1], v[0:1], v[8:9]
	v_pk_add_f32 v[2:3], v[2:3], v[10:11]
	v_pk_add_f32 v[4:5], v[4:5], v[12:13]
	v_pk_add_f32 v[6:7], v[6:7], v[14:15]
	v_mov_b32_e32 v38, 0x3eaaaaab
	v_cndmask_b32_e32 v37, v36, v38, vcc
	v_fma_f32 v24, v37, v0, -v8
	v_fma_f32 v25, v37, v1, -v9
	v_fma_f32 v26, v37, v2, -v10
	v_fma_f32 v27, v37, v3, -v11
	v_fma_f32 v28, v37, v4, -v12
	v_fma_f32 v29, v37, v5, -v13
	v_fma_f32 v30, v37, v6, -v14
	v_fma_f32 v31, v37, v7, -v15
	v_pk_mul_f32 v[24:25], v[24:25], 4.0 op_sel_hi:[1,0]
	v_pk_mul_f32 v[26:27], v[26:27], 4.0 op_sel_hi:[1,0]
	v_pk_mul_f32 v[28:29], v[28:29], 4.0 op_sel_hi:[1,0]
	v_pk_mul_f32 v[30:31], v[30:31], 4.0 op_sel_hi:[1,0]
	v_med3_f32 v24, v24, s33, v229
	v_med3_f32 v25, v25, s33, v229
	v_med3_f32 v26, v26, s33, v229
	v_med3_f32 v27, v27, s33, v229
	v_med3_f32 v28, v28, s33, v229
	v_med3_f32 v29, v29, s33, v229
	v_med3_f32 v30, v30, s33, v229
	v_med3_f32 v31, v31, s33, v229
	v_add_u32_e32 v35, 0x1800, v34
	v_cvt_pk_fp8_f32 v40, v24, v25
	v_cvt_pk_fp8_f32 v41, v28, v29
	v_cvt_pk_fp8_f32 v40, v26, v27 op_sel:[0,0,1]
	v_cvt_pk_fp8_f32 v41, v30, v31 op_sel:[0,0,1]
	global_store_dwordx2 v35, v[40:41], s[4:5]
	v_lshlrev_b32_e32 v16, 16, v68
	v_and_b32_e32 v17, 0xffff0000, v68
	v_lshlrev_b32_e32 v18, 16, v69
	v_and_b32_e32 v19, 0xffff0000, v69
	v_lshlrev_b32_e32 v20, 16, v70
	v_and_b32_e32 v21, 0xffff0000, v70
	v_lshlrev_b32_e32 v22, 16, v71
	v_and_b32_e32 v23, 0xffff0000, v71
	v_pk_add_f32 v[0:1], v[0:1], v[16:17] neg_lo:[0,1] neg_hi:[0,1]
	v_pk_add_f32 v[2:3], v[2:3], v[18:19] neg_lo:[0,1] neg_hi:[0,1]
	v_pk_add_f32 v[4:5], v[4:5], v[20:21] neg_lo:[0,1] neg_hi:[0,1]
	v_pk_add_f32 v[6:7], v[6:7], v[22:23] neg_lo:[0,1] neg_hi:[0,1]
	s_waitcnt vmcnt(15)
	v_lshlrev_b32_e32 v8, 16, v84
	v_and_b32_e32 v9, 0xffff0000, v84
	v_lshlrev_b32_e32 v10, 16, v85
	v_and_b32_e32 v11, 0xffff0000, v85
	v_lshlrev_b32_e32 v12, 16, v86
	v_and_b32_e32 v13, 0xffff0000, v86
	v_lshlrev_b32_e32 v14, 16, v87
	v_and_b32_e32 v15, 0xffff0000, v87
	v_pk_add_f32 v[0:1], v[0:1], v[8:9]
	v_pk_add_f32 v[2:3], v[2:3], v[10:11]
	v_pk_add_f32 v[4:5], v[4:5], v[12:13]
	v_pk_add_f32 v[6:7], v[6:7], v[14:15]
	v_fma_f32 v24, v36, v0, -v8
	v_fma_f32 v25, v36, v1, -v9
	v_fma_f32 v26, v36, v2, -v10
	v_fma_f32 v27, v36, v3, -v11
	v_fma_f32 v28, v36, v4, -v12
	v_fma_f32 v29, v36, v5, -v13
	v_fma_f32 v30, v36, v6, -v14
	v_fma_f32 v31, v36, v7, -v15
	v_pk_mul_f32 v[24:25], v[24:25], 4.0 op_sel_hi:[1,0]
	v_pk_mul_f32 v[26:27], v[26:27], 4.0 op_sel_hi:[1,0]
	v_pk_mul_f32 v[28:29], v[28:29], 4.0 op_sel_hi:[1,0]
	v_pk_mul_f32 v[30:31], v[30:31], 4.0 op_sel_hi:[1,0]
	v_med3_f32 v24, v24, s33, v229
	v_med3_f32 v25, v25, s33, v229
	v_med3_f32 v26, v26, s33, v229
	v_med3_f32 v27, v27, s33, v229
	v_med3_f32 v28, v28, s33, v229
	v_med3_f32 v29, v29, s33, v229
	v_med3_f32 v30, v30, s33, v229
	v_med3_f32 v31, v31, s33, v229
	v_add_u32_e32 v35, 0x2400, v34
	v_cvt_pk_fp8_f32 v40, v24, v25
	v_cvt_pk_fp8_f32 v41, v28, v29
	v_cvt_pk_fp8_f32 v40, v26, v27 op_sel:[0,0,1]
	v_cvt_pk_fp8_f32 v41, v30, v31 op_sel:[0,0,1]
	global_store_dwordx2 v35, v[40:41], s[4:5]
	v_lshlrev_b32_e32 v16, 16, v72
	v_and_b32_e32 v17, 0xffff0000, v72
	v_lshlrev_b32_e32 v18, 16, v73
	v_and_b32_e32 v19, 0xffff0000, v73
	v_lshlrev_b32_e32 v20, 16, v74
	v_and_b32_e32 v21, 0xffff0000, v74
	v_lshlrev_b32_e32 v22, 16, v75
	v_and_b32_e32 v23, 0xffff0000, v75
	v_pk_add_f32 v[0:1], v[0:1], v[16:17] neg_lo:[0,1] neg_hi:[0,1]
	v_pk_add_f32 v[2:3], v[2:3], v[18:19] neg_lo:[0,1] neg_hi:[0,1]
	v_pk_add_f32 v[4:5], v[4:5], v[20:21] neg_lo:[0,1] neg_hi:[0,1]
	v_pk_add_f32 v[6:7], v[6:7], v[22:23] neg_lo:[0,1] neg_hi:[0,1]
	s_waitcnt vmcnt(15)
; __device__ __forceinline__ unsigned pk4_fp8(float a, float b, float c, float d) { unsigned w = 0u; w = __builtin_amdgcn_cvt_pk_fp8_f32(clamp8(a), clamp8(b), w, false); w = __builtin_amdgcn_cvt_pk_fp8_f32(clamp8(c), clamp8(d), w, true); return w; }
; __device__ __forceinline__ void st8q(unsigned char* ptr, const float (&f)[8]) {
;     u32x2 w; w.x = pk4_fp8(4.f * f[0], 4.f * f[1], 4.f * f[2], 4.f * f[3]); w.y = pk4_fp8(4.f * f[4], 4.f * f[5], 4.f * f[6], 4.f * f[7]); *(u32x2*)ptr = w;
; }
; template <int WIN> __device__ __forceinline__ void pool_task(const Params& p, int t0, int c) {
;     ...
; #pragma unroll
;     for (int k = 0; k < 16; ++k) { const int t = t0 + k;
;         float cur[8], o[8]; ld8(PROJ + (size_t)t * INC + 5120 + c, cur);
;         const float inv = (k + 1 < WIN && t0 == 0) ? 1.0f / (float)(k + 1) : 1.0f / (float)WIN;
; #pragma unroll
;         for (int i = 0; i < 8; ++i) { tot[i] += cur[i]; o[i] = tot[i] * inv - cur[i]; ring[k % WIN][i] = cur[i]; }
;         st8q(YABC + (size_t)t * 3072 + 2048 + c, o);
; #pragma unroll
;         for (int i = 0; i < 8; ++i) tot[i] -= ring[(k + 1) % WIN][i];
;     }
; }
	v_lshlrev_b32_e32 v8, 16, v88
	v_and_b32_e32 v9, 0xffff0000, v88
	v_lshlrev_b32_e32 v10, 16, v89
	v_and_b32_e32 v11, 0xffff0000, v89
	v_lshlrev_b32_e32 v12, 16, v90
	v_and_b32_e32 v13, 0xffff0000, v90
	v_lshlrev_b32_e32 v14, 16, v91
	v_and_b32_e32 v15, 0xffff0000, v91
	v_pk_add_f32 v[0:1], v[0:1], v[8:9]
	v_pk_add_f32 v[2:3], v[2:3], v[10:11]
	v_pk_add_f32 v[4:5], v[4:5], v[12:13]
	v_pk_add_f32 v[6:7], v[6:7], v[14:15]
	v_fma_f32 v24, v36, v0, -v8
	v_fma_f32 v25, v36, v1, -v9
	v_fma_f32 v26, v36, v2, -v10
	v_fma_f32 v27, v36, v3, -v11
	v_fma_f32 v28, v36, v4, -v12
	v_fma_f32 v29, v36, v5, -v13
	v_fma_f32 v30, v36, v6, -v14
	v_fma_f32 v31, v36, v7, -v15
	v_pk_mul_f32 v[24:25], v[24:25], 4.0 op_sel_hi:[1,0]
	v_pk_mul_f32 v[26:27], v[26:27], 4.0 op_sel_hi:[1,0]
	v_pk_mul_f32 v[28:29], v[28:29], 4.0 op_sel_hi:[1,0]
	v_pk_mul_f32 v[30:31], v[30:31], 4.0 op_sel_hi:[1,0]
	v_med3_f32 v24, v24, s33, v229
	v_med3_f32 v25, v25, s33, v229
	v_med3_f32 v26, v26, s33, v229
	v_med3_f32 v27, v27, s33, v229
	v_med3_f32 v28, v28, s33, v229
	v_med3_f32 v29, v29, s33, v229
	v_med3_f32 v30, v30, s33, v229
	v_med3_f32 v31, v31, s33, v229
	v_add_u32_e32 v35, 0x3000, v34
	v_cvt_pk_fp8_f32 v40, v24, v25
	v_cvt_pk_fp8_f32 v41, v28, v29
	v_cvt_pk_fp8_f32 v40, v26, v27 op_sel:[0,0,1]
	v_cvt_pk_fp8_f32 v41, v30, v31 op_sel:[0,0,1]
	global_store_dwordx2 v35, v[40:41], s[4:5]
	v_lshlrev_b32_e32 v16, 16, v76
	v_and_b32_e32 v17, 0xffff0000, v76
	v_lshlrev_b32_e32 v18, 16, v77
	v_and_b32_e32 v19, 0xffff0000, v77
	v_lshlrev_b32_e32 v20, 16, v78
	v_and_b32_e32 v21, 0xffff0000, v78
	v_lshlrev_b32_e32 v22, 16, v79
	v_and_b32_e32 v23, 0xffff0000, v79
	v_pk_add_f32 v[0:1], v[0:1], v[16:17] neg_lo:[0,1] neg_hi:[0,1]
	v_pk_add_f32 v[2:3], v[2:3], v[18:19] neg_lo:[0,1] neg_hi:[0,1]
	v_pk_add_f32 v[4:5], v[4:5], v[20:21] neg_lo:[0,1] neg_hi:[0,1]
	v_pk_add_f32 v[6:7], v[6:7], v[22:23] neg_lo:[0,1] neg_hi:[0,1]
	s_waitcnt vmcnt(15)
	v_lshlrev_b32_e32 v8, 16, v92
	v_and_b32_e32 v9, 0xffff0000, v92
	v_lshlrev_b32_e32 v10, 16, v93
	v_and_b32_e32 v11, 0xffff0000, v93
	v_lshlrev_b32_e32 v12, 16, v94
	v_and_b32_e32 v13, 0xffff0000, v94
	v_lshlrev_b32_e32 v14, 16, v95
	v_and_b32_e32 v15, 0xffff0000, v95
	v_pk_add_f32 v[0:1], v[0:1], v[8:9]
	v_pk_add_f32 v[2:3], v[2:3], v[10:11]
	v_pk_add_f32 v[4:5], v[4:5], v[12:13]
	v_pk_add_f32 v[6:7], v[6:7], v[14:15]
	v_fma_f32 v24, v36, v0, -v8
	v_fma_f32 v25, v36, v1, -v9
	v_fma_f32 v26, v36, v2, -v10
	v_fma_f32 v27, v36, v3, -v11
	v_fma_f32 v28, v36, v4, -v12
	v_fma_f32 v29, v36, v5, -v13
	v_fma_f32 v30, v36, v6, -v14
	v_fma_f32 v31, v36, v7, -v15
	v_pk_mul_f32 v[24:25], v[24:25], 4.0 op_sel_hi:[1,0]
	v_pk_mul_f32 v[26:27], v[26:27], 4.0 op_sel_hi:[1,0]
	v_pk_mul_f32 v[28:29], v[28:29], 4.0 op_sel_hi:[1,0]
	v_pk_mul_f32 v[30:31], v[30:31], 4.0 op_sel_hi:[1,0]
	v_med3_f32 v24, v24, s33, v229
	v_med3_f32 v25, v25, s33, v229
	v_med3_f32 v26, v26, s33, v229
	v_med3_f32 v27, v27, s33, v229
	v_med3_f32 v28, v28, s33, v229
	v_med3_f32 v29, v29, s33, v229
	v_med3_f32 v30, v30, s33, v229
	v_med3_f32 v31, v31, s33, v229
	v_add_u32_e32 v35, 0x3c00, v34
	v_cvt_pk_fp8_f32 v40, v24, v25
	v_cvt_pk_fp8_f32 v41, v28, v29
	v_cvt_pk_fp8_f32 v40, v26, v27 op_sel:[0,0,1]
	v_cvt_pk_fp8_f32 v41, v30, v31 op_sel:[0,0,1]
	global_store_dwordx2 v35, v[40:41], s[4:5]
	v_lshlrev_b32_e32 v16, 16, v80
	v_and_b32_e32 v17, 0xffff0000, v80
	v_lshlrev_b32_e32 v18, 16, v81
	v_and_b32_e32 v19, 0xffff0000, v81
	v_lshlrev_b32_e32 v20, 16, v82
	v_and_b32_e32 v21, 0xffff0000, v82
	v_lshlrev_b32_e32 v22, 16, v83
	v_and_b32_e32 v23, 0xffff0000, v83
	v_pk_add_f32 v[0:1], v[0:1], v[16:17] neg_lo:[0,1] neg_hi:[0,1]
	v_pk_add_f32 v[2:3], v[2:3], v[18:19] neg_lo:[0,1] neg_hi:[0,1]
	v_pk_add_f32 v[4:5], v[4:5], v[20:21] neg_lo:[0,1] neg_hi:[0,1]
	v_pk_add_f32 v[6:7], v[6:7], v[22:23] neg_lo:[0,1] neg_hi:[0,1]
	s_waitcnt vmcnt(15)
	v_lshlrev_b32_e32 v8, 16, v96
	v_and_b32_e32 v9, 0xffff0000, v96
	v_lshlrev_b32_e32 v10, 16, v97
	v_and_b32_e32 v11, 0xffff0000, v97
	v_lshlrev_b32_e32 v12, 16, v98
	v_and_b32_e32 v13, 0xffff0000, v98
	v_lshlrev_b32_e32 v14, 16, v99
	v_and_b32_e32 v15, 0xffff0000, v99
	v_pk_add_f32 v[0:1], v[0:1], v[8:9]
	v_pk_add_f32 v[2:3], v[2:3], v[10:11]
	v_pk_add_f32 v[4:5], v[4:5], v[12:13]
	v_pk_add_f32 v[6:7], v[6:7], v[14:15]
	v_fma_f32 v24, v36, v0, -v8
	v_fma_f32 v25, v36, v1, -v9
	v_fma_f32 v26, v36, v2, -v10
	v_fma_f32 v27, v36, v3, -v11
	v_fma_f32 v28, v36, v4, -v12
	v_fma_f32 v29, v36, v5, -v13
	v_fma_f32 v30, v36, v6, -v14
	v_fma_f32 v31, v36, v7, -v15
	v_pk_mul_f32 v[24:25], v[24:25], 4.0 op_sel_hi:[1,0]
	v_pk_mul_f32 v[26:27], v[26:27], 4.0 op_sel_hi:[1,0]
	v_pk_mul_f32 v[28:29], v[28:29], 4.0 op_sel_hi:[1,0]
	v_pk_mul_f32 v[30:31], v[30:31], 4.0 op_sel_hi:[1,0]
	v_med3_f32 v24, v24, s33, v229
	v_med3_f32 v25, v25, s33, v229
	v_med3_f32 v26, v26, s33, v229
	v_med3_f32 v27, v27, s33, v229
	v_med3_f32 v28, v28, s33, v229
	v_med3_f32 v29, v29, s33, v229
	v_med3_f32 v30, v30, s33, v229
	v_med3_f32 v31, v31, s33, v229
	v_add_u32_e32 v35, 0x4800, v34
	v_cvt_pk_fp8_f32 v40, v24, v25
	v_cvt_pk_fp8_f32 v41, v28, v29
	v_cvt_pk_fp8_f32 v40, v26, v27 op_sel:[0,0,1]
	v_cvt_pk_fp8_f32 v41, v30, v31 op_sel:[0,0,1]
	global_store_dwordx2 v35, v[40:41], s[4:5]
	v_lshlrev_b32_e32 v16, 16, v84
	v_and_b32_e32 v17, 0xffff0000, v84
	v_lshlrev_b32_e32 v18, 16, v85
	v_and_b32_e32 v19, 0xffff0000, v85
	v_lshlrev_b32_e32 v20, 16, v86
	v_and_b32_e32 v21, 0xffff0000, v86
	v_lshlrev_b32_e32 v22, 16, v87
	v_and_b32_e32 v23, 0xffff0000, v87
	v_pk_add_f32 v[0:1], v[0:1], v[16:17] neg_lo:[0,1] neg_hi:[0,1]
	v_pk_add_f32 v[2:3], v[2:3], v[18:19] neg_lo:[0,1] neg_hi:[0,1]
	v_pk_add_f32 v[4:5], v[4:5], v[20:21] neg_lo:[0,1] neg_hi:[0,1]
	v_pk_add_f32 v[6:7], v[6:7], v[22:23] neg_lo:[0,1] neg_hi:[0,1]
	s_waitcnt vmcnt(15)
; __device__ __forceinline__ unsigned pk4_fp8(float a, float b, float c, float d) { unsigned w = 0u; w = __builtin_amdgcn_cvt_pk_fp8_f32(clamp8(a), clamp8(b), w, false); w = __builtin_amdgcn_cvt_pk_fp8_f32(clamp8(c), clamp8(d), w, true); return w; }
; __device__ __forceinline__ void st8q(unsigned char* ptr, const float (&f)[8]) {
;     u32x2 w; w.x = pk4_fp8(4.f * f[0], 4.f * f[1], 4.f * f[2], 4.f * f[3]); w.y = pk4_fp8(4.f * f[4], 4.f * f[5], 4.f * f[6], 4.f * f[7]); *(u32x2*)ptr = w;
; }
; template <int WIN> __device__ __forceinline__ void pool_task(const Params& p, int t0, int c) {
;     ...
; #pragma unroll
;     for (int k = 0; k < 16; ++k) { const int t = t0 + k;
;         float cur[8], o[8]; ld8(PROJ + (size_t)t * INC + 5120 + c, cur);
;         const float inv = (k + 1 < WIN && t0 == 0) ? 1.0f / (float)(k + 1) : 1.0f / (float)WIN;
; #pragma unroll
;         for (int i = 0; i < 8; ++i) { tot[i] += cur[i]; o[i] = tot[i] * inv - cur[i]; ring[k % WIN][i] = cur[i]; }
;         st8q(YABC + (size_t)t * 3072 + 2048 + c, o);
; #pragma unroll
;         for (int i = 0; i < 8; ++i) tot[i] -= ring[(k + 1) % WIN][i];
;     }
; }
	v_lshlrev_b32_e32 v8, 16, v100
	v_and_b32_e32 v9, 0xffff0000, v100
	v_lshlrev_b32_e32 v10, 16, v101
	v_and_b32_e32 v11, 0xffff0000, v101
	v_lshlrev_b32_e32 v12, 16, v102
	v_and_b32_e32 v13, 0xffff0000, v102
	v_lshlrev_b32_e32 v14, 16, v103
	v_and_b32_e32 v15, 0xffff0000, v103
	v_pk_add_f32 v[0:1], v[0:1], v[8:9]
	v_pk_add_f32 v[2:3], v[2:3], v[10:11]
	v_pk_add_f32 v[4:5], v[4:5], v[12:13]
	v_pk_add_f32 v[6:7], v[6:7], v[14:15]
	v_fma_f32 v24, v36, v0, -v8
	v_fma_f32 v25, v36, v1, -v9
	v_fma_f32 v26, v36, v2, -v10
	v_fma_f32 v27, v36, v3, -v11
	v_fma_f32 v28, v36, v4, -v12
	v_fma_f32 v29, v36, v5, -v13
	v_fma_f32 v30, v36, v6, -v14
	v_fma_f32 v31, v36, v7, -v15
	v_pk_mul_f32 v[24:25], v[24:25], 4.0 op_sel_hi:[1,0]
	v_pk_mul_f32 v[26:27], v[26:27], 4.0 op_sel_hi:[1,0]
	v_pk_mul_f32 v[28:29], v[28:29], 4.0 op_sel_hi:[1,0]
	v_pk_mul_f32 v[30:31], v[30:31], 4.0 op_sel_hi:[1,0]
	v_med3_f32 v24, v24, s33, v229
	v_med3_f32 v25, v25, s33, v229
	v_med3_f32 v26, v26, s33, v229
	v_med3_f32 v27, v27, s33, v229
	v_med3_f32 v28, v28, s33, v229
	v_med3_f32 v29, v29, s33, v229
	v_med3_f32 v30, v30, s33, v229
	v_med3_f32 v31, v31, s33, v229
	v_add_u32_e32 v35, 0x5400, v34
	v_cvt_pk_fp8_f32 v40, v24, v25
	v_cvt_pk_fp8_f32 v41, v28, v29
	v_cvt_pk_fp8_f32 v40, v26, v27 op_sel:[0,0,1]
	v_cvt_pk_fp8_f32 v41, v30, v31 op_sel:[0,0,1]
	global_store_dwordx2 v35, v[40:41], s[4:5]
	v_lshlrev_b32_e32 v16, 16, v88
	v_and_b32_e32 v17, 0xffff0000, v88
	v_lshlrev_b32_e32 v18, 16, v89
	v_and_b32_e32 v19, 0xffff0000, v89
	v_lshlrev_b32_e32 v20, 16, v90
	v_and_b32_e32 v21, 0xffff0000, v90
	v_lshlrev_b32_e32 v22, 16, v91
	v_and_b32_e32 v23, 0xffff0000, v91
	v_pk_add_f32 v[0:1], v[0:1], v[16:17] neg_lo:[0,1] neg_hi:[0,1]
	v_pk_add_f32 v[2:3], v[2:3], v[18:19] neg_lo:[0,1] neg_hi:[0,1]
	v_pk_add_f32 v[4:5], v[4:5], v[20:21] neg_lo:[0,1] neg_hi:[0,1]
	v_pk_add_f32 v[6:7], v[6:7], v[22:23] neg_lo:[0,1] neg_hi:[0,1]
	s_waitcnt vmcnt(15)
	v_lshlrev_b32_e32 v8, 16, v104
	v_and_b32_e32 v9, 0xffff0000, v104
	v_lshlrev_b32_e32 v10, 16, v105
	v_and_b32_e32 v11, 0xffff0000, v105
	v_lshlrev_b32_e32 v12, 16, v106
	v_and_b32_e32 v13, 0xffff0000, v106
	v_lshlrev_b32_e32 v14, 16, v107
	v_and_b32_e32 v15, 0xffff0000, v107
	v_pk_add_f32 v[0:1], v[0:1], v[8:9]
	v_pk_add_f32 v[2:3], v[2:3], v[10:11]
	v_pk_add_f32 v[4:5], v[4:5], v[12:13]
	v_pk_add_f32 v[6:7], v[6:7], v[14:15]
	v_fma_f32 v24, v36, v0, -v8
	v_fma_f32 v25, v36, v1, -v9
	v_fma_f32 v26, v36, v2, -v10
	v_fma_f32 v27, v36, v3, -v11
	v_fma_f32 v28, v36, v4, -v12
	v_fma_f32 v29, v36, v5, -v13
	v_fma_f32 v30, v36, v6, -v14
	v_fma_f32 v31, v36, v7, -v15
	v_pk_mul_f32 v[24:25], v[24:25], 4.0 op_sel_hi:[1,0]
	v_pk_mul_f32 v[26:27], v[26:27], 4.0 op_sel_hi:[1,0]
	v_pk_mul_f32 v[28:29], v[28:29], 4.0 op_sel_hi:[1,0]
	v_pk_mul_f32 v[30:31], v[30:31], 4.0 op_sel_hi:[1,0]
	v_med3_f32 v24, v24, s33, v229
	v_med3_f32 v25, v25, s33, v229
	v_med3_f32 v26, v26, s33, v229
	v_med3_f32 v27, v27, s33, v229
	v_med3_f32 v28, v28, s33, v229
	v_med3_f32 v29, v29, s33, v229
	v_med3_f32 v30, v30, s33, v229
	v_med3_f32 v31, v31, s33, v229
	v_add_u32_e32 v35, 0x6000, v34
	v_cvt_pk_fp8_f32 v40, v24, v25
	v_cvt_pk_fp8_f32 v41, v28, v29
	v_cvt_pk_fp8_f32 v40, v26, v27 op_sel:[0,0,1]
	v_cvt_pk_fp8_f32 v41, v30, v31 op_sel:[0,0,1]
	global_store_dwordx2 v35, v[40:41], s[4:5]
	v_lshlrev_b32_e32 v16, 16, v92
	v_and_b32_e32 v17, 0xffff0000, v92
	v_lshlrev_b32_e32 v18, 16, v93
	v_and_b32_e32 v19, 0xffff0000, v93
	v_lshlrev_b32_e32 v20, 16, v94
	v_and_b32_e32 v21, 0xffff0000, v94
	v_lshlrev_b32_e32 v22, 16, v95
	v_and_b32_e32 v23, 0xffff0000, v95
	v_pk_add_f32 v[0:1], v[0:1], v[16:17] neg_lo:[0,1] neg_hi:[0,1]
	v_pk_add_f32 v[2:3], v[2:3], v[18:19] neg_lo:[0,1] neg_hi:[0,1]
	v_pk_add_f32 v[4:5], v[4:5], v[20:21] neg_lo:[0,1] neg_hi:[0,1]
	v_pk_add_f32 v[6:7], v[6:7], v[22:23] neg_lo:[0,1] neg_hi:[0,1]
	s_waitcnt vmcnt(15)
	v_lshlrev_b32_e32 v8, 16, v108
	v_and_b32_e32 v9, 0xffff0000, v108
	v_lshlrev_b32_e32 v10, 16, v109
	v_and_b32_e32 v11, 0xffff0000, v109
	v_lshlrev_b32_e32 v12, 16, v110
	v_and_b32_e32 v13, 0xffff0000, v110
	v_lshlrev_b32_e32 v14, 16, v111
	v_and_b32_e32 v15, 0xffff0000, v111
	v_pk_add_f32 v[0:1], v[0:1], v[8:9]
	v_pk_add_f32 v[2:3], v[2:3], v[10:11]
	v_pk_add_f32 v[4:5], v[4:5], v[12:13]
	v_pk_add_f32 v[6:7], v[6:7], v[14:15]
	v_fma_f32 v24, v36, v0, -v8
	v_fma_f32 v25, v36, v1, -v9
	v_fma_f32 v26, v36, v2, -v10
	v_fma_f32 v27, v36, v3, -v11
	v_fma_f32 v28, v36, v4, -v12
	v_fma_f32 v29, v36, v5, -v13
	v_fma_f32 v30, v36, v6, -v14
	v_fma_f32 v31, v36, v7, -v15
	v_pk_mul_f32 v[24:25], v[24:25], 4.0 op_sel_hi:[1,0]
	v_pk_mul_f32 v[26:27], v[26:27], 4.0 op_sel_hi:[1,0]
	v_pk_mul_f32 v[28:29], v[28:29], 4.0 op_sel_hi:[1,0]
	v_pk_mul_f32 v[30:31], v[30:31], 4.0 op_sel_hi:[1,0]
	v_med3_f32 v24, v24, s33, v229
	v_med3_f32 v25, v25, s33, v229
	v_med3_f32 v26, v26, s33, v229
	v_med3_f32 v27, v27, s33, v229
	v_med3_f32 v28, v28, s33, v229
	v_med3_f32 v29, v29, s33, v229
	v_med3_f32 v30, v30, s33, v229
	v_med3_f32 v31, v31, s33, v229
	v_add_u32_e32 v35, 0x6c00, v34
	v_cvt_pk_fp8_f32 v40, v24, v25
	v_cvt_pk_fp8_f32 v41, v28, v29
	v_cvt_pk_fp8_f32 v40, v26, v27 op_sel:[0,0,1]
	v_cvt_pk_fp8_f32 v41, v30, v31 op_sel:[0,0,1]
	global_store_dwordx2 v35, v[40:41], s[4:5]
	v_lshlrev_b32_e32 v16, 16, v96
	v_and_b32_e32 v17, 0xffff0000, v96
	v_lshlrev_b32_e32 v18, 16, v97
	v_and_b32_e32 v19, 0xffff0000, v97
	v_lshlrev_b32_e32 v20, 16, v98
	v_and_b32_e32 v21, 0xffff0000, v98
	v_lshlrev_b32_e32 v22, 16, v99
	v_and_b32_e32 v23, 0xffff0000, v99
	v_pk_add_f32 v[0:1], v[0:1], v[16:17] neg_lo:[0,1] neg_hi:[0,1]
	v_pk_add_f32 v[2:3], v[2:3], v[18:19] neg_lo:[0,1] neg_hi:[0,1]
	v_pk_add_f32 v[4:5], v[4:5], v[20:21] neg_lo:[0,1] neg_hi:[0,1]
	v_pk_add_f32 v[6:7], v[6:7], v[22:23] neg_lo:[0,1] neg_hi:[0,1]
	s_waitcnt vmcnt(15)
; __device__ __forceinline__ unsigned pk4_fp8(float a, float b, float c, float d) { unsigned w = 0u; w = __builtin_amdgcn_cvt_pk_fp8_f32(clamp8(a), clamp8(b), w, false); w = __builtin_amdgcn_cvt_pk_fp8_f32(clamp8(c), clamp8(d), w, true); return w; }
; __device__ __forceinline__ void st8q(unsigned char* ptr, const float (&f)[8]) {
;     u32x2 w; w.x = pk4_fp8(4.f * f[0], 4.f * f[1], 4.f * f[2], 4.f * f[3]); w.y = pk4_fp8(4.f * f[4], 4.f * f[5], 4.f * f[6], 4.f * f[7]); *(u32x2*)ptr = w;
; }
; template <int WIN> __device__ __forceinline__ void pool_task(const Params& p, int t0, int c) {
;     ...
; #pragma unroll
;     for (int k = 0; k < 16; ++k) { const int t = t0 + k;
;         float cur[8], o[8]; ld8(PROJ + (size_t)t * INC + 5120 + c, cur);
;         const float inv = (k + 1 < WIN && t0 == 0) ? 1.0f / (float)(k + 1) : 1.0f / (float)WIN;
; #pragma unroll
;         for (int i = 0; i < 8; ++i) { tot[i] += cur[i]; o[i] = tot[i] * inv - cur[i]; ring[k % WIN][i] = cur[i]; }
;         st8q(YABC + (size_t)t * 3072 + 2048 + c, o);
; #pragma unroll
;         for (int i = 0; i < 8; ++i) tot[i] -= ring[(k + 1) % WIN][i];
;     }
; }
	v_lshlrev_b32_e32 v8, 16, v112
	v_and_b32_e32 v9, 0xffff0000, v112
	v_lshlrev_b32_e32 v10, 16, v113
	v_and_b32_e32 v11, 0xffff0000, v113
	v_lshlrev_b32_e32 v12, 16, v114
	v_and_b32_e32 v13, 0xffff0000, v114
	v_lshlrev_b32_e32 v14, 16, v115
	v_and_b32_e32 v15, 0xffff0000, v115
	v_pk_add_f32 v[0:1], v[0:1], v[8:9]
	v_pk_add_f32 v[2:3], v[2:3], v[10:11]
	v_pk_add_f32 v[4:5], v[4:5], v[12:13]
	v_pk_add_f32 v[6:7], v[6:7], v[14:15]
	v_fma_f32 v24, v36, v0, -v8
	v_fma_f32 v25, v36, v1, -v9
	v_fma_f32 v26, v36, v2, -v10
	v_fma_f32 v27, v36, v3, -v11
	v_fma_f32 v28, v36, v4, -v12
	v_fma_f32 v29, v36, v5, -v13
	v_fma_f32 v30, v36, v6, -v14
	v_fma_f32 v31, v36, v7, -v15
	v_pk_mul_f32 v[24:25], v[24:25], 4.0 op_sel_hi:[1,0]
	v_pk_mul_f32 v[26:27], v[26:27], 4.0 op_sel_hi:[1,0]
	v_pk_mul_f32 v[28:29], v[28:29], 4.0 op_sel_hi:[1,0]
	v_pk_mul_f32 v[30:31], v[30:31], 4.0 op_sel_hi:[1,0]
	v_med3_f32 v24, v24, s33, v229
	v_med3_f32 v25, v25, s33, v229
	v_med3_f32 v26, v26, s33, v229
	v_med3_f32 v27, v27, s33, v229
	v_med3_f32 v28, v28, s33, v229
	v_med3_f32 v29, v29, s33, v229
	v_med3_f32 v30, v30, s33, v229
	v_med3_f32 v31, v31, s33, v229
	v_add_u32_e32 v35, 0x7800, v34
	v_cvt_pk_fp8_f32 v40, v24, v25
	v_cvt_pk_fp8_f32 v41, v28, v29
	v_cvt_pk_fp8_f32 v40, v26, v27 op_sel:[0,0,1]
	v_cvt_pk_fp8_f32 v41, v30, v31 op_sel:[0,0,1]
	global_store_dwordx2 v35, v[40:41], s[4:5]
	v_lshlrev_b32_e32 v16, 16, v100
	v_and_b32_e32 v17, 0xffff0000, v100
	v_lshlrev_b32_e32 v18, 16, v101
	v_and_b32_e32 v19, 0xffff0000, v101
	v_lshlrev_b32_e32 v20, 16, v102
	v_and_b32_e32 v21, 0xffff0000, v102
	v_lshlrev_b32_e32 v22, 16, v103
	v_and_b32_e32 v23, 0xffff0000, v103
	v_pk_add_f32 v[0:1], v[0:1], v[16:17] neg_lo:[0,1] neg_hi:[0,1]
	v_pk_add_f32 v[2:3], v[2:3], v[18:19] neg_lo:[0,1] neg_hi:[0,1]
	v_pk_add_f32 v[4:5], v[4:5], v[20:21] neg_lo:[0,1] neg_hi:[0,1]
	v_pk_add_f32 v[6:7], v[6:7], v[22:23] neg_lo:[0,1] neg_hi:[0,1]
	s_waitcnt vmcnt(15)
	v_lshlrev_b32_e32 v8, 16, v116
	v_and_b32_e32 v9, 0xffff0000, v116
	v_lshlrev_b32_e32 v10, 16, v117
	v_and_b32_e32 v11, 0xffff0000, v117
	v_lshlrev_b32_e32 v12, 16, v118
	v_and_b32_e32 v13, 0xffff0000, v118
	v_lshlrev_b32_e32 v14, 16, v119
	v_and_b32_e32 v15, 0xffff0000, v119
	v_pk_add_f32 v[0:1], v[0:1], v[8:9]
	v_pk_add_f32 v[2:3], v[2:3], v[10:11]
	v_pk_add_f32 v[4:5], v[4:5], v[12:13]
	v_pk_add_f32 v[6:7], v[6:7], v[14:15]
	v_fma_f32 v24, v36, v0, -v8
	v_fma_f32 v25, v36, v1, -v9
	v_fma_f32 v26, v36, v2, -v10
	v_fma_f32 v27, v36, v3, -v11
	v_fma_f32 v28, v36, v4, -v12
	v_fma_f32 v29, v36, v5, -v13
	v_fma_f32 v30, v36, v6, -v14
	v_fma_f32 v31, v36, v7, -v15
	v_pk_mul_f32 v[24:25], v[24:25], 4.0 op_sel_hi:[1,0]
	v_pk_mul_f32 v[26:27], v[26:27], 4.0 op_sel_hi:[1,0]
	v_pk_mul_f32 v[28:29], v[28:29], 4.0 op_sel_hi:[1,0]
	v_pk_mul_f32 v[30:31], v[30:31], 4.0 op_sel_hi:[1,0]
	v_med3_f32 v24, v24, s33, v229
	v_med3_f32 v25, v25, s33, v229
	v_med3_f32 v26, v26, s33, v229
	v_med3_f32 v27, v27, s33, v229
	v_med3_f32 v28, v28, s33, v229
	v_med3_f32 v29, v29, s33, v229
	v_med3_f32 v30, v30, s33, v229
	v_med3_f32 v31, v31, s33, v229
	v_add_u32_e32 v35, 0x8400, v34
	v_cvt_pk_fp8_f32 v40, v24, v25
	v_cvt_pk_fp8_f32 v41, v28, v29
	v_cvt_pk_fp8_f32 v40, v26, v27 op_sel:[0,0,1]
	v_cvt_pk_fp8_f32 v41, v30, v31 op_sel:[0,0,1]
	global_store_dwordx2 v35, v[40:41], s[4:5]
	v_lshlrev_b32_e32 v16, 16, v104
	v_and_b32_e32 v17, 0xffff0000, v104
	v_lshlrev_b32_e32 v18, 16, v105
	v_and_b32_e32 v19, 0xffff0000, v105
	v_lshlrev_b32_e32 v20, 16, v106
	v_and_b32_e32 v21, 0xffff0000, v106
	v_lshlrev_b32_e32 v22, 16, v107
	v_and_b32_e32 v23, 0xffff0000, v107
	v_pk_add_f32 v[0:1], v[0:1], v[16:17] neg_lo:[0,1] neg_hi:[0,1]
	v_pk_add_f32 v[2:3], v[2:3], v[18:19] neg_lo:[0,1] neg_hi:[0,1]
	v_pk_add_f32 v[4:5], v[4:5], v[20:21] neg_lo:[0,1] neg_hi:[0,1]
	v_pk_add_f32 v[6:7], v[6:7], v[22:23] neg_lo:[0,1] neg_hi:[0,1]
	s_waitcnt vmcnt(15)
	v_lshlrev_b32_e32 v8, 16, v120
	v_and_b32_e32 v9, 0xffff0000, v120
	v_lshlrev_b32_e32 v10, 16, v121
	v_and_b32_e32 v11, 0xffff0000, v121
	v_lshlrev_b32_e32 v12, 16, v122
	v_and_b32_e32 v13, 0xffff0000, v122
	v_lshlrev_b32_e32 v14, 16, v123
	v_and_b32_e32 v15, 0xffff0000, v123
	v_pk_add_f32 v[0:1], v[0:1], v[8:9]
	v_pk_add_f32 v[2:3], v[2:3], v[10:11]
	v_pk_add_f32 v[4:5], v[4:5], v[12:13]
	v_pk_add_f32 v[6:7], v[6:7], v[14:15]
	v_fma_f32 v24, v36, v0, -v8
	v_fma_f32 v25, v36, v1, -v9
	v_fma_f32 v26, v36, v2, -v10
	v_fma_f32 v27, v36, v3, -v11
	v_fma_f32 v28, v36, v4, -v12
	v_fma_f32 v29, v36, v5, -v13
	v_fma_f32 v30, v36, v6, -v14
	v_fma_f32 v31, v36, v7, -v15
	v_pk_mul_f32 v[24:25], v[24:25], 4.0 op_sel_hi:[1,0]
	v_pk_mul_f32 v[26:27], v[26:27], 4.0 op_sel_hi:[1,0]
	v_pk_mul_f32 v[28:29], v[28:29], 4.0 op_sel_hi:[1,0]
	v_pk_mul_f32 v[30:31], v[30:31], 4.0 op_sel_hi:[1,0]
	v_med3_f32 v24, v24, s33, v229
	v_med3_f32 v25, v25, s33, v229
	v_med3_f32 v26, v26, s33, v229
	v_med3_f32 v27, v27, s33, v229
	v_med3_f32 v28, v28, s33, v229
	v_med3_f32 v29, v29, s33, v229
	v_med3_f32 v30, v30, s33, v229
	v_med3_f32 v31, v31, s33, v229
	v_add_u32_e32 v35, 0x9000, v34
	v_cvt_pk_fp8_f32 v40, v24, v25
	v_cvt_pk_fp8_f32 v41, v28, v29
	v_cvt_pk_fp8_f32 v40, v26, v27 op_sel:[0,0,1]
	v_cvt_pk_fp8_f32 v41, v30, v31 op_sel:[0,0,1]
	global_store_dwordx2 v35, v[40:41], s[4:5]
	v_lshlrev_b32_e32 v16, 16, v108
	v_and_b32_e32 v17, 0xffff0000, v108
	v_lshlrev_b32_e32 v18, 16, v109
	v_and_b32_e32 v19, 0xffff0000, v109
	v_lshlrev_b32_e32 v20, 16, v110
	v_and_b32_e32 v21, 0xffff0000, v110
	v_lshlrev_b32_e32 v22, 16, v111
	v_and_b32_e32 v23, 0xffff0000, v111
	v_pk_add_f32 v[0:1], v[0:1], v[16:17] neg_lo:[0,1] neg_hi:[0,1]
	v_pk_add_f32 v[2:3], v[2:3], v[18:19] neg_lo:[0,1] neg_hi:[0,1]
	v_pk_add_f32 v[4:5], v[4:5], v[20:21] neg_lo:[0,1] neg_hi:[0,1]
	v_pk_add_f32 v[6:7], v[6:7], v[22:23] neg_lo:[0,1] neg_hi:[0,1]
	s_waitcnt vmcnt(15)
; template <int WIN> __device__ __forceinline__ void pool_task(const Params& p, int t0, int c) {
;     ...
;     for (int k = 0; k < 16; ++k) { const int t = t0 + k;
;         float cur[8], o[8]; ld8(PROJ + (size_t)t * INC + 5120 + c, cur);
;         const float inv = (k + 1 < WIN && t0 == 0) ? 1.0f / (float)(k + 1) : 1.0f / (float)WIN;
; #pragma unroll
;         for (int i = 0; i < 8; ++i) { tot[i] += cur[i]; o[i] = tot[i] * inv - cur[i]; ring[k % WIN][i] = cur[i]; }
;         st8q(YABC + (size_t)t * 3072 + 2048 + c, o);
; #pragma unroll
;         for (int i = 0; i < 8; ++i) tot[i] -= ring[(k + 1) % WIN][i];
;     }
	v_lshlrev_b32_e32 v8, 16, v124
	v_and_b32_e32 v9, 0xffff0000, v124
	v_lshlrev_b32_e32 v10, 16, v125
	v_and_b32_e32 v11, 0xffff0000, v125
	v_lshlrev_b32_e32 v12, 16, v126
	v_and_b32_e32 v13, 0xffff0000, v126
	v_lshlrev_b32_e32 v14, 16, v127
	v_and_b32_e32 v15, 0xffff0000, v127
	v_pk_add_f32 v[0:1], v[0:1], v[8:9]
	v_pk_add_f32 v[2:3], v[2:3], v[10:11]
	v_pk_add_f32 v[4:5], v[4:5], v[12:13]
	v_pk_add_f32 v[6:7], v[6:7], v[14:15]
	v_fma_f32 v24, v36, v0, -v8
	v_fma_f32 v25, v36, v1, -v9
	v_fma_f32 v26, v36, v2, -v10
	v_fma_f32 v27, v36, v3, -v11
	v_fma_f32 v28, v36, v4, -v12
	v_fma_f32 v29, v36, v5, -v13
	v_fma_f32 v30, v36, v6, -v14
	v_fma_f32 v31, v36, v7, -v15
	v_pk_mul_f32 v[24:25], v[24:25], 4.0 op_sel_hi:[1,0]
	v_pk_mul_f32 v[26:27], v[26:27], 4.0 op_sel_hi:[1,0]
	v_pk_mul_f32 v[28:29], v[28:29], 4.0 op_sel_hi:[1,0]
	v_pk_mul_f32 v[30:31], v[30:31], 4.0 op_sel_hi:[1,0]
	v_med3_f32 v24, v24, s33, v229
	v_med3_f32 v25, v25, s33, v229
	v_med3_f32 v26, v26, s33, v229
	v_med3_f32 v27, v27, s33, v229
	v_med3_f32 v28, v28, s33, v229
	v_med3_f32 v29, v29, s33, v229
	v_med3_f32 v30, v30, s33, v229
	v_med3_f32 v31, v31, s33, v229
	v_add_u32_e32 v35, 0x9c00, v34
	v_cvt_pk_fp8_f32 v40, v24, v25
	v_cvt_pk_fp8_f32 v41, v28, v29
	v_cvt_pk_fp8_f32 v40, v26, v27 op_sel:[0,0,1]
	v_cvt_pk_fp8_f32 v41, v30, v31 op_sel:[0,0,1]
	global_store_dwordx2 v35, v[40:41], s[4:5]
	v_lshlrev_b32_e32 v16, 16, v112
	v_and_b32_e32 v17, 0xffff0000, v112
	v_lshlrev_b32_e32 v18, 16, v113
	v_and_b32_e32 v19, 0xffff0000, v113
	v_lshlrev_b32_e32 v20, 16, v114
	v_and_b32_e32 v21, 0xffff0000, v114
	v_lshlrev_b32_e32 v22, 16, v115
	v_and_b32_e32 v23, 0xffff0000, v115
	v_pk_add_f32 v[0:1], v[0:1], v[16:17] neg_lo:[0,1] neg_hi:[0,1]
	v_pk_add_f32 v[2:3], v[2:3], v[18:19] neg_lo:[0,1] neg_hi:[0,1]
	v_pk_add_f32 v[4:5], v[4:5], v[20:21] neg_lo:[0,1] neg_hi:[0,1]
	v_pk_add_f32 v[6:7], v[6:7], v[22:23] neg_lo:[0,1] neg_hi:[0,1]
	s_waitcnt vmcnt(15)
	v_lshlrev_b32_e32 v8, 16, v128
	v_and_b32_e32 v9, 0xffff0000, v128
	v_lshlrev_b32_e32 v10, 16, v129
	v_and_b32_e32 v11, 0xffff0000, v129
	v_lshlrev_b32_e32 v12, 16, v130
	v_and_b32_e32 v13, 0xffff0000, v130
	v_lshlrev_b32_e32 v14, 16, v131
	v_and_b32_e32 v15, 0xffff0000, v131
	v_pk_add_f32 v[0:1], v[0:1], v[8:9]
	v_pk_add_f32 v[2:3], v[2:3], v[10:11]
	v_pk_add_f32 v[4:5], v[4:5], v[12:13]
	v_pk_add_f32 v[6:7], v[6:7], v[14:15]
	v_fma_f32 v24, v36, v0, -v8
	v_fma_f32 v25, v36, v1, -v9
	v_fma_f32 v26, v36, v2, -v10
	v_fma_f32 v27, v36, v3, -v11
	v_fma_f32 v28, v36, v4, -v12
	v_fma_f32 v29, v36, v5, -v13
	v_fma_f32 v30, v36, v6, -v14
	v_fma_f32 v31, v36, v7, -v15
	v_pk_mul_f32 v[24:25], v[24:25], 4.0 op_sel_hi:[1,0]
	v_pk_mul_f32 v[26:27], v[26:27], 4.0 op_sel_hi:[1,0]
	v_pk_mul_f32 v[28:29], v[28:29], 4.0 op_sel_hi:[1,0]
	v_pk_mul_f32 v[30:31], v[30:31], 4.0 op_sel_hi:[1,0]
	v_med3_f32 v24, v24, s33, v229
	v_med3_f32 v25, v25, s33, v229
	v_med3_f32 v26, v26, s33, v229
	v_med3_f32 v27, v27, s33, v229
	v_med3_f32 v28, v28, s33, v229
	v_med3_f32 v29, v29, s33, v229
	v_med3_f32 v30, v30, s33, v229
	v_med3_f32 v31, v31, s33, v229
	v_add_u32_e32 v35, 0xa800, v34
	v_cvt_pk_fp8_f32 v40, v24, v25
	v_cvt_pk_fp8_f32 v41, v28, v29
	v_cvt_pk_fp8_f32 v40, v26, v27 op_sel:[0,0,1]
	v_cvt_pk_fp8_f32 v41, v30, v31 op_sel:[0,0,1]
	global_store_dwordx2 v35, v[40:41], s[4:5]
	v_lshlrev_b32_e32 v16, 16, v116
	v_and_b32_e32 v17, 0xffff0000, v116
	v_lshlrev_b32_e32 v18, 16, v117
	v_and_b32_e32 v19, 0xffff0000, v117
	v_lshlrev_b32_e32 v20, 16, v118
	v_and_b32_e32 v21, 0xffff0000, v118
	v_lshlrev_b32_e32 v22, 16, v119
	v_and_b32_e32 v23, 0xffff0000, v119
	v_pk_add_f32 v[0:1], v[0:1], v[16:17] neg_lo:[0,1] neg_hi:[0,1]
	v_pk_add_f32 v[2:3], v[2:3], v[18:19] neg_lo:[0,1] neg_hi:[0,1]
	v_pk_add_f32 v[4:5], v[4:5], v[20:21] neg_lo:[0,1] neg_hi:[0,1]
	v_pk_add_f32 v[6:7], v[6:7], v[22:23] neg_lo:[0,1] neg_hi:[0,1]
	s_waitcnt vmcnt(15)
	v_lshlrev_b32_e32 v8, 16, v132
	v_and_b32_e32 v9, 0xffff0000, v132
	v_lshlrev_b32_e32 v10, 16, v133
	v_and_b32_e32 v11, 0xffff0000, v133
	v_lshlrev_b32_e32 v12, 16, v134
	v_and_b32_e32 v13, 0xffff0000, v134
	v_lshlrev_b32_e32 v14, 16, v135
	v_and_b32_e32 v15, 0xffff0000, v135
	v_pk_add_f32 v[0:1], v[0:1], v[8:9]
	v_pk_add_f32 v[2:3], v[2:3], v[10:11]
	v_pk_add_f32 v[4:5], v[4:5], v[12:13]
	v_pk_add_f32 v[6:7], v[6:7], v[14:15]
	v_fma_f32 v24, v36, v0, -v8
	v_fma_f32 v25, v36, v1, -v9
	v_fma_f32 v26, v36, v2, -v10
	v_fma_f32 v27, v36, v3, -v11
	v_fma_f32 v28, v36, v4, -v12
	v_fma_f32 v29, v36, v5, -v13
	v_fma_f32 v30, v36, v6, -v14
	v_fma_f32 v31, v36, v7, -v15
	v_pk_mul_f32 v[24:25], v[24:25], 4.0 op_sel_hi:[1,0]
	v_pk_mul_f32 v[26:27], v[26:27], 4.0 op_sel_hi:[1,0]
	v_pk_mul_f32 v[28:29], v[28:29], 4.0 op_sel_hi:[1,0]
	v_pk_mul_f32 v[30:31], v[30:31], 4.0 op_sel_hi:[1,0]
	v_med3_f32 v24, v24, s33, v229
	v_med3_f32 v25, v25, s33, v229
	v_med3_f32 v26, v26, s33, v229
	v_med3_f32 v27, v27, s33, v229
	v_med3_f32 v28, v28, s33, v229
	v_med3_f32 v29, v29, s33, v229
	v_med3_f32 v30, v30, s33, v229
	v_med3_f32 v31, v31, s33, v229
	v_add_u32_e32 v35, 0xb400, v34
	v_cvt_pk_fp8_f32 v40, v24, v25
	v_cvt_pk_fp8_f32 v41, v28, v29
	v_cvt_pk_fp8_f32 v40, v26, v27 op_sel:[0,0,1]
	v_cvt_pk_fp8_f32 v41, v30, v31 op_sel:[0,0,1]
	global_store_dwordx2 v35, v[40:41], s[4:5]
	s_branch .Lmy_cp_next
; template <int WIN> __device__ __forceinline__ void pool_task(const Params& p, int t0, int c) {
;     const bf16* PROJ = (const bf16*)(p.ws + WS_PROJ); unsigned char* YABC = p.ws + WS_YABC;
;     float ring[WIN][8], tot[8];
; #pragma unroll
;     for (int i = 0; i < 8; ++i) tot[i] = 0.f;
; #pragma unroll
;     for (int d = 1 - WIN; d < 0; ++d) {
;         if (t0 > 0) { ld8(PROJ + (size_t)(t0 + d) * INC + 5120 + c, ring[(d + WIN) % WIN]);
; #pragma unroll
;             for (int i = 0; i < 8; ++i) tot[i] += ring[(d + WIN) % WIN][i]; }
;         else {
; #pragma unroll
;             for (int i = 0; i < 8; ++i) ring[(d + WIN) % WIN][i] = 0.f; }
;     }
; #pragma unroll
;     for (int k = 0; k < 16; ++k) { const int t = t0 + k;
;         float cur[8], o[8]; ld8(PROJ + (size_t)t * INC + 5120 + c, cur);
;         const float inv = (k + 1 < WIN && t0 == 0) ? 1.0f / (float)(k + 1) : 1.0f / (float)WIN;
; #pragma unroll
;         for (int i = 0; i < 8; ++i) { tot[i] += cur[i]; o[i] = tot[i] * inv - cur[i]; ring[k % WIN][i] = cur[i]; }
; __device__ __forceinline__ void convpool_task(const Params& p, int l, int task) {
;     ...
;     const int k = task - 65536, g = __builtin_amdgcn_readfirstlane((k >> 6) & 3), run = ((k >> 8) << 1) + ((k >> 5) & 1), c = (g * 32 + (k & 31)) * 8, t0 = run * 16;
;     if (g == 0) pool_task<2>(p, t0, c); else if (g == 1) pool_task<4>(p, t0, c); else if (g == 2) pool_task<8>(p, t0, c); else pool_task<16>(p, t0, c);
.Lmy_pool_w8:
	v_and_b32_e32 v35, 31, v67
	v_lshrrev_b32_e32 v32, 8, v67
	s_lshl_b32 s10, s7, 1
	v_add_lshl_u32 v32, v32, s10, 1
	v_bfe_u32 v38, v67, 5, 1
	v_add_lshl_u32 v32, v32, v38, 4
	v_or_b32_e32 v35, 64, v35
	v_mul_u32_u24_e32 v33, 0x3000, v32
	v_lshl_add_u32 v33, v35, 4, v33
	v_add_u32_e32 v33, 0x1000, v33
	v_mul_u32_u24_e32 v34, 0xc00, v32
	v_lshl_add_u32 v34, v35, 3, v34
	v_add_u32_e32 v34, 0x800, v34
	v_mov_b32_e32 v56, 0
	v_mov_b32_e32 v57, 0
	v_mov_b32_e32 v58, 0
	v_mov_b32_e32 v59, 0
	v_mov_b32_e32 v60, 0
	v_mov_b32_e32 v61, 0
	v_mov_b32_e32 v62, 0
	v_mov_b32_e32 v63, 0
	v_mov_b32_e32 v68, 0
	v_mov_b32_e32 v69, 0
	v_mov_b32_e32 v70, 0
	v_mov_b32_e32 v71, 0
	v_mov_b32_e32 v72, 0
	v_mov_b32_e32 v73, 0
	v_mov_b32_e32 v74, 0
	v_mov_b32_e32 v75, 0
	v_mov_b32_e32 v76, 0
	v_mov_b32_e32 v77, 0
	v_mov_b32_e32 v78, 0
	v_mov_b32_e32 v79, 0
	v_mov_b32_e32 v80, 0
	v_mov_b32_e32 v81, 0
	v_mov_b32_e32 v82, 0
	v_mov_b32_e32 v83, 0
	v_mov_b32_e32 v84, 0
	v_mov_b32_e32 v85, 0
	v_mov_b32_e32 v86, 0
	v_mov_b32_e32 v87, 0
	v_cmp_ne_u32_e32 vcc, 0, v32
	s_and_saveexec_b64 s[10:11], vcc
	v_add_u32_e32 v35, 0xfffeb000, v33
	global_load_dwordx4 v[56:59], v35, s[2:3] nt
	v_add_u32_e32 v35, 0xfffee000, v33
	global_load_dwordx4 v[60:63], v35, s[2:3] nt
	v_add_u32_e32 v35, 0xffff1000, v33
	global_load_dwordx4 v[68:71], v35, s[2:3] nt
	v_add_u32_e32 v35, 0xffff4000, v33
	global_load_dwordx4 v[72:75], v35, s[2:3] nt
	v_add_u32_e32 v35, 0xffff7000, v33
	global_load_dwordx4 v[76:79], v35, s[2:3] nt
	v_add_u32_e32 v35, 0xffffa000, v33
	global_load_dwordx4 v[80:83], v35, s[2:3] nt
	v_add_u32_e32 v35, 0xffffd000, v33
	global_load_dwordx4 v[84:87], v35, s[2:3] nt
	s_mov_b64 exec, s[0:1]
	global_load_dwordx4 v[88:91], v33, s[2:3] nt
	v_add_u32_e32 v35, 0x3000, v33
	global_load_dwordx4 v[92:95], v35, s[2:3] nt
	v_add_u32_e32 v35, 0x6000, v33
	global_load_dwordx4 v[96:99], v35, s[2:3] nt
	v_add_u32_e32 v35, 0x9000, v33
	global_load_dwordx4 v[100:103], v35, s[2:3] nt
	v_add_u32_e32 v35, 0xc000, v33
	global_load_dwordx4 v[104:107], v35, s[2:3] nt
	v_add_u32_e32 v35, 0xf000, v33
	global_load_dwordx4 v[108:111], v35, s[2:3] nt
	v_add_u32_e32 v35, 0x12000, v33
	global_load_dwordx4 v[112:115], v35, s[2:3] nt
	v_add_u32_e32 v35, 0x15000, v33
	global_load_dwordx4 v[116:119], v35, s[2:3] nt
	v_add_u32_e32 v35, 0x18000, v33
	global_load_dwordx4 v[120:123], v35, s[2:3] nt
	v_add_u32_e32 v35, 0x1b000, v33
	global_load_dwordx4 v[124:127], v35, s[2:3] nt
	v_add_u32_e32 v35, 0x1e000, v33
	global_load_dwordx4 v[128:131], v35, s[2:3] nt
	v_add_u32_e32 v35, 0x21000, v33
	global_load_dwordx4 v[132:135], v35, s[2:3] nt
	v_add_u32_e32 v35, 0x24000, v33
	global_load_dwordx4 v[136:139], v35, s[2:3] nt
	v_add_u32_e32 v35, 0x27000, v33
	global_load_dwordx4 v[140:143], v35, s[2:3] nt
	v_add_u32_e32 v35, 0x2a000, v33
	global_load_dwordx4 v[144:147], v35, s[2:3] nt
	v_add_u32_e32 v35, 0x2d000, v33
	global_load_dwordx4 v[148:151], v35, s[2:3] nt
	v_cmp_eq_u32_e32 vcc, 0, v32
	v_mov_b32_e32 v36, 0x3e000000
	v_mov_b64_e32 v[0:1], 0
	v_mov_b64_e32 v[2:3], 0
	v_mov_b64_e32 v[4:5], 0
	v_mov_b64_e32 v[6:7], 0
	s_waitcnt vmcnt(22)
	v_lshlrev_b32_e32 v8, 16, v56
	v_and_b32_e32 v9, 0xffff0000, v56
	v_lshlrev_b32_e32 v10, 16, v57
	v_and_b32_e32 v11, 0xffff0000, v57
	v_lshlrev_b32_e32 v12, 16, v58
	v_and_b32_e32 v13, 0xffff0000, v58
	v_lshlrev_b32_e32 v14, 16, v59
	v_and_b32_e32 v15, 0xffff0000, v59
	v_pk_add_f32 v[0:1], v[0:1], v[8:9]
	v_pk_add_f32 v[2:3], v[2:3], v[10:11]
	v_pk_add_f32 v[4:5], v[4:5], v[12:13]
	v_pk_add_f32 v[6:7], v[6:7], v[14:15]
	s_waitcnt vmcnt(21)
	v_lshlrev_b32_e32 v8, 16, v60
	v_and_b32_e32 v9, 0xffff0000, v60
	v_lshlrev_b32_e32 v10, 16, v61
	v_and_b32_e32 v11, 0xffff0000, v61
	v_lshlrev_b32_e32 v12, 16, v62
	v_and_b32_e32 v13, 0xffff0000, v62
	v_lshlrev_b32_e32 v14, 16, v63
	v_and_b32_e32 v15, 0xffff0000, v63
	v_pk_add_f32 v[0:1], v[0:1], v[8:9]
	v_pk_add_f32 v[2:3], v[2:3], v[10:11]
	v_pk_add_f32 v[4:5], v[4:5], v[12:13]
	v_pk_add_f32 v[6:7], v[6:7], v[14:15]
	s_waitcnt vmcnt(20)
	v_lshlrev_b32_e32 v8, 16, v68
	v_and_b32_e32 v9, 0xffff0000, v68
	v_lshlrev_b32_e32 v10, 16, v69
	v_and_b32_e32 v11, 0xffff0000, v69
	v_lshlrev_b32_e32 v12, 16, v70
	v_and_b32_e32 v13, 0xffff0000, v70
	v_lshlrev_b32_e32 v14, 16, v71
	v_and_b32_e32 v15, 0xffff0000, v71
	v_pk_add_f32 v[0:1], v[0:1], v[8:9]
	v_pk_add_f32 v[2:3], v[2:3], v[10:11]
	v_pk_add_f32 v[4:5], v[4:5], v[12:13]
	v_pk_add_f32 v[6:7], v[6:7], v[14:15]
	s_waitcnt vmcnt(19)
	v_lshlrev_b32_e32 v8, 16, v72
	v_and_b32_e32 v9, 0xffff0000, v72
	v_lshlrev_b32_e32 v10, 16, v73
	v_and_b32_e32 v11, 0xffff0000, v73
	v_lshlrev_b32_e32 v12, 16, v74
	v_and_b32_e32 v13, 0xffff0000, v74
	v_lshlrev_b32_e32 v14, 16, v75
	v_and_b32_e32 v15, 0xffff0000, v75
	v_pk_add_f32 v[0:1], v[0:1], v[8:9]
	v_pk_add_f32 v[2:3], v[2:3], v[10:11]
	v_pk_add_f32 v[4:5], v[4:5], v[12:13]
	v_pk_add_f32 v[6:7], v[6:7], v[14:15]
	s_waitcnt vmcnt(18)
	v_lshlrev_b32_e32 v8, 16, v76
	v_and_b32_e32 v9, 0xffff0000, v76
	v_lshlrev_b32_e32 v10, 16, v77
	v_and_b32_e32 v11, 0xffff0000, v77
	v_lshlrev_b32_e32 v12, 16, v78
	v_and_b32_e32 v13, 0xffff0000, v78
	v_lshlrev_b32_e32 v14, 16, v79
	v_and_b32_e32 v15, 0xffff0000, v79
	v_pk_add_f32 v[0:1], v[0:1], v[8:9]
	v_pk_add_f32 v[2:3], v[2:3], v[10:11]
	v_pk_add_f32 v[4:5], v[4:5], v[12:13]
	v_pk_add_f32 v[6:7], v[6:7], v[14:15]
	s_waitcnt vmcnt(17)
	v_lshlrev_b32_e32 v8, 16, v80
	v_and_b32_e32 v9, 0xffff0000, v80
	v_lshlrev_b32_e32 v10, 16, v81
	v_and_b32_e32 v11, 0xffff0000, v81
	v_lshlrev_b32_e32 v12, 16, v82
	v_and_b32_e32 v13, 0xffff0000, v82
	v_lshlrev_b32_e32 v14, 16, v83
	v_and_b32_e32 v15, 0xffff0000, v83
	v_pk_add_f32 v[0:1], v[0:1], v[8:9]
	v_pk_add_f32 v[2:3], v[2:3], v[10:11]
	v_pk_add_f32 v[4:5], v[4:5], v[12:13]
	v_pk_add_f32 v[6:7], v[6:7], v[14:15]
	s_waitcnt vmcnt(16)
; template <int WIN> __device__ __forceinline__ void pool_task(const Params& p, int t0, int c) {
;     ...
;         if (t0 > 0) { ld8(PROJ + (size_t)(t0 + d) * INC + 5120 + c, ring[(d + WIN) % WIN]);
; #pragma unroll
;             for (int i = 0; i < 8; ++i) tot[i] += ring[(d + WIN) % WIN][i]; }
;         else {
; #pragma unroll
;             for (int i = 0; i < 8; ++i) ring[(d + WIN) % WIN][i] = 0.f; }
;     }
; #pragma unroll
;     for (int k = 0; k < 16; ++k) { const int t = t0 + k;
;         float cur[8], o[8]; ld8(PROJ + (size_t)t * INC + 5120 + c, cur);
;         const float inv = (k + 1 < WIN && t0 == 0) ? 1.0f / (float)(k + 1) : 1.0f / (float)WIN;
; #pragma unroll
;         for (int i = 0; i < 8; ++i) { tot[i] += cur[i]; o[i] = tot[i] * inv - cur[i]; ring[k % WIN][i] = cur[i]; }
;         st8q(YABC + (size_t)t * 3072 + 2048 + c, o);
; #pragma unroll
;         for (int i = 0; i < 8; ++i) tot[i] -= ring[(k + 1) % WIN][i];
;     }
	v_lshlrev_b32_e32 v8, 16, v84
	v_and_b32_e32 v9, 0xffff0000, v84
	v_lshlrev_b32_e32 v10, 16, v85
	v_and_b32_e32 v11, 0xffff0000, v85
	v_lshlrev_b32_e32 v12, 16, v86
	v_and_b32_e32 v13, 0xffff0000, v86
	v_lshlrev_b32_e32 v14, 16, v87
	v_and_b32_e32 v15, 0xffff0000, v87
	v_pk_add_f32 v[0:1], v[0:1], v[8:9]
	v_pk_add_f32 v[2:3], v[2:3], v[10:11]
	v_pk_add_f32 v[4:5], v[4:5], v[12:13]
	v_pk_add_f32 v[6:7], v[6:7], v[14:15]
	s_waitcnt vmcnt(15)
	v_lshlrev_b32_e32 v8, 16, v88
	v_and_b32_e32 v9, 0xffff0000, v88
	v_lshlrev_b32_e32 v10, 16, v89
	v_and_b32_e32 v11, 0xffff0000, v89
	v_lshlrev_b32_e32 v12, 16, v90
	v_and_b32_e32 v13, 0xffff0000, v90
	v_lshlrev_b32_e32 v14, 16, v91
	v_and_b32_e32 v15, 0xffff0000, v91
	v_pk_add_f32 v[0:1], v[0:1], v[8:9]
	v_pk_add_f32 v[2:3], v[2:3], v[10:11]
	v_pk_add_f32 v[4:5], v[4:5], v[12:13]
	v_pk_add_f32 v[6:7], v[6:7], v[14:15]
	v_mov_b32_e32 v38, 0x3f800000
	v_cndmask_b32_e32 v37, v36, v38, vcc
	v_fma_f32 v24, v37, v0, -v8
	v_fma_f32 v25, v37, v1, -v9
	v_fma_f32 v26, v37, v2, -v10
	v_fma_f32 v27, v37, v3, -v11
	v_fma_f32 v28, v37, v4, -v12
	v_fma_f32 v29, v37, v5, -v13
	v_fma_f32 v30, v37, v6, -v14
	v_fma_f32 v31, v37, v7, -v15
	v_pk_mul_f32 v[24:25], v[24:25], 4.0 op_sel_hi:[1,0]
	v_pk_mul_f32 v[26:27], v[26:27], 4.0 op_sel_hi:[1,0]
	v_pk_mul_f32 v[28:29], v[28:29], 4.0 op_sel_hi:[1,0]
	v_pk_mul_f32 v[30:31], v[30:31], 4.0 op_sel_hi:[1,0]
	v_med3_f32 v24, v24, s33, v229
	v_med3_f32 v25, v25, s33, v229
	v_med3_f32 v26, v26, s33, v229
	v_med3_f32 v27, v27, s33, v229
	v_med3_f32 v28, v28, s33, v229
	v_med3_f32 v29, v29, s33, v229
	v_med3_f32 v30, v30, s33, v229
	v_med3_f32 v31, v31, s33, v229
	v_cvt_pk_fp8_f32 v40, v24, v25
	v_cvt_pk_fp8_f32 v41, v28, v29
	v_cvt_pk_fp8_f32 v40, v26, v27 op_sel:[0,0,1]
	v_cvt_pk_fp8_f32 v41, v30, v31 op_sel:[0,0,1]
	global_store_dwordx2 v34, v[40:41], s[4:5]
	v_lshlrev_b32_e32 v16, 16, v56
	v_and_b32_e32 v17, 0xffff0000, v56
	v_lshlrev_b32_e32 v18, 16, v57
	v_and_b32_e32 v19, 0xffff0000, v57
	v_lshlrev_b32_e32 v20, 16, v58
	v_and_b32_e32 v21, 0xffff0000, v58
	v_lshlrev_b32_e32 v22, 16, v59
	v_and_b32_e32 v23, 0xffff0000, v59
	v_pk_add_f32 v[0:1], v[0:1], v[16:17] neg_lo:[0,1] neg_hi:[0,1]
	v_pk_add_f32 v[2:3], v[2:3], v[18:19] neg_lo:[0,1] neg_hi:[0,1]
	v_pk_add_f32 v[4:5], v[4:5], v[20:21] neg_lo:[0,1] neg_hi:[0,1]
	v_pk_add_f32 v[6:7], v[6:7], v[22:23] neg_lo:[0,1] neg_hi:[0,1]
	s_waitcnt vmcnt(15)
	v_lshlrev_b32_e32 v8, 16, v92
	v_and_b32_e32 v9, 0xffff0000, v92
	v_lshlrev_b32_e32 v10, 16, v93
	v_and_b32_e32 v11, 0xffff0000, v93
	v_lshlrev_b32_e32 v12, 16, v94
	v_and_b32_e32 v13, 0xffff0000, v94
	v_lshlrev_b32_e32 v14, 16, v95
	v_and_b32_e32 v15, 0xffff0000, v95
	v_pk_add_f32 v[0:1], v[0:1], v[8:9]
	v_pk_add_f32 v[2:3], v[2:3], v[10:11]
	v_pk_add_f32 v[4:5], v[4:5], v[12:13]
	v_pk_add_f32 v[6:7], v[6:7], v[14:15]
	v_mov_b32_e32 v38, 0x3f000000
	v_cndmask_b32_e32 v37, v36, v38, vcc
	v_fma_f32 v24, v37, v0, -v8
	v_fma_f32 v25, v37, v1, -v9
	v_fma_f32 v26, v37, v2, -v10
	v_fma_f32 v27, v37, v3, -v11
	v_fma_f32 v28, v37, v4, -v12
	v_fma_f32 v29, v37, v5, -v13
	v_fma_f32 v30, v37, v6, -v14
	v_fma_f32 v31, v37, v7, -v15
	v_pk_mul_f32 v[24:25], v[24:25], 4.0 op_sel_hi:[1,0]
	v_pk_mul_f32 v[26:27], v[26:27], 4.0 op_sel_hi:[1,0]
	v_pk_mul_f32 v[28:29], v[28:29], 4.0 op_sel_hi:[1,0]
	v_pk_mul_f32 v[30:31], v[30:31], 4.0 op_sel_hi:[1,0]
	v_med3_f32 v24, v24, s33, v229
	v_med3_f32 v25, v25, s33, v229
	v_med3_f32 v26, v26, s33, v229
	v_med3_f32 v27, v27, s33, v229
	v_med3_f32 v28, v28, s33, v229
	v_med3_f32 v29, v29, s33, v229
	v_med3_f32 v30, v30, s33, v229
	v_med3_f32 v31, v31, s33, v229
	v_add_u32_e32 v35, 0xc00, v34
	v_cvt_pk_fp8_f32 v40, v24, v25
	v_cvt_pk_fp8_f32 v41, v28, v29
	v_cvt_pk_fp8_f32 v40, v26, v27 op_sel:[0,0,1]
	v_cvt_pk_fp8_f32 v41, v30, v31 op_sel:[0,0,1]
	global_store_dwordx2 v35, v[40:41], s[4:5]
	v_lshlrev_b32_e32 v16, 16, v60
	v_and_b32_e32 v17, 0xffff0000, v60
	v_lshlrev_b32_e32 v18, 16, v61
	v_and_b32_e32 v19, 0xffff0000, v61
	v_lshlrev_b32_e32 v20, 16, v62
	v_and_b32_e32 v21, 0xffff0000, v62
	v_lshlrev_b32_e32 v22, 16, v63
	v_and_b32_e32 v23, 0xffff0000, v63
	v_pk_add_f32 v[0:1], v[0:1], v[16:17] neg_lo:[0,1] neg_hi:[0,1]
	v_pk_add_f32 v[2:3], v[2:3], v[18:19] neg_lo:[0,1] neg_hi:[0,1]
	v_pk_add_f32 v[4:5], v[4:5], v[20:21] neg_lo:[0,1] neg_hi:[0,1]
	v_pk_add_f32 v[6:7], v[6:7], v[22:23] neg_lo:[0,1] neg_hi:[0,1]
	s_waitcnt vmcnt(15)
	v_lshlrev_b32_e32 v8, 16, v96
	v_and_b32_e32 v9, 0xffff0000, v96
	v_lshlrev_b32_e32 v10, 16, v97
	v_and_b32_e32 v11, 0xffff0000, v97
	v_lshlrev_b32_e32 v12, 16, v98
	v_and_b32_e32 v13, 0xffff0000, v98
	v_lshlrev_b32_e32 v14, 16, v99
	v_and_b32_e32 v15, 0xffff0000, v99
	v_pk_add_f32 v[0:1], v[0:1], v[8:9]
	v_pk_add_f32 v[2:3], v[2:3], v[10:11]
	v_pk_add_f32 v[4:5], v[4:5], v[12:13]
	v_pk_add_f32 v[6:7], v[6:7], v[14:15]
	v_mov_b32_e32 v38, 0x3eaaaaab
	v_cndmask_b32_e32 v37, v36, v38, vcc
	v_fma_f32 v24, v37, v0, -v8
	v_fma_f32 v25, v37, v1, -v9
	v_fma_f32 v26, v37, v2, -v10
	v_fma_f32 v27, v37, v3, -v11
	v_fma_f32 v28, v37, v4, -v12
	v_fma_f32 v29, v37, v5, -v13
	v_fma_f32 v30, v37, v6, -v14
	v_fma_f32 v31, v37, v7, -v15
	v_pk_mul_f32 v[24:25], v[24:25], 4.0 op_sel_hi:[1,0]
	v_pk_mul_f32 v[26:27], v[26:27], 4.0 op_sel_hi:[1,0]
	v_pk_mul_f32 v[28:29], v[28:29], 4.0 op_sel_hi:[1,0]
	v_pk_mul_f32 v[30:31], v[30:31], 4.0 op_sel_hi:[1,0]
	v_med3_f32 v24, v24, s33, v229
	v_med3_f32 v25, v25, s33, v229
	v_med3_f32 v26, v26, s33, v229
	v_med3_f32 v27, v27, s33, v229
	v_med3_f32 v28, v28, s33, v229
	v_med3_f32 v29, v29, s33, v229
	v_med3_f32 v30, v30, s33, v229
	v_med3_f32 v31, v31, s33, v229
	v_add_u32_e32 v35, 0x1800, v34
	v_cvt_pk_fp8_f32 v40, v24, v25
	v_cvt_pk_fp8_f32 v41, v28, v29
	v_cvt_pk_fp8_f32 v40, v26, v27 op_sel:[0,0,1]
	v_cvt_pk_fp8_f32 v41, v30, v31 op_sel:[0,0,1]
	global_store_dwordx2 v35, v[40:41], s[4:5]
	v_lshlrev_b32_e32 v16, 16, v68
	v_and_b32_e32 v17, 0xffff0000, v68
	v_lshlrev_b32_e32 v18, 16, v69
	v_and_b32_e32 v19, 0xffff0000, v69
	v_lshlrev_b32_e32 v20, 16, v70
	v_and_b32_e32 v21, 0xffff0000, v70
	v_lshlrev_b32_e32 v22, 16, v71
	v_and_b32_e32 v23, 0xffff0000, v71
	v_pk_add_f32 v[0:1], v[0:1], v[16:17] neg_lo:[0,1] neg_hi:[0,1]
	v_pk_add_f32 v[2:3], v[2:3], v[18:19] neg_lo:[0,1] neg_hi:[0,1]
	v_pk_add_f32 v[4:5], v[4:5], v[20:21] neg_lo:[0,1] neg_hi:[0,1]
	v_pk_add_f32 v[6:7], v[6:7], v[22:23] neg_lo:[0,1] neg_hi:[0,1]
	s_waitcnt vmcnt(15)
; template <int WIN> __device__ __forceinline__ void pool_task(const Params& p, int t0, int c) {
;     ...
;         if (t0 > 0) { ld8(PROJ + (size_t)(t0 + d) * INC + 5120 + c, ring[(d + WIN) % WIN]);
; #pragma unroll
;             for (int i = 0; i < 8; ++i) tot[i] += ring[(d + WIN) % WIN][i]; }
;         else {
; #pragma unroll
;             for (int i = 0; i < 8; ++i) ring[(d + WIN) % WIN][i] = 0.f; }
;     }
; #pragma unroll
;     for (int k = 0; k < 16; ++k) { const int t = t0 + k;
;         float cur[8], o[8]; ld8(PROJ + (size_t)t * INC + 5120 + c, cur);
;         const float inv = (k + 1 < WIN && t0 == 0) ? 1.0f / (float)(k + 1) : 1.0f / (float)WIN;
; #pragma unroll
;         for (int i = 0; i < 8; ++i) { tot[i] += cur[i]; o[i] = tot[i] * inv - cur[i]; ring[k % WIN][i] = cur[i]; }
;         st8q(YABC + (size_t)t * 3072 + 2048 + c, o);
; #pragma unroll
;         for (int i = 0; i < 8; ++i) tot[i] -= ring[(k + 1) % WIN][i];
;     }
	v_lshlrev_b32_e32 v8, 16, v100
	v_and_b32_e32 v9, 0xffff0000, v100
	v_lshlrev_b32_e32 v10, 16, v101
	v_and_b32_e32 v11, 0xffff0000, v101
	v_lshlrev_b32_e32 v12, 16, v102
	v_and_b32_e32 v13, 0xffff0000, v102
	v_lshlrev_b32_e32 v14, 16, v103
	v_and_b32_e32 v15, 0xffff0000, v103
	v_pk_add_f32 v[0:1], v[0:1], v[8:9]
	v_pk_add_f32 v[2:3], v[2:3], v[10:11]
	v_pk_add_f32 v[4:5], v[4:5], v[12:13]
	v_pk_add_f32 v[6:7], v[6:7], v[14:15]
	v_mov_b32_e32 v38, 0x3e800000
	v_cndmask_b32_e32 v37, v36, v38, vcc
	v_fma_f32 v24, v37, v0, -v8
	v_fma_f32 v25, v37, v1, -v9
	v_fma_f32 v26, v37, v2, -v10
	v_fma_f32 v27, v37, v3, -v11
	v_fma_f32 v28, v37, v4, -v12
	v_fma_f32 v29, v37, v5, -v13
	v_fma_f32 v30, v37, v6, -v14
	v_fma_f32 v31, v37, v7, -v15
	v_pk_mul_f32 v[24:25], v[24:25], 4.0 op_sel_hi:[1,0]
	v_pk_mul_f32 v[26:27], v[26:27], 4.0 op_sel_hi:[1,0]
	v_pk_mul_f32 v[28:29], v[28:29], 4.0 op_sel_hi:[1,0]
	v_pk_mul_f32 v[30:31], v[30:31], 4.0 op_sel_hi:[1,0]
	v_med3_f32 v24, v24, s33, v229
	v_med3_f32 v25, v25, s33, v229
	v_med3_f32 v26, v26, s33, v229
	v_med3_f32 v27, v27, s33, v229
	v_med3_f32 v28, v28, s33, v229
	v_med3_f32 v29, v29, s33, v229
	v_med3_f32 v30, v30, s33, v229
	v_med3_f32 v31, v31, s33, v229
	v_add_u32_e32 v35, 0x2400, v34
	v_cvt_pk_fp8_f32 v40, v24, v25
	v_cvt_pk_fp8_f32 v41, v28, v29
	v_cvt_pk_fp8_f32 v40, v26, v27 op_sel:[0,0,1]
	v_cvt_pk_fp8_f32 v41, v30, v31 op_sel:[0,0,1]
	global_store_dwordx2 v35, v[40:41], s[4:5]
	v_lshlrev_b32_e32 v16, 16, v72
	v_and_b32_e32 v17, 0xffff0000, v72
	v_lshlrev_b32_e32 v18, 16, v73
	v_and_b32_e32 v19, 0xffff0000, v73
	v_lshlrev_b32_e32 v20, 16, v74
	v_and_b32_e32 v21, 0xffff0000, v74
	v_lshlrev_b32_e32 v22, 16, v75
	v_and_b32_e32 v23, 0xffff0000, v75
	v_pk_add_f32 v[0:1], v[0:1], v[16:17] neg_lo:[0,1] neg_hi:[0,1]
	v_pk_add_f32 v[2:3], v[2:3], v[18:19] neg_lo:[0,1] neg_hi:[0,1]
	v_pk_add_f32 v[4:5], v[4:5], v[20:21] neg_lo:[0,1] neg_hi:[0,1]
	v_pk_add_f32 v[6:7], v[6:7], v[22:23] neg_lo:[0,1] neg_hi:[0,1]
	s_waitcnt vmcnt(15)
	v_lshlrev_b32_e32 v8, 16, v104
	v_and_b32_e32 v9, 0xffff0000, v104
	v_lshlrev_b32_e32 v10, 16, v105
	v_and_b32_e32 v11, 0xffff0000, v105
	v_lshlrev_b32_e32 v12, 16, v106
	v_and_b32_e32 v13, 0xffff0000, v106
	v_lshlrev_b32_e32 v14, 16, v107
	v_and_b32_e32 v15, 0xffff0000, v107
	v_pk_add_f32 v[0:1], v[0:1], v[8:9]
	v_pk_add_f32 v[2:3], v[2:3], v[10:11]
	v_pk_add_f32 v[4:5], v[4:5], v[12:13]
	v_pk_add_f32 v[6:7], v[6:7], v[14:15]
	v_mov_b32_e32 v38, 0x3e4ccccd
	v_cndmask_b32_e32 v37, v36, v38, vcc
	v_fma_f32 v24, v37, v0, -v8
	v_fma_f32 v25, v37, v1, -v9
	v_fma_f32 v26, v37, v2, -v10
	v_fma_f32 v27, v37, v3, -v11
	v_fma_f32 v28, v37, v4, -v12
	v_fma_f32 v29, v37, v5, -v13
	v_fma_f32 v30, v37, v6, -v14
	v_fma_f32 v31, v37, v7, -v15
	v_pk_mul_f32 v[24:25], v[24:25], 4.0 op_sel_hi:[1,0]
	v_pk_mul_f32 v[26:27], v[26:27], 4.0 op_sel_hi:[1,0]
	v_pk_mul_f32 v[28:29], v[28:29], 4.0 op_sel_hi:[1,0]
	v_pk_mul_f32 v[30:31], v[30:31], 4.0 op_sel_hi:[1,0]
	v_med3_f32 v24, v24, s33, v229
	v_med3_f32 v25, v25, s33, v229
	v_med3_f32 v26, v26, s33, v229
	v_med3_f32 v27, v27, s33, v229
	v_med3_f32 v28, v28, s33, v229
	v_med3_f32 v29, v29, s33, v229
	v_med3_f32 v30, v30, s33, v229
	v_med3_f32 v31, v31, s33, v229
	v_add_u32_e32 v35, 0x3000, v34
	v_cvt_pk_fp8_f32 v40, v24, v25
	v_cvt_pk_fp8_f32 v41, v28, v29
	v_cvt_pk_fp8_f32 v40, v26, v27 op_sel:[0,0,1]
	v_cvt_pk_fp8_f32 v41, v30, v31 op_sel:[0,0,1]
	global_store_dwordx2 v35, v[40:41], s[4:5]
	v_lshlrev_b32_e32 v16, 16, v76
	v_and_b32_e32 v17, 0xffff0000, v76
	v_lshlrev_b32_e32 v18, 16, v77
	v_and_b32_e32 v19, 0xffff0000, v77
	v_lshlrev_b32_e32 v20, 16, v78
	v_and_b32_e32 v21, 0xffff0000, v78
	v_lshlrev_b32_e32 v22, 16, v79
	v_and_b32_e32 v23, 0xffff0000, v79
	v_pk_add_f32 v[0:1], v[0:1], v[16:17] neg_lo:[0,1] neg_hi:[0,1]
	v_pk_add_f32 v[2:3], v[2:3], v[18:19] neg_lo:[0,1] neg_hi:[0,1]
	v_pk_add_f32 v[4:5], v[4:5], v[20:21] neg_lo:[0,1] neg_hi:[0,1]
	v_pk_add_f32 v[6:7], v[6:7], v[22:23] neg_lo:[0,1] neg_hi:[0,1]
	s_waitcnt vmcnt(15)
	v_lshlrev_b32_e32 v8, 16, v108
	v_and_b32_e32 v9, 0xffff0000, v108
	v_lshlrev_b32_e32 v10, 16, v109
	v_and_b32_e32 v11, 0xffff0000, v109
	v_lshlrev_b32_e32 v12, 16, v110
	v_and_b32_e32 v13, 0xffff0000, v110
	v_lshlrev_b32_e32 v14, 16, v111
	v_and_b32_e32 v15, 0xffff0000, v111
	v_pk_add_f32 v[0:1], v[0:1], v[8:9]
	v_pk_add_f32 v[2:3], v[2:3], v[10:11]
	v_pk_add_f32 v[4:5], v[4:5], v[12:13]
	v_pk_add_f32 v[6:7], v[6:7], v[14:15]
	v_mov_b32_e32 v38, 0x3e2aaaab
	v_cndmask_b32_e32 v37, v36, v38, vcc
	v_fma_f32 v24, v37, v0, -v8
	v_fma_f32 v25, v37, v1, -v9
	v_fma_f32 v26, v37, v2, -v10
	v_fma_f32 v27, v37, v3, -v11
	v_fma_f32 v28, v37, v4, -v12
	v_fma_f32 v29, v37, v5, -v13
	v_fma_f32 v30, v37, v6, -v14
	v_fma_f32 v31, v37, v7, -v15
	v_pk_mul_f32 v[24:25], v[24:25], 4.0 op_sel_hi:[1,0]
	v_pk_mul_f32 v[26:27], v[26:27], 4.0 op_sel_hi:[1,0]
	v_pk_mul_f32 v[28:29], v[28:29], 4.0 op_sel_hi:[1,0]
	v_pk_mul_f32 v[30:31], v[30:31], 4.0 op_sel_hi:[1,0]
	v_med3_f32 v24, v24, s33, v229
	v_med3_f32 v25, v25, s33, v229
	v_med3_f32 v26, v26, s33, v229
	v_med3_f32 v27, v27, s33, v229
	v_med3_f32 v28, v28, s33, v229
	v_med3_f32 v29, v29, s33, v229
	v_med3_f32 v30, v30, s33, v229
	v_med3_f32 v31, v31, s33, v229
	v_add_u32_e32 v35, 0x3c00, v34
	v_cvt_pk_fp8_f32 v40, v24, v25
	v_cvt_pk_fp8_f32 v41, v28, v29
	v_cvt_pk_fp8_f32 v40, v26, v27 op_sel:[0,0,1]
	v_cvt_pk_fp8_f32 v41, v30, v31 op_sel:[0,0,1]
	global_store_dwordx2 v35, v[40:41], s[4:5]
	v_lshlrev_b32_e32 v16, 16, v80
	v_and_b32_e32 v17, 0xffff0000, v80
	v_lshlrev_b32_e32 v18, 16, v81
	v_and_b32_e32 v19, 0xffff0000, v81
	v_lshlrev_b32_e32 v20, 16, v82
	v_and_b32_e32 v21, 0xffff0000, v82
	v_lshlrev_b32_e32 v22, 16, v83
	v_and_b32_e32 v23, 0xffff0000, v83
	v_pk_add_f32 v[0:1], v[0:1], v[16:17] neg_lo:[0,1] neg_hi:[0,1]
	v_pk_add_f32 v[2:3], v[2:3], v[18:19] neg_lo:[0,1] neg_hi:[0,1]
	v_pk_add_f32 v[4:5], v[4:5], v[20:21] neg_lo:[0,1] neg_hi:[0,1]
	v_pk_add_f32 v[6:7], v[6:7], v[22:23] neg_lo:[0,1] neg_hi:[0,1]
	s_waitcnt vmcnt(15)
; template <int WIN> __device__ __forceinline__ void pool_task(const Params& p, int t0, int c) {
;     ...
;         if (t0 > 0) { ld8(PROJ + (size_t)(t0 + d) * INC + 5120 + c, ring[(d + WIN) % WIN]);
; #pragma unroll
;             for (int i = 0; i < 8; ++i) tot[i] += ring[(d + WIN) % WIN][i]; }
;         else {
; #pragma unroll
;             for (int i = 0; i < 8; ++i) ring[(d + WIN) % WIN][i] = 0.f; }
;     }
; #pragma unroll
;     for (int k = 0; k < 16; ++k) { const int t = t0 + k;
;         float cur[8], o[8]; ld8(PROJ + (size_t)t * INC + 5120 + c, cur);
;         const float inv = (k + 1 < WIN && t0 == 0) ? 1.0f / (float)(k + 1) : 1.0f / (float)WIN;
; #pragma unroll
;         for (int i = 0; i < 8; ++i) { tot[i] += cur[i]; o[i] = tot[i] * inv - cur[i]; ring[k % WIN][i] = cur[i]; }
;         st8q(YABC + (size_t)t * 3072 + 2048 + c, o);
; #pragma unroll
;         for (int i = 0; i < 8; ++i) tot[i] -= ring[(k + 1) % WIN][i];
;     }
	v_lshlrev_b32_e32 v8, 16, v112
	v_and_b32_e32 v9, 0xffff0000, v112
	v_lshlrev_b32_e32 v10, 16, v113
	v_and_b32_e32 v11, 0xffff0000, v113
	v_lshlrev_b32_e32 v12, 16, v114
	v_and_b32_e32 v13, 0xffff0000, v114
	v_lshlrev_b32_e32 v14, 16, v115
	v_and_b32_e32 v15, 0xffff0000, v115
	v_pk_add_f32 v[0:1], v[0:1], v[8:9]
	v_pk_add_f32 v[2:3], v[2:3], v[10:11]
	v_pk_add_f32 v[4:5], v[4:5], v[12:13]
	v_pk_add_f32 v[6:7], v[6:7], v[14:15]
	v_mov_b32_e32 v38, 0x3e124925
	v_cndmask_b32_e32 v37, v36, v38, vcc
	v_fma_f32 v24, v37, v0, -v8
	v_fma_f32 v25, v37, v1, -v9
	v_fma_f32 v26, v37, v2, -v10
	v_fma_f32 v27, v37, v3, -v11
	v_fma_f32 v28, v37, v4, -v12
	v_fma_f32 v29, v37, v5, -v13
	v_fma_f32 v30, v37, v6, -v14
	v_fma_f32 v31, v37, v7, -v15
	v_pk_mul_f32 v[24:25], v[24:25], 4.0 op_sel_hi:[1,0]
	v_pk_mul_f32 v[26:27], v[26:27], 4.0 op_sel_hi:[1,0]
	v_pk_mul_f32 v[28:29], v[28:29], 4.0 op_sel_hi:[1,0]
	v_pk_mul_f32 v[30:31], v[30:31], 4.0 op_sel_hi:[1,0]
	v_med3_f32 v24, v24, s33, v229
	v_med3_f32 v25, v25, s33, v229
	v_med3_f32 v26, v26, s33, v229
	v_med3_f32 v27, v27, s33, v229
	v_med3_f32 v28, v28, s33, v229
	v_med3_f32 v29, v29, s33, v229
	v_med3_f32 v30, v30, s33, v229
	v_med3_f32 v31, v31, s33, v229
	v_add_u32_e32 v35, 0x4800, v34
	v_cvt_pk_fp8_f32 v40, v24, v25
	v_cvt_pk_fp8_f32 v41, v28, v29
	v_cvt_pk_fp8_f32 v40, v26, v27 op_sel:[0,0,1]
	v_cvt_pk_fp8_f32 v41, v30, v31 op_sel:[0,0,1]
	global_store_dwordx2 v35, v[40:41], s[4:5]
	v_lshlrev_b32_e32 v16, 16, v84
	v_and_b32_e32 v17, 0xffff0000, v84
	v_lshlrev_b32_e32 v18, 16, v85
	v_and_b32_e32 v19, 0xffff0000, v85
	v_lshlrev_b32_e32 v20, 16, v86
	v_and_b32_e32 v21, 0xffff0000, v86
	v_lshlrev_b32_e32 v22, 16, v87
	v_and_b32_e32 v23, 0xffff0000, v87
	v_pk_add_f32 v[0:1], v[0:1], v[16:17] neg_lo:[0,1] neg_hi:[0,1]
	v_pk_add_f32 v[2:3], v[2:3], v[18:19] neg_lo:[0,1] neg_hi:[0,1]
	v_pk_add_f32 v[4:5], v[4:5], v[20:21] neg_lo:[0,1] neg_hi:[0,1]
	v_pk_add_f32 v[6:7], v[6:7], v[22:23] neg_lo:[0,1] neg_hi:[0,1]
	s_waitcnt vmcnt(15)
	v_lshlrev_b32_e32 v8, 16, v116
	v_and_b32_e32 v9, 0xffff0000, v116
	v_lshlrev_b32_e32 v10, 16, v117
	v_and_b32_e32 v11, 0xffff0000, v117
	v_lshlrev_b32_e32 v12, 16, v118
	v_and_b32_e32 v13, 0xffff0000, v118
	v_lshlrev_b32_e32 v14, 16, v119
	v_and_b32_e32 v15, 0xffff0000, v119
	v_pk_add_f32 v[0:1], v[0:1], v[8:9]
	v_pk_add_f32 v[2:3], v[2:3], v[10:11]
	v_pk_add_f32 v[4:5], v[4:5], v[12:13]
	v_pk_add_f32 v[6:7], v[6:7], v[14:15]
	v_fma_f32 v24, v36, v0, -v8
	v_fma_f32 v25, v36, v1, -v9
	v_fma_f32 v26, v36, v2, -v10
	v_fma_f32 v27, v36, v3, -v11
	v_fma_f32 v28, v36, v4, -v12
	v_fma_f32 v29, v36, v5, -v13
	v_fma_f32 v30, v36, v6, -v14
	v_fma_f32 v31, v36, v7, -v15
	v_pk_mul_f32 v[24:25], v[24:25], 4.0 op_sel_hi:[1,0]
	v_pk_mul_f32 v[26:27], v[26:27], 4.0 op_sel_hi:[1,0]
	v_pk_mul_f32 v[28:29], v[28:29], 4.0 op_sel_hi:[1,0]
	v_pk_mul_f32 v[30:31], v[30:31], 4.0 op_sel_hi:[1,0]
	v_med3_f32 v24, v24, s33, v229
	v_med3_f32 v25, v25, s33, v229
	v_med3_f32 v26, v26, s33, v229
	v_med3_f32 v27, v27, s33, v229
	v_med3_f32 v28, v28, s33, v229
	v_med3_f32 v29, v29, s33, v229
	v_med3_f32 v30, v30, s33, v229
	v_med3_f32 v31, v31, s33, v229
	v_add_u32_e32 v35, 0x5400, v34
	v_cvt_pk_fp8_f32 v40, v24, v25
	v_cvt_pk_fp8_f32 v41, v28, v29
	v_cvt_pk_fp8_f32 v40, v26, v27 op_sel:[0,0,1]
	v_cvt_pk_fp8_f32 v41, v30, v31 op_sel:[0,0,1]
	global_store_dwordx2 v35, v[40:41], s[4:5]
	v_lshlrev_b32_e32 v16, 16, v88
	v_and_b32_e32 v17, 0xffff0000, v88
	v_lshlrev_b32_e32 v18, 16, v89
	v_and_b32_e32 v19, 0xffff0000, v89
	v_lshlrev_b32_e32 v20, 16, v90
	v_and_b32_e32 v21, 0xffff0000, v90
	v_lshlrev_b32_e32 v22, 16, v91
	v_and_b32_e32 v23, 0xffff0000, v91
	v_pk_add_f32 v[0:1], v[0:1], v[16:17] neg_lo:[0,1] neg_hi:[0,1]
	v_pk_add_f32 v[2:3], v[2:3], v[18:19] neg_lo:[0,1] neg_hi:[0,1]
	v_pk_add_f32 v[4:5], v[4:5], v[20:21] neg_lo:[0,1] neg_hi:[0,1]
	v_pk_add_f32 v[6:7], v[6:7], v[22:23] neg_lo:[0,1] neg_hi:[0,1]
	s_waitcnt vmcnt(15)
	v_lshlrev_b32_e32 v8, 16, v120
	v_and_b32_e32 v9, 0xffff0000, v120
	v_lshlrev_b32_e32 v10, 16, v121
	v_and_b32_e32 v11, 0xffff0000, v121
	v_lshlrev_b32_e32 v12, 16, v122
	v_and_b32_e32 v13, 0xffff0000, v122
	v_lshlrev_b32_e32 v14, 16, v123
	v_and_b32_e32 v15, 0xffff0000, v123
	v_pk_add_f32 v[0:1], v[0:1], v[8:9]
	v_pk_add_f32 v[2:3], v[2:3], v[10:11]
	v_pk_add_f32 v[4:5], v[4:5], v[12:13]
	v_pk_add_f32 v[6:7], v[6:7], v[14:15]
	v_fma_f32 v24, v36, v0, -v8
	v_fma_f32 v25, v36, v1, -v9
	v_fma_f32 v26, v36, v2, -v10
	v_fma_f32 v27, v36, v3, -v11
	v_fma_f32 v28, v36, v4, -v12
	v_fma_f32 v29, v36, v5, -v13
	v_fma_f32 v30, v36, v6, -v14
	v_fma_f32 v31, v36, v7, -v15
	v_pk_mul_f32 v[24:25], v[24:25], 4.0 op_sel_hi:[1,0]
	v_pk_mul_f32 v[26:27], v[26:27], 4.0 op_sel_hi:[1,0]
	v_pk_mul_f32 v[28:29], v[28:29], 4.0 op_sel_hi:[1,0]
	v_pk_mul_f32 v[30:31], v[30:31], 4.0 op_sel_hi:[1,0]
	v_med3_f32 v24, v24, s33, v229
	v_med3_f32 v25, v25, s33, v229
	v_med3_f32 v26, v26, s33, v229
	v_med3_f32 v27, v27, s33, v229
	v_med3_f32 v28, v28, s33, v229
	v_med3_f32 v29, v29, s33, v229
	v_med3_f32 v30, v30, s33, v229
	v_med3_f32 v31, v31, s33, v229
	v_add_u32_e32 v35, 0x6000, v34
	v_cvt_pk_fp8_f32 v40, v24, v25
	v_cvt_pk_fp8_f32 v41, v28, v29
	v_cvt_pk_fp8_f32 v40, v26, v27 op_sel:[0,0,1]
	v_cvt_pk_fp8_f32 v41, v30, v31 op_sel:[0,0,1]
	global_store_dwordx2 v35, v[40:41], s[4:5]
	v_lshlrev_b32_e32 v16, 16, v92
	v_and_b32_e32 v17, 0xffff0000, v92
	v_lshlrev_b32_e32 v18, 16, v93
	v_and_b32_e32 v19, 0xffff0000, v93
	v_lshlrev_b32_e32 v20, 16, v94
	v_and_b32_e32 v21, 0xffff0000, v94
	v_lshlrev_b32_e32 v22, 16, v95
	v_and_b32_e32 v23, 0xffff0000, v95
	v_pk_add_f32 v[0:1], v[0:1], v[16:17] neg_lo:[0,1] neg_hi:[0,1]
	v_pk_add_f32 v[2:3], v[2:3], v[18:19] neg_lo:[0,1] neg_hi:[0,1]
	v_pk_add_f32 v[4:5], v[4:5], v[20:21] neg_lo:[0,1] neg_hi:[0,1]
	v_pk_add_f32 v[6:7], v[6:7], v[22:23] neg_lo:[0,1] neg_hi:[0,1]
	s_waitcnt vmcnt(15)
; template <int WIN> __device__ __forceinline__ void pool_task(const Params& p, int t0, int c) {
;     ...
;     for (int k = 0; k < 16; ++k) { const int t = t0 + k;
;         float cur[8], o[8]; ld8(PROJ + (size_t)t * INC + 5120 + c, cur);
;         const float inv = (k + 1 < WIN && t0 == 0) ? 1.0f / (float)(k + 1) : 1.0f / (float)WIN;
; #pragma unroll
;         for (int i = 0; i < 8; ++i) { tot[i] += cur[i]; o[i] = tot[i] * inv - cur[i]; ring[k % WIN][i] = cur[i]; }
;         st8q(YABC + (size_t)t * 3072 + 2048 + c, o);
; #pragma unroll
;         for (int i = 0; i < 8; ++i) tot[i] -= ring[(k + 1) % WIN][i];
;     }
	v_lshlrev_b32_e32 v8, 16, v124
	v_and_b32_e32 v9, 0xffff0000, v124
	v_lshlrev_b32_e32 v10, 16, v125
	v_and_b32_e32 v11, 0xffff0000, v125
	v_lshlrev_b32_e32 v12, 16, v126
	v_and_b32_e32 v13, 0xffff0000, v126
	v_lshlrev_b32_e32 v14, 16, v127
	v_and_b32_e32 v15, 0xffff0000, v127
	v_pk_add_f32 v[0:1], v[0:1], v[8:9]
	v_pk_add_f32 v[2:3], v[2:3], v[10:11]
	v_pk_add_f32 v[4:5], v[4:5], v[12:13]
	v_pk_add_f32 v[6:7], v[6:7], v[14:15]
	v_fma_f32 v24, v36, v0, -v8
	v_fma_f32 v25, v36, v1, -v9
	v_fma_f32 v26, v36, v2, -v10
	v_fma_f32 v27, v36, v3, -v11
	v_fma_f32 v28, v36, v4, -v12
	v_fma_f32 v29, v36, v5, -v13
	v_fma_f32 v30, v36, v6, -v14
	v_fma_f32 v31, v36, v7, -v15
	v_pk_mul_f32 v[24:25], v[24:25], 4.0 op_sel_hi:[1,0]
	v_pk_mul_f32 v[26:27], v[26:27], 4.0 op_sel_hi:[1,0]
	v_pk_mul_f32 v[28:29], v[28:29], 4.0 op_sel_hi:[1,0]
	v_pk_mul_f32 v[30:31], v[30:31], 4.0 op_sel_hi:[1,0]
	v_med3_f32 v24, v24, s33, v229
	v_med3_f32 v25, v25, s33, v229
	v_med3_f32 v26, v26, s33, v229
	v_med3_f32 v27, v27, s33, v229
	v_med3_f32 v28, v28, s33, v229
	v_med3_f32 v29, v29, s33, v229
	v_med3_f32 v30, v30, s33, v229
	v_med3_f32 v31, v31, s33, v229
	v_add_u32_e32 v35, 0x6c00, v34
	v_cvt_pk_fp8_f32 v40, v24, v25
	v_cvt_pk_fp8_f32 v41, v28, v29
	v_cvt_pk_fp8_f32 v40, v26, v27 op_sel:[0,0,1]
	v_cvt_pk_fp8_f32 v41, v30, v31 op_sel:[0,0,1]
	global_store_dwordx2 v35, v[40:41], s[4:5]
	v_lshlrev_b32_e32 v16, 16, v96
	v_and_b32_e32 v17, 0xffff0000, v96
	v_lshlrev_b32_e32 v18, 16, v97
	v_and_b32_e32 v19, 0xffff0000, v97
	v_lshlrev_b32_e32 v20, 16, v98
	v_and_b32_e32 v21, 0xffff0000, v98
	v_lshlrev_b32_e32 v22, 16, v99
	v_and_b32_e32 v23, 0xffff0000, v99
	v_pk_add_f32 v[0:1], v[0:1], v[16:17] neg_lo:[0,1] neg_hi:[0,1]
	v_pk_add_f32 v[2:3], v[2:3], v[18:19] neg_lo:[0,1] neg_hi:[0,1]
	v_pk_add_f32 v[4:5], v[4:5], v[20:21] neg_lo:[0,1] neg_hi:[0,1]
	v_pk_add_f32 v[6:7], v[6:7], v[22:23] neg_lo:[0,1] neg_hi:[0,1]
	s_waitcnt vmcnt(15)
	v_lshlrev_b32_e32 v8, 16, v128
	v_and_b32_e32 v9, 0xffff0000, v128
	v_lshlrev_b32_e32 v10, 16, v129
	v_and_b32_e32 v11, 0xffff0000, v129
	v_lshlrev_b32_e32 v12, 16, v130
	v_and_b32_e32 v13, 0xffff0000, v130
	v_lshlrev_b32_e32 v14, 16, v131
	v_and_b32_e32 v15, 0xffff0000, v131
	v_pk_add_f32 v[0:1], v[0:1], v[8:9]
	v_pk_add_f32 v[2:3], v[2:3], v[10:11]
	v_pk_add_f32 v[4:5], v[4:5], v[12:13]
	v_pk_add_f32 v[6:7], v[6:7], v[14:15]
	v_fma_f32 v24, v36, v0, -v8
	v_fma_f32 v25, v36, v1, -v9
	v_fma_f32 v26, v36, v2, -v10
	v_fma_f32 v27, v36, v3, -v11
	v_fma_f32 v28, v36, v4, -v12
	v_fma_f32 v29, v36, v5, -v13
	v_fma_f32 v30, v36, v6, -v14
	v_fma_f32 v31, v36, v7, -v15
	v_pk_mul_f32 v[24:25], v[24:25], 4.0 op_sel_hi:[1,0]
	v_pk_mul_f32 v[26:27], v[26:27], 4.0 op_sel_hi:[1,0]
	v_pk_mul_f32 v[28:29], v[28:29], 4.0 op_sel_hi:[1,0]
	v_pk_mul_f32 v[30:31], v[30:31], 4.0 op_sel_hi:[1,0]
	v_med3_f32 v24, v24, s33, v229
	v_med3_f32 v25, v25, s33, v229
	v_med3_f32 v26, v26, s33, v229
	v_med3_f32 v27, v27, s33, v229
	v_med3_f32 v28, v28, s33, v229
	v_med3_f32 v29, v29, s33, v229
	v_med3_f32 v30, v30, s33, v229
	v_med3_f32 v31, v31, s33, v229
	v_add_u32_e32 v35, 0x7800, v34
	v_cvt_pk_fp8_f32 v40, v24, v25
	v_cvt_pk_fp8_f32 v41, v28, v29
	v_cvt_pk_fp8_f32 v40, v26, v27 op_sel:[0,0,1]
	v_cvt_pk_fp8_f32 v41, v30, v31 op_sel:[0,0,1]
	global_store_dwordx2 v35, v[40:41], s[4:5]
	v_lshlrev_b32_e32 v16, 16, v100
	v_and_b32_e32 v17, 0xffff0000, v100
	v_lshlrev_b32_e32 v18, 16, v101
	v_and_b32_e32 v19, 0xffff0000, v101
	v_lshlrev_b32_e32 v20, 16, v102
	v_and_b32_e32 v21, 0xffff0000, v102
	v_lshlrev_b32_e32 v22, 16, v103
	v_and_b32_e32 v23, 0xffff0000, v103
	v_pk_add_f32 v[0:1], v[0:1], v[16:17] neg_lo:[0,1] neg_hi:[0,1]
	v_pk_add_f32 v[2:3], v[2:3], v[18:19] neg_lo:[0,1] neg_hi:[0,1]
	v_pk_add_f32 v[4:5], v[4:5], v[20:21] neg_lo:[0,1] neg_hi:[0,1]
	v_pk_add_f32 v[6:7], v[6:7], v[22:23] neg_lo:[0,1] neg_hi:[0,1]
	s_waitcnt vmcnt(15)
	v_lshlrev_b32_e32 v8, 16, v132
	v_and_b32_e32 v9, 0xffff0000, v132
	v_lshlrev_b32_e32 v10, 16, v133
	v_and_b32_e32 v11, 0xffff0000, v133
	v_lshlrev_b32_e32 v12, 16, v134
	v_and_b32_e32 v13, 0xffff0000, v134
	v_lshlrev_b32_e32 v14, 16, v135
	v_and_b32_e32 v15, 0xffff0000, v135
	v_pk_add_f32 v[0:1], v[0:1], v[8:9]
	v_pk_add_f32 v[2:3], v[2:3], v[10:11]
	v_pk_add_f32 v[4:5], v[4:5], v[12:13]
	v_pk_add_f32 v[6:7], v[6:7], v[14:15]
	v_fma_f32 v24, v36, v0, -v8
	v_fma_f32 v25, v36, v1, -v9
	v_fma_f32 v26, v36, v2, -v10
	v_fma_f32 v27, v36, v3, -v11
	v_fma_f32 v28, v36, v4, -v12
	v_fma_f32 v29, v36, v5, -v13
	v_fma_f32 v30, v36, v6, -v14
	v_fma_f32 v31, v36, v7, -v15
	v_pk_mul_f32 v[24:25], v[24:25], 4.0 op_sel_hi:[1,0]
	v_pk_mul_f32 v[26:27], v[26:27], 4.0 op_sel_hi:[1,0]
	v_pk_mul_f32 v[28:29], v[28:29], 4.0 op_sel_hi:[1,0]
	v_pk_mul_f32 v[30:31], v[30:31], 4.0 op_sel_hi:[1,0]
	v_med3_f32 v24, v24, s33, v229
	v_med3_f32 v25, v25, s33, v229
	v_med3_f32 v26, v26, s33, v229
	v_med3_f32 v27, v27, s33, v229
	v_med3_f32 v28, v28, s33, v229
	v_med3_f32 v29, v29, s33, v229
	v_med3_f32 v30, v30, s33, v229
	v_med3_f32 v31, v31, s33, v229
	v_add_u32_e32 v35, 0x8400, v34
	v_cvt_pk_fp8_f32 v40, v24, v25
	v_cvt_pk_fp8_f32 v41, v28, v29
	v_cvt_pk_fp8_f32 v40, v26, v27 op_sel:[0,0,1]
	v_cvt_pk_fp8_f32 v41, v30, v31 op_sel:[0,0,1]
	global_store_dwordx2 v35, v[40:41], s[4:5]
	v_lshlrev_b32_e32 v16, 16, v104
	v_and_b32_e32 v17, 0xffff0000, v104
	v_lshlrev_b32_e32 v18, 16, v105
	v_and_b32_e32 v19, 0xffff0000, v105
	v_lshlrev_b32_e32 v20, 16, v106
	v_and_b32_e32 v21, 0xffff0000, v106
	v_lshlrev_b32_e32 v22, 16, v107
	v_and_b32_e32 v23, 0xffff0000, v107
	v_pk_add_f32 v[0:1], v[0:1], v[16:17] neg_lo:[0,1] neg_hi:[0,1]
	v_pk_add_f32 v[2:3], v[2:3], v[18:19] neg_lo:[0,1] neg_hi:[0,1]
	v_pk_add_f32 v[4:5], v[4:5], v[20:21] neg_lo:[0,1] neg_hi:[0,1]
	v_pk_add_f32 v[6:7], v[6:7], v[22:23] neg_lo:[0,1] neg_hi:[0,1]
	s_waitcnt vmcnt(15)
; template <int WIN> __device__ __forceinline__ void pool_task(const Params& p, int t0, int c) {
;     ...
;     for (int k = 0; k < 16; ++k) { const int t = t0 + k;
;         float cur[8], o[8]; ld8(PROJ + (size_t)t * INC + 5120 + c, cur);
;         const float inv = (k + 1 < WIN && t0 == 0) ? 1.0f / (float)(k + 1) : 1.0f / (float)WIN;
; #pragma unroll
;         for (int i = 0; i < 8; ++i) { tot[i] += cur[i]; o[i] = tot[i] * inv - cur[i]; ring[k % WIN][i] = cur[i]; }
;         st8q(YABC + (size_t)t * 3072 + 2048 + c, o);
; #pragma unroll
;         for (int i = 0; i < 8; ++i) tot[i] -= ring[(k + 1) % WIN][i];
;     }
	v_lshlrev_b32_e32 v8, 16, v136
	v_and_b32_e32 v9, 0xffff0000, v136
	v_lshlrev_b32_e32 v10, 16, v137
	v_and_b32_e32 v11, 0xffff0000, v137
	v_lshlrev_b32_e32 v12, 16, v138
	v_and_b32_e32 v13, 0xffff0000, v138
	v_lshlrev_b32_e32 v14, 16, v139
	v_and_b32_e32 v15, 0xffff0000, v139
	v_pk_add_f32 v[0:1], v[0:1], v[8:9]
	v_pk_add_f32 v[2:3], v[2:3], v[10:11]
	v_pk_add_f32 v[4:5], v[4:5], v[12:13]
	v_pk_add_f32 v[6:7], v[6:7], v[14:15]
	v_fma_f32 v24, v36, v0, -v8
	v_fma_f32 v25, v36, v1, -v9
	v_fma_f32 v26, v36, v2, -v10
	v_fma_f32 v27, v36, v3, -v11
	v_fma_f32 v28, v36, v4, -v12
	v_fma_f32 v29, v36, v5, -v13
	v_fma_f32 v30, v36, v6, -v14
	v_fma_f32 v31, v36, v7, -v15
	v_pk_mul_f32 v[24:25], v[24:25], 4.0 op_sel_hi:[1,0]
	v_pk_mul_f32 v[26:27], v[26:27], 4.0 op_sel_hi:[1,0]
	v_pk_mul_f32 v[28:29], v[28:29], 4.0 op_sel_hi:[1,0]
	v_pk_mul_f32 v[30:31], v[30:31], 4.0 op_sel_hi:[1,0]
	v_med3_f32 v24, v24, s33, v229
	v_med3_f32 v25, v25, s33, v229
	v_med3_f32 v26, v26, s33, v229
	v_med3_f32 v27, v27, s33, v229
	v_med3_f32 v28, v28, s33, v229
	v_med3_f32 v29, v29, s33, v229
	v_med3_f32 v30, v30, s33, v229
	v_med3_f32 v31, v31, s33, v229
	v_add_u32_e32 v35, 0x9000, v34
	v_cvt_pk_fp8_f32 v40, v24, v25
	v_cvt_pk_fp8_f32 v41, v28, v29
	v_cvt_pk_fp8_f32 v40, v26, v27 op_sel:[0,0,1]
	v_cvt_pk_fp8_f32 v41, v30, v31 op_sel:[0,0,1]
	global_store_dwordx2 v35, v[40:41], s[4:5]
	v_lshlrev_b32_e32 v16, 16, v108
	v_and_b32_e32 v17, 0xffff0000, v108
	v_lshlrev_b32_e32 v18, 16, v109
	v_and_b32_e32 v19, 0xffff0000, v109
	v_lshlrev_b32_e32 v20, 16, v110
	v_and_b32_e32 v21, 0xffff0000, v110
	v_lshlrev_b32_e32 v22, 16, v111
	v_and_b32_e32 v23, 0xffff0000, v111
	v_pk_add_f32 v[0:1], v[0:1], v[16:17] neg_lo:[0,1] neg_hi:[0,1]
	v_pk_add_f32 v[2:3], v[2:3], v[18:19] neg_lo:[0,1] neg_hi:[0,1]
	v_pk_add_f32 v[4:5], v[4:5], v[20:21] neg_lo:[0,1] neg_hi:[0,1]
	v_pk_add_f32 v[6:7], v[6:7], v[22:23] neg_lo:[0,1] neg_hi:[0,1]
	s_waitcnt vmcnt(15)
	v_lshlrev_b32_e32 v8, 16, v140
	v_and_b32_e32 v9, 0xffff0000, v140
	v_lshlrev_b32_e32 v10, 16, v141
	v_and_b32_e32 v11, 0xffff0000, v141
	v_lshlrev_b32_e32 v12, 16, v142
	v_and_b32_e32 v13, 0xffff0000, v142
	v_lshlrev_b32_e32 v14, 16, v143
	v_and_b32_e32 v15, 0xffff0000, v143
	v_pk_add_f32 v[0:1], v[0:1], v[8:9]
	v_pk_add_f32 v[2:3], v[2:3], v[10:11]
	v_pk_add_f32 v[4:5], v[4:5], v[12:13]
	v_pk_add_f32 v[6:7], v[6:7], v[14:15]
	v_fma_f32 v24, v36, v0, -v8
	v_fma_f32 v25, v36, v1, -v9
	v_fma_f32 v26, v36, v2, -v10
	v_fma_f32 v27, v36, v3, -v11
	v_fma_f32 v28, v36, v4, -v12
	v_fma_f32 v29, v36, v5, -v13
	v_fma_f32 v30, v36, v6, -v14
	v_fma_f32 v31, v36, v7, -v15
	v_pk_mul_f32 v[24:25], v[24:25], 4.0 op_sel_hi:[1,0]
	v_pk_mul_f32 v[26:27], v[26:27], 4.0 op_sel_hi:[1,0]
	v_pk_mul_f32 v[28:29], v[28:29], 4.0 op_sel_hi:[1,0]
	v_pk_mul_f32 v[30:31], v[30:31], 4.0 op_sel_hi:[1,0]
	v_med3_f32 v24, v24, s33, v229
	v_med3_f32 v25, v25, s33, v229
	v_med3_f32 v26, v26, s33, v229
	v_med3_f32 v27, v27, s33, v229
	v_med3_f32 v28, v28, s33, v229
	v_med3_f32 v29, v29, s33, v229
	v_med3_f32 v30, v30, s33, v229
	v_med3_f32 v31, v31, s33, v229
	v_add_u32_e32 v35, 0x9c00, v34
	v_cvt_pk_fp8_f32 v40, v24, v25
	v_cvt_pk_fp8_f32 v41, v28, v29
	v_cvt_pk_fp8_f32 v40, v26, v27 op_sel:[0,0,1]
	v_cvt_pk_fp8_f32 v41, v30, v31 op_sel:[0,0,1]
	global_store_dwordx2 v35, v[40:41], s[4:5]
	v_lshlrev_b32_e32 v16, 16, v112
	v_and_b32_e32 v17, 0xffff0000, v112
	v_lshlrev_b32_e32 v18, 16, v113
	v_and_b32_e32 v19, 0xffff0000, v113
	v_lshlrev_b32_e32 v20, 16, v114
	v_and_b32_e32 v21, 0xffff0000, v114
	v_lshlrev_b32_e32 v22, 16, v115
	v_and_b32_e32 v23, 0xffff0000, v115
	v_pk_add_f32 v[0:1], v[0:1], v[16:17] neg_lo:[0,1] neg_hi:[0,1]
	v_pk_add_f32 v[2:3], v[2:3], v[18:19] neg_lo:[0,1] neg_hi:[0,1]
	v_pk_add_f32 v[4:5], v[4:5], v[20:21] neg_lo:[0,1] neg_hi:[0,1]
	v_pk_add_f32 v[6:7], v[6:7], v[22:23] neg_lo:[0,1] neg_hi:[0,1]
	s_waitcnt vmcnt(15)
; __device__ __forceinline__ void xcd_barrier(const XcdBarrier& b) {
;     asm volatile("s_waitcnt vmcnt(0)" ::: "memory");
;     __syncthreads();
;     if (threadIdx.x == 0) {
;         unsigned* bar = b.bar;
;         __builtin_amdgcn_s_waitcnt(0);
;         unsigned nloc = b.st[0], nx = b.st[1];
;         if (nloc == 0u) { xcd_barrier_complete(bar, b.x, nloc, nx); b.st[0] = nloc; b.st[1] = nx; }
; template <int WIN> __device__ __forceinline__ void pool_task(const Params& p, int t0, int c) {
;     ...
;     for (int k = 0; k < 16; ++k) { const int t = t0 + k;
;         float cur[8], o[8]; ld8(PROJ + (size_t)t * INC + 5120 + c, cur);
;         const float inv = (k + 1 < WIN && t0 == 0) ? 1.0f / (float)(k + 1) : 1.0f / (float)WIN;
; #pragma unroll
;         for (int i = 0; i < 8; ++i) { tot[i] += cur[i]; o[i] = tot[i] * inv - cur[i]; ring[k % WIN][i] = cur[i]; }
;         st8q(YABC + (size_t)t * 3072 + 2048 + c, o);
; #pragma unroll
;         for (int i = 0; i < 8; ++i) tot[i] -= ring[(k + 1) % WIN][i];
;     }
	v_lshlrev_b32_e32 v8, 16, v144
	v_and_b32_e32 v9, 0xffff0000, v144
	v_lshlrev_b32_e32 v10, 16, v145
	v_and_b32_e32 v11, 0xffff0000, v145
	v_lshlrev_b32_e32 v12, 16, v146
	v_and_b32_e32 v13, 0xffff0000, v146
	v_lshlrev_b32_e32 v14, 16, v147
	v_and_b32_e32 v15, 0xffff0000, v147
	v_pk_add_f32 v[0:1], v[0:1], v[8:9]
	v_pk_add_f32 v[2:3], v[2:3], v[10:11]
	v_pk_add_f32 v[4:5], v[4:5], v[12:13]
	v_pk_add_f32 v[6:7], v[6:7], v[14:15]
	v_fma_f32 v24, v36, v0, -v8
	v_fma_f32 v25, v36, v1, -v9
	v_fma_f32 v26, v36, v2, -v10
	v_fma_f32 v27, v36, v3, -v11
	v_fma_f32 v28, v36, v4, -v12
	v_fma_f32 v29, v36, v5, -v13
	v_fma_f32 v30, v36, v6, -v14
	v_fma_f32 v31, v36, v7, -v15
	v_pk_mul_f32 v[24:25], v[24:25], 4.0 op_sel_hi:[1,0]
	v_pk_mul_f32 v[26:27], v[26:27], 4.0 op_sel_hi:[1,0]
	v_pk_mul_f32 v[28:29], v[28:29], 4.0 op_sel_hi:[1,0]
	v_pk_mul_f32 v[30:31], v[30:31], 4.0 op_sel_hi:[1,0]
	v_med3_f32 v24, v24, s33, v229
	v_med3_f32 v25, v25, s33, v229
	v_med3_f32 v26, v26, s33, v229
	v_med3_f32 v27, v27, s33, v229
	v_med3_f32 v28, v28, s33, v229
	v_med3_f32 v29, v29, s33, v229
	v_med3_f32 v30, v30, s33, v229
	v_med3_f32 v31, v31, s33, v229
	v_add_u32_e32 v35, 0xa800, v34
	v_cvt_pk_fp8_f32 v40, v24, v25
	v_cvt_pk_fp8_f32 v41, v28, v29
	v_cvt_pk_fp8_f32 v40, v26, v27 op_sel:[0,0,1]
	v_cvt_pk_fp8_f32 v41, v30, v31 op_sel:[0,0,1]
	global_store_dwordx2 v35, v[40:41], s[4:5]
	v_lshlrev_b32_e32 v16, 16, v116
	v_and_b32_e32 v17, 0xffff0000, v116
	v_lshlrev_b32_e32 v18, 16, v117
	v_and_b32_e32 v19, 0xffff0000, v117
	v_lshlrev_b32_e32 v20, 16, v118
	v_and_b32_e32 v21, 0xffff0000, v118
	v_lshlrev_b32_e32 v22, 16, v119
	v_and_b32_e32 v23, 0xffff0000, v119
	v_pk_add_f32 v[0:1], v[0:1], v[16:17] neg_lo:[0,1] neg_hi:[0,1]
	v_pk_add_f32 v[2:3], v[2:3], v[18:19] neg_lo:[0,1] neg_hi:[0,1]
	v_pk_add_f32 v[4:5], v[4:5], v[20:21] neg_lo:[0,1] neg_hi:[0,1]
	v_pk_add_f32 v[6:7], v[6:7], v[22:23] neg_lo:[0,1] neg_hi:[0,1]
	s_waitcnt vmcnt(15)
	v_lshlrev_b32_e32 v8, 16, v148
	v_and_b32_e32 v9, 0xffff0000, v148
	v_lshlrev_b32_e32 v10, 16, v149
	v_and_b32_e32 v11, 0xffff0000, v149
	v_lshlrev_b32_e32 v12, 16, v150
	v_and_b32_e32 v13, 0xffff0000, v150
	v_lshlrev_b32_e32 v14, 16, v151
	v_and_b32_e32 v15, 0xffff0000, v151
	v_pk_add_f32 v[0:1], v[0:1], v[8:9]
	v_pk_add_f32 v[2:3], v[2:3], v[10:11]
	v_pk_add_f32 v[4:5], v[4:5], v[12:13]
	v_pk_add_f32 v[6:7], v[6:7], v[14:15]
	v_fma_f32 v24, v36, v0, -v8
	v_fma_f32 v25, v36, v1, -v9
	v_fma_f32 v26, v36, v2, -v10
	v_fma_f32 v27, v36, v3, -v11
	v_fma_f32 v28, v36, v4, -v12
	v_fma_f32 v29, v36, v5, -v13
	v_fma_f32 v30, v36, v6, -v14
	v_fma_f32 v31, v36, v7, -v15
	v_pk_mul_f32 v[24:25], v[24:25], 4.0 op_sel_hi:[1,0]
	v_pk_mul_f32 v[26:27], v[26:27], 4.0 op_sel_hi:[1,0]
	v_pk_mul_f32 v[28:29], v[28:29], 4.0 op_sel_hi:[1,0]
	v_pk_mul_f32 v[30:31], v[30:31], 4.0 op_sel_hi:[1,0]
	v_med3_f32 v24, v24, s33, v229
	v_med3_f32 v25, v25, s33, v229
	v_med3_f32 v26, v26, s33, v229
	v_med3_f32 v27, v27, s33, v229
	v_med3_f32 v28, v28, s33, v229
	v_med3_f32 v29, v29, s33, v229
	v_med3_f32 v30, v30, s33, v229
	v_med3_f32 v31, v31, s33, v229
	v_add_u32_e32 v35, 0xb400, v34
	v_cvt_pk_fp8_f32 v40, v24, v25
	v_cvt_pk_fp8_f32 v41, v28, v29
	v_cvt_pk_fp8_f32 v40, v26, v27 op_sel:[0,0,1]
	v_cvt_pk_fp8_f32 v41, v30, v31 op_sel:[0,0,1]
	global_store_dwordx2 v35, v[40:41], s[4:5]
	s_branch .Lmy_cp_next
.Lmy_cp_next:
	s_add_i32 s6, s6, s78
	s_branch .Lmy_cp_loop
.Lmy_cp_done:
.LBB0_555:
	s_or_b64 exec, exec, s[0:1]
	v_readlane_b32 s0, v254, 21
	s_or_b32 s16, s0, 3
	v_readlane_b32 s0, v249, 3
	v_readlane_b32 s1, v249, 4
	s_cmp_lt_i32 s16, s1
	s_cbranch_scc0 .LBB0_605
	s_waitcnt vmcnt(0)
	s_waitcnt lgkmcnt(0)
	s_barrier
	s_mov_b64 s[0:1], exec
	v_readlane_b32 s2, v251, 55
	v_readlane_b32 s3, v251, 56
	s_and_b64 s[2:3], s[0:1], s[2:3]
	s_mov_b64 exec, s[2:3]
	s_cbranch_execz .LBB0_604
	v_readlane_b32 s2, v249, 5
	s_waitcnt vmcnt(0) expcnt(0) lgkmcnt(0)
	s_nop 0
	v_mov_b32_e32 v0, s2
	ds_read_b32 v2, v0
	ds_read_b32 v0, v0 offset:4
	s_waitcnt lgkmcnt(1)
	v_cmp_ne_u32_e32 vcc, 0, v2
	s_cbranch_vccnz .LBB0_572
	v_readlane_b32 s4, v249, 0
	v_readlane_b32 s5, v249, 1
	s_load_dwordx2 s[2:3], s[4:5], 0x4
	s_mov_b32 s9, 1
	s_waitcnt lgkmcnt(0)
	s_mul_i32 s8, s2, s78
	s_mul_i32 s8, s8, s3
	s_branch .LBB0_560

; __device__ __forceinline__ float bflo(unsigned w) { return __uint_as_float(w << 16); }
; __device__ __forceinline__ float bfhi(unsigned w) { return __uint_as_float(w & 0xffff0000u); }
; template <int MAP>
; __device__ __forceinline__ void ln_finish(float (&v)[32], const float* __restrict__ g, const float* __restrict__ b, float* xout, bf16* xbout, int lane, bf16* xlout = nullptr, unsigned char* x8out = nullptr, unsigned char* xi8out = nullptr, float* sxout = nullptr) {
;     float s = 0.f;
; #pragma unroll
;     for (int i = 0; i < 32; ++i) s += v[i];
;     const float mean = wave_sum(s, lane) * (1.0f / D);
; __device__ __forceinline__ void ln1_router_unit(const Params& p, int l, int unit, LAS unsigned char* lds, int tid, bool dry = false) {
;     ...
;     for (int r = 0; r < 4; ++r) {
;         const int t = t0 + wid * 4 + r; float v[32]; const bf16* xr = XB + (size_t)t * D; const bf16* mr = MIX + (size_t)t * D;
; #pragma unroll
;         for (int j = 0; j < 8; ++j) { const int c = 4 * (lane + 64 * j); const u32x2 a = __builtin_nontemporal_load((const u32x2*)(xr + c)); const u32x2 mw = __builtin_nontemporal_load((const u32x2*)(mr + c));
;             v[4 * j] = ALPHA * bflo(a.x) + bflo(mw.x); v[4 * j + 1] = ALPHA * bfhi(a.x) + bfhi(mw.x); v[4 * j + 2] = ALPHA * bflo(a.y) + bflo(mw.y); v[4 * j + 3] = ALPHA * bfhi(a.y) + bfhi(mw.y); }
;         ln_finish<0>(v, p.in[15] + (size_t)l * D, p.in[16] + (size_t)l * D, nullptr, XB + (size_t)t * D, lane, XL + (size_t)t * D, p.ws + WS_X8 + (size_t)t * D);
.LBB0_872:
	s_add_i32 s12, s6, s7
	s_ashr_i32 s13, s12, 31
	s_lshl_b64 s[14:15], s[12:13], 11
	s_lshl_b64 s[12:13], s[12:13], 12
	v_lshl_add_u64 v[114:115], v[80:81], 0, s[12:13]
	v_lshl_add_u64 v[116:117], v[82:83], 0, s[12:13]
	global_load_dwordx2 v[198:199], v[114:115], off nt
	global_load_dwordx2 v[200:201], v[116:117], off nt
	global_load_dwordx2 v[202:203], v[114:115], off offset:512 nt
	global_load_dwordx2 v[204:205], v[116:117], off offset:512 nt
	global_load_dwordx2 v[206:207], v[114:115], off offset:1024 nt
	global_load_dwordx2 v[208:209], v[116:117], off offset:1024 nt
	global_load_dwordx2 v[210:211], v[114:115], off offset:1536 nt
	global_load_dwordx2 v[212:213], v[116:117], off offset:1536 nt
	global_load_dwordx2 v[214:215], v[114:115], off offset:2048 nt
	global_load_dwordx2 v[216:217], v[116:117], off offset:2048 nt
	global_load_dwordx2 v[218:219], v[114:115], off offset:2560 nt
	global_load_dwordx2 v[220:221], v[116:117], off offset:2560 nt
	global_load_dwordx2 v[232:233], v[114:115], off offset:3072 nt
	global_load_dwordx2 v[234:235], v[116:117], off offset:3072 nt
	global_load_dwordx2 v[236:237], v[114:115], off offset:3584 nt
	global_load_dwordx2 v[238:239], v[116:117], off offset:3584 nt
	s_waitcnt vmcnt(15)
	v_mov_b64_e32 v[112:113], v[198:199]
	s_waitcnt vmcnt(14)
	v_mov_b64_e32 v[118:119], v[200:201]
	s_add_i32 s7, s7, 1
	s_cmp_eq_u32 s7, 4
	v_lshlrev_b32_e32 v120, 16, v112
	v_lshlrev_b32_e32 v122, 16, v118
	v_and_b32_e32 v126, 0xffff0000, v112
	v_and_b32_e32 v128, 0xffff0000, v118
	v_lshlrev_b32_e32 v127, 16, v113
	v_lshlrev_b32_e32 v129, 16, v119
	v_and_b32_e32 v121, 0xffff0000, v113
	v_and_b32_e32 v123, 0xffff0000, v119
	s_waitcnt vmcnt(13)
	v_mov_b64_e32 v[112:113], v[202:203]
	s_waitcnt vmcnt(12)
	v_mov_b64_e32 v[118:119], v[204:205]
	v_pk_fma_f32 v[120:121], v[120:121], s[96:97], v[122:123] op_sel_hi:[1,0,1]
	v_pk_fma_f32 v[126:127], v[126:127], s[96:97], v[128:129] op_sel_hi:[1,0,1]
	v_add_f32_e32 v91, 0, v120
	v_add_f32_e32 v91, v126, v91
	v_add_f32_e32 v91, v127, v91
	v_add_f32_e32 v91, v121, v91
	v_lshlrev_b32_e32 v130, 16, v112
	v_lshlrev_b32_e32 v132, 16, v118
	v_and_b32_e32 v134, 0xffff0000, v112
	v_and_b32_e32 v136, 0xffff0000, v118
	v_lshlrev_b32_e32 v135, 16, v113
	v_lshlrev_b32_e32 v137, 16, v119
	v_and_b32_e32 v131, 0xffff0000, v113
	v_and_b32_e32 v133, 0xffff0000, v119
	s_waitcnt vmcnt(11)
	v_mov_b64_e32 v[112:113], v[206:207]
	s_waitcnt vmcnt(10)
	v_mov_b64_e32 v[118:119], v[208:209]
	v_pk_fma_f32 v[130:131], v[130:131], s[96:97], v[132:133] op_sel_hi:[1,0,1]
	v_pk_fma_f32 v[128:129], v[134:135], s[96:97], v[136:137] op_sel_hi:[1,0,1]
	v_add_f32_e32 v91, v130, v91
	v_add_f32_e32 v91, v128, v91
	v_add_f32_e32 v91, v129, v91
	v_add_f32_e32 v91, v131, v91
	v_lshlrev_b32_e32 v138, 16, v112
	v_lshlrev_b32_e32 v140, 16, v118
	v_and_b32_e32 v142, 0xffff0000, v112
	v_and_b32_e32 v144, 0xffff0000, v118
	v_lshlrev_b32_e32 v143, 16, v113
	v_lshlrev_b32_e32 v145, 16, v119
	v_and_b32_e32 v139, 0xffff0000, v113
	v_and_b32_e32 v141, 0xffff0000, v119
	s_waitcnt vmcnt(9)
	v_mov_b64_e32 v[112:113], v[210:211]
	s_waitcnt vmcnt(8)
	v_mov_b64_e32 v[118:119], v[212:213]
	v_pk_fma_f32 v[134:135], v[138:139], s[96:97], v[140:141] op_sel_hi:[1,0,1]
	v_pk_fma_f32 v[132:133], v[142:143], s[96:97], v[144:145] op_sel_hi:[1,0,1]
	v_add_f32_e32 v91, v134, v91
	v_add_f32_e32 v91, v132, v91
	v_add_f32_e32 v91, v133, v91
	v_add_f32_e32 v91, v135, v91
	v_lshlrev_b32_e32 v146, 16, v112
	v_lshlrev_b32_e32 v148, 16, v118
	v_and_b32_e32 v168, 0xffff0000, v112
	v_and_b32_e32 v170, 0xffff0000, v118
	v_lshlrev_b32_e32 v169, 16, v113
	v_lshlrev_b32_e32 v171, 16, v119
	v_and_b32_e32 v147, 0xffff0000, v113
	v_and_b32_e32 v149, 0xffff0000, v119
	s_waitcnt vmcnt(7)
	v_mov_b64_e32 v[112:113], v[214:215]
	s_waitcnt vmcnt(6)
	v_mov_b64_e32 v[118:119], v[216:217]
	v_pk_fma_f32 v[138:139], v[146:147], s[96:97], v[148:149] op_sel_hi:[1,0,1]
	v_pk_fma_f32 v[136:137], v[168:169], s[96:97], v[170:171] op_sel_hi:[1,0,1]
	v_add_f32_e32 v91, v138, v91
	v_add_f32_e32 v91, v136, v91
	v_add_f32_e32 v91, v137, v91
	v_add_f32_e32 v91, v139, v91
	v_lshlrev_b32_e32 v172, 16, v112
	v_lshlrev_b32_e32 v174, 16, v118
	v_and_b32_e32 v176, 0xffff0000, v112
	v_and_b32_e32 v178, 0xffff0000, v118
	v_lshlrev_b32_e32 v177, 16, v113
	v_lshlrev_b32_e32 v179, 16, v119
	v_and_b32_e32 v173, 0xffff0000, v113
	v_and_b32_e32 v175, 0xffff0000, v119
	s_waitcnt vmcnt(5)
	v_mov_b64_e32 v[112:113], v[218:219]
	s_waitcnt vmcnt(4)
	v_mov_b64_e32 v[118:119], v[220:221]
	v_pk_fma_f32 v[170:171], v[172:173], s[96:97], v[174:175] op_sel_hi:[1,0,1]
	v_pk_fma_f32 v[168:169], v[176:177], s[96:97], v[178:179] op_sel_hi:[1,0,1]
	v_add_f32_e32 v91, v170, v91
	v_add_f32_e32 v91, v168, v91
	v_add_f32_e32 v91, v169, v91
	v_add_f32_e32 v91, v171, v91
	v_lshlrev_b32_e32 v180, 16, v112
	v_lshlrev_b32_e32 v182, 16, v118
	v_and_b32_e32 v184, 0xffff0000, v112
	v_and_b32_e32 v186, 0xffff0000, v118
	v_lshlrev_b32_e32 v185, 16, v113
	v_lshlrev_b32_e32 v187, 16, v119
	v_and_b32_e32 v181, 0xffff0000, v113
	v_and_b32_e32 v183, 0xffff0000, v119
	s_waitcnt vmcnt(3)
	v_mov_b64_e32 v[112:113], v[232:233]
	s_waitcnt vmcnt(2)
	v_mov_b64_e32 v[118:119], v[234:235]
	v_pk_fma_f32 v[174:175], v[180:181], s[96:97], v[182:183] op_sel_hi:[1,0,1]
	v_pk_fma_f32 v[172:173], v[184:185], s[96:97], v[186:187] op_sel_hi:[1,0,1]
	v_add_f32_e32 v91, v174, v91
	v_add_f32_e32 v91, v172, v91
	v_add_f32_e32 v91, v173, v91
	v_add_f32_e32 v91, v175, v91
	v_lshlrev_b32_e32 v188, 16, v112
	v_and_b32_e32 v192, 0xffff0000, v112
	v_lshlrev_b32_e32 v193, 16, v113
	v_and_b32_e32 v189, 0xffff0000, v113
	s_waitcnt vmcnt(1)
; __device__ __forceinline__ float shx(float v, int mask, int lane) { return __int_as_float(__builtin_amdgcn_ds_bpermute((lane ^ mask) << 2, __float_as_int(v))); }
; __device__ __forceinline__ float wave_sum(float v, int lane) {
; #pragma unroll
;     for (int o = 1; o < 64; o <<= 1) v += shx(v, o, lane);
;     return v;
; template <int MAP>
; __device__ __forceinline__ void ln_finish(float (&v)[32], const float* __restrict__ g, const float* __restrict__ b, float* xout, bf16* xbout, int lane, bf16* xlout = nullptr, unsigned char* x8out = nullptr, unsigned char* xi8out = nullptr, float* sxout = nullptr) {
;     float s = 0.f;
; #pragma unroll
;     for (int i = 0; i < 32; ++i) s += v[i];
;     const float mean = wave_sum(s, lane) * (1.0f / D);
;     float q = 0.f;
; #pragma unroll
;     for (int i = 0; i < 32; ++i) { v[i] -= mean; q += v[i] * v[i]; }
;     const float rstd = 1.0f / sqrtf(wave_sum(q, lane) * (1.0f / D) + LN_EPS);
	v_mov_b64_e32 v[112:113], v[236:237]
	s_nop 0
	s_waitcnt vmcnt(0)
	v_mov_b64_e32 v[116:117], v[238:239]
	v_lshlrev_b32_e32 v190, 16, v118
	v_and_b32_e32 v191, 0xffff0000, v119
	v_and_b32_e32 v194, 0xffff0000, v118
	v_lshlrev_b32_e32 v195, 16, v119
	v_pk_fma_f32 v[178:179], v[188:189], s[96:97], v[190:191] op_sel_hi:[1,0,1]
	v_pk_fma_f32 v[176:177], v[192:193], s[96:97], v[194:195] op_sel_hi:[1,0,1]
	v_add_f32_e32 v91, v178, v91
	v_add_f32_e32 v91, v176, v91
	v_add_f32_e32 v91, v177, v91
	v_add_f32_e32 v91, v179, v91
	v_and_b32_e32 v118, 0xffff0000, v112
	v_lshlrev_b32_e32 v119, 16, v112
	v_and_b32_e32 v196, 0xffff0000, v116
	v_lshlrev_b32_e32 v197, 16, v116
	v_pk_fma_f32 v[118:119], v[118:119], s[96:97], v[196:197] op_sel_hi:[1,0,1]
	v_and_b32_e32 v112, 0xffff0000, v113
	v_lshlrev_b32_e32 v113, 16, v113
	v_and_b32_e32 v116, 0xffff0000, v117
	v_lshlrev_b32_e32 v117, 16, v117
	v_add_f32_e32 v91, v119, v91
	v_pk_fma_f32 v[122:123], v[112:113], s[96:97], v[116:117] op_sel_hi:[1,0,1]
	v_add_f32_e32 v91, v118, v91
	v_add_f32_e32 v91, v123, v91
	v_add_f32_e32 v91, v122, v91
	ds_bpermute_b32 v93, v125, v91
	v_lshl_add_u64 v[116:117], v[84:85], 0, s[12:13]
	v_lshl_add_u64 v[112:113], v[86:87], 0, s[14:15]
	s_waitcnt lgkmcnt(0)
	v_add_f32_e32 v91, v91, v93
	ds_bpermute_b32 v93, v150, v91
	s_waitcnt lgkmcnt(0)
	v_add_f32_e32 v91, v91, v93
	ds_bpermute_b32 v93, v151, v91
	s_waitcnt lgkmcnt(0)
	v_add_f32_e32 v91, v91, v93
	ds_bpermute_b32 v93, v152, v91
	s_waitcnt lgkmcnt(0)
	v_add_f32_e32 v91, v91, v93
	ds_bpermute_b32 v93, v153, v91
	s_waitcnt lgkmcnt(0)
	v_add_f32_e32 v91, v91, v93
	ds_bpermute_b32 v93, v154, v91
	s_waitcnt lgkmcnt(0)
	v_add_f32_e32 v91, v91, v93
	v_mul_f32_e32 v124, 0x3a000000, v91
	v_pk_add_f32 v[180:181], v[120:121], v[124:125] op_sel_hi:[1,0] neg_lo:[0,1] neg_hi:[0,1]
	v_pk_add_f32 v[182:183], v[126:127], v[124:125] op_sel_hi:[1,0] neg_lo:[0,1] neg_hi:[0,1]
	v_pk_mul_f32 v[120:121], v[180:181], v[180:181]
	v_pk_mul_f32 v[184:185], v[182:183], v[182:183]
	v_pk_add_f32 v[146:147], v[130:131], v[124:125] op_sel_hi:[1,0] neg_lo:[0,1] neg_hi:[0,1]
	v_add_f32_e32 v93, v120, v184
	v_add_f32_e32 v93, v185, v93
	v_pk_mul_f32 v[186:187], v[146:147], v[146:147]
	v_pk_add_f32 v[148:149], v[128:129], v[124:125] op_sel_hi:[1,0] neg_lo:[0,1] neg_hi:[0,1]
	v_add_f32_e32 v93, v121, v93
	v_pk_mul_f32 v[188:189], v[148:149], v[148:149]
	v_add_f32_e32 v93, v186, v93
	v_add_f32_e32 v93, v188, v93
	v_pk_add_f32 v[142:143], v[134:135], v[124:125] op_sel_hi:[1,0] neg_lo:[0,1] neg_hi:[0,1]
	v_add_f32_e32 v93, v189, v93
	v_pk_mul_f32 v[190:191], v[142:143], v[142:143]
	v_pk_add_f32 v[144:145], v[132:133], v[124:125] op_sel_hi:[1,0] neg_lo:[0,1] neg_hi:[0,1]
	v_add_f32_e32 v93, v187, v93
	v_pk_mul_f32 v[192:193], v[144:145], v[144:145]
	v_add_f32_e32 v93, v190, v93
	v_add_f32_e32 v93, v192, v93
	v_pk_add_f32 v[138:139], v[138:139], v[124:125] op_sel_hi:[1,0] neg_lo:[0,1] neg_hi:[0,1]
	v_add_f32_e32 v93, v193, v93
	v_pk_mul_f32 v[194:195], v[138:139], v[138:139]
	v_pk_add_f32 v[140:141], v[136:137], v[124:125] op_sel_hi:[1,0] neg_lo:[0,1] neg_hi:[0,1]
	v_add_f32_e32 v93, v191, v93
	v_pk_mul_f32 v[196:197], v[140:141], v[140:141]
	v_add_f32_e32 v93, v194, v93
	v_add_f32_e32 v93, v196, v93
	v_pk_add_f32 v[134:135], v[170:171], v[124:125] op_sel_hi:[1,0] neg_lo:[0,1] neg_hi:[0,1]
	v_add_f32_e32 v93, v197, v93
	v_pk_mul_f32 v[170:171], v[134:135], v[134:135]
	v_pk_add_f32 v[136:137], v[168:169], v[124:125] op_sel_hi:[1,0] neg_lo:[0,1] neg_hi:[0,1]
	v_add_f32_e32 v93, v195, v93
	v_pk_mul_f32 v[168:169], v[136:137], v[136:137]
	v_add_f32_e32 v93, v170, v93
	v_add_f32_e32 v93, v168, v93
	v_pk_add_f32 v[130:131], v[174:175], v[124:125] op_sel_hi:[1,0] neg_lo:[0,1] neg_hi:[0,1]
	v_add_f32_e32 v93, v169, v93
	v_pk_mul_f32 v[174:175], v[130:131], v[130:131]
	v_pk_add_f32 v[132:133], v[172:173], v[124:125] op_sel_hi:[1,0] neg_lo:[0,1] neg_hi:[0,1]
	v_add_f32_e32 v93, v171, v93
	v_pk_mul_f32 v[172:173], v[132:133], v[132:133]
	v_add_f32_e32 v93, v174, v93
	v_add_f32_e32 v93, v172, v93
	v_pk_add_f32 v[126:127], v[178:179], v[124:125] op_sel_hi:[1,0] neg_lo:[0,1] neg_hi:[0,1]
	v_add_f32_e32 v93, v173, v93
	v_pk_mul_f32 v[178:179], v[126:127], v[126:127]
	v_pk_add_f32 v[128:129], v[176:177], v[124:125] op_sel_hi:[1,0] neg_lo:[0,1] neg_hi:[0,1]
	v_add_f32_e32 v93, v175, v93
	v_pk_mul_f32 v[176:177], v[128:129], v[128:129]
	v_add_f32_e32 v93, v178, v93
	v_add_f32_e32 v93, v176, v93
	v_add_f32_e32 v93, v177, v93
	v_add_f32_e32 v93, v179, v93
	v_fmamk_f32 v120, v91, 0xba000000, v119
	v_fmac_f32_e32 v93, v120, v120
	v_fmac_f32_e32 v118, 0xba000000, v91
	v_pk_add_f32 v[122:123], v[122:123], v[124:125] op_sel_hi:[1,0] neg_lo:[0,1] neg_hi:[0,1]
	v_fmac_f32_e32 v93, v118, v118
	v_pk_mul_f32 v[168:169], v[122:123], v[122:123]
	s_nop 0
	v_add_f32_e32 v91, v169, v93
	v_add_f32_e32 v91, v168, v91
	ds_bpermute_b32 v93, v125, v91
	s_waitcnt lgkmcnt(0)
	v_add_f32_e32 v91, v91, v93
	ds_bpermute_b32 v93, v150, v91
	s_waitcnt lgkmcnt(0)
	v_add_f32_e32 v91, v91, v93
	ds_bpermute_b32 v93, v151, v91
	s_waitcnt lgkmcnt(0)
	v_add_f32_e32 v91, v91, v93
	ds_bpermute_b32 v93, v152, v91
	s_waitcnt lgkmcnt(0)
	v_add_f32_e32 v91, v91, v93
	ds_bpermute_b32 v93, v153, v91
	s_waitcnt lgkmcnt(0)
	v_add_f32_e32 v91, v91, v93
	ds_bpermute_b32 v93, v154, v91
	s_waitcnt lgkmcnt(0)
; template <int MAP>
; __device__ __forceinline__ void ln_finish(float (&v)[32], const float* __restrict__ g, const float* __restrict__ b, float* xout, bf16* xbout, int lane, bf16* xlout = nullptr, unsigned char* x8out = nullptr, unsigned char* xi8out = nullptr, float* sxout = nullptr) {
;     ...
;     const float rstd = 1.0f / sqrtf(wave_sum(q, lane) * (1.0f / D) + LN_EPS);
;     const bool two = (xi8out != nullptr);
;     float qm = 0.f;
;     if (two) {
;         float am = 0.f;
;         if (MAP == 0) {
; #pragma unroll
;             for (int j = 0; j < 8; ++j) { const int c = 4 * (lane + 64 * j); const f32x4 gv = *(const f32x4*)(g + c), bv = *(const f32x4*)(b + c);
;                 v[4 * j] = v[4 * j] * rstd * gv.x + bv.x; v[4 * j + 1] = v[4 * j + 1] * rstd * gv.y + bv.y; v[4 * j + 2] = v[4 * j + 2] * rstd * gv.z + bv.z; v[4 * j + 3] = v[4 * j + 3] * rstd * gv.w + bv.w; }
;         } else {
; #pragma unroll
;             for (int j = 0; j < 4; ++j) { const int c = 8 * (lane + 64 * j); const f32x4 g0 = *(const f32x4*)(g + c), g1 = *(const f32x4*)(g + c + 4), b0 = *(const f32x4*)(b + c), b1 = *(const f32x4*)(b + c + 4);
;                 v[8 * j] = v[8 * j] * rstd * g0.x + b0.x; v[8 * j + 1] = v[8 * j + 1] * rstd * g0.y + b0.y; v[8 * j + 2] = v[8 * j + 2] * rstd * g0.z + b0.z; v[8 * j + 3] = v[8 * j + 3] * rstd * g0.w + b0.w;
;                 v[8 * j + 4] = v[8 * j + 4] * rstd * g1.x + b1.x; v[8 * j + 5] = v[8 * j + 5] * rstd * g1.y + b1.y; v[8 * j + 6] = v[8 * j + 6] * rstd * g1.z + b1.z; v[8 * j + 7] = v[8 * j + 7] * rstd * g1.w + b1.w; }
;         }
; #pragma unroll
;         for (int i = 0; i < 32; ++i) am = fmaxf(am, fabsf(v[i]));
; #pragma unroll
;         for (int o = 1; o < 64; o <<= 1) am = fmaxf(am, shx(am, o, lane));
;         am = fmaxf(am, 1e-20f); qm = 127.0f / am;
;         if (lane == 0) *sxout = am * (1.0f / 127.0f);
;     }
;     if (MAP == 0) {
; #pragma unroll
;         for (int j = 0; j < 8; ++j) {
;             const int c = 4 * (lane + 64 * j);
;             f32x4 o;
;             if (two) { o.x = v[4 * j]; o.y = v[4 * j + 1]; o.z = v[4 * j + 2]; o.w = v[4 * j + 3]; *(unsigned*)(xi8out + c) = pk4_i8(o.x, o.y, o.z, o.w, qm); }
;             else { const f32x4 gv = *(const f32x4*)(g + c), bv = *(const f32x4*)(b + c);
	v_add_f32_e32 v91, v91, v93
	v_fmamk_f32 v91, v91, 0x3a000000, v223
	v_cmp_gt_f32_e32 vcc, s88, v91
	v_mul_f32_e32 v93, 0x4f800000, v91
	s_nop 0
	v_cndmask_b32_e32 v91, v91, v93, vcc
	v_sqrt_f32_e32 v93, v91
	s_nop 0
	v_add_u32_e32 v95, -1, v93
	v_fma_f32 v119, -v95, v93, v91
	v_cmp_ge_f32_e64 s[86:87], 0, v119
	v_add_u32_e32 v119, 1, v93
	s_nop 0
	v_cndmask_b32_e64 v95, v93, v95, s[86:87]
	v_fma_f32 v93, -v119, v93, v91
	v_cmp_lt_f32_e64 s[86:87], 0, v93
	s_nop 1
	v_cndmask_b32_e64 v93, v95, v119, s[86:87]
	v_mul_f32_e32 v95, 0x37800000, v93
	v_cndmask_b32_e32 v93, v93, v95, vcc
	v_cmp_class_f32_e32 vcc, v91, v224
	s_nop 1
	v_cndmask_b32_e32 v91, v93, v91, vcc
	v_div_scale_f32 v93, s[12:13], v91, v91, 1.0
	v_rcp_f32_e32 v95, v93
	s_nop 0
	v_fma_f32 v119, -v93, v95, 1.0
	v_fmac_f32_e32 v95, v119, v95
	v_div_scale_f32 v119, vcc, 1.0, v91, 1.0
	v_mul_f32_e32 v121, v119, v95
	v_fma_f32 v124, -v93, v121, v119
	v_fmac_f32_e32 v121, v124, v95
	v_fma_f32 v93, -v93, v121, v119
	v_div_fmas_f32 v93, v93, v95, v121
	v_div_fixup_f32 v124, v93, v91, 1.0
	v_pk_mul_f32 v[168:169], v[182:183], v[124:125] op_sel_hi:[1,0]
	v_pk_mul_f32 v[170:171], v[180:181], v[124:125] op_sel_hi:[1,0]
	v_pk_fma_f32 v[168:169], v[6:7], v[168:169], v[4:5]
	v_pk_fma_f32 v[170:171], v[2:3], v[170:171], v[0:1]
	v_and_b32_sdwa v93, v168, v222 dst_sel:DWORD dst_unused:UNUSED_PAD src0_sel:WORD_1 src1_sel:DWORD
	v_add3_u32 v93, v168, v93, s30
	v_and_b32_e32 v172, 0xffff0000, v93
	v_and_b32_sdwa v93, v171, v222 dst_sel:DWORD dst_unused:UNUSED_PAD src0_sel:WORD_1 src1_sel:DWORD
	v_and_b32_sdwa v91, v169, v222 dst_sel:DWORD dst_unused:UNUSED_PAD src0_sel:WORD_1 src1_sel:DWORD
	v_and_b32_sdwa v95, v170, v222 dst_sel:DWORD dst_unused:UNUSED_PAD src0_sel:WORD_1 src1_sel:DWORD
	v_add3_u32 v93, v171, v93, s30
	v_add3_u32 v91, v169, v91, s30
	v_add3_u32 v95, v170, v95, s30
	v_and_b32_e32 v173, 0xffff0000, v93
	v_or_b32_sdwa v175, v173, v91 dst_sel:DWORD dst_unused:UNUSED_PAD src0_sel:DWORD src1_sel:WORD_1
	v_or_b32_sdwa v174, v95, v172 dst_sel:DWORD dst_unused:UNUSED_PAD src0_sel:WORD_1 src1_sel:DWORD
	global_store_dwordx2 v[114:115], v[174:175], off
	v_and_b32_e32 v175, 0xffff0000, v91
	v_and_b32_e32 v174, 0xffff0000, v95
	v_mov_b32_e32 v176, v170
	v_mov_b32_e32 v177, v169
	v_pk_add_f32 v[174:175], v[176:177], v[174:175] neg_lo:[0,1] neg_hi:[0,1]
	v_mov_b32_e32 v176, v168
	v_mov_b32_e32 v177, v171
	v_pk_add_f32 v[172:173], v[176:177], v[172:173] neg_lo:[0,1] neg_hi:[0,1]
	v_and_b32_sdwa v91, v175, v222 dst_sel:DWORD dst_unused:UNUSED_PAD src0_sel:WORD_1 src1_sel:DWORD
	v_and_b32_sdwa v95, v173, v222 dst_sel:DWORD dst_unused:UNUSED_PAD src0_sel:WORD_1 src1_sel:DWORD
	v_and_b32_sdwa v119, v172, v222 dst_sel:DWORD dst_unused:UNUSED_PAD src0_sel:WORD_1 src1_sel:DWORD
	v_and_b32_sdwa v93, v174, v222 dst_sel:DWORD dst_unused:UNUSED_PAD src0_sel:WORD_1 src1_sel:DWORD
	v_add3_u32 v95, v173, v95, s30
	v_add3_u32 v119, v172, v119, s30
	v_add3_u32 v93, v174, v93, s30
	v_add3_u32 v91, v175, v91, s30
	v_and_b32_e32 v95, 0xffff0000, v95
	v_and_b32_e32 v119, 0xffff0000, v119
	v_or_b32_sdwa v173, v95, v91 dst_sel:DWORD dst_unused:UNUSED_PAD src0_sel:DWORD src1_sel:WORD_1
	v_or_b32_sdwa v172, v119, v93 dst_sel:DWORD dst_unused:UNUSED_PAD src0_sel:DWORD src1_sel:WORD_1
	v_med3_f32 v95, v168, s33, v229
	v_med3_f32 v119, v170, s33, v229
	v_mov_b32_e32 v121, 0
	v_cvt_pk_fp8_f32 v121, v119, v95
	v_pk_mul_f32 v[148:149], v[148:149], v[124:125] op_sel_hi:[1,0]
	v_med3_f32 v91, v171, s33, v229
	v_med3_f32 v93, v169, s33, v229
	v_pk_fma_f32 v[148:149], v[14:15], v[148:149], v[12:13]
	v_cvt_pk_fp8_f32 v121, v93, v91 op_sel:[0,0,1]
	v_pk_mul_f32 v[146:147], v[146:147], v[124:125] op_sel_hi:[1,0]
	v_and_b32_sdwa v93, v148, v222 dst_sel:DWORD dst_unused:UNUSED_PAD src0_sel:WORD_1 src1_sel:DWORD
	v_pk_fma_f32 v[146:147], v[10:11], v[146:147], v[8:9]
	v_add3_u32 v93, v148, v93, s30
	v_and_b32_e32 v168, 0xffff0000, v93
	v_and_b32_sdwa v93, v147, v222 dst_sel:DWORD dst_unused:UNUSED_PAD src0_sel:WORD_1 src1_sel:DWORD
	v_and_b32_sdwa v91, v149, v222 dst_sel:DWORD dst_unused:UNUSED_PAD src0_sel:WORD_1 src1_sel:DWORD
	v_and_b32_sdwa v95, v146, v222 dst_sel:DWORD dst_unused:UNUSED_PAD src0_sel:WORD_1 src1_sel:DWORD
	v_add3_u32 v93, v147, v93, s30
	v_add3_u32 v91, v149, v91, s30
	v_add3_u32 v95, v146, v95, s30
	v_and_b32_e32 v169, 0xffff0000, v93
	v_or_b32_sdwa v171, v169, v91 dst_sel:DWORD dst_unused:UNUSED_PAD src0_sel:DWORD src1_sel:WORD_1
	v_or_b32_sdwa v170, v95, v168 dst_sel:DWORD dst_unused:UNUSED_PAD src0_sel:WORD_1 src1_sel:DWORD
	global_store_dwordx2 v[116:117], v[172:173], off
	global_store_dword v[112:113], v121, off
	global_store_dwordx2 v[114:115], v[170:171], off offset:512
	v_and_b32_e32 v171, 0xffff0000, v91
	v_and_b32_e32 v170, 0xffff0000, v95
	v_mov_b32_e32 v172, v146
	v_mov_b32_e32 v173, v149
	v_pk_add_f32 v[170:171], v[172:173], v[170:171] neg_lo:[0,1] neg_hi:[0,1]
	v_mov_b32_e32 v172, v148
	v_mov_b32_e32 v173, v147
	v_pk_add_f32 v[168:169], v[172:173], v[168:169] neg_lo:[0,1] neg_hi:[0,1]
	v_and_b32_sdwa v91, v171, v222 dst_sel:DWORD dst_unused:UNUSED_PAD src0_sel:WORD_1 src1_sel:DWORD
	v_and_b32_sdwa v95, v169, v222 dst_sel:DWORD dst_unused:UNUSED_PAD src0_sel:WORD_1 src1_sel:DWORD
	v_and_b32_sdwa v119, v168, v222 dst_sel:DWORD dst_unused:UNUSED_PAD src0_sel:WORD_1 src1_sel:DWORD
	v_and_b32_sdwa v93, v170, v222 dst_sel:DWORD dst_unused:UNUSED_PAD src0_sel:WORD_1 src1_sel:DWORD
	v_add3_u32 v95, v169, v95, s30
	v_add3_u32 v119, v168, v119, s30
	v_add3_u32 v93, v170, v93, s30
	v_add3_u32 v91, v171, v91, s30
	v_and_b32_e32 v95, 0xffff0000, v95
	v_and_b32_e32 v119, 0xffff0000, v119
; __device__ __forceinline__ float bf2f(unsigned b) { return __uint_as_float(b << 16); }
; __device__ __forceinline__ unsigned f2bf(float f) { unsigned u = __float_as_uint(f); return (u + 0x7fffu + ((u >> 16) & 1u)) >> 16; }
; __device__ __forceinline__ unsigned pk2(float lo, float hi) { return f2bf(lo) | (f2bf(hi) << 16); }
; __device__ __forceinline__ unsigned pk4_fp8(float a, float b, float c, float d) { unsigned w = 0u; w = __builtin_amdgcn_cvt_pk_fp8_f32(clamp8(a), clamp8(b), w, false); w = __builtin_amdgcn_cvt_pk_fp8_f32(clamp8(c), clamp8(d), w, true); return w; }
; template <int MAP>
; __device__ __forceinline__ void ln_finish(float (&v)[32], const float* __restrict__ g, const float* __restrict__ b, float* xout, bf16* xbout, int lane, bf16* xlout = nullptr, unsigned char* x8out = nullptr, unsigned char* xi8out = nullptr, float* sxout = nullptr) {
;     ...
;     if (MAP == 0) {
; #pragma unroll
;         for (int j = 0; j < 8; ++j) {
;             const int c = 4 * (lane + 64 * j);
;             f32x4 o;
;             if (two) { o.x = v[4 * j]; o.y = v[4 * j + 1]; o.z = v[4 * j + 2]; o.w = v[4 * j + 3]; *(unsigned*)(xi8out + c) = pk4_i8(o.x, o.y, o.z, o.w, qm); }
;             else { const f32x4 gv = *(const f32x4*)(g + c), bv = *(const f32x4*)(b + c);
;                 o.x = v[4 * j] * rstd * gv.x + bv.x; o.y = v[4 * j + 1] * rstd * gv.y + bv.y; o.z = v[4 * j + 2] * rstd * gv.z + bv.z; o.w = v[4 * j + 3] * rstd * gv.w + bv.w; }
;             if (xout) *(f32x4*)(xout + c) = o;
;             if (xbout) { u32x2 w; w.x = pk2(o.x, o.y); w.y = pk2(o.z, o.w); *(u32x2*)(xbout + c) = w; }
;             if (xlout) { u32x2 w; w.x = pk2(o.x - bf2f(f2bf(o.x)), o.y - bf2f(f2bf(o.y))); w.y = pk2(o.z - bf2f(f2bf(o.z)), o.w - bf2f(f2bf(o.w))); *(u32x2*)(xlout + c) = w; }
;             if (x8out) *(unsigned*)(x8out + c) = pk4_fp8(o.x, o.y, o.z, o.w);
	v_or_b32_sdwa v169, v95, v91 dst_sel:DWORD dst_unused:UNUSED_PAD src0_sel:DWORD src1_sel:WORD_1
	v_or_b32_sdwa v168, v119, v93 dst_sel:DWORD dst_unused:UNUSED_PAD src0_sel:DWORD src1_sel:WORD_1
	v_med3_f32 v95, v148, s33, v229
	v_med3_f32 v119, v146, s33, v229
	v_mov_b32_e32 v121, 0
	v_cvt_pk_fp8_f32 v121, v119, v95
	v_pk_mul_f32 v[144:145], v[144:145], v[124:125] op_sel_hi:[1,0]
	v_med3_f32 v91, v147, s33, v229
	v_med3_f32 v93, v149, s33, v229
	v_pk_fma_f32 v[144:145], v[22:23], v[144:145], v[20:21]
	v_cvt_pk_fp8_f32 v121, v93, v91 op_sel:[0,0,1]
	v_pk_mul_f32 v[142:143], v[142:143], v[124:125] op_sel_hi:[1,0]
	v_and_b32_sdwa v93, v144, v222 dst_sel:DWORD dst_unused:UNUSED_PAD src0_sel:WORD_1 src1_sel:DWORD
	v_pk_fma_f32 v[142:143], v[18:19], v[142:143], v[16:17]
	v_add3_u32 v93, v144, v93, s30
	v_and_b32_e32 v146, 0xffff0000, v93
	v_and_b32_sdwa v93, v143, v222 dst_sel:DWORD dst_unused:UNUSED_PAD src0_sel:WORD_1 src1_sel:DWORD
	v_and_b32_sdwa v91, v145, v222 dst_sel:DWORD dst_unused:UNUSED_PAD src0_sel:WORD_1 src1_sel:DWORD
	v_and_b32_sdwa v95, v142, v222 dst_sel:DWORD dst_unused:UNUSED_PAD src0_sel:WORD_1 src1_sel:DWORD
	v_add3_u32 v93, v143, v93, s30
	v_add3_u32 v91, v145, v91, s30
	v_add3_u32 v95, v142, v95, s30
	v_and_b32_e32 v147, 0xffff0000, v93
	v_or_b32_sdwa v149, v147, v91 dst_sel:DWORD dst_unused:UNUSED_PAD src0_sel:DWORD src1_sel:WORD_1
	v_or_b32_sdwa v148, v95, v146 dst_sel:DWORD dst_unused:UNUSED_PAD src0_sel:WORD_1 src1_sel:DWORD
	global_store_dwordx2 v[116:117], v[168:169], off offset:512
	global_store_dword v[112:113], v121, off offset:256
	global_store_dwordx2 v[114:115], v[148:149], off offset:1024
	v_and_b32_e32 v149, 0xffff0000, v91
	v_and_b32_e32 v148, 0xffff0000, v95
	v_mov_b32_e32 v168, v142
	v_mov_b32_e32 v169, v145
	v_pk_add_f32 v[148:149], v[168:169], v[148:149] neg_lo:[0,1] neg_hi:[0,1]
	v_mov_b32_e32 v168, v144
	v_mov_b32_e32 v169, v143
	v_pk_add_f32 v[146:147], v[168:169], v[146:147] neg_lo:[0,1] neg_hi:[0,1]
	v_and_b32_sdwa v91, v149, v222 dst_sel:DWORD dst_unused:UNUSED_PAD src0_sel:WORD_1 src1_sel:DWORD
	v_and_b32_sdwa v95, v147, v222 dst_sel:DWORD dst_unused:UNUSED_PAD src0_sel:WORD_1 src1_sel:DWORD
	v_and_b32_sdwa v119, v146, v222 dst_sel:DWORD dst_unused:UNUSED_PAD src0_sel:WORD_1 src1_sel:DWORD
	v_and_b32_sdwa v93, v148, v222 dst_sel:DWORD dst_unused:UNUSED_PAD src0_sel:WORD_1 src1_sel:DWORD
	v_add3_u32 v95, v147, v95, s30
	v_add3_u32 v119, v146, v119, s30
	v_add3_u32 v93, v148, v93, s30
	v_add3_u32 v91, v149, v91, s30
	v_and_b32_e32 v95, 0xffff0000, v95
	v_and_b32_e32 v119, 0xffff0000, v119
	v_or_b32_sdwa v147, v95, v91 dst_sel:DWORD dst_unused:UNUSED_PAD src0_sel:DWORD src1_sel:WORD_1
	v_or_b32_sdwa v146, v119, v93 dst_sel:DWORD dst_unused:UNUSED_PAD src0_sel:DWORD src1_sel:WORD_1
	v_med3_f32 v95, v144, s33, v229
	v_med3_f32 v119, v142, s33, v229
	v_mov_b32_e32 v121, 0
	v_cvt_pk_fp8_f32 v121, v119, v95
	v_pk_mul_f32 v[140:141], v[140:141], v[124:125] op_sel_hi:[1,0]
	v_med3_f32 v91, v143, s33, v229
	v_med3_f32 v93, v145, s33, v229
	v_pk_fma_f32 v[140:141], v[30:31], v[140:141], v[28:29]
	v_cvt_pk_fp8_f32 v121, v93, v91 op_sel:[0,0,1]
	v_pk_mul_f32 v[138:139], v[138:139], v[124:125] op_sel_hi:[1,0]
	v_and_b32_sdwa v93, v140, v222 dst_sel:DWORD dst_unused:UNUSED_PAD src0_sel:WORD_1 src1_sel:DWORD
	v_pk_fma_f32 v[138:139], v[26:27], v[138:139], v[24:25]
	v_add3_u32 v93, v140, v93, s30
	v_and_b32_e32 v142, 0xffff0000, v93
	v_and_b32_sdwa v93, v139, v222 dst_sel:DWORD dst_unused:UNUSED_PAD src0_sel:WORD_1 src1_sel:DWORD
	v_and_b32_sdwa v91, v141, v222 dst_sel:DWORD dst_unused:UNUSED_PAD src0_sel:WORD_1 src1_sel:DWORD
	v_and_b32_sdwa v95, v138, v222 dst_sel:DWORD dst_unused:UNUSED_PAD src0_sel:WORD_1 src1_sel:DWORD
	v_add3_u32 v93, v139, v93, s30
	v_add3_u32 v91, v141, v91, s30
	v_add3_u32 v95, v138, v95, s30
	v_and_b32_e32 v143, 0xffff0000, v93
	v_or_b32_sdwa v145, v143, v91 dst_sel:DWORD dst_unused:UNUSED_PAD src0_sel:DWORD src1_sel:WORD_1
	v_or_b32_sdwa v144, v95, v142 dst_sel:DWORD dst_unused:UNUSED_PAD src0_sel:WORD_1 src1_sel:DWORD
	global_store_dwordx2 v[116:117], v[146:147], off offset:1024
	global_store_dword v[112:113], v121, off offset:512
	global_store_dwordx2 v[114:115], v[144:145], off offset:1536
	v_and_b32_e32 v145, 0xffff0000, v91
	v_and_b32_e32 v144, 0xffff0000, v95
	v_mov_b32_e32 v146, v138
	v_mov_b32_e32 v147, v141
	v_pk_add_f32 v[144:145], v[146:147], v[144:145] neg_lo:[0,1] neg_hi:[0,1]
	v_mov_b32_e32 v146, v140
	v_mov_b32_e32 v147, v139
	v_pk_add_f32 v[142:143], v[146:147], v[142:143] neg_lo:[0,1] neg_hi:[0,1]
	v_and_b32_sdwa v91, v145, v222 dst_sel:DWORD dst_unused:UNUSED_PAD src0_sel:WORD_1 src1_sel:DWORD
	v_and_b32_sdwa v95, v143, v222 dst_sel:DWORD dst_unused:UNUSED_PAD src0_sel:WORD_1 src1_sel:DWORD
	v_and_b32_sdwa v119, v142, v222 dst_sel:DWORD dst_unused:UNUSED_PAD src0_sel:WORD_1 src1_sel:DWORD
	v_and_b32_sdwa v93, v144, v222 dst_sel:DWORD dst_unused:UNUSED_PAD src0_sel:WORD_1 src1_sel:DWORD
	v_add3_u32 v95, v143, v95, s30
	v_add3_u32 v119, v142, v119, s30
	v_add3_u32 v93, v144, v93, s30
	v_add3_u32 v91, v145, v91, s30
	v_and_b32_e32 v95, 0xffff0000, v95
	v_and_b32_e32 v119, 0xffff0000, v119
	v_or_b32_sdwa v143, v95, v91 dst_sel:DWORD dst_unused:UNUSED_PAD src0_sel:DWORD src1_sel:WORD_1
	v_or_b32_sdwa v142, v119, v93 dst_sel:DWORD dst_unused:UNUSED_PAD src0_sel:DWORD src1_sel:WORD_1
	v_med3_f32 v95, v140, s33, v229
	v_med3_f32 v119, v138, s33, v229
	v_mov_b32_e32 v121, 0
	v_cvt_pk_fp8_f32 v121, v119, v95
	v_pk_mul_f32 v[136:137], v[136:137], v[124:125] op_sel_hi:[1,0]
	v_med3_f32 v91, v139, s33, v229
	v_med3_f32 v93, v141, s33, v229
	v_pk_fma_f32 v[136:137], v[38:39], v[136:137], v[36:37]
; __device__ __forceinline__ float bf2f(unsigned b) { return __uint_as_float(b << 16); }
; __device__ __forceinline__ unsigned f2bf(float f) { unsigned u = __float_as_uint(f); return (u + 0x7fffu + ((u >> 16) & 1u)) >> 16; }
; __device__ __forceinline__ unsigned pk2(float lo, float hi) { return f2bf(lo) | (f2bf(hi) << 16); }
; __device__ __forceinline__ unsigned pk4_fp8(float a, float b, float c, float d) { unsigned w = 0u; w = __builtin_amdgcn_cvt_pk_fp8_f32(clamp8(a), clamp8(b), w, false); w = __builtin_amdgcn_cvt_pk_fp8_f32(clamp8(c), clamp8(d), w, true); return w; }
; template <int MAP>
; __device__ __forceinline__ void ln_finish(float (&v)[32], const float* __restrict__ g, const float* __restrict__ b, float* xout, bf16* xbout, int lane, bf16* xlout = nullptr, unsigned char* x8out = nullptr, unsigned char* xi8out = nullptr, float* sxout = nullptr) {
;     ...
;     if (MAP == 0) {
; #pragma unroll
;         for (int j = 0; j < 8; ++j) {
;             const int c = 4 * (lane + 64 * j);
;             f32x4 o;
;             if (two) { o.x = v[4 * j]; o.y = v[4 * j + 1]; o.z = v[4 * j + 2]; o.w = v[4 * j + 3]; *(unsigned*)(xi8out + c) = pk4_i8(o.x, o.y, o.z, o.w, qm); }
;             else { const f32x4 gv = *(const f32x4*)(g + c), bv = *(const f32x4*)(b + c);
;                 o.x = v[4 * j] * rstd * gv.x + bv.x; o.y = v[4 * j + 1] * rstd * gv.y + bv.y; o.z = v[4 * j + 2] * rstd * gv.z + bv.z; o.w = v[4 * j + 3] * rstd * gv.w + bv.w; }
;             if (xout) *(f32x4*)(xout + c) = o;
;             if (xbout) { u32x2 w; w.x = pk2(o.x, o.y); w.y = pk2(o.z, o.w); *(u32x2*)(xbout + c) = w; }
;             if (xlout) { u32x2 w; w.x = pk2(o.x - bf2f(f2bf(o.x)), o.y - bf2f(f2bf(o.y))); w.y = pk2(o.z - bf2f(f2bf(o.z)), o.w - bf2f(f2bf(o.w))); *(u32x2*)(xlout + c) = w; }
;             if (x8out) *(unsigned*)(x8out + c) = pk4_fp8(o.x, o.y, o.z, o.w);
	v_cvt_pk_fp8_f32 v121, v93, v91 op_sel:[0,0,1]
	v_pk_mul_f32 v[134:135], v[134:135], v[124:125] op_sel_hi:[1,0]
	v_and_b32_sdwa v93, v136, v222 dst_sel:DWORD dst_unused:UNUSED_PAD src0_sel:WORD_1 src1_sel:DWORD
	v_pk_fma_f32 v[134:135], v[34:35], v[134:135], v[32:33]
	v_add3_u32 v93, v136, v93, s30
	v_and_b32_e32 v138, 0xffff0000, v93
	v_and_b32_sdwa v93, v135, v222 dst_sel:DWORD dst_unused:UNUSED_PAD src0_sel:WORD_1 src1_sel:DWORD
	v_and_b32_sdwa v91, v137, v222 dst_sel:DWORD dst_unused:UNUSED_PAD src0_sel:WORD_1 src1_sel:DWORD
	v_and_b32_sdwa v95, v134, v222 dst_sel:DWORD dst_unused:UNUSED_PAD src0_sel:WORD_1 src1_sel:DWORD
	v_add3_u32 v93, v135, v93, s30
	v_add3_u32 v91, v137, v91, s30
	v_add3_u32 v95, v134, v95, s30
	v_and_b32_e32 v139, 0xffff0000, v93
	v_or_b32_sdwa v141, v139, v91 dst_sel:DWORD dst_unused:UNUSED_PAD src0_sel:DWORD src1_sel:WORD_1
	v_or_b32_sdwa v140, v95, v138 dst_sel:DWORD dst_unused:UNUSED_PAD src0_sel:WORD_1 src1_sel:DWORD
	global_store_dwordx2 v[116:117], v[142:143], off offset:1536
	global_store_dword v[112:113], v121, off offset:768
	global_store_dwordx2 v[114:115], v[140:141], off offset:2048
	v_and_b32_e32 v141, 0xffff0000, v91
	v_and_b32_e32 v140, 0xffff0000, v95
	v_mov_b32_e32 v142, v134
	v_mov_b32_e32 v143, v137
	v_pk_add_f32 v[140:141], v[142:143], v[140:141] neg_lo:[0,1] neg_hi:[0,1]
	v_mov_b32_e32 v142, v136
	v_mov_b32_e32 v143, v135
	v_pk_add_f32 v[138:139], v[142:143], v[138:139] neg_lo:[0,1] neg_hi:[0,1]
	v_and_b32_sdwa v91, v141, v222 dst_sel:DWORD dst_unused:UNUSED_PAD src0_sel:WORD_1 src1_sel:DWORD
	v_and_b32_sdwa v95, v139, v222 dst_sel:DWORD dst_unused:UNUSED_PAD src0_sel:WORD_1 src1_sel:DWORD
	v_and_b32_sdwa v119, v138, v222 dst_sel:DWORD dst_unused:UNUSED_PAD src0_sel:WORD_1 src1_sel:DWORD
	v_and_b32_sdwa v93, v140, v222 dst_sel:DWORD dst_unused:UNUSED_PAD src0_sel:WORD_1 src1_sel:DWORD
	v_add3_u32 v95, v139, v95, s30
	v_add3_u32 v119, v138, v119, s30
	v_add3_u32 v93, v140, v93, s30
	v_add3_u32 v91, v141, v91, s30
	v_and_b32_e32 v95, 0xffff0000, v95
	v_and_b32_e32 v119, 0xffff0000, v119
	v_or_b32_sdwa v139, v95, v91 dst_sel:DWORD dst_unused:UNUSED_PAD src0_sel:DWORD src1_sel:WORD_1
	v_or_b32_sdwa v138, v119, v93 dst_sel:DWORD dst_unused:UNUSED_PAD src0_sel:DWORD src1_sel:WORD_1
	v_med3_f32 v95, v136, s33, v229
	v_med3_f32 v119, v134, s33, v229
	v_mov_b32_e32 v121, 0
	v_cvt_pk_fp8_f32 v121, v119, v95
	v_pk_mul_f32 v[132:133], v[132:133], v[124:125] op_sel_hi:[1,0]
	v_med3_f32 v91, v135, s33, v229
	v_med3_f32 v93, v137, s33, v229
	v_pk_fma_f32 v[132:133], v[46:47], v[132:133], v[44:45]
	v_cvt_pk_fp8_f32 v121, v93, v91 op_sel:[0,0,1]
	v_pk_mul_f32 v[130:131], v[130:131], v[124:125] op_sel_hi:[1,0]
	v_and_b32_sdwa v93, v132, v222 dst_sel:DWORD dst_unused:UNUSED_PAD src0_sel:WORD_1 src1_sel:DWORD
	v_pk_fma_f32 v[130:131], v[42:43], v[130:131], v[40:41]
	v_add3_u32 v93, v132, v93, s30
	v_and_b32_e32 v134, 0xffff0000, v93
	v_and_b32_sdwa v93, v131, v222 dst_sel:DWORD dst_unused:UNUSED_PAD src0_sel:WORD_1 src1_sel:DWORD
	v_and_b32_sdwa v91, v133, v222 dst_sel:DWORD dst_unused:UNUSED_PAD src0_sel:WORD_1 src1_sel:DWORD
	v_and_b32_sdwa v95, v130, v222 dst_sel:DWORD dst_unused:UNUSED_PAD src0_sel:WORD_1 src1_sel:DWORD
	v_add3_u32 v93, v131, v93, s30
	v_add3_u32 v91, v133, v91, s30
	v_add3_u32 v95, v130, v95, s30
	v_and_b32_e32 v135, 0xffff0000, v93
	v_or_b32_sdwa v137, v135, v91 dst_sel:DWORD dst_unused:UNUSED_PAD src0_sel:DWORD src1_sel:WORD_1
	v_or_b32_sdwa v136, v95, v134 dst_sel:DWORD dst_unused:UNUSED_PAD src0_sel:WORD_1 src1_sel:DWORD
	global_store_dwordx2 v[116:117], v[138:139], off offset:2048
	global_store_dword v[112:113], v121, off offset:1024
	global_store_dwordx2 v[114:115], v[136:137], off offset:2560
	v_and_b32_e32 v137, 0xffff0000, v91
	v_and_b32_e32 v136, 0xffff0000, v95
	v_mov_b32_e32 v138, v130
	v_mov_b32_e32 v139, v133
	v_pk_add_f32 v[136:137], v[138:139], v[136:137] neg_lo:[0,1] neg_hi:[0,1]
	v_mov_b32_e32 v138, v132
	v_mov_b32_e32 v139, v131
	v_pk_add_f32 v[134:135], v[138:139], v[134:135] neg_lo:[0,1] neg_hi:[0,1]
	v_and_b32_sdwa v91, v137, v222 dst_sel:DWORD dst_unused:UNUSED_PAD src0_sel:WORD_1 src1_sel:DWORD
	v_and_b32_sdwa v95, v135, v222 dst_sel:DWORD dst_unused:UNUSED_PAD src0_sel:WORD_1 src1_sel:DWORD
	v_and_b32_sdwa v119, v134, v222 dst_sel:DWORD dst_unused:UNUSED_PAD src0_sel:WORD_1 src1_sel:DWORD
	v_and_b32_sdwa v93, v136, v222 dst_sel:DWORD dst_unused:UNUSED_PAD src0_sel:WORD_1 src1_sel:DWORD
	v_add3_u32 v95, v135, v95, s30
	v_add3_u32 v119, v134, v119, s30
	v_add3_u32 v93, v136, v93, s30
	v_add3_u32 v91, v137, v91, s30
	v_and_b32_e32 v95, 0xffff0000, v95
	v_and_b32_e32 v119, 0xffff0000, v119
	v_or_b32_sdwa v135, v95, v91 dst_sel:DWORD dst_unused:UNUSED_PAD src0_sel:DWORD src1_sel:WORD_1
	v_or_b32_sdwa v134, v119, v93 dst_sel:DWORD dst_unused:UNUSED_PAD src0_sel:DWORD src1_sel:WORD_1
	v_med3_f32 v95, v132, s33, v229
	v_med3_f32 v119, v130, s33, v229
	v_mov_b32_e32 v121, 0
	v_cvt_pk_fp8_f32 v121, v119, v95
	v_pk_mul_f32 v[128:129], v[128:129], v[124:125] op_sel_hi:[1,0]
	v_med3_f32 v91, v131, s33, v229
	v_med3_f32 v93, v133, s33, v229
	v_pk_fma_f32 v[128:129], v[102:103], v[128:129], v[100:101]
	v_cvt_pk_fp8_f32 v121, v93, v91 op_sel:[0,0,1]
	v_pk_mul_f32 v[126:127], v[126:127], v[124:125] op_sel_hi:[1,0]
	v_and_b32_sdwa v93, v128, v222 dst_sel:DWORD dst_unused:UNUSED_PAD src0_sel:WORD_1 src1_sel:DWORD
	v_pk_fma_f32 v[126:127], v[98:99], v[126:127], v[96:97]
	v_add3_u32 v93, v128, v93, s30
	v_and_b32_e32 v130, 0xffff0000, v93
	v_and_b32_sdwa v93, v127, v222 dst_sel:DWORD dst_unused:UNUSED_PAD src0_sel:WORD_1 src1_sel:DWORD
; __device__ __forceinline__ float bf2f(unsigned b) { return __uint_as_float(b << 16); }
; __device__ __forceinline__ unsigned f2bf(float f) { unsigned u = __float_as_uint(f); return (u + 0x7fffu + ((u >> 16) & 1u)) >> 16; }
; __device__ __forceinline__ unsigned pk2(float lo, float hi) { return f2bf(lo) | (f2bf(hi) << 16); }
; template <int MAP>
; __device__ __forceinline__ void ln_finish(float (&v)[32], const float* __restrict__ g, const float* __restrict__ b, float* xout, bf16* xbout, int lane, bf16* xlout = nullptr, unsigned char* x8out = nullptr, unsigned char* xi8out = nullptr, float* sxout = nullptr) {
;     ...
;     if (MAP == 0) {
; #pragma unroll
;         for (int j = 0; j < 8; ++j) {
;             const int c = 4 * (lane + 64 * j);
;             f32x4 o;
;             if (two) { o.x = v[4 * j]; o.y = v[4 * j + 1]; o.z = v[4 * j + 2]; o.w = v[4 * j + 3]; *(unsigned*)(xi8out + c) = pk4_i8(o.x, o.y, o.z, o.w, qm); }
;             else { const f32x4 gv = *(const f32x4*)(g + c), bv = *(const f32x4*)(b + c);
;                 o.x = v[4 * j] * rstd * gv.x + bv.x; o.y = v[4 * j + 1] * rstd * gv.y + bv.y; o.z = v[4 * j + 2] * rstd * gv.z + bv.z; o.w = v[4 * j + 3] * rstd * gv.w + bv.w; }
;             if (xout) *(f32x4*)(xout + c) = o;
;             if (xbout) { u32x2 w; w.x = pk2(o.x, o.y); w.y = pk2(o.z, o.w); *(u32x2*)(xbout + c) = w; }
;             if (xlout) { u32x2 w; w.x = pk2(o.x - bf2f(f2bf(o.x)), o.y - bf2f(f2bf(o.y))); w.y = pk2(o.z - bf2f(f2bf(o.z)), o.w - bf2f(f2bf(o.w))); *(u32x2*)(xlout + c) = w; }
;             if (x8out) *(unsigned*)(x8out + c) = pk4_fp8(o.x, o.y, o.z, o.w);
; __device__ __forceinline__ void ln1_router_unit(const Params& p, int l, int unit, LAS unsigned char* lds, int tid, bool dry = false) {
;     ...
;     if (tid < 64) cnt[tid] = 0;
;     __threadfence_block();
;     __syncthreads();
;     {
;         const int fr = lane & 15, fq = lane >> 4;
;         const bf16* wrh = (const bf16*)(p.ws + WS_WR) + (size_t)l * 2 * NE * D; const bf16* wrl = wrh + (size_t)NE * D;
;         f32x4 racc[2][4];
; #pragma unroll
;         for (int a2 = 0; a2 < 2; ++a2)
; #pragma unroll
;             for (int b2 = 0; b2 < 4; ++b2) racc[a2][b2] = (f32x4){0.f, 0.f, 0.f, 0.f};
	v_and_b32_sdwa v91, v129, v222 dst_sel:DWORD dst_unused:UNUSED_PAD src0_sel:WORD_1 src1_sel:DWORD
	v_and_b32_sdwa v95, v126, v222 dst_sel:DWORD dst_unused:UNUSED_PAD src0_sel:WORD_1 src1_sel:DWORD
	v_add3_u32 v93, v127, v93, s30
	v_add3_u32 v91, v129, v91, s30
	v_add3_u32 v95, v126, v95, s30
	v_and_b32_e32 v131, 0xffff0000, v93
	v_or_b32_sdwa v133, v131, v91 dst_sel:DWORD dst_unused:UNUSED_PAD src0_sel:DWORD src1_sel:WORD_1
	v_or_b32_sdwa v132, v95, v130 dst_sel:DWORD dst_unused:UNUSED_PAD src0_sel:WORD_1 src1_sel:DWORD
	global_store_dwordx2 v[116:117], v[134:135], off offset:2560
	global_store_dword v[112:113], v121, off offset:1280
	global_store_dwordx2 v[114:115], v[132:133], off offset:3072
	v_and_b32_e32 v133, 0xffff0000, v91
	v_and_b32_e32 v132, 0xffff0000, v95
	v_mov_b32_e32 v134, v126
	v_mov_b32_e32 v135, v129
	v_pk_add_f32 v[132:133], v[134:135], v[132:133] neg_lo:[0,1] neg_hi:[0,1]
	v_mov_b32_e32 v134, v128
	v_mov_b32_e32 v135, v127
	v_pk_add_f32 v[130:131], v[134:135], v[130:131] neg_lo:[0,1] neg_hi:[0,1]
	v_and_b32_sdwa v91, v133, v222 dst_sel:DWORD dst_unused:UNUSED_PAD src0_sel:WORD_1 src1_sel:DWORD
	v_and_b32_sdwa v95, v131, v222 dst_sel:DWORD dst_unused:UNUSED_PAD src0_sel:WORD_1 src1_sel:DWORD
	v_and_b32_sdwa v119, v130, v222 dst_sel:DWORD dst_unused:UNUSED_PAD src0_sel:WORD_1 src1_sel:DWORD
	v_and_b32_sdwa v93, v132, v222 dst_sel:DWORD dst_unused:UNUSED_PAD src0_sel:WORD_1 src1_sel:DWORD
	v_add3_u32 v95, v131, v95, s30
	v_add3_u32 v119, v130, v119, s30
	v_add3_u32 v93, v132, v93, s30
	v_add3_u32 v91, v133, v91, s30
	v_and_b32_e32 v95, 0xffff0000, v95
	v_and_b32_e32 v119, 0xffff0000, v119
	v_or_b32_sdwa v131, v95, v91 dst_sel:DWORD dst_unused:UNUSED_PAD src0_sel:DWORD src1_sel:WORD_1
	v_or_b32_sdwa v130, v119, v93 dst_sel:DWORD dst_unused:UNUSED_PAD src0_sel:DWORD src1_sel:WORD_1
	v_med3_f32 v95, v128, s33, v229
	v_med3_f32 v119, v126, s33, v229
	v_mov_b32_e32 v121, 0
	v_cvt_pk_fp8_f32 v121, v119, v95
	v_med3_f32 v91, v127, s33, v229
	v_med3_f32 v93, v129, s33, v229
	v_mov_b32_e32 v119, v123
	v_cvt_pk_fp8_f32 v121, v93, v91 op_sel:[0,0,1]
	v_pk_mul_f32 v[118:119], v[118:119], v[124:125] op_sel_hi:[1,0]
	global_store_dwordx2 v[116:117], v[130:131], off offset:3072
	v_pk_fma_f32 v[118:119], v[110:111], v[118:119], v[108:109]
	global_store_dword v[112:113], v121, off offset:1536
	v_mov_b32_e32 v121, v122
	v_pk_mul_f32 v[120:121], v[120:121], v[124:125] op_sel_hi:[1,0]
	v_and_b32_sdwa v93, v118, v222 dst_sel:DWORD dst_unused:UNUSED_PAD src0_sel:WORD_1 src1_sel:DWORD
	v_pk_fma_f32 v[120:121], v[106:107], v[120:121], v[104:105]
	v_add3_u32 v93, v118, v93, s30
	v_and_b32_e32 v122, 0xffff0000, v93
	v_and_b32_sdwa v93, v121, v222 dst_sel:DWORD dst_unused:UNUSED_PAD src0_sel:WORD_1 src1_sel:DWORD
	v_and_b32_sdwa v91, v119, v222 dst_sel:DWORD dst_unused:UNUSED_PAD src0_sel:WORD_1 src1_sel:DWORD
	v_and_b32_sdwa v95, v120, v222 dst_sel:DWORD dst_unused:UNUSED_PAD src0_sel:WORD_1 src1_sel:DWORD
	v_add3_u32 v93, v121, v93, s30
	v_add3_u32 v91, v119, v91, s30
	v_add3_u32 v95, v120, v95, s30
	v_and_b32_e32 v123, 0xffff0000, v93
	v_or_b32_sdwa v127, v123, v91 dst_sel:DWORD dst_unused:UNUSED_PAD src0_sel:DWORD src1_sel:WORD_1
	v_or_b32_sdwa v126, v95, v122 dst_sel:DWORD dst_unused:UNUSED_PAD src0_sel:WORD_1 src1_sel:DWORD
	global_store_dwordx2 v[114:115], v[126:127], off offset:3584
	v_and_b32_e32 v115, 0xffff0000, v91
	v_and_b32_e32 v114, 0xffff0000, v95
	v_mov_b32_e32 v126, v120
	v_mov_b32_e32 v127, v119
	v_pk_add_f32 v[114:115], v[126:127], v[114:115] neg_lo:[0,1] neg_hi:[0,1]
	v_mov_b32_e32 v126, v118
	v_mov_b32_e32 v127, v121
	v_pk_add_f32 v[122:123], v[126:127], v[122:123] neg_lo:[0,1] neg_hi:[0,1]
	v_and_b32_sdwa v93, v114, v222 dst_sel:DWORD dst_unused:UNUSED_PAD src0_sel:WORD_1 src1_sel:DWORD
	v_add3_u32 v93, v114, v93, s30
	v_and_b32_sdwa v95, v123, v222 dst_sel:DWORD dst_unused:UNUSED_PAD src0_sel:WORD_1 src1_sel:DWORD
	v_and_b32_sdwa v114, v122, v222 dst_sel:DWORD dst_unused:UNUSED_PAD src0_sel:WORD_1 src1_sel:DWORD
	v_and_b32_sdwa v91, v115, v222 dst_sel:DWORD dst_unused:UNUSED_PAD src0_sel:WORD_1 src1_sel:DWORD
	v_add3_u32 v95, v123, v95, s30
	v_add3_u32 v114, v122, v114, s30
	v_add3_u32 v91, v115, v91, s30
	v_and_b32_e32 v95, 0xffff0000, v95
	v_and_b32_e32 v114, 0xffff0000, v114
	v_or_b32_sdwa v115, v95, v91 dst_sel:DWORD dst_unused:UNUSED_PAD src0_sel:DWORD src1_sel:WORD_1
	v_or_b32_sdwa v114, v114, v93 dst_sel:DWORD dst_unused:UNUSED_PAD src0_sel:DWORD src1_sel:WORD_1
	global_store_dwordx2 v[116:117], v[114:115], off offset:3584
	v_med3_f32 v95, v118, s33, v229
	v_med3_f32 v114, v120, s33, v229
	v_mov_b32_e32 v115, 0
	v_cvt_pk_fp8_f32 v115, v114, v95
	v_med3_f32 v91, v121, s33, v229
	v_med3_f32 v93, v119, s33, v229
	v_cvt_pk_fp8_f32 v115, v93, v91 op_sel:[0,0,1]
	global_store_dword v[112:113], v115, off offset:1792
	s_cbranch_scc0 .LBB0_872
	s_mov_b64 s[6:7], exec
	v_readlane_b32 s12, v254, 30
	v_readlane_b32 s13, v254, 31
	s_and_b64 s[12:13], s[6:7], s[12:13]
	s_mov_b64 exec, s[12:13]
	ds_write_b32 v155, v65
	s_or_b64 exec, exec, s[6:7]
	s_lshl_b32 s15, s31, 5
	v_or_b32_e32 v0, s15, v156
	v_ashrrev_i32_e32 v1, 31, v0
	v_lshlrev_b64 v[96:97], 11, v[0:1]
	v_or_b32_e32 v0, 16, v0
	v_lshl_or_b32 v100, s8, 8, v157
	v_ashrrev_i32_e32 v1, 31, v0
	v_ashrrev_i32_e32 v101, 31, v100
	v_mov_b32_e32 v16, 0
	v_lshlrev_b64 v[98:99], 11, v[0:1]
	v_lshl_add_u64 v[102:103], v[100:101], 1, v[78:79]
	s_mov_b64 s[6:7], 0
	v_mov_b32_e32 v17, v16
	v_mov_b32_e32 v18, v16
	v_mov_b32_e32 v19, v16
	v_mov_b32_e32 v0, v16
	v_mov_b32_e32 v1, v16
	v_mov_b32_e32 v2, v16
	v_mov_b32_e32 v3, v16
	v_mov_b32_e32 v4, v16
	v_mov_b32_e32 v5, v16
	v_mov_b32_e32 v6, v16
	v_mov_b32_e32 v7, v16
	v_mov_b32_e32 v24, v16
	v_mov_b32_e32 v25, v16
	v_mov_b32_e32 v26, v16
	v_mov_b32_e32 v27, v16
	v_mov_b32_e32 v20, v16
	v_mov_b32_e32 v21, v16
	v_mov_b32_e32 v22, v16
	v_mov_b32_e32 v23, v16
	v_mov_b32_e32 v12, v16
	v_mov_b32_e32 v13, v16
	v_mov_b32_e32 v14, v16
	v_mov_b32_e32 v15, v16
	v_mov_b32_e32 v8, v16
	v_mov_b32_e32 v9, v16
	v_mov_b32_e32 v10, v16
	v_mov_b32_e32 v11, v16
	v_mov_b32_e32 v28, v16
	v_mov_b32_e32 v29, v16
	v_mov_b32_e32 v30, v16
	v_mov_b32_e32 v31, v16
	s_waitcnt lgkmcnt(0)
	s_barrier
; __device__ __forceinline__ void ln1_router_unit(const Params& p, int l, int unit, LAS unsigned char* lds, int tid, bool dry = false) {
;     ...
;         for (int ks = 0; ks < 8; ++ks) {
;             const int k0 = 256 * wid + 32 * ks + 8 * fq;
;             bf16x8 ah[2], al[2];
; #pragma unroll
;             for (int mf = 0; mf < 2; ++mf) { const size_t xo = (size_t)(t0 + mf * 16 + fr) * D + k0; ah[mf] = *(const bf16x8*)(XB + xo); al[mf] = *(const bf16x8*)(XL + xo); }
; #pragma unroll
;             for (int nf = 0; nf < 4; ++nf) {
;                 const bf16x8 bh = *(const bf16x8*)(wrh + (size_t)(nf * 16 + fr) * D + k0), bl = *(const bf16x8*)(wrl + (size_t)(nf * 16 + fr) * D + k0);
; #pragma unroll
;                 for (int mf = 0; mf < 2; ++mf) {
;                     racc[mf][nf] = __builtin_amdgcn_mfma_f32_16x16x32_bf16(ah[mf], bh, racc[mf][nf], 0, 0, 0);
;                     racc[mf][nf] = __builtin_amdgcn_mfma_f32_16x16x32_bf16(ah[mf], bl, racc[mf][nf], 0, 0, 0);
;                     racc[mf][nf] = __builtin_amdgcn_mfma_f32_16x16x32_bf16(al[mf], bh, racc[mf][nf], 0, 0, 0); }
;             }
;         }
.LBB0_876:
	v_ashrrev_i32_e32 v101, 31, v100
	v_lshl_add_u64 v[32:33], v[96:97], 0, v[100:101]
	v_lshlrev_b64 v[32:33], 1, v[32:33]
	v_lshl_add_u64 v[34:35], s[92:93], 0, v[32:33]
	v_lshl_add_u64 v[32:33], s[90:91], 0, v[32:33]
	global_load_dwordx4 v[40:43], v[34:35], off
	global_load_dwordx4 v[44:47], v[32:33], off
	v_lshl_add_u64 v[32:33], v[98:99], 0, v[100:101]
	v_lshlrev_b64 v[36:37], 1, v[32:33]
	v_lshl_add_u64 v[32:33], s[92:93], 0, v[36:37]
	global_load_dwordx4 v[32:35], v[32:33], off
	v_lshlrev_b64 v[104:105], 1, v[100:101]
	v_lshl_add_u64 v[106:107], s[2:3], 0, v[104:105]
	v_lshl_add_u64 v[108:109], v[106:107], 0, v[64:65]
	global_load_dwordx4 v[108:111], v[108:109], off
	v_lshl_add_u64 v[104:105], s[4:5], 0, v[104:105]
	v_lshl_add_u64 v[36:37], s[90:91], 0, v[36:37]
	v_lshl_add_u64 v[112:113], v[104:105], 0, v[64:65]
	global_load_dwordx4 v[36:39], v[36:37], off
	v_mov_b32_e32 v91, v65
	global_load_dwordx4 v[112:115], v[112:113], off
	v_mov_b32_e32 v93, v65
	v_mov_b32_e32 v95, v65
	v_lshl_add_u64 v[232:233], v[104:105], 0, v[90:91]
	global_load_dwordx4 v[198:201], v[232:233], off
	v_lshl_add_u64 v[232:233], v[106:107], 0, v[90:91]
	global_load_dwordx4 v[202:205], v[232:233], off
	v_lshl_add_u64 v[232:233], v[104:105], 0, v[92:93]
	global_load_dwordx4 v[206:209], v[232:233], off
	v_lshl_add_u64 v[232:233], v[106:107], 0, v[92:93]
	global_load_dwordx4 v[210:213], v[232:233], off
	v_lshl_add_u64 v[232:233], v[106:107], 0, v[94:95]
	global_load_dwordx4 v[214:217], v[232:233], off
	v_lshl_add_u64 v[232:233], v[104:105], 0, v[94:95]
	global_load_dwordx4 v[218:221], v[232:233], off
	s_mov_b32 s12, 0x600000
	s_waitcnt vmcnt(8)
	v_mfma_f32_16x16x32_bf16 v[24:27], v[40:43], v[108:111], v[24:27]
	v_mfma_f32_16x16x32_bf16 v[20:23], v[32:35], v[108:111], v[20:23]
	s_waitcnt vmcnt(6)
	v_mfma_f32_16x16x32_bf16 v[24:27], v[40:43], v[112:115], v[24:27]
	v_mfma_f32_16x16x32_bf16 v[20:23], v[32:35], v[112:115], v[20:23]
	v_lshl_add_u64 v[112:113], v[104:105], 0, v[90:91]
	s_waitcnt vmcnt(5)
	v_mov_b64_e32 v[112:113], v[198:199]
	v_mov_b64_e32 v[114:115], v[200:201]
	s_nop 1
	v_mfma_f32_16x16x32_bf16 v[24:27], v[44:47], v[108:111], v[24:27]
	v_mfma_f32_16x16x32_bf16 v[20:23], v[36:39], v[108:111], v[20:23]
	v_lshl_add_u64 v[108:109], v[106:107], 0, v[90:91]
	s_waitcnt vmcnt(4)
	v_mov_b64_e32 v[108:109], v[202:203]
	v_mov_b64_e32 v[110:111], v[204:205]
	s_nop 1
	v_mfma_f32_16x16x32_bf16 v[4:7], v[40:43], v[108:111], v[4:7]
	v_mfma_f32_16x16x32_bf16 v[12:15], v[32:35], v[108:111], v[12:15]
	v_mfma_f32_16x16x32_bf16 v[4:7], v[40:43], v[112:115], v[4:7]
	v_mfma_f32_16x16x32_bf16 v[12:15], v[32:35], v[112:115], v[12:15]
	v_lshl_add_u64 v[112:113], v[104:105], 0, v[92:93]
	s_waitcnt vmcnt(3)
	v_mov_b64_e32 v[112:113], v[206:207]
	v_mov_b64_e32 v[114:115], v[208:209]
	s_nop 1
	v_lshl_add_u64 v[104:105], v[104:105], 0, v[94:95]
	v_mfma_f32_16x16x32_bf16 v[4:7], v[44:47], v[108:111], v[4:7]
	v_mfma_f32_16x16x32_bf16 v[12:15], v[36:39], v[108:111], v[12:15]
	v_lshl_add_u64 v[108:109], v[106:107], 0, v[92:93]
	s_waitcnt vmcnt(2)
	v_mov_b64_e32 v[108:109], v[210:211]
	v_mov_b64_e32 v[110:111], v[212:213]
	s_nop 1
	v_lshl_add_u64 v[106:107], v[106:107], 0, v[94:95]
	v_mfma_f32_16x16x32_bf16 v[0:3], v[40:43], v[108:111], v[0:3]
	v_mfma_f32_16x16x32_bf16 v[8:11], v[32:35], v[108:111], v[8:11]
	v_mfma_f32_16x16x32_bf16 v[0:3], v[40:43], v[112:115], v[0:3]
	v_mfma_f32_16x16x32_bf16 v[8:11], v[32:35], v[112:115], v[8:11]
	v_mfma_f32_16x16x32_bf16 v[0:3], v[44:47], v[108:111], v[0:3]
	v_mfma_f32_16x16x32_bf16 v[8:11], v[36:39], v[108:111], v[8:11]
	s_waitcnt vmcnt(1)
	v_mov_b64_e32 v[106:107], v[214:215]
	v_mov_b64_e32 v[108:109], v[216:217]
	s_nop 1
	s_nop 0
	s_waitcnt vmcnt(0)
	v_mov_b64_e32 v[110:111], v[218:219]
	v_mov_b64_e32 v[112:113], v[220:221]
	s_nop 1
	v_add_u32_e32 v104, 32, v100
	v_ashrrev_i32_e32 v105, 31, v104
	v_add_u32_e32 v100, 64, v100
	v_mfma_f32_16x16x32_bf16 v[16:19], v[40:43], v[106:109], v[16:19]
	v_mfma_f32_16x16x32_bf16 v[28:31], v[32:35], v[106:109], v[28:31]
	v_mfma_f32_16x16x32_bf16 v[16:19], v[40:43], v[110:113], v[16:19]
	v_mfma_f32_16x16x32_bf16 v[28:31], v[32:35], v[110:113], v[28:31]
	v_lshl_add_u64 v[32:33], v[96:97], 0, v[104:105]
	v_lshlrev_b64 v[32:33], 1, v[32:33]
	v_lshl_add_u64 v[34:35], s[92:93], 0, v[32:33]
	v_lshl_add_u64 v[32:33], s[90:91], 0, v[32:33]
	v_mfma_f32_16x16x32_bf16 v[16:19], v[44:47], v[106:109], v[16:19]
	global_load_dwordx4 v[40:43], v[34:35], off
	global_load_dwordx4 v[44:47], v[32:33], off
	v_lshl_add_u64 v[32:33], v[98:99], 0, v[104:105]
	v_mfma_f32_16x16x32_bf16 v[28:31], v[36:39], v[106:109], v[28:31]
	v_lshlrev_b64 v[36:37], 1, v[32:33]
	v_lshl_add_u64 v[32:33], s[92:93], 0, v[36:37]
	global_load_dwordx4 v[32:35], v[32:33], off
	v_lshl_add_u64 v[106:107], v[102:103], 0, s[6:7]
	v_add_co_u32_e32 v108, vcc, s12, v106
	v_lshlrev_b64 v[112:113], 1, v[104:105]
	s_nop 0
	v_addc_co_u32_e32 v109, vcc, 0, v107, vcc
	global_load_dwordx4 v[108:111], v[108:109], off offset:64
	v_lshl_add_u64 v[36:37], s[90:91], 0, v[36:37]
	v_lshl_add_u64 v[104:105], s[4:5], 0, v[112:113]
	v_lshl_add_u64 v[112:113], v[88:89], 0, v[112:113]
	global_load_dwordx4 v[36:39], v[36:37], off
	s_mov_b32 s12, 0x610000
	global_load_dwordx4 v[112:115], v[112:113], off
	v_lshl_add_u64 v[232:233], v[104:105], 0, v[90:91]
	global_load_dwordx4 v[198:201], v[232:233], off
	s_mov_b32 s13, 0x610000
	v_add_co_u32_e32 v232, vcc, s13, v106
	s_nop 1
	v_addc_co_u32_e32 v233, vcc, 0, v107, vcc
	global_load_dwordx4 v[202:205], v[232:233], off offset:64
	v_lshl_add_u64 v[232:233], v[104:105], 0, v[92:93]
	global_load_dwordx4 v[206:209], v[232:233], off
	s_mov_b32 s13, 0x620000
	v_add_co_u32_e32 v232, vcc, s13, v106
	s_nop 1
	v_addc_co_u32_e32 v233, vcc, 0, v107, vcc
	global_load_dwordx4 v[210:213], v[232:233], off offset:64
	s_mov_b32 s13, 0x630000
	v_add_co_u32_e32 v232, vcc, s13, v106
	s_nop 1
	v_addc_co_u32_e32 v233, vcc, 0, v107, vcc
	global_load_dwordx4 v[214:217], v[232:233], off offset:64
	v_lshl_add_u64 v[232:233], v[104:105], 0, v[94:95]
	global_load_dwordx4 v[218:221], v[232:233], off
	s_add_u32 s6, s6, 0x80
	s_addc_u32 s7, s7, 0
	s_cmpk_eq_i32 s6, 0x200
	s_waitcnt vmcnt(8)
; #define LAS __attribute__((address_space(3)))
; __device__ __forceinline__ float sigmoidf_(float v) { return 1.0f / (1.0f + __expf(-v)); }
; __device__ __forceinline__ void ln1_router_unit(const Params& p, int l, int unit, LAS unsigned char* lds, int tid, bool dry = false) {
;     ...
;         for (int ks = 0; ks < 8; ++ks) {
;             const int k0 = 256 * wid + 32 * ks + 8 * fq;
;             bf16x8 ah[2], al[2];
; #pragma unroll
;             for (int mf = 0; mf < 2; ++mf) { const size_t xo = (size_t)(t0 + mf * 16 + fr) * D + k0; ah[mf] = *(const bf16x8*)(XB + xo); al[mf] = *(const bf16x8*)(XL + xo); }
; #pragma unroll
;             for (int nf = 0; nf < 4; ++nf) {
;                 const bf16x8 bh = *(const bf16x8*)(wrh + (size_t)(nf * 16 + fr) * D + k0), bl = *(const bf16x8*)(wrl + (size_t)(nf * 16 + fr) * D + k0);
; #pragma unroll
;                 for (int mf = 0; mf < 2; ++mf) {
;                     racc[mf][nf] = __builtin_amdgcn_mfma_f32_16x16x32_bf16(ah[mf], bh, racc[mf][nf], 0, 0, 0);
;                     racc[mf][nf] = __builtin_amdgcn_mfma_f32_16x16x32_bf16(ah[mf], bl, racc[mf][nf], 0, 0, 0);
;                     racc[mf][nf] = __builtin_amdgcn_mfma_f32_16x16x32_bf16(al[mf], bh, racc[mf][nf], 0, 0, 0); }
;             }
;         }
; #pragma unroll
;         for (int mf = 0; mf < 2; ++mf)
; #pragma unroll
;             for (int nf = 0; nf < 4; ++nf)
; #pragma unroll
;                 for (int r = 0; r < 4; ++r) part[(wid * 32 + mf * 16 + 4 * fq + r) * 64 + nf * 16 + fr] = racc[mf][nf][r];
;     }
;     __syncthreads();
;     { f32x4 sm = *(const LAS f32x4*)(part + tid * 4);
; #pragma unroll
;       for (int w = 1; w < 8; ++w) sm += *(const LAS f32x4*)(part + w * 2048 + tid * 4);
;       *(LAS f32x4*)(lg + tid * 4) = (f32x4){sigmoidf_(sm.x), sigmoidf_(sm.y), sigmoidf_(sm.z), sigmoidf_(sm.w)}; }
;     __syncthreads();
;     {
;         const float rbias = p.in[18][(size_t)l * NE + lane]; const int gi = lane >> 3;
	v_mfma_f32_16x16x32_bf16 v[24:27], v[40:43], v[108:111], v[24:27]
	v_mfma_f32_16x16x32_bf16 v[20:23], v[32:35], v[108:111], v[20:23]
	s_waitcnt vmcnt(6)
	v_mfma_f32_16x16x32_bf16 v[24:27], v[40:43], v[112:115], v[24:27]
	v_mfma_f32_16x16x32_bf16 v[20:23], v[32:35], v[112:115], v[20:23]
	v_lshl_add_u64 v[112:113], v[104:105], 0, v[90:91]
	s_waitcnt vmcnt(5)
	v_mov_b64_e32 v[112:113], v[198:199]
	v_mov_b64_e32 v[114:115], v[200:201]
	s_nop 1
	v_mfma_f32_16x16x32_bf16 v[24:27], v[44:47], v[108:111], v[24:27]
	v_mfma_f32_16x16x32_bf16 v[20:23], v[36:39], v[108:111], v[20:23]
	v_add_co_u32_e32 v108, vcc, s12, v106
	s_mov_b32 s12, 0x620000
	s_nop 0
	v_addc_co_u32_e32 v109, vcc, 0, v107, vcc
	s_waitcnt vmcnt(4)
	v_mov_b64_e32 v[108:109], v[202:203]
	v_mov_b64_e32 v[110:111], v[204:205]
	s_nop 1
	v_mfma_f32_16x16x32_bf16 v[4:7], v[40:43], v[108:111], v[4:7]
	v_mfma_f32_16x16x32_bf16 v[12:15], v[32:35], v[108:111], v[12:15]
	v_mfma_f32_16x16x32_bf16 v[4:7], v[40:43], v[112:115], v[4:7]
	v_mfma_f32_16x16x32_bf16 v[12:15], v[32:35], v[112:115], v[12:15]
	v_lshl_add_u64 v[112:113], v[104:105], 0, v[92:93]
	s_waitcnt vmcnt(3)
	v_mov_b64_e32 v[112:113], v[206:207]
	v_mov_b64_e32 v[114:115], v[208:209]
	s_nop 1
	v_lshl_add_u64 v[104:105], v[104:105], 0, v[94:95]
	v_mfma_f32_16x16x32_bf16 v[4:7], v[44:47], v[108:111], v[4:7]
	v_mfma_f32_16x16x32_bf16 v[12:15], v[36:39], v[108:111], v[12:15]
	v_add_co_u32_e32 v108, vcc, s12, v106
	s_mov_b32 s12, 0x630000
	s_nop 0
	v_addc_co_u32_e32 v109, vcc, 0, v107, vcc
	s_waitcnt vmcnt(2)
	v_mov_b64_e32 v[108:109], v[210:211]
	v_mov_b64_e32 v[110:111], v[212:213]
	s_nop 1
	v_mfma_f32_16x16x32_bf16 v[0:3], v[40:43], v[108:111], v[0:3]
	v_add_co_u32_e32 v106, vcc, s12, v106
	v_mfma_f32_16x16x32_bf16 v[8:11], v[32:35], v[108:111], v[8:11]
	s_nop 0
	v_addc_co_u32_e32 v107, vcc, 0, v107, vcc
	v_mfma_f32_16x16x32_bf16 v[0:3], v[40:43], v[112:115], v[0:3]
	v_mfma_f32_16x16x32_bf16 v[8:11], v[32:35], v[112:115], v[8:11]
	v_mfma_f32_16x16x32_bf16 v[0:3], v[44:47], v[108:111], v[0:3]
	v_mfma_f32_16x16x32_bf16 v[8:11], v[36:39], v[108:111], v[8:11]
	s_waitcnt vmcnt(1)
	v_mov_b64_e32 v[106:107], v[214:215]
	v_mov_b64_e32 v[108:109], v[216:217]
	s_nop 1
	s_nop 0
	s_waitcnt vmcnt(0)
	v_mov_b64_e32 v[110:111], v[218:219]
	v_mov_b64_e32 v[112:113], v[220:221]
	s_nop 1
	v_mfma_f32_16x16x32_bf16 v[16:19], v[40:43], v[106:109], v[16:19]
	v_mfma_f32_16x16x32_bf16 v[28:31], v[32:35], v[106:109], v[28:31]
	v_mfma_f32_16x16x32_bf16 v[16:19], v[40:43], v[110:113], v[16:19]
	v_mfma_f32_16x16x32_bf16 v[28:31], v[32:35], v[110:113], v[28:31]
	v_mfma_f32_16x16x32_bf16 v[16:19], v[44:47], v[106:109], v[16:19]
	v_mfma_f32_16x16x32_bf16 v[28:31], v[36:39], v[106:109], v[28:31]
	s_cbranch_scc0 .LBB0_876
	v_lshl_or_b32 v32, s8, 13, v158
	v_add_u32_e32 v32, v159, v32
	ds_write2_b32 v32, v24, v4 offset1:16
	ds_write2_b32 v32, v25, v5 offset0:64 offset1:80
	ds_write2_b32 v32, v26, v6 offset0:128 offset1:144
	ds_write2_b32 v32, v27, v7 offset0:192 offset1:208
	ds_write2_b32 v32, v0, v16 offset0:32 offset1:48
	ds_write2_b32 v32, v1, v17 offset0:96 offset1:112
	ds_write2_b32 v32, v2, v18 offset0:160 offset1:176
	ds_write2_b32 v32, v3, v19 offset0:224 offset1:240
	v_add_u32_e32 v0, 0x1000, v32
	ds_write2_b32 v0, v20, v12 offset1:16
	ds_write2_b32 v0, v21, v13 offset0:64 offset1:80
	ds_write2_b32 v0, v22, v14 offset0:128 offset1:144
	ds_write2_b32 v0, v23, v15 offset0:192 offset1:208
	ds_write2_b32 v0, v8, v28 offset0:32 offset1:48
	ds_write2_b32 v0, v9, v29 offset0:96 offset1:112
	ds_write2_b32 v0, v10, v30 offset0:160 offset1:176
	ds_write2_b32 v0, v11, v31 offset0:224 offset1:240
	s_waitcnt lgkmcnt(0)
	s_barrier
	ds_read_b128 v[0:3], v160
	ds_read_b128 v[4:7], v160 offset:8192
	s_lshl_b32 s13, s8, 5
	s_mov_b32 s14, 0
	s_waitcnt lgkmcnt(0)
	v_pk_add_f32 v[6:7], v[2:3], v[6:7]
	v_pk_add_f32 v[4:5], v[0:1], v[4:5]
	ds_read_b128 v[0:3], v160 offset:16384
	s_waitcnt lgkmcnt(0)
	v_pk_add_f32 v[6:7], v[6:7], v[2:3]
	v_pk_add_f32 v[4:5], v[4:5], v[0:1]
	ds_read_b128 v[0:3], v160 offset:24576
	s_waitcnt lgkmcnt(0)
	v_pk_add_f32 v[6:7], v[6:7], v[2:3]
	v_pk_add_f32 v[4:5], v[4:5], v[0:1]
	ds_read_b128 v[0:3], v160 offset:32768
	s_waitcnt lgkmcnt(0)
	v_pk_add_f32 v[6:7], v[6:7], v[2:3]
	v_pk_add_f32 v[4:5], v[4:5], v[0:1]
	ds_read_b128 v[0:3], v160 offset:40960
	s_waitcnt lgkmcnt(0)
	v_pk_add_f32 v[6:7], v[6:7], v[2:3]
	v_pk_add_f32 v[4:5], v[4:5], v[0:1]
	ds_read_b128 v[0:3], v160 offset:49152
	s_waitcnt lgkmcnt(0)
	v_pk_add_f32 v[6:7], v[6:7], v[2:3]
	v_pk_add_f32 v[4:5], v[4:5], v[0:1]
	ds_read_b128 v[0:3], v160 offset:57344
	s_waitcnt lgkmcnt(0)
	v_pk_add_f32 v[2:3], v[6:7], v[2:3]
	s_nop 0
	v_mul_f32_e32 v2, 0xbfb8aa3b, v2
	v_mul_f32_e32 v3, 0xbfb8aa3b, v3
	v_exp_f32_e32 v2, v2
	v_exp_f32_e32 v3, v3
	v_pk_add_f32 v[0:1], v[4:5], v[0:1]
	v_pk_add_f32 v[2:3], v[2:3], 1.0 op_sel_hi:[1,0]
	s_nop 0
	v_div_scale_f32 v4, s[6:7], v3, v3, 1.0
	v_rcp_f32_e32 v5, v4
	v_mul_f32_e32 v0, 0xbfb8aa3b, v0
	v_mul_f32_e32 v1, 0xbfb8aa3b, v1
	v_exp_f32_e32 v0, v0
	v_fma_f32 v6, -v4, v5, 1.0
	v_fmac_f32_e32 v5, v6, v5
	v_div_scale_f32 v6, vcc, 1.0, v3, 1.0
	v_mul_f32_e32 v7, v6, v5
	v_fma_f32 v8, -v4, v7, v6
	v_fmac_f32_e32 v7, v8, v5
	v_fma_f32 v4, -v4, v7, v6
	v_div_fmas_f32 v4, v4, v5, v7
	v_div_fixup_f32 v3, v4, v3, 1.0
	v_div_scale_f32 v4, s[6:7], v2, v2, 1.0
	v_rcp_f32_e32 v5, v4
	v_exp_f32_e32 v1, v1
	v_fma_f32 v6, -v4, v5, 1.0
	v_fmac_f32_e32 v5, v6, v5
	v_div_scale_f32 v6, vcc, 1.0, v2, 1.0
	v_mul_f32_e32 v7, v6, v5
	v_fma_f32 v8, -v4, v7, v6
	v_fmac_f32_e32 v7, v8, v5
	v_fma_f32 v4, -v4, v7, v6
	v_pk_add_f32 v[0:1], v[0:1], 1.0 op_sel_hi:[1,0]
	v_div_fmas_f32 v4, v4, v5, v7
	v_div_fixup_f32 v2, v4, v2, 1.0
	v_div_scale_f32 v4, s[6:7], v1, v1, 1.0
	v_rcp_f32_e32 v5, v4
	s_nop 0
	v_fma_f32 v6, -v4, v5, 1.0
	v_fmac_f32_e32 v5, v6, v5
	v_div_scale_f32 v6, vcc, 1.0, v1, 1.0
	v_mul_f32_e32 v7, v6, v5
	v_fma_f32 v8, -v4, v7, v6
	v_fmac_f32_e32 v7, v8, v5
	v_fma_f32 v4, -v4, v7, v6
	v_div_fmas_f32 v4, v4, v5, v7
	v_div_fixup_f32 v1, v4, v1, 1.0
	v_div_scale_f32 v4, s[6:7], v0, v0, 1.0
	v_rcp_f32_e32 v5, v4
	s_and_b32 s6, s9, 0x3fffffc0
	s_lshl_b32 s6, s6, 2
	s_add_i32 s12, s6, 0
	v_fma_f32 v6, -v4, v5, 1.0
	v_fmac_f32_e32 v5, v6, v5
	v_div_scale_f32 v6, vcc, 1.0, v0, 1.0
	v_mul_f32_e32 v7, v6, v5
	v_fma_f32 v8, -v4, v7, v6
	v_fmac_f32_e32 v7, v8, v5
	v_fma_f32 v4, -v4, v7, v6
	v_div_fmas_f32 v4, v4, v5, v7
	v_div_fixup_f32 v0, v4, v0, 1.0
	ds_write_b128 v161, v[0:3]
	s_waitcnt lgkmcnt(0)
	s_barrier
	global_load_dword v4, v[72:73], off
	s_add_i32 s12, s12, 0x12000
	v_lshl_add_u32 v5, v75, 2, s12
	v_lshl_add_u32 v6, s8, 10, v166
	s_mov_b32 s7, 0
	s_branch .LBB0_879
